# speedup vs baseline: 1.0149x; 1.0149x over previous
.LBB0_15:
	s_waitcnt lgkmcnt(0)
	s_mul_i32 s0, s10, s11
	s_abs_i32 s1, s0
	v_cvt_f32_u32_e32 v1, s1
	s_sub_i32 s16, 0, s1
	s_sub_i32 s2, s2, s24
	s_add_i32 s2, s2, s21
	v_rcp_iflag_f32_e32 v1, v1
	s_abs_i32 s11, s2
	s_xor_b32 s3, s2, s0
	s_ashr_i32 s3, s3, 31
	v_mul_f32_e32 v1, 0x4f7ffffe, v1
	v_cvt_u32_f32_e32 v1, v1
	v_lshrrev_b32_e32 v36, 4, v0
	v_lshlrev_b32_e32 v2, 4, v0
	v_and_b32_e32 v34, 0xf0, v2
	v_readfirstlane_b32 s17, v1
	s_mul_i32 s16, s16, s17
	s_mul_hi_u32 s16, s17, s16
	s_add_i32 s17, s17, s16
	s_mul_hi_u32 s16, s11, s17
	s_mul_i32 s17, s16, s1
	s_sub_i32 s11, s11, s17
	s_add_i32 s18, s16, 1
	s_sub_i32 s17, s11, s1
	s_cmp_ge_u32 s11, s1
	s_cselect_b32 s16, s18, s16
	s_cselect_b32 s11, s17, s11
	s_add_i32 s17, s16, 1
	s_cmp_ge_u32 s11, s1
	s_cselect_b32 s1, s17, s16
	s_abs_i32 s11, s10
	v_cvt_f32_u32_e32 v1, s11
	s_xor_b32 s1, s1, s3
	s_sub_i32 s16, 0, s11
	s_sub_i32 s3, s1, s3
	v_rcp_iflag_f32_e32 v1, v1
	s_mul_i32 s0, s3, s0
	s_sub_i32 s0, s2, s0
	s_abs_i32 s2, s0
	v_mul_f32_e32 v1, 0x4f7ffffe, v1
	v_cvt_u32_f32_e32 v1, v1
	s_xor_b32 s1, s0, s10
	s_ashr_i32 s1, s1, 31
	v_mov_b32_e32 v35, 0
	v_readfirstlane_b32 s17, v1
	s_mul_i32 s16, s16, s17
	s_mul_hi_u32 s16, s17, s16
	s_add_i32 s17, s17, s16
	s_mul_hi_u32 s16, s2, s17
	s_mul_i32 s17, s16, s11
	s_sub_i32 s2, s2, s17
	s_add_i32 s18, s16, 1
	s_sub_i32 s17, s2, s11
	s_cmp_ge_u32 s2, s11
	s_cselect_b32 s16, s18, s16
	s_cselect_b32 s2, s17, s2
	s_add_i32 s17, s16, 1
	s_cmp_ge_u32 s2, s11
	s_cselect_b32 s2, s17, s16
	s_xor_b32 s2, s2, s1
	s_sub_i32 s2, s2, s1
	s_mul_i32 s1, s2, s10
	s_ashr_i32 s11, s3, 31
	s_sub_i32 s10, s0, s1
	s_mul_i32 s0, s12, s11
	s_mul_hi_u32 s1, s12, s3
	s_add_i32 s0, s1, s0
	s_mul_i32 s1, s13, s3
	s_add_i32 s1, s0, s1
	s_mul_i32 s0, s12, s3
	s_lshl_b64 s[0:1], s[0:1], 2
	s_add_u32 s4, s4, s0
	s_addc_u32 s12, s5, s1
	s_mul_i32 s0, s14, s11
	s_mul_hi_u32 s1, s14, s3
	s_add_i32 s0, s1, s0
	s_mul_i32 s1, s15, s3
	s_add_i32 s5, s0, s1
	s_lshl_b32 s0, s10, 6
	s_ashr_i32 s1, s0, 31
	s_lshl_b32 s2, s2, 7
	s_lshl_b64 s[10:11], s[0:1], 2
	s_add_u32 s10, s4, s10
	v_or_b32_e32 v1, s2, v36
	s_addc_u32 s11, s12, s11
	v_lshl_add_u64 v[30:31], s[10:11], 0, v[34:35]
	v_mad_i64_i32 v[2:3], s[10:11], v1, s9, 0
	v_lshl_add_u64 v[10:11], v[2:3], 2, v[30:31]
	v_or_b32_e32 v2, 16, v1
	v_mad_i64_i32 v[2:3], s[10:11], v2, s9, 0
	v_lshl_add_u64 v[12:13], v[2:3], 2, v[30:31]
	global_load_dwordx4 v[2:5], v[10:11], off nt
	global_load_dwordx4 v[6:9], v[12:13], off nt
	v_or_b32_e32 v10, 32, v1
	v_mad_i64_i32 v[10:11], s[10:11], v10, s9, 0
	v_lshl_add_u64 v[18:19], v[10:11], 2, v[30:31]
	v_or_b32_e32 v10, 48, v1
	v_mad_i64_i32 v[10:11], s[10:11], v10, s9, 0
	v_lshl_add_u64 v[20:21], v[10:11], 2, v[30:31]
	global_load_dwordx4 v[10:13], v[18:19], off nt
	global_load_dwordx4 v[14:17], v[20:21], off nt
	v_or_b32_e32 v18, 64, v1
	v_mad_i64_i32 v[18:19], s[10:11], v18, s9, 0
	v_lshl_add_u64 v[26:27], v[18:19], 2, v[30:31]
	v_or_b32_e32 v18, 0x50, v1
	v_mad_i64_i32 v[18:19], s[10:11], v18, s9, 0
	v_lshl_add_u64 v[28:29], v[18:19], 2, v[30:31]
	global_load_dwordx4 v[18:21], v[26:27], off nt
	global_load_dwordx4 v[22:25], v[28:29], off nt
	v_or_b32_e32 v26, 0x60, v1
	v_mad_i64_i32 v[26:27], s[10:11], v26, s9, 0
	v_lshl_add_u64 v[26:27], v[26:27], 2, v[30:31]
	v_or_b32_e32 v1, 0x70, v1
	global_load_dwordx4 v[26:29], v[26:27], off nt
	v_mad_i64_i32 v[32:33], s[10:11], v1, s9, 0
	v_lshl_add_u64 v[30:31], v[32:33], 2, v[30:31]
	global_load_dwordx4 v[30:33], v[30:31], off nt
	s_movk_i32 s1, 0x104
	v_mad_u32_u24 v1, v36, s1, v34
	v_lshlrev_b32_e32 v0, 3, v0
	v_add_u32_e32 v34, 0x1040, v1
	v_add_u32_e32 v37, 0x1048, v1
	v_add_u32_e32 v38, 0x2080, v1
	v_add_u32_e32 v39, 0x2088, v1
	v_add_u32_e32 v40, 0x30c0, v1
	v_add_u32_e32 v41, 0x30c8, v1
	v_add_u32_e32 v42, 0x4100, v1
	v_add_u32_e32 v43, 0x4108, v1
	v_add_u32_e32 v44, 0x5140, v1
	v_and_b32_e32 v0, 0x78, v0
	s_mul_i32 s4, s14, s3
	s_lshl_b64 s[4:5], s[4:5], 1
	s_add_u32 s1, s6, s4
	s_addc_u32 s4, s7, s5
	s_ashr_i32 s3, s2, 31
	s_lshl_b64 s[2:3], s[2:3], 1
	s_add_u32 s2, s1, s2
	s_addc_u32 s3, s4, s3
	s_waitcnt vmcnt(7)
	ds_write2_b32 v1, v2, v3 offset1:1
	ds_write2_b32 v1, v4, v5 offset0:2 offset1:3
	s_waitcnt vmcnt(6)
	ds_write2_b32 v34, v6, v7 offset1:1
	ds_write2_b32 v37, v8, v9 offset1:1
	s_waitcnt vmcnt(5)
	ds_write2_b32 v38, v10, v11 offset1:1
	ds_write2_b32 v39, v12, v13 offset1:1
	s_waitcnt vmcnt(4)
	ds_write2_b32 v40, v14, v15 offset1:1
	ds_write2_b32 v41, v16, v17 offset1:1
	s_waitcnt vmcnt(3)
	ds_write2_b32 v42, v18, v19 offset1:1
	ds_write2_b32 v43, v20, v21 offset1:1
	s_waitcnt vmcnt(2)
	ds_write2_b32 v44, v22, v23 offset1:1
	v_add_u32_e32 v2, 0x5148, v1
	ds_write2_b32 v2, v24, v25 offset1:1
	v_add_u32_e32 v2, 0x6180, v1
	v_lshlrev_b32_e32 v34, 1, v0
	v_mul_u32_u24_e32 v0, 0x104, v0
	s_waitcnt vmcnt(1)
	ds_write2_b32 v2, v26, v27 offset1:1
	v_add_u32_e32 v2, 0x6188, v1
	v_lshl_add_u32 v24, v36, 2, v0
	ds_write2_b32 v2, v28, v29 offset1:1
	v_add_u32_e32 v2, 0x71c0, v1
	v_add_u32_e32 v1, 0x71c8, v1
	v_add_u32_e32 v25, 0x400, v24
	s_waitcnt vmcnt(0)
	ds_write2_b32 v2, v30, v31 offset1:1
	ds_write2_b32 v1, v32, v33 offset1:1
	s_waitcnt lgkmcnt(0)
	s_barrier
	ds_read2_b32 v[4:5], v24 offset1:16
	ds_read2_b32 v[6:7], v24 offset0:130 offset1:146
	ds_read2_b32 v[8:9], v25 offset0:4 offset1:20
	ds_read2_b32 v[10:11], v25 offset0:134 offset1:150
	ds_read2_b32 v[12:13], v25 offset0:199 offset1:215
	ds_read2_b32 v[14:15], v25 offset0:69 offset1:85
	ds_read2_b32 v[16:17], v24 offset0:195 offset1:211
	ds_read2_b32 v[18:19], v24 offset0:65 offset1:81
	v_or_b32_e32 v26, s0, v36
	v_lshl_add_u64 v[20:21], s[2:3], 0, v[34:35]
	v_mad_i64_i32 v[22:23], s[0:1], v26, s8, 0
	s_waitcnt lgkmcnt(3)
	v_cvt_pk_f16_f32 v3, v10, v12
	s_waitcnt lgkmcnt(2)
	v_cvt_pk_f16_f32 v2, v8, v14
	s_waitcnt lgkmcnt(1)
	v_cvt_pk_f16_f32 v1, v6, v16
	s_waitcnt lgkmcnt(0)
	v_cvt_pk_f16_f32 v0, v4, v18
	v_lshl_add_u64 v[22:23], v[22:23], 1, v[20:21]
	global_store_dwordx4 v[22:23], v[0:3], off
	v_or_b32_e32 v4, 16, v26
	s_nop 0
	v_cvt_pk_f16_f32 v3, v11, v13
	v_cvt_pk_f16_f32 v2, v9, v15
	v_cvt_pk_f16_f32 v1, v7, v17
	v_cvt_pk_f16_f32 v0, v5, v19
	ds_read2_b32 v[6:7], v24 offset0:32 offset1:48
	ds_read2_b32 v[8:9], v24 offset0:162 offset1:178
	ds_read2_b32 v[10:11], v25 offset0:36 offset1:52
	ds_read2_b32 v[12:13], v25 offset0:166 offset1:182
	ds_read2_b32 v[14:15], v25 offset0:231 offset1:247
	ds_read2_b32 v[16:17], v25 offset0:101 offset1:117
	ds_read2_b32 v[18:19], v24 offset0:227 offset1:243
	ds_read2_b32 v[22:23], v24 offset0:97 offset1:113
	v_mad_i64_i32 v[4:5], s[0:1], v4, s8, 0
	v_lshl_add_u64 v[4:5], v[4:5], 1, v[20:21]
	global_store_dwordx4 v[4:5], v[0:3], off
	v_or_b32_e32 v4, 32, v26
	v_mad_i64_i32 v[4:5], s[0:1], v4, s8, 0
	s_waitcnt lgkmcnt(3)
	v_cvt_pk_f16_f32 v3, v12, v14
	s_waitcnt lgkmcnt(2)
	v_cvt_pk_f16_f32 v2, v10, v16
	s_waitcnt lgkmcnt(1)
	v_cvt_pk_f16_f32 v1, v8, v18
	s_waitcnt lgkmcnt(0)
	v_cvt_pk_f16_f32 v0, v6, v22
	v_lshl_add_u64 v[4:5], v[4:5], 1, v[20:21]
	global_store_dwordx4 v[4:5], v[0:3], off
	v_or_b32_e32 v4, 48, v26
	v_mad_i64_i32 v[4:5], s[0:1], v4, s8, 0
	v_cvt_pk_f16_f32 v3, v13, v15
	v_cvt_pk_f16_f32 v2, v11, v17
	v_cvt_pk_f16_f32 v1, v9, v19
	v_cvt_pk_f16_f32 v0, v7, v23
	v_lshl_add_u64 v[4:5], v[4:5], 1, v[20:21]
	global_store_dwordx4 v[4:5], v[0:3], off
	s_endpgm
	s_endpgm
	s_endpgm
	s_endpgm
	s_endpgm
	s_endpgm
	s_endpgm
	s_endpgm
	s_endpgm
	s_endpgm
	s_endpgm
	s_endpgm
	s_endpgm
	s_endpgm
	s_endpgm
	s_endpgm
	s_endpgm
	s_endpgm

.LBB1_18:
	s_waitcnt lgkmcnt(0)
	s_mul_i32 s0, s10, s11
	s_abs_i32 s1, s0
	v_cvt_f32_u32_e32 v1, s1
	s_sub_i32 s16, 0, s1
	s_sub_i32 s2, s19, s2
	s_add_i32 s2, s2, s21
	v_rcp_iflag_f32_e32 v1, v1
	s_abs_i32 s11, s2
	s_xor_b32 s3, s2, s0
	s_ashr_i32 s3, s3, 31
	v_mul_f32_e32 v1, 0x4f7ffffe, v1
	v_cvt_u32_f32_e32 v1, v1
	v_lshrrev_b32_e32 v36, 4, v0
	v_lshlrev_b32_e32 v2, 4, v0
	v_and_b32_e32 v34, 0xf0, v2
	v_readfirstlane_b32 s17, v1
	s_mul_i32 s16, s16, s17
	s_mul_hi_u32 s16, s17, s16
	s_add_i32 s17, s17, s16
	s_mul_hi_u32 s16, s11, s17
	s_mul_i32 s17, s16, s1
	s_sub_i32 s11, s11, s17
	s_add_i32 s18, s16, 1
	s_sub_i32 s17, s11, s1
	s_cmp_ge_u32 s11, s1
	s_cselect_b32 s16, s18, s16
	s_cselect_b32 s11, s17, s11
	s_add_i32 s17, s16, 1
	s_cmp_ge_u32 s11, s1
	s_cselect_b32 s1, s17, s16
	s_abs_i32 s11, s10
	v_cvt_f32_u32_e32 v1, s11
	s_xor_b32 s1, s1, s3
	s_sub_i32 s16, 0, s11
	s_sub_i32 s3, s1, s3
	v_rcp_iflag_f32_e32 v1, v1
	s_mul_i32 s0, s3, s0
	s_sub_i32 s0, s2, s0
	s_abs_i32 s2, s0
	v_mul_f32_e32 v1, 0x4f7ffffe, v1
	v_cvt_u32_f32_e32 v1, v1
	s_xor_b32 s1, s0, s10
	s_ashr_i32 s1, s1, 31
	v_mov_b32_e32 v35, 0
	v_readfirstlane_b32 s17, v1
	s_mul_i32 s16, s16, s17
	s_mul_hi_u32 s16, s17, s16
	s_add_i32 s17, s17, s16
	s_mul_hi_u32 s16, s2, s17
	s_mul_i32 s17, s16, s11
	s_sub_i32 s2, s2, s17
	s_add_i32 s18, s16, 1
	s_sub_i32 s17, s2, s11
	s_cmp_ge_u32 s2, s11
	s_cselect_b32 s16, s18, s16
	s_cselect_b32 s2, s17, s2
	s_add_i32 s17, s16, 1
	s_cmp_ge_u32 s2, s11
	s_cselect_b32 s2, s17, s16
	s_xor_b32 s2, s2, s1
	s_sub_i32 s2, s2, s1
	s_mul_i32 s1, s2, s10
	s_ashr_i32 s11, s3, 31
	s_sub_i32 s10, s0, s1
	s_mul_i32 s0, s12, s11
	s_mul_hi_u32 s1, s12, s3
	s_add_i32 s0, s1, s0
	s_mul_i32 s1, s13, s3
	s_add_i32 s1, s0, s1
	s_mul_i32 s0, s12, s3
	s_lshl_b64 s[0:1], s[0:1], 2
	s_add_u32 s4, s4, s0
	s_addc_u32 s12, s5, s1
	s_mul_i32 s0, s14, s11
	s_mul_hi_u32 s1, s14, s3
	s_add_i32 s0, s1, s0
	s_mul_i32 s1, s15, s3
	s_add_i32 s5, s0, s1
	s_lshl_b32 s0, s10, 6
	s_ashr_i32 s1, s0, 31
	s_lshl_b32 s2, s2, 7
	s_lshl_b64 s[10:11], s[0:1], 2
	s_add_u32 s10, s4, s10
	v_or_b32_e32 v1, s2, v36
	s_addc_u32 s11, s12, s11
	v_lshl_add_u64 v[30:31], s[10:11], 0, v[34:35]
	v_mad_i64_i32 v[2:3], s[10:11], v1, s9, 0
	v_lshl_add_u64 v[10:11], v[2:3], 2, v[30:31]
	v_or_b32_e32 v2, 16, v1
	v_mad_i64_i32 v[2:3], s[10:11], v2, s9, 0
	v_lshl_add_u64 v[12:13], v[2:3], 2, v[30:31]
	global_load_dwordx4 v[2:5], v[10:11], off nt
	global_load_dwordx4 v[6:9], v[12:13], off nt
	v_or_b32_e32 v10, 32, v1
	v_mad_i64_i32 v[10:11], s[10:11], v10, s9, 0
	v_lshl_add_u64 v[18:19], v[10:11], 2, v[30:31]
	v_or_b32_e32 v10, 48, v1
	v_mad_i64_i32 v[10:11], s[10:11], v10, s9, 0
	v_lshl_add_u64 v[20:21], v[10:11], 2, v[30:31]
	global_load_dwordx4 v[10:13], v[18:19], off nt
	global_load_dwordx4 v[14:17], v[20:21], off nt
	v_or_b32_e32 v18, 64, v1
	v_mad_i64_i32 v[18:19], s[10:11], v18, s9, 0
	v_lshl_add_u64 v[26:27], v[18:19], 2, v[30:31]
	v_or_b32_e32 v18, 0x50, v1
	v_mad_i64_i32 v[18:19], s[10:11], v18, s9, 0
	v_lshl_add_u64 v[28:29], v[18:19], 2, v[30:31]
	global_load_dwordx4 v[18:21], v[26:27], off nt
	global_load_dwordx4 v[22:25], v[28:29], off nt
	v_or_b32_e32 v26, 0x60, v1
	v_mad_i64_i32 v[26:27], s[10:11], v26, s9, 0
	v_lshl_add_u64 v[26:27], v[26:27], 2, v[30:31]
	v_or_b32_e32 v1, 0x70, v1
	global_load_dwordx4 v[26:29], v[26:27], off nt
	v_mad_i64_i32 v[32:33], s[10:11], v1, s9, 0
	v_lshl_add_u64 v[30:31], v[32:33], 2, v[30:31]
	global_load_dwordx4 v[30:33], v[30:31], off nt
	s_movk_i32 s1, 0x104
	v_mad_u32_u24 v1, v36, s1, v34
	v_lshlrev_b32_e32 v0, 3, v0
	v_add_u32_e32 v34, 0x1040, v1
	v_add_u32_e32 v37, 0x1048, v1
	v_add_u32_e32 v38, 0x2080, v1
	v_add_u32_e32 v39, 0x2088, v1
	v_add_u32_e32 v40, 0x30c0, v1
	v_add_u32_e32 v41, 0x30c8, v1
	v_add_u32_e32 v42, 0x4100, v1
	v_add_u32_e32 v43, 0x4108, v1
	v_add_u32_e32 v44, 0x5140, v1
	v_and_b32_e32 v0, 0x78, v0
	s_mul_i32 s4, s14, s3
	s_lshl_b64 s[4:5], s[4:5], 1
	s_add_u32 s1, s6, s4
	s_addc_u32 s4, s7, s5
	s_ashr_i32 s3, s2, 31
	s_lshl_b64 s[2:3], s[2:3], 1
	s_add_u32 s2, s1, s2
	s_addc_u32 s3, s4, s3
	s_waitcnt vmcnt(7)
	ds_write2_b32 v1, v2, v3 offset1:1
	ds_write2_b32 v1, v4, v5 offset0:2 offset1:3
	s_waitcnt vmcnt(6)
	ds_write2_b32 v34, v6, v7 offset1:1
	ds_write2_b32 v37, v8, v9 offset1:1
	s_waitcnt vmcnt(5)
	ds_write2_b32 v38, v10, v11 offset1:1
	ds_write2_b32 v39, v12, v13 offset1:1
	s_waitcnt vmcnt(4)
	ds_write2_b32 v40, v14, v15 offset1:1
	ds_write2_b32 v41, v16, v17 offset1:1
	s_waitcnt vmcnt(3)
	ds_write2_b32 v42, v18, v19 offset1:1
	ds_write2_b32 v43, v20, v21 offset1:1
	s_waitcnt vmcnt(2)
	ds_write2_b32 v44, v22, v23 offset1:1
	v_add_u32_e32 v2, 0x5148, v1
	ds_write2_b32 v2, v24, v25 offset1:1
	v_add_u32_e32 v2, 0x6180, v1
	v_lshlrev_b32_e32 v34, 1, v0
	v_mul_u32_u24_e32 v0, 0x104, v0
	s_waitcnt vmcnt(1)
	ds_write2_b32 v2, v26, v27 offset1:1
	v_add_u32_e32 v2, 0x6188, v1
	v_lshl_add_u32 v24, v36, 2, v0
	ds_write2_b32 v2, v28, v29 offset1:1
	v_add_u32_e32 v2, 0x71c0, v1
	v_add_u32_e32 v1, 0x71c8, v1
	v_add_u32_e32 v25, 0x400, v24
	s_waitcnt vmcnt(0)
	ds_write2_b32 v2, v30, v31 offset1:1
	ds_write2_b32 v1, v32, v33 offset1:1
	s_waitcnt lgkmcnt(0)
	s_barrier
	ds_read2_b32 v[4:5], v24 offset1:16
	ds_read2_b32 v[6:7], v24 offset0:130 offset1:146
	ds_read2_b32 v[8:9], v25 offset0:4 offset1:20
	ds_read2_b32 v[10:11], v25 offset0:134 offset1:150
	ds_read2_b32 v[12:13], v25 offset0:199 offset1:215
	ds_read2_b32 v[14:15], v25 offset0:69 offset1:85
	ds_read2_b32 v[16:17], v24 offset0:195 offset1:211
	ds_read2_b32 v[18:19], v24 offset0:65 offset1:81
	v_or_b32_e32 v26, s0, v36
	v_lshl_add_u64 v[20:21], s[2:3], 0, v[34:35]
	v_mad_i64_i32 v[22:23], s[0:1], v26, s8, 0
	s_waitcnt lgkmcnt(3)
	v_cvt_pk_f16_f32 v3, v10, v12
	s_waitcnt lgkmcnt(2)
	v_cvt_pk_f16_f32 v2, v8, v14
	s_waitcnt lgkmcnt(1)
	v_cvt_pk_f16_f32 v1, v6, v16
	s_waitcnt lgkmcnt(0)
	v_cvt_pk_f16_f32 v0, v4, v18
	v_lshl_add_u64 v[22:23], v[22:23], 1, v[20:21]
	global_store_dwordx4 v[22:23], v[0:3], off
	v_or_b32_e32 v4, 16, v26
	s_nop 0
	v_cvt_pk_f16_f32 v3, v11, v13
	v_cvt_pk_f16_f32 v2, v9, v15
	v_cvt_pk_f16_f32 v1, v7, v17
	v_cvt_pk_f16_f32 v0, v5, v19
	ds_read2_b32 v[6:7], v24 offset0:32 offset1:48
	ds_read2_b32 v[8:9], v24 offset0:162 offset1:178
	ds_read2_b32 v[10:11], v25 offset0:36 offset1:52
	ds_read2_b32 v[12:13], v25 offset0:166 offset1:182
	ds_read2_b32 v[14:15], v25 offset0:231 offset1:247
	ds_read2_b32 v[16:17], v25 offset0:101 offset1:117
	ds_read2_b32 v[18:19], v24 offset0:227 offset1:243
	ds_read2_b32 v[22:23], v24 offset0:97 offset1:113
	v_mad_i64_i32 v[4:5], s[0:1], v4, s8, 0
	v_lshl_add_u64 v[4:5], v[4:5], 1, v[20:21]
	global_store_dwordx4 v[4:5], v[0:3], off
	v_or_b32_e32 v4, 32, v26
	v_mad_i64_i32 v[4:5], s[0:1], v4, s8, 0
	s_waitcnt lgkmcnt(3)
	v_cvt_pk_f16_f32 v3, v12, v14
	s_waitcnt lgkmcnt(2)
	v_cvt_pk_f16_f32 v2, v10, v16
	s_waitcnt lgkmcnt(1)
	v_cvt_pk_f16_f32 v1, v8, v18
	s_waitcnt lgkmcnt(0)
	v_cvt_pk_f16_f32 v0, v6, v22
	v_lshl_add_u64 v[4:5], v[4:5], 1, v[20:21]
	global_store_dwordx4 v[4:5], v[0:3], off
	v_or_b32_e32 v4, 48, v26
	v_mad_i64_i32 v[4:5], s[0:1], v4, s8, 0
	v_cvt_pk_f16_f32 v3, v13, v15
	v_cvt_pk_f16_f32 v2, v11, v17
	v_cvt_pk_f16_f32 v1, v9, v19
	v_cvt_pk_f16_f32 v0, v7, v23
	v_lshl_add_u64 v[4:5], v[4:5], 1, v[20:21]
	global_store_dwordx4 v[4:5], v[0:3], off
	s_endpgm
	s_endpgm
	s_endpgm
	s_endpgm
	s_endpgm
	s_endpgm
	s_endpgm
	s_endpgm
	s_endpgm
	s_endpgm
	s_endpgm
	s_endpgm
	s_endpgm
	s_endpgm
	s_endpgm
	s_endpgm
	s_endpgm
	s_endpgm
	s_endpgm
	s_endpgm
	s_endpgm
	s_endpgm
	s_endpgm
	s_endpgm
	s_endpgm
	s_endpgm
	s_endpgm
	s_endpgm
	s_endpgm
	s_endpgm
	s_endpgm
	s_endpgm
	s_endpgm
	s_endpgm
	s_endpgm
	s_endpgm
	s_endpgm
	s_endpgm
	s_endpgm
	s_endpgm
	s_endpgm
	s_endpgm
	s_endpgm
	s_endpgm
	s_endpgm
	s_endpgm
	s_endpgm
	s_endpgm

.LBB2_15:
	s_or_b64 exec, exec, s[6:7]
	s_lshl_b64 s[6:7], s[12:13], 2
	v_and_b32_e32 v0, 63, v0
	s_add_u32 s2, s2, s6
	s_addc_u32 s3, s3, s7
	v_lshlrev_b32_e32 v140, 4, v0
	global_load_dwordx4 v[0:3], v140, s[2:3]
	v_lshl_or_b32 v133, v136, 5, v138
	v_lshl_add_u32 v142, v137, 7, 0
	v_mul_u32_u24_e32 v143, 0x410, v133
	v_lshlrev_b32_e32 v148, 3, v153
	s_movk_i32 s2, 0x2080
	v_add_u32_e32 v145, 0, v140
	v_add3_u32 v135, v142, v135, v143
	v_and_b32_e32 v132, 64, v154
	v_and_b32_e32 v134, 16, v134
	s_movk_i32 s8, 0x410
	v_or_b32_e32 v144, 1, v148
	v_mad_u32_u24 v151, v153, s2, v145
	s_barrier
	ds_write_b128 v135, v[100:103]
	ds_write_b128 v135, v[108:111] offset:64
	ds_write_b128 v135, v[116:119] offset:512
	ds_write_b128 v135, v[124:127] offset:576
	ds_write_b128 v135, v[104:107] offset:16640
	ds_write_b128 v135, v[112:115] offset:16704
	ds_write_b128 v135, v[120:123] offset:17152
	ds_write_b128 v135, v[128:131] offset:17216
	v_or3_b32 v132, v134, v132, s4
	v_and_b32_e32 v138, 8, v148
	s_add_u32 s0, s0, s6
	v_mad_u32_u24 v102, v144, s8, v145
	s_waitcnt lgkmcnt(0)
	s_barrier
	ds_read_b128 v[104:107], v151
	ds_read_b128 v[108:111], v102
	ds_read_b128 v[112:115], v102 offset:1040
	ds_read_b128 v[116:119], v102 offset:2080
	ds_read_b128 v[120:123], v102 offset:3120
	ds_read_b128 v[124:127], v102 offset:4160
	v_mov_b32_e32 v141, 0
	v_bitop3_b32 v139, v148, 9, 1 bitop3:0xc8
	v_bitop3_b32 v137, v148, 10, 2 bitop3:0xc8
	v_bitop3_b32 v136, v148, 11, 3 bitop3:0xc8
	v_bitop3_b32 v134, v148, 12, 4 bitop3:0xc8
	v_or_b32_e32 v142, v132, v138
	s_addc_u32 s1, s1, s7
	v_bitop3_b32 v133, v148, 13, 5 bitop3:0xc8
	v_or_b32_e32 v143, v132, v139
	v_or_b32_e32 v146, v132, v137
	v_or_b32_e32 v147, v132, v136
	v_or_b32_e32 v149, v132, v134
	v_mad_i64_i32 v[128:129], s[2:3], v142, s5, 0
	v_lshl_add_u64 v[100:101], s[0:1], 0, v[140:141]
	v_or_b32_e32 v150, v132, v133
	v_mad_i64_i32 v[130:131], s[2:3], v143, s5, 0
	v_mad_i64_i32 v[142:143], s[2:3], v146, s5, 0
	v_mad_i64_i32 v[144:145], s[2:3], v147, s5, 0
	v_mad_i64_i32 v[146:147], s[2:3], v149, s5, 0
	v_lshl_add_u64 v[128:129], v[128:129], 2, v[100:101]
	v_lshl_add_u64 v[130:131], v[130:131], 2, v[100:101]
	v_lshl_add_u64 v[140:141], v[142:143], 2, v[100:101]
	v_lshl_add_u64 v[142:143], v[144:145], 2, v[100:101]
	v_lshl_add_u64 v[144:145], v[146:147], 2, v[100:101]
	v_bitop3_b32 v103, v148, 14, 6 bitop3:0xc8
	s_waitcnt vmcnt(0) lgkmcnt(0)
	v_pk_add_f32 v[106:107], v[2:3], v[106:107]
	v_pk_add_f32 v[104:105], v[0:1], v[104:105]
	v_pk_add_f32 v[110:111], v[2:3], v[110:111]
	v_pk_add_f32 v[108:109], v[0:1], v[108:109]
	v_pk_add_f32 v[114:115], v[2:3], v[114:115]
	v_pk_add_f32 v[112:113], v[0:1], v[112:113]
	v_pk_add_f32 v[118:119], v[2:3], v[118:119]
	v_pk_add_f32 v[116:117], v[0:1], v[116:117]
	v_pk_add_f32 v[122:123], v[2:3], v[122:123]
	v_pk_add_f32 v[120:121], v[0:1], v[120:121]
	global_store_dwordx4 v[128:129], v[104:107], off nt
	global_store_dwordx4 v[130:131], v[108:111], off nt
	global_store_dwordx4 v[140:141], v[112:115], off nt
	global_store_dwordx4 v[142:143], v[116:119], off nt
	global_store_dwordx4 v[144:145], v[120:123], off nt
	v_mad_i64_i32 v[104:105], s[0:1], v150, s5, 0
	v_lshl_add_u64 v[108:109], v[104:105], 2, v[100:101]
	ds_read_b128 v[104:107], v102 offset:5200
	v_pk_add_f32 v[126:127], v[2:3], v[126:127]
	v_pk_add_f32 v[124:125], v[0:1], v[124:125]
	global_store_dwordx4 v[108:109], v[124:127], off nt
	v_or_b32_e32 v112, v132, v103
	ds_read_b128 v[108:111], v102 offset:6240
	v_mad_i64_i32 v[112:113], s[0:1], v112, s5, 0
	s_waitcnt lgkmcnt(1)
	v_pk_add_f32 v[106:107], v[2:3], v[106:107]
	v_pk_add_f32 v[104:105], v[0:1], v[104:105]
	v_lshl_add_u64 v[112:113], v[112:113], 2, v[100:101]
	global_store_dwordx4 v[112:113], v[104:107], off nt
	v_bitop3_b32 v112, v148, 15, 7 bitop3:0xc8
	v_or_b32_e32 v113, v132, v112
	s_waitcnt lgkmcnt(0)
	v_pk_add_f32 v[104:105], v[0:1], v[108:109]
	v_mad_i64_i32 v[108:109], s[0:1], v113, s5, 0
	v_pk_add_f32 v[106:107], v[2:3], v[110:111]
	v_lshl_add_u64 v[108:109], v[108:109], 2, v[100:101]
	global_store_dwordx4 v[108:109], v[104:107], off nt
	s_waitcnt lgkmcnt(0)
	s_barrier
	ds_write_b128 v135, v[68:71]
	ds_write_b128 v135, v[76:79] offset:64
	ds_write_b128 v135, v[84:87] offset:512
	ds_write_b128 v135, v[92:95] offset:576
	ds_write_b128 v135, v[72:75] offset:16640
	ds_write_b128 v135, v[80:83] offset:16704
	ds_write_b128 v135, v[88:91] offset:17152
	ds_write_b128 v135, v[96:99] offset:17216
	s_waitcnt lgkmcnt(0)
	s_barrier
	ds_read_b128 v[68:71], v151
	ds_read_b128 v[72:75], v102
	v_or_b32_e32 v78, 32, v132
	v_or_b32_e32 v76, v78, v138
	v_mad_i64_i32 v[76:77], s[0:1], v76, s5, 0
	s_waitcnt lgkmcnt(1)
	v_pk_add_f32 v[70:71], v[2:3], v[70:71]
	v_pk_add_f32 v[68:69], v[0:1], v[68:69]
	v_lshl_add_u64 v[76:77], v[76:77], 2, v[100:101]
	global_store_dwordx4 v[76:77], v[68:71], off nt
	v_or_b32_e32 v76, v78, v139
	v_mad_i64_i32 v[76:77], s[0:1], v76, s5, 0
	s_waitcnt lgkmcnt(0)
	v_pk_add_f32 v[70:71], v[2:3], v[74:75]
	v_pk_add_f32 v[68:69], v[0:1], v[72:73]
	ds_read_b128 v[72:75], v102 offset:1040
	v_lshl_add_u64 v[76:77], v[76:77], 2, v[100:101]
	global_store_dwordx4 v[76:77], v[68:71], off nt
	v_or_b32_e32 v76, v78, v137
	ds_read_b128 v[68:71], v102 offset:2080
	v_mad_i64_i32 v[76:77], s[0:1], v76, s5, 0
	s_waitcnt lgkmcnt(1)
	v_pk_add_f32 v[74:75], v[2:3], v[74:75]
	v_pk_add_f32 v[72:73], v[0:1], v[72:73]
	v_lshl_add_u64 v[76:77], v[76:77], 2, v[100:101]
	global_store_dwordx4 v[76:77], v[72:75], off nt
	s_waitcnt lgkmcnt(0)
	v_pk_add_f32 v[70:71], v[2:3], v[70:71]
	v_pk_add_f32 v[68:69], v[0:1], v[68:69]
	v_or_b32_e32 v72, v78, v136
	v_mad_i64_i32 v[76:77], s[0:1], v72, s5, 0
	ds_read_b128 v[72:75], v102 offset:3120
	v_lshl_add_u64 v[76:77], v[76:77], 2, v[100:101]
	global_store_dwordx4 v[76:77], v[68:71], off nt
	v_or_b32_e32 v76, v78, v134
	ds_read_b128 v[68:71], v102 offset:4160
	v_mad_i64_i32 v[76:77], s[0:1], v76, s5, 0
	s_waitcnt lgkmcnt(1)
	v_pk_add_f32 v[74:75], v[2:3], v[74:75]
	v_pk_add_f32 v[72:73], v[0:1], v[72:73]
	v_lshl_add_u64 v[76:77], v[76:77], 2, v[100:101]
	global_store_dwordx4 v[76:77], v[72:75], off nt
	s_waitcnt lgkmcnt(0)
	v_pk_add_f32 v[70:71], v[2:3], v[70:71]
	v_pk_add_f32 v[68:69], v[0:1], v[68:69]
	v_or_b32_e32 v72, v78, v133
	v_mad_i64_i32 v[76:77], s[0:1], v72, s5, 0
	ds_read_b128 v[72:75], v102 offset:5200
	v_lshl_add_u64 v[76:77], v[76:77], 2, v[100:101]
	global_store_dwordx4 v[76:77], v[68:71], off nt
	v_or_b32_e32 v76, v78, v103
	ds_read_b128 v[68:71], v102 offset:6240
	v_mad_i64_i32 v[76:77], s[0:1], v76, s5, 0
	s_waitcnt lgkmcnt(1)
	v_pk_add_f32 v[74:75], v[2:3], v[74:75]
	v_pk_add_f32 v[72:73], v[0:1], v[72:73]
	v_lshl_add_u64 v[76:77], v[76:77], 2, v[100:101]
	global_store_dwordx4 v[76:77], v[72:75], off nt
	s_waitcnt lgkmcnt(0)
	v_pk_add_f32 v[70:71], v[2:3], v[70:71]
	v_pk_add_f32 v[68:69], v[0:1], v[68:69]
	v_or_b32_e32 v72, v78, v112
	v_mad_i64_i32 v[72:73], s[0:1], v72, s5, 0
	v_lshl_add_u64 v[72:73], v[72:73], 2, v[100:101]
	global_store_dwordx4 v[72:73], v[68:71], off nt
	s_waitcnt lgkmcnt(0)
	s_barrier
	ds_write_b128 v135, v[36:39]
	ds_write_b128 v135, v[44:47] offset:64
	ds_write_b128 v135, v[52:55] offset:512
	ds_write_b128 v135, v[60:63] offset:576
	ds_write_b128 v135, v[40:43] offset:16640
	ds_write_b128 v135, v[48:51] offset:16704
	ds_write_b128 v135, v[56:59] offset:17152
	ds_write_b128 v135, v[64:67] offset:17216
	s_waitcnt lgkmcnt(0)
	s_barrier
	ds_read_b128 v[36:39], v151
	ds_read_b128 v[40:43], v102
	v_add_u32_e32 v46, 0x80, v132
	v_or_b32_e32 v44, v46, v138
	v_mad_i64_i32 v[44:45], s[0:1], v44, s5, 0
	s_waitcnt lgkmcnt(1)
	v_pk_add_f32 v[38:39], v[2:3], v[38:39]
	v_pk_add_f32 v[36:37], v[0:1], v[36:37]
	v_lshl_add_u64 v[44:45], v[44:45], 2, v[100:101]
	global_store_dwordx4 v[44:45], v[36:39], off nt
	v_or_b32_e32 v44, v46, v139
	v_mad_i64_i32 v[44:45], s[0:1], v44, s5, 0
	s_waitcnt lgkmcnt(0)
	v_pk_add_f32 v[38:39], v[2:3], v[42:43]
	v_pk_add_f32 v[36:37], v[0:1], v[40:41]
	ds_read_b128 v[40:43], v102 offset:1040
	v_lshl_add_u64 v[44:45], v[44:45], 2, v[100:101]
	global_store_dwordx4 v[44:45], v[36:39], off nt
	v_or_b32_e32 v44, v46, v137
	ds_read_b128 v[36:39], v102 offset:2080
	v_mad_i64_i32 v[44:45], s[0:1], v44, s5, 0
	s_waitcnt lgkmcnt(1)
	v_pk_add_f32 v[42:43], v[2:3], v[42:43]
	v_pk_add_f32 v[40:41], v[0:1], v[40:41]
	v_lshl_add_u64 v[44:45], v[44:45], 2, v[100:101]
	global_store_dwordx4 v[44:45], v[40:43], off nt
	s_waitcnt lgkmcnt(0)
	v_pk_add_f32 v[38:39], v[2:3], v[38:39]
	v_pk_add_f32 v[36:37], v[0:1], v[36:37]
	v_or_b32_e32 v40, v46, v136
	v_mad_i64_i32 v[44:45], s[0:1], v40, s5, 0
	ds_read_b128 v[40:43], v102 offset:3120
	v_lshl_add_u64 v[44:45], v[44:45], 2, v[100:101]
	global_store_dwordx4 v[44:45], v[36:39], off nt
	v_or_b32_e32 v44, v46, v134
	ds_read_b128 v[36:39], v102 offset:4160
	v_mad_i64_i32 v[44:45], s[0:1], v44, s5, 0
	s_waitcnt lgkmcnt(1)
	v_pk_add_f32 v[42:43], v[2:3], v[42:43]
	v_pk_add_f32 v[40:41], v[0:1], v[40:41]
	v_lshl_add_u64 v[44:45], v[44:45], 2, v[100:101]
	global_store_dwordx4 v[44:45], v[40:43], off nt
	s_waitcnt lgkmcnt(0)
	v_pk_add_f32 v[38:39], v[2:3], v[38:39]
	v_pk_add_f32 v[36:37], v[0:1], v[36:37]
	v_or_b32_e32 v40, v46, v133
	v_mad_i64_i32 v[44:45], s[0:1], v40, s5, 0
	ds_read_b128 v[40:43], v102 offset:5200
	v_lshl_add_u64 v[44:45], v[44:45], 2, v[100:101]
	global_store_dwordx4 v[44:45], v[36:39], off nt
	v_or_b32_e32 v44, v46, v103
	ds_read_b128 v[36:39], v102 offset:6240
	v_mad_i64_i32 v[44:45], s[0:1], v44, s5, 0
	s_waitcnt lgkmcnt(1)
	v_pk_add_f32 v[42:43], v[2:3], v[42:43]
	v_pk_add_f32 v[40:41], v[0:1], v[40:41]
	v_lshl_add_u64 v[44:45], v[44:45], 2, v[100:101]
	global_store_dwordx4 v[44:45], v[40:43], off nt
	s_waitcnt lgkmcnt(0)
	v_pk_add_f32 v[38:39], v[2:3], v[38:39]
	v_pk_add_f32 v[36:37], v[0:1], v[36:37]
	v_or_b32_e32 v40, v46, v112
	v_mad_i64_i32 v[40:41], s[0:1], v40, s5, 0
	v_lshl_add_u64 v[40:41], v[40:41], 2, v[100:101]
	global_store_dwordx4 v[40:41], v[36:39], off nt
	s_waitcnt lgkmcnt(0)
	s_barrier
	ds_write_b128 v135, v[4:7]
	ds_write_b128 v135, v[12:15] offset:64
	ds_write_b128 v135, v[20:23] offset:512
	ds_write_b128 v135, v[28:31] offset:576
	ds_write_b128 v135, v[8:11] offset:16640
	ds_write_b128 v135, v[16:19] offset:16704
	ds_write_b128 v135, v[24:27] offset:17152
	ds_write_b128 v135, v[32:35] offset:17216
	s_waitcnt lgkmcnt(0)
	s_barrier
	ds_read_b128 v[4:7], v151
	ds_read_b128 v[8:11], v102
	v_add_u32_e32 v14, 0xa0, v132
	v_or_b32_e32 v12, v14, v138
	v_mad_i64_i32 v[12:13], s[0:1], v12, s5, 0
	s_waitcnt lgkmcnt(1)
	v_pk_add_f32 v[6:7], v[2:3], v[6:7]
	v_pk_add_f32 v[4:5], v[0:1], v[4:5]
	v_lshl_add_u64 v[12:13], v[12:13], 2, v[100:101]
	global_store_dwordx4 v[12:13], v[4:7], off nt
	v_or_b32_e32 v12, v14, v139
	v_mad_i64_i32 v[12:13], s[0:1], v12, s5, 0
	s_waitcnt lgkmcnt(0)
	v_pk_add_f32 v[6:7], v[2:3], v[10:11]
	v_pk_add_f32 v[4:5], v[0:1], v[8:9]
	ds_read_b128 v[8:11], v102 offset:1040
	v_lshl_add_u64 v[12:13], v[12:13], 2, v[100:101]
	global_store_dwordx4 v[12:13], v[4:7], off nt
	v_or_b32_e32 v12, v14, v137
	ds_read_b128 v[4:7], v102 offset:2080
	v_mad_i64_i32 v[12:13], s[0:1], v12, s5, 0
	s_waitcnt lgkmcnt(1)
	v_pk_add_f32 v[10:11], v[2:3], v[10:11]
	v_pk_add_f32 v[8:9], v[0:1], v[8:9]
	v_lshl_add_u64 v[12:13], v[12:13], 2, v[100:101]
	global_store_dwordx4 v[12:13], v[8:11], off nt
	s_waitcnt lgkmcnt(0)
	v_pk_add_f32 v[6:7], v[2:3], v[6:7]
	v_pk_add_f32 v[4:5], v[0:1], v[4:5]
	v_or_b32_e32 v8, v14, v136
	v_mad_i64_i32 v[12:13], s[0:1], v8, s5, 0
	ds_read_b128 v[8:11], v102 offset:3120
	v_lshl_add_u64 v[12:13], v[12:13], 2, v[100:101]
	global_store_dwordx4 v[12:13], v[4:7], off nt
	v_or_b32_e32 v12, v14, v134
	ds_read_b128 v[4:7], v102 offset:4160
	v_mad_i64_i32 v[12:13], s[0:1], v12, s5, 0
	s_waitcnt lgkmcnt(1)
	v_pk_add_f32 v[10:11], v[2:3], v[10:11]
	v_pk_add_f32 v[8:9], v[0:1], v[8:9]
	v_lshl_add_u64 v[12:13], v[12:13], 2, v[100:101]
	global_store_dwordx4 v[12:13], v[8:11], off nt
	s_waitcnt lgkmcnt(0)
	v_pk_add_f32 v[6:7], v[2:3], v[6:7]
	v_pk_add_f32 v[4:5], v[0:1], v[4:5]
	v_or_b32_e32 v8, v14, v133
	v_mad_i64_i32 v[12:13], s[0:1], v8, s5, 0
	ds_read_b128 v[8:11], v102 offset:5200
	v_lshl_add_u64 v[12:13], v[12:13], 2, v[100:101]
	global_store_dwordx4 v[12:13], v[4:7], off nt
	ds_read_b128 v[4:7], v102 offset:6240
	v_or_b32_e32 v12, v14, v103
	v_mad_i64_i32 v[12:13], s[0:1], v12, s5, 0
	s_waitcnt lgkmcnt(1)
	v_pk_add_f32 v[10:11], v[2:3], v[10:11]
	v_pk_add_f32 v[8:9], v[0:1], v[8:9]
	v_lshl_add_u64 v[12:13], v[12:13], 2, v[100:101]
	global_store_dwordx4 v[12:13], v[8:11], off nt
	s_waitcnt lgkmcnt(0)
	v_pk_add_f32 v[0:1], v[0:1], v[4:5]
	v_pk_add_f32 v[2:3], v[2:3], v[6:7]
	v_or_b32_e32 v8, v14, v112
	v_mad_i64_i32 v[4:5], s[0:1], v8, s5, 0
	v_lshl_add_u64 v[4:5], v[4:5], 2, v[100:101]
	global_store_dwordx4 v[4:5], v[0:3], off nt
	s_waitcnt lgkmcnt(0)
	s_endpgm
	s_endpgm
	s_endpgm
	s_endpgm
	s_endpgm
	s_endpgm
	s_endpgm
	s_endpgm
	s_endpgm
	s_endpgm
	s_endpgm
	s_endpgm
	s_endpgm
	s_endpgm
	s_endpgm
	s_endpgm
	s_endpgm
	s_endpgm
	s_endpgm
	s_endpgm
	s_endpgm
	s_endpgm
	s_endpgm
	s_endpgm
	s_endpgm
	s_endpgm
	s_endpgm
	s_endpgm
	s_endpgm
	s_endpgm
	s_endpgm
	s_endpgm
	s_endpgm
	s_endpgm
	s_endpgm
	s_endpgm
	s_endpgm

_Z11attn_kernelPKDF16_S0_S0_PDF16_7CvtJobs:
	s_mov_b64 s[4:5], -1
	s_cmpk_lt_u32 s2, 0x200
	v_lshrrev_b32_e32 v29, 4, v0
	v_lshlrev_b32_e32 v10, 4, v0
	v_lshlrev_b32_e32 v30, 3, v0
	s_cbranch_scc0 .LBB3_11
	s_load_dwordx8 s[4:11], s[0:1], 0x0
	s_lshl_b32 s13, s2, 10
	s_lshr_b32 s3, s2, 5
	s_sub_i32 s18, 23, s3
	s_cmp_ge_u32 s3, 8
	s_cselect_b32 s3, s18, s3
	s_and_b32 s13, s13, 0x7c00
	s_lshl_b32 s12, s3, 6
	s_lshl_b32 s14, s13, 7
	v_mov_b32_e32 v13, 0
	s_waitcnt lgkmcnt(0)
	s_add_u32 s6, s6, s14
	s_addc_u32 s7, s7, 0
	v_mov_b32_e32 v11, v13
	s_add_u32 s8, s8, s14
	v_lshl_add_u64 v[2:3], s[6:7], 0, v[10:11]
	s_movk_i32 s14, 0x1000
	v_add_co_u32_e32 v2, vcc, s14, v2
	s_addc_u32 s9, s9, 0
	s_nop 0
	v_addc_co_u32_e32 v3, vcc, 0, v3, vcc
	global_load_dwordx4 v[62:65], v10, s[6:7]
	global_load_dwordx4 v[66:69], v[2:3], off
	v_lshl_add_u64 v[2:3], s[8:9], 0, v[10:11]
	v_add_co_u32_e32 v2, vcc, s14, v2
	v_and_b32_e32 v31, 15, v0
	s_nop 0
	v_addc_co_u32_e32 v3, vcc, 0, v3, vcc
	global_load_dwordx4 v[70:73], v10, s[8:9]
	global_load_dwordx4 v[74:77], v[2:3], off
	v_lshrrev_b32_e32 v2, 2, v0
	v_and_b32_e32 v2, 48, v2
	v_subrev_u32_e32 v2, s12, v2
	v_add_u32_e32 v32, 0x3c0, v2
	v_add_u32_e32 v12, s13, v32
	v_lshlrev_b64 v[2:3], 7, v[12:13]
	v_bfe_u32 v1, v0, 4, 2
	v_lshl_add_u64 v[2:3], s[4:5], 0, v[2:3]
	v_lshlrev_b32_e32 v12, 7, v31
	v_lshl_add_u64 v[2:3], v[2:3], 0, v[12:13]
	v_lshlrev_b32_e32 v4, 4, v1
	v_mov_b32_e32 v5, v13
	v_lshl_add_u64 v[14:15], v[2:3], 0, v[4:5]
	global_load_dwordx4 v[2:5], v[14:15], off
	global_load_dwordx4 v[6:9], v[14:15], off offset:64
	v_lshrrev_b32_e32 v14, 3, v0
	v_bfe_u32 v17, v0, 1, 3
	v_mbcnt_lo_u32_b32 v19, -1, 0
	v_xor_b32_e32 v15, v10, v0
	v_bfe_u32 v16, v0, 1, 2
	s_movk_i32 s5, 0x820
	v_bfe_u32 v0, v0, 2, 2
	v_lshlrev_b32_e32 v20, 7, v14
	v_lshlrev_b32_e32 v14, 5, v14
	v_bitop3_b32 v21, v29, v17, 3 bitop3:0x6c
	v_bitop3_b32 v17, v1, v17, 4 bitop3:0x36
	v_lshlrev_b32_e32 v33, 2, v1
	v_mbcnt_hi_u32_b32 v1, -1, v19
	s_movk_i32 s4, 0x70
	v_and_b32_e32 v18, 24, v30
	v_mad_u32_u24 v14, v16, s5, v14
	v_or_b32_e32 v0, v33, v0
	v_and_b32_e32 v16, 64, v1
	v_and_or_b32 v34, v15, s4, v20
	v_xor_b32_e32 v15, 16, v1
	v_lshl_or_b32 v38, v0, 5, v18
	v_add_u32_e32 v0, 64, v16
	v_cmp_lt_i32_e32 vcc, v15, v0
	v_and_or_b32 v37, v10, 16, v14
	v_mov_b32_e32 v115, 0
	v_cndmask_b32_e32 v14, v1, v15, vcc
	v_lshlrev_b32_e32 v40, 2, v14
	v_xor_b32_e32 v14, 32, v1
	v_cmp_lt_i32_e32 vcc, v14, v0
	v_mov_b32_e32 v114, 0
	v_mov_b32_e32 v113, 0
	v_cndmask_b32_e32 v0, v1, v14, vcc
	v_mov_b32_e32 v112, 0
	v_mov_b32_e32 v111, 0
	v_mov_b32_e32 v110, 0
	v_mov_b32_e32 v109, 0
	v_mov_b32_e32 v108, 0
	v_mov_b32_e32 v107, 0
	v_mov_b32_e32 v106, 0
	v_mov_b32_e32 v105, 0
	v_mov_b32_e32 v104, 0
	v_mov_b32_e32 v103, 0
	v_mov_b32_e32 v102, 0
	v_mov_b32_e32 v101, 0
	v_mov_b32_e32 v100, 0
	v_lshlrev_b32_e32 v35, 4, v21
	v_lshlrev_b32_e32 v36, 4, v17
	v_or_b32_e32 v39, v32, v31
	s_sub_i32 s3, 16, s3
	v_lshlrev_b32_e32 v41, 2, v0
	v_or_b32_e32 v42, 51, v33
	v_mov_b32_e32 v43, 0xff800000
	s_mov_b32 s16, 1
	v_mov_b32_e32 v28, 0xff800000
	s_waitcnt vmcnt(5)
	ds_write_b128 v34, v[62:65]
	s_waitcnt vmcnt(4)
	ds_write_b128 v34, v[66:69] offset:4096
	s_waitcnt vmcnt(3)
	ds_write_b128 v37, v[70:73] offset:16384
	s_waitcnt vmcnt(2)
	ds_write_b128 v37, v[74:77] offset:17408
	v_add_u32_e32 v98, 0x1000, v10
	s_waitcnt vmcnt(0) lgkmcnt(0)
	s_barrier
.LBB3_2:
	s_cmp_lt_u32 s16, s3
	s_cbranch_scc0 .Lat_nopf
	s_add_u32 s18, s6, 0x2000
	s_addc_u32 s19, s7, 0
	s_add_u32 s20, s8, 0x2000
	s_addc_u32 s21, s9, 0
	global_load_dwordx4 v[62:65], v10, s[18:19]
	global_load_dwordx4 v[66:69], v98, s[18:19]
	global_load_dwordx4 v[70:73], v10, s[20:21]
	global_load_dwordx4 v[74:77], v98, s[20:21]
.Lat_nopf:
	s_add_i32 s17, s16, -1
	s_and_b32 s17, s17, 1
	v_lshl_or_b32 v60, s17, 13, v12
	v_add_u32_e32 v61, v60, v36
	v_add_u32_e32 v60, v60, v35
	ds_read_b128 v[14:17], v60
	ds_read_b128 v[18:21], v61
	ds_read_b128 v[22:25], v60 offset:2048
	ds_read_b128 v[78:81], v61 offset:2048
	s_mul_i32 s14, s17, 0x2080
	s_waitcnt lgkmcnt(3)
	v_mfma_f32_16x16x32_f16 v[44:47], v[14:17], v[2:5], 0
	ds_read_b128 v[14:17], v60 offset:4096
	s_waitcnt lgkmcnt(3)
	v_mfma_f32_16x16x32_f16 v[44:47], v[18:21], v[6:9], v[44:47]
	ds_read_b128 v[18:21], v61 offset:4096
	s_waitcnt lgkmcnt(3)
	v_mfma_f32_16x16x32_f16 v[48:51], v[22:25], v[2:5], 0
	ds_read_b128 v[22:25], v60 offset:6144
	s_waitcnt lgkmcnt(3)
	v_mfma_f32_16x16x32_f16 v[48:51], v[78:81], v[6:9], v[48:51]
	ds_read_b128 v[78:81], v61 offset:6144
	v_add_u32_e32 v0, s14, v38
	s_waitcnt lgkmcnt(3)
	v_mfma_f32_16x16x32_f16 v[52:55], v[14:17], v[2:5], 0
	s_waitcnt lgkmcnt(2)
	v_mfma_f32_16x16x32_f16 v[52:55], v[18:21], v[6:9], v[52:55]
	s_waitcnt lgkmcnt(1)
	v_mfma_f32_16x16x32_f16 v[56:59], v[22:25], v[2:5], 0
	s_waitcnt lgkmcnt(0)
	v_mfma_f32_16x16x32_f16 v[56:59], v[78:81], v[6:9], v[56:59]
	ds_read_b64_tr_b16 v[86:87], v0 offset:16384
	ds_read_b64_tr_b16 v[88:89], v0 offset:16896
	ds_read_b64_tr_b16 v[90:91], v0 offset:18464
	ds_read_b64_tr_b16 v[92:93], v0 offset:18976
	ds_read_b64_tr_b16 v[94:95], v0 offset:20544
	ds_read_b64_tr_b16 v[96:97], v0 offset:21056
	ds_read_b64_tr_b16 v[14:15], v0 offset:22624
	ds_read_b64_tr_b16 v[16:17], v0 offset:23136
	s_cmp_lt_u32 s16, s3
	s_cbranch_scc1 .Lat_nomask
	v_sub_u32_e32 v1, v39, v42
	v_add_u32_e32 v1, 51, v1
	v_cmp_gt_i32_e64 s[22:23], 0, v1
	v_cmp_gt_i32_e64 s[24:25], 1, v1
	v_cmp_gt_i32_e64 s[26:27], 2, v1
	v_cmp_gt_i32_e64 s[28:29], 3, v1
	v_cndmask_b32_e64 v44, v44, v43, s[22:23]
	v_cndmask_b32_e64 v45, v45, v43, s[24:25]
	v_cndmask_b32_e64 v46, v46, v43, s[26:27]
	v_cndmask_b32_e64 v47, v47, v43, s[28:29]
	v_cmp_gt_i32_e64 s[22:23], 16, v1
	v_cmp_gt_i32_e64 s[24:25], 17, v1
	v_cmp_gt_i32_e64 s[26:27], 18, v1
	v_cmp_gt_i32_e64 s[28:29], 19, v1
	v_cndmask_b32_e64 v48, v48, v43, s[22:23]
	v_cndmask_b32_e64 v49, v49, v43, s[24:25]
	v_cndmask_b32_e64 v50, v50, v43, s[26:27]
	v_cndmask_b32_e64 v51, v51, v43, s[28:29]
	v_cmp_gt_i32_e64 s[22:23], 32, v1
	v_cmp_gt_i32_e64 s[24:25], 33, v1
	v_cmp_gt_i32_e64 s[26:27], 34, v1
	v_cmp_gt_i32_e64 s[28:29], 35, v1
	v_cndmask_b32_e64 v52, v52, v43, s[22:23]
	v_cndmask_b32_e64 v53, v53, v43, s[24:25]
	v_cndmask_b32_e64 v54, v54, v43, s[26:27]
	v_cndmask_b32_e64 v55, v55, v43, s[28:29]
	v_cmp_gt_i32_e64 s[22:23], 48, v1
	v_cmp_gt_i32_e64 s[24:25], 49, v1
	v_cmp_gt_i32_e64 s[26:27], 50, v1
	v_cmp_gt_i32_e64 s[28:29], 51, v1
	v_cndmask_b32_e64 v56, v56, v43, s[22:23]
	v_cndmask_b32_e64 v57, v57, v43, s[24:25]
	v_cndmask_b32_e64 v58, v58, v43, s[26:27]
	v_cndmask_b32_e64 v59, v59, v43, s[28:29]
.Lat_nomask:
	v_max3_f32 v1, v44, v45, v46
	v_max3_f32 v26, v47, v48, v49
	v_max3_f32 v27, v50, v51, v52
	v_max3_f32 v1, v1, v53, v54
	v_max3_f32 v26, v26, v55, v56
	v_max3_f32 v27, v27, v57, v58
	v_max3_f32 v1, v1, v26, v27
	v_max_f32_e32 v1, v1, v59
	ds_bpermute_b32 v26, v40, v1
	s_waitcnt lgkmcnt(0)
	v_max_f32_e32 v1, v1, v26
	ds_bpermute_b32 v26, v41, v1
	s_waitcnt lgkmcnt(0)
	v_max3_f32 v1, v28, v1, v26
	v_sub_f32_e32 v26, v28, v1
	v_exp_f32_e32 v26, v26
	v_mov_b32_e32 v28, v1
	v_sub_f32_e32 v44, v44, v1
	v_sub_f32_e32 v45, v45, v1
	v_sub_f32_e32 v46, v46, v1
	v_sub_f32_e32 v47, v47, v1
	v_sub_f32_e32 v48, v48, v1
	v_sub_f32_e32 v49, v49, v1
	v_sub_f32_e32 v50, v50, v1
	v_sub_f32_e32 v51, v51, v1
	v_sub_f32_e32 v52, v52, v1
	v_sub_f32_e32 v53, v53, v1
	v_sub_f32_e32 v54, v54, v1
	v_sub_f32_e32 v55, v55, v1
	v_sub_f32_e32 v56, v56, v1
	v_sub_f32_e32 v57, v57, v1
	v_sub_f32_e32 v58, v58, v1
	v_sub_f32_e32 v59, v59, v1
	v_exp_f32_e32 v44, v44
	v_exp_f32_e32 v45, v45
	v_exp_f32_e32 v46, v46
	v_exp_f32_e32 v47, v47
	v_exp_f32_e32 v48, v48
	v_exp_f32_e32 v49, v49
	v_exp_f32_e32 v50, v50
	v_exp_f32_e32 v51, v51
	v_pk_mul_f32 v[100:101], v[26:27], v[100:101] op_sel_hi:[0,1]
	v_pk_mul_f32 v[102:103], v[26:27], v[102:103] op_sel_hi:[0,1]
	v_pk_mul_f32 v[104:105], v[26:27], v[104:105] op_sel_hi:[0,1]
	v_pk_mul_f32 v[106:107], v[26:27], v[106:107] op_sel_hi:[0,1]
	v_pk_mul_f32 v[108:109], v[26:27], v[108:109] op_sel_hi:[0,1]
	v_pk_mul_f32 v[110:111], v[26:27], v[110:111] op_sel_hi:[0,1]
	v_pk_mul_f32 v[112:113], v[26:27], v[112:113] op_sel_hi:[0,1]
	v_pk_mul_f32 v[114:115], v[26:27], v[114:115] op_sel_hi:[0,1]
	v_cvt_pk_f16_f32 v82, v44, v45
	v_cvt_pk_f16_f32 v83, v46, v47
	v_cvt_pk_f16_f32 v84, v48, v49
	v_cvt_pk_f16_f32 v85, v50, v51
	v_exp_f32_e32 v52, v52
	v_exp_f32_e32 v53, v53
	v_exp_f32_e32 v54, v54
	v_exp_f32_e32 v55, v55
	v_exp_f32_e32 v56, v56
	v_exp_f32_e32 v57, v57
	v_exp_f32_e32 v58, v58
	v_exp_f32_e32 v59, v59
	v_mfma_f32_16x16x32_f16 v[100:103], v[86:89], v[82:85], v[100:103]
	ds_read_b64_tr_b16 v[86:87], v0 offset:17408
	ds_read_b64_tr_b16 v[88:89], v0 offset:17920
	v_mfma_f32_16x16x32_f16 v[104:107], v[90:93], v[82:85], v[104:107]
	ds_read_b64_tr_b16 v[90:91], v0 offset:19488
	ds_read_b64_tr_b16 v[92:93], v0 offset:20000
	v_mfma_f32_16x16x32_f16 v[108:111], v[94:97], v[82:85], v[108:111]
	ds_read_b64_tr_b16 v[94:95], v0 offset:21568
	ds_read_b64_tr_b16 v[96:97], v0 offset:22080
	v_mfma_f32_16x16x32_f16 v[112:115], v[14:17], v[82:85], v[112:115]
	ds_read_b64_tr_b16 v[14:15], v0 offset:23648
	ds_read_b64_tr_b16 v[16:17], v0 offset:24160
	v_cvt_pk_f16_f32 v78, v52, v53
	v_cvt_pk_f16_f32 v79, v54, v55
	v_cvt_pk_f16_f32 v80, v56, v57
	v_cvt_pk_f16_f32 v81, v58, v59
	v_pk_add_f32 v[18:19], v[44:45], v[46:47]
	v_pk_add_f32 v[20:21], v[48:49], v[50:51]
	v_pk_add_f32 v[22:23], v[52:53], v[54:55]
	v_pk_add_f32 v[24:25], v[56:57], v[58:59]
	v_pk_add_f32 v[18:19], v[18:19], v[20:21]
	v_pk_add_f32 v[22:23], v[22:23], v[24:25]
	s_waitcnt lgkmcnt(6)
	v_mfma_f32_16x16x32_f16 v[100:103], v[86:89], v[78:81], v[100:103]
	s_waitcnt lgkmcnt(4)
	v_mfma_f32_16x16x32_f16 v[104:107], v[90:93], v[78:81], v[104:107]
	s_waitcnt lgkmcnt(2)
	v_mfma_f32_16x16x32_f16 v[108:111], v[94:97], v[78:81], v[108:111]
	s_waitcnt lgkmcnt(0)
	v_mfma_f32_16x16x32_f16 v[112:115], v[14:17], v[78:81], v[112:115]
	v_pk_add_f32 v[18:19], v[18:19], v[22:23]
	s_cmp_lt_u32 s16, s3
	s_cbranch_scc0 .Lat_nowr
	s_xor_b32 s12, s17, 1
	s_mul_i32 s13, s12, 0x2080
	s_lshl_b32 s12, s12, 13
	v_add_u32_e32 v1, s12, v34
	v_add_u32_e32 v60, s13, v37
	s_waitcnt vmcnt(0)
	ds_write_b128 v1, v[62:65]
	ds_write_b128 v1, v[66:69] offset:4096
	ds_write_b128 v60, v[70:73] offset:16384
	ds_write_b128 v60, v[74:77] offset:17408
.Lat_nowr:
	v_add_f32_e32 v18, v18, v19
	s_add_u32 s6, s6, 0x2000
	s_addc_u32 s7, s7, 0
	s_add_u32 s8, s8, 0x2000
	s_addc_u32 s9, s9, 0
	v_fma_f32 v13, v13, v26, v18
	s_add_i32 s16, s16, 1
	v_add_u32_e32 v42, 64, v42
	s_waitcnt lgkmcnt(0)
	s_barrier
	s_cmp_le_u32 s16, s3
	s_cbranch_scc1 .LBB3_2
	v_mov_b32_e32 v0, v13
.LBB3_10:
	ds_bpermute_b32 v1, v40, v0
	v_mov_b32_e32 v19, v103
	v_mov_b32_e32 v18, v102
	v_mov_b32_e32 v17, v101
	v_mov_b32_e32 v16, v100
	s_waitcnt lgkmcnt(0)
	v_add_f32_e32 v0, v0, v1
	ds_bpermute_b32 v1, v41, v0
	v_mov_b32_e32 v15, v107
	v_mov_b32_e32 v14, v106
	v_mov_b32_e32 v13, v105
	v_mov_b32_e32 v12, v104
	s_waitcnt lgkmcnt(0)
	v_add_f32_e32 v0, v0, v1
	v_div_scale_f32 v1, s[4:5], v0, v0, 1.0
	v_rcp_f32_e32 v11, v1
	v_div_scale_f32 v21, vcc, 1.0, v0, 1.0
	v_mov_b32_e32 v6, v108
	v_fma_f32 v22, -v1, v11, 1.0
	v_fmac_f32_e32 v11, v22, v11
	v_mul_f32_e32 v22, v21, v11
	v_fma_f32 v23, -v1, v22, v21
	v_fmac_f32_e32 v22, v23, v11
	v_fma_f32 v1, -v1, v22, v21
	v_div_fmas_f32 v1, v1, v11, v22
	v_div_fixup_f32 v0, v1, v0, 1.0
	v_fma_mixlo_f16 v1, v0, v16, 0
	v_mov_b32_e32 v16, v17
	v_mov_b32_e32 v17, v18
	v_pk_mul_f32 v[16:17], v[0:1], v[16:17] op_sel_hi:[0,1]
	v_cvt_pk_f16_f32 v11, v16, v17
	v_pack_b32_f16 v16, v1, v11
	v_fma_mixlo_f16 v1, v0, v19, 0
	v_alignbit_b32 v17, v1, v11, 16
	v_fma_mixlo_f16 v1, v0, v12, 0
	v_mov_b32_e32 v12, v13
	v_mov_b32_e32 v13, v14
	v_pk_mul_f32 v[12:13], v[0:1], v[12:13] op_sel_hi:[0,1]
	v_cvt_pk_f16_f32 v11, v12, v13
	v_mov_b32_e32 v7, v109
	v_mov_b32_e32 v8, v110
	v_pack_b32_f16 v12, v1, v11
	v_fma_mixlo_f16 v1, v0, v15, 0
	s_lshl_b32 s3, s2, 6
	v_alignbit_b32 v13, v1, v11, 16
	v_fma_mixlo_f16 v1, v0, v6, 0
	v_mov_b32_e32 v6, v7
	v_mov_b32_e32 v7, v8
	s_and_b32 s3, s3, 0x400
	v_pk_mul_f32 v[6:7], v[0:1], v[6:7] op_sel_hi:[0,1]
	v_mov_b32_e32 v2, v112
	v_mov_b32_e32 v9, v111
	v_add_u32_e32 v20, s3, v32
	v_cvt_pk_f16_f32 v7, v6, v7
	v_mov_b32_e32 v3, v113
	v_mov_b32_e32 v4, v114
	v_or_b32_e32 v20, v20, v31
	v_mov_b32_e32 v21, 0
	v_pack_b32_f16 v6, v1, v7
	v_fma_mixlo_f16 v1, v0, v9, 0
	v_lshlrev_b64 v[22:23], 11, v[20:21]
	s_lshl_b32 s3, s2, 7
	v_alignbit_b32 v7, v1, v7, 16
	v_fma_mixlo_f16 v1, v0, v2, 0
	v_mov_b32_e32 v2, v3
	v_mov_b32_e32 v3, v4
	v_mov_b32_e32 v5, v115
	s_mov_b32 s5, 0
	v_lshl_add_u64 v[22:23], s[10:11], 0, v[22:23]
	s_and_b32 s4, s3, 0x780
	v_pk_mul_f32 v[2:3], v[0:1], v[2:3] op_sel_hi:[0,1]
	v_lshl_add_u64 v[22:23], v[22:23], 0, s[4:5]
	v_lshlrev_b32_e32 v20, 1, v33
	v_cvt_pk_f16_f32 v3, v2, v3
	v_fma_mixlo_f16 v0, v0, v5, 0
	v_lshl_add_u64 v[20:21], v[22:23], 0, v[20:21]
	v_pack_b32_f16 v2, v1, v3
	v_alignbit_b32 v3, v0, v3, 16
	s_mov_b64 s[4:5], 0
	global_store_dwordx2 v[20:21], v[16:17], off
	global_store_dwordx2 v[20:21], v[12:13], off offset:32
	global_store_dwordx2 v[20:21], v[6:7], off offset:64
	global_store_dwordx2 v[20:21], v[2:3], off offset:96

.LBB3_27:
	s_waitcnt lgkmcnt(0)
	s_mul_i32 s0, s10, s11
	s_abs_i32 s1, s0
	v_cvt_f32_u32_e32 v0, s1
	s_sub_i32 s16, 0, s1
	s_sub_i32 s2, s19, s2
	s_add_i32 s2, s2, s21
	v_rcp_iflag_f32_e32 v0, v0
	s_abs_i32 s11, s2
	s_xor_b32 s3, s2, s0
	s_ashr_i32 s3, s3, 31
	v_mul_f32_e32 v0, 0x4f7ffffe, v0
	v_cvt_u32_f32_e32 v0, v0
	v_and_b32_e32 v36, 0xf0, v10
	v_mov_b32_e32 v37, 0
	v_readfirstlane_b32 s17, v0
	s_mul_i32 s16, s16, s17
	s_mul_hi_u32 s16, s17, s16
	s_add_i32 s17, s17, s16
	s_mul_hi_u32 s16, s11, s17
	s_mul_i32 s17, s16, s1
	s_sub_i32 s11, s11, s17
	s_add_i32 s18, s16, 1
	s_sub_i32 s17, s11, s1
	s_cmp_ge_u32 s11, s1
	s_cselect_b32 s16, s18, s16
	s_cselect_b32 s11, s17, s11
	s_add_i32 s17, s16, 1
	s_cmp_ge_u32 s11, s1
	s_cselect_b32 s1, s17, s16
	s_abs_i32 s11, s10
	v_cvt_f32_u32_e32 v0, s11
	s_xor_b32 s1, s1, s3
	s_sub_i32 s16, 0, s11
	s_sub_i32 s3, s1, s3
	v_rcp_iflag_f32_e32 v0, v0
	s_mul_i32 s0, s3, s0
	s_sub_i32 s0, s2, s0
	s_abs_i32 s2, s0
	v_mul_f32_e32 v0, 0x4f7ffffe, v0
	v_cvt_u32_f32_e32 v0, v0
	s_xor_b32 s1, s0, s10
	s_ashr_i32 s1, s1, 31
	v_readfirstlane_b32 s17, v0
	s_mul_i32 s16, s16, s17
	s_mul_hi_u32 s16, s17, s16
	s_add_i32 s17, s17, s16
	s_mul_hi_u32 s16, s2, s17
	s_mul_i32 s17, s16, s11
	s_sub_i32 s2, s2, s17
	s_add_i32 s18, s16, 1
	s_sub_i32 s17, s2, s11
	s_cmp_ge_u32 s2, s11
	s_cselect_b32 s16, s18, s16
	s_cselect_b32 s2, s17, s2
	s_add_i32 s17, s16, 1
	s_cmp_ge_u32 s2, s11
	s_cselect_b32 s2, s17, s16
	s_xor_b32 s2, s2, s1
	s_sub_i32 s2, s2, s1
	s_mul_i32 s1, s2, s10
	s_ashr_i32 s11, s3, 31
	s_sub_i32 s10, s0, s1
	s_mul_i32 s0, s12, s11
	s_mul_hi_u32 s1, s12, s3
	s_add_i32 s0, s1, s0
	s_mul_i32 s1, s13, s3
	s_add_i32 s1, s0, s1
	s_mul_i32 s0, s12, s3
	s_lshl_b64 s[0:1], s[0:1], 2
	s_add_u32 s4, s4, s0
	s_addc_u32 s12, s5, s1
	s_mul_i32 s0, s14, s11
	s_mul_hi_u32 s1, s14, s3
	s_add_i32 s0, s1, s0
	s_mul_i32 s1, s15, s3
	s_add_i32 s5, s0, s1
	s_lshl_b32 s0, s10, 6
	s_ashr_i32 s1, s0, 31
	s_lshl_b32 s2, s2, 7
	s_lshl_b64 s[10:11], s[0:1], 2
	s_add_u32 s10, s4, s10
	v_or_b32_e32 v28, s2, v29
	s_addc_u32 s11, s12, s11
	v_lshl_add_u64 v[32:33], s[10:11], 0, v[36:37]
	v_mad_i64_i32 v[0:1], s[10:11], v28, s9, 0
	v_lshl_add_u64 v[8:9], v[0:1], 2, v[32:33]
	v_or_b32_e32 v0, 16, v28
	v_mad_i64_i32 v[0:1], s[10:11], v0, s9, 0
	v_lshl_add_u64 v[10:11], v[0:1], 2, v[32:33]
	global_load_dwordx4 v[0:3], v[8:9], off nt
	global_load_dwordx4 v[4:7], v[10:11], off nt
	v_or_b32_e32 v8, 32, v28
	v_mad_i64_i32 v[8:9], s[10:11], v8, s9, 0
	v_lshl_add_u64 v[16:17], v[8:9], 2, v[32:33]
	v_or_b32_e32 v8, 48, v28
	v_mad_i64_i32 v[8:9], s[10:11], v8, s9, 0
	v_lshl_add_u64 v[18:19], v[8:9], 2, v[32:33]
	global_load_dwordx4 v[8:11], v[16:17], off nt
	global_load_dwordx4 v[12:15], v[18:19], off nt
	v_or_b32_e32 v16, 64, v28
	v_mad_i64_i32 v[16:17], s[10:11], v16, s9, 0
	v_lshl_add_u64 v[24:25], v[16:17], 2, v[32:33]
	v_or_b32_e32 v16, 0x50, v28
	v_mad_i64_i32 v[16:17], s[10:11], v16, s9, 0
	v_lshl_add_u64 v[26:27], v[16:17], 2, v[32:33]
	global_load_dwordx4 v[16:19], v[24:25], off nt
	global_load_dwordx4 v[20:23], v[26:27], off nt
	v_or_b32_e32 v24, 0x60, v28
	v_mad_i64_i32 v[24:25], s[10:11], v24, s9, 0
	v_lshl_add_u64 v[24:25], v[24:25], 2, v[32:33]
	v_or_b32_e32 v28, 0x70, v28
	global_load_dwordx4 v[24:27], v[24:25], off nt
	v_mad_i64_i32 v[34:35], s[10:11], v28, s9, 0
	v_lshl_add_u64 v[32:33], v[34:35], 2, v[32:33]
	global_load_dwordx4 v[32:35], v[32:33], off nt
	s_movk_i32 s1, 0x104
	v_mad_u32_u24 v28, v29, s1, v36
	v_add_u32_e32 v31, 0x1040, v28
	v_add_u32_e32 v36, 0x1048, v28
	v_add_u32_e32 v38, 0x2080, v28
	v_add_u32_e32 v39, 0x2088, v28
	v_add_u32_e32 v40, 0x30c0, v28
	v_add_u32_e32 v41, 0x30c8, v28
	v_add_u32_e32 v42, 0x4100, v28
	v_add_u32_e32 v43, 0x4108, v28
	v_add_u32_e32 v44, 0x5140, v28
	v_add_u32_e32 v45, 0x5148, v28
	s_mul_i32 s4, s14, s3
	s_lshl_b64 s[4:5], s[4:5], 1
	s_add_u32 s1, s6, s4
	s_addc_u32 s4, s7, s5
	s_ashr_i32 s3, s2, 31
	s_lshl_b64 s[2:3], s[2:3], 1
	s_add_u32 s2, s1, s2
	s_addc_u32 s3, s4, s3
	s_waitcnt vmcnt(7)
	ds_write2_b32 v28, v0, v1 offset1:1
	ds_write2_b32 v28, v2, v3 offset0:2 offset1:3
	s_waitcnt vmcnt(6)
	ds_write2_b32 v31, v4, v5 offset1:1
	ds_write2_b32 v36, v6, v7 offset1:1
	s_waitcnt vmcnt(5)
	ds_write2_b32 v38, v8, v9 offset1:1
	ds_write2_b32 v39, v10, v11 offset1:1
	s_waitcnt vmcnt(4)
	ds_write2_b32 v40, v12, v13 offset1:1
	ds_write2_b32 v41, v14, v15 offset1:1
	s_waitcnt vmcnt(3)
	ds_write2_b32 v42, v16, v17 offset1:1
	ds_write2_b32 v43, v18, v19 offset1:1
	s_waitcnt vmcnt(2)
	ds_write2_b32 v44, v20, v21 offset1:1
	ds_write2_b32 v45, v22, v23 offset1:1
	v_add_u32_e32 v0, 0x6180, v28
	s_waitcnt vmcnt(1)
	ds_write2_b32 v0, v24, v25 offset1:1
	v_add_u32_e32 v0, 0x6188, v28
	ds_write2_b32 v0, v26, v27 offset1:1
	v_add_u32_e32 v0, 0x71c0, v28
	s_waitcnt vmcnt(0)
	ds_write2_b32 v0, v32, v33 offset1:1
	v_add_u32_e32 v0, 0x71c8, v28
	ds_write2_b32 v0, v34, v35 offset1:1
	v_and_b32_e32 v0, 0x78, v30
	v_lshlrev_b32_e32 v36, 1, v0
	v_mul_u32_u24_e32 v0, 0x104, v0
	v_lshl_add_u32 v24, v29, 2, v0
	v_add_u32_e32 v25, 0x400, v24
	s_waitcnt lgkmcnt(0)
	s_barrier
	ds_read2_b32 v[4:5], v24 offset1:16
	ds_read2_b32 v[6:7], v24 offset0:130 offset1:146
	ds_read2_b32 v[8:9], v25 offset0:4 offset1:20
	ds_read2_b32 v[10:11], v25 offset0:134 offset1:150
	ds_read2_b32 v[12:13], v25 offset0:199 offset1:215
	ds_read2_b32 v[14:15], v25 offset0:69 offset1:85
	ds_read2_b32 v[16:17], v24 offset0:195 offset1:211
	ds_read2_b32 v[18:19], v24 offset0:65 offset1:81
	v_or_b32_e32 v26, s0, v29
	v_lshl_add_u64 v[20:21], s[2:3], 0, v[36:37]
	v_mad_i64_i32 v[22:23], s[0:1], v26, s8, 0
	s_waitcnt lgkmcnt(3)
	v_cvt_pk_f16_f32 v3, v10, v12
	s_waitcnt lgkmcnt(2)
	v_cvt_pk_f16_f32 v2, v8, v14
	s_waitcnt lgkmcnt(1)
	v_cvt_pk_f16_f32 v1, v6, v16
	s_waitcnt lgkmcnt(0)
	v_cvt_pk_f16_f32 v0, v4, v18
	v_lshl_add_u64 v[22:23], v[22:23], 1, v[20:21]
	global_store_dwordx4 v[22:23], v[0:3], off
	v_or_b32_e32 v4, 16, v26
	s_nop 0
	v_cvt_pk_f16_f32 v3, v11, v13
	v_cvt_pk_f16_f32 v2, v9, v15
	v_cvt_pk_f16_f32 v1, v7, v17
	v_cvt_pk_f16_f32 v0, v5, v19
	ds_read2_b32 v[6:7], v24 offset0:32 offset1:48
	ds_read2_b32 v[8:9], v24 offset0:162 offset1:178
	ds_read2_b32 v[10:11], v25 offset0:36 offset1:52
	ds_read2_b32 v[12:13], v25 offset0:166 offset1:182
	ds_read2_b32 v[14:15], v25 offset0:231 offset1:247
	ds_read2_b32 v[16:17], v25 offset0:101 offset1:117
	ds_read2_b32 v[18:19], v24 offset0:227 offset1:243
	ds_read2_b32 v[22:23], v24 offset0:97 offset1:113
	v_mad_i64_i32 v[4:5], s[0:1], v4, s8, 0
	v_lshl_add_u64 v[4:5], v[4:5], 1, v[20:21]
	global_store_dwordx4 v[4:5], v[0:3], off
	v_or_b32_e32 v4, 32, v26
	v_mad_i64_i32 v[4:5], s[0:1], v4, s8, 0
	s_waitcnt lgkmcnt(3)
	v_cvt_pk_f16_f32 v3, v12, v14
	s_waitcnt lgkmcnt(2)
	v_cvt_pk_f16_f32 v2, v10, v16
	s_waitcnt lgkmcnt(1)
	v_cvt_pk_f16_f32 v1, v8, v18
	s_waitcnt lgkmcnt(0)
	v_cvt_pk_f16_f32 v0, v6, v22
	v_lshl_add_u64 v[4:5], v[4:5], 1, v[20:21]
	global_store_dwordx4 v[4:5], v[0:3], off
	v_or_b32_e32 v4, 48, v26
	v_mad_i64_i32 v[4:5], s[0:1], v4, s8, 0
	v_cvt_pk_f16_f32 v3, v13, v15
	v_cvt_pk_f16_f32 v2, v11, v17
	v_cvt_pk_f16_f32 v1, v9, v19
	v_cvt_pk_f16_f32 v0, v7, v23
	v_lshl_add_u64 v[4:5], v[4:5], 1, v[20:21]
	global_store_dwordx4 v[4:5], v[0:3], off
	s_endpgm
	s_endpgm
	s_endpgm
	s_endpgm
	s_endpgm
	s_endpgm
	s_endpgm
	s_endpgm
	s_endpgm
	s_endpgm
	s_endpgm
	s_endpgm
	s_endpgm
	s_endpgm
	s_endpgm
	s_endpgm
	s_endpgm
	s_endpgm
	s_endpgm
	s_endpgm
	s_endpgm
	s_endpgm
	s_endpgm
	s_endpgm
	s_endpgm
	s_endpgm
	s_endpgm
	s_endpgm
	s_endpgm
	s_endpgm
	s_endpgm
	s_endpgm
	s_endpgm
	s_endpgm
	s_endpgm
	s_endpgm
	s_endpgm
	s_endpgm
	s_endpgm
	s_endpgm
	s_endpgm
	s_endpgm

	.amdhsa_kernel _Z11attn_kernelPKDF16_S0_S0_PDF16_7CvtJobs
		.amdhsa_group_segment_fixed_size 33280
		.amdhsa_private_segment_fixed_size 0
		.amdhsa_kernarg_size 432
		.amdhsa_user_sgpr_count 2
		.amdhsa_user_sgpr_dispatch_ptr 0
		.amdhsa_user_sgpr_queue_ptr 0
		.amdhsa_user_sgpr_kernarg_segment_ptr 1
		.amdhsa_user_sgpr_dispatch_id 0
		.amdhsa_user_sgpr_kernarg_preload_length 0
		.amdhsa_user_sgpr_kernarg_preload_offset 0
		.amdhsa_user_sgpr_private_segment_size 0
		.amdhsa_uses_dynamic_stack 0
		.amdhsa_enable_private_segment 0
		.amdhsa_system_sgpr_workgroup_id_x 1
		.amdhsa_system_sgpr_workgroup_id_y 0
		.amdhsa_system_sgpr_workgroup_id_z 0
		.amdhsa_system_sgpr_workgroup_info 0
		.amdhsa_system_vgpr_workitem_id 0
		.amdhsa_next_free_vgpr 116
		.amdhsa_next_free_sgpr 96
		.amdhsa_accum_offset 116
		.amdhsa_reserve_vcc 1
		.amdhsa_float_round_mode_32 0
		.amdhsa_float_round_mode_16_64 0
		.amdhsa_float_denorm_mode_32 3
		.amdhsa_float_denorm_mode_16_64 3
		.amdhsa_dx10_clamp 1
		.amdhsa_ieee_mode 1
		.amdhsa_fp16_overflow 0
		.amdhsa_tg_split 0
		.amdhsa_exception_fp_ieee_invalid_op 0
		.amdhsa_exception_fp_denorm_src 0
		.amdhsa_exception_fp_ieee_div_zero 0
		.amdhsa_exception_fp_ieee_overflow 0
		.amdhsa_exception_fp_ieee_underflow 0
		.amdhsa_exception_fp_ieee_inexact 0
		.amdhsa_exception_int_div_zero 0
	.end_amdhsa_kernel

.LBB4_4:
	s_load_dword s2, s[0:1], 0x18
	v_lshrrev_b32_e32 v6, 4, v0
	v_xor_b32_e32 v1, v6, v0
	v_lshlrev_b32_e32 v1, 3, v1
	v_and_b32_e32 v2, 56, v1
	v_lshrrev_b32_e32 v1, 3, v0
	s_waitcnt lgkmcnt(0)
	v_mad_u64_u32 v[4:5], s[0:1], v1, s2, v[2:3]
	v_or_b32_e32 v3, 0x200, v0
	v_lshrrev_b32_e32 v3, 3, v3
	s_lshl_b32 s10, s12, 7
	s_ashr_i32 s13, s2, 31
	v_mul_lo_u32 v3, v3, s2
	s_lshl_b32 s0, s2, 7
	v_add_lshl_u32 v2, v3, v2, 1
	v_add_lshl_u32 v3, v4, s0, 1
	s_mul_i32 s0, s10, s13
	s_mul_hi_u32 s1, s10, s2
	s_add_i32 s1, s1, s0
	s_mul_i32 s0, s10, s2
	s_mul_i32 s11, s3, 0xc0
	s_lshl_b64 s[0:1], s[0:1], 1
	v_lshlrev_b32_e32 v122, 4, v0
	v_lshlrev_b32_e32 v1, 1, v4
	s_add_u32 s0, s4, s0
	s_mul_i32 s3, s11, s13
	s_mul_hi_u32 s4, s11, s2
	v_add_u32_e32 v4, 0, v122
	s_addc_u32 s1, s5, s1
	s_add_i32 s3, s4, s3
	s_mul_i32 s2, s11, s2
	v_readfirstlane_b32 s13, v4
	v_add_u32_e32 v5, 0x2000, v4
	s_lshl_b64 s[2:3], s[2:3], 1
	s_mov_b32 m0, s13
	v_readfirstlane_b32 s4, v5
	v_add_u32_e32 v5, 0x4000, v4
	s_add_u32 s2, s6, s2
	global_load_lds_dwordx4 v1, s[0:1]
	s_mov_b32 m0, s4
	v_readfirstlane_b32 s5, v5
	v_add_u32_e32 v5, 0x6000, v4
	s_addc_u32 s3, s7, s3
	global_load_lds_dwordx4 v2, s[0:1]
	s_mov_b32 m0, s5
	v_readfirstlane_b32 s6, v5
	v_add_u32_e32 v5, 0x8000, v4
	global_load_lds_dwordx4 v1, s[2:3]
	s_mov_b32 m0, s6
	v_readfirstlane_b32 s7, v5
	v_add_u32_e32 v5, 0xa000, v4
	global_load_lds_dwordx4 v2, s[2:3]
	s_mov_b32 m0, s7
	s_add_u32 s16, s0, 0x80
	v_readfirstlane_b32 s18, v5
	v_add_u32_e32 v5, 0xc000, v4
	global_load_lds_dwordx4 v3, s[2:3]
	s_addc_u32 s17, s1, 0
	s_mov_b32 m0, s18
	v_readfirstlane_b32 s14, v5
	v_add_u32_e32 v5, 0xe000, v4
	s_add_u32 s20, s2, 0x80
	global_load_lds_dwordx4 v1, s[16:17]
	s_mov_b32 m0, s14
	v_readfirstlane_b32 s15, v5
	v_add_u32_e32 v5, 0x10000, v4
	s_addc_u32 s21, s3, 0
	global_load_lds_dwordx4 v2, s[16:17]
	s_mov_b32 m0, s15
	v_readfirstlane_b32 s16, v5
	v_add_u32_e32 v5, 0x12000, v4
	global_load_lds_dwordx4 v1, s[20:21]
	s_mov_b32 m0, s16
	v_readfirstlane_b32 s17, v5
	global_load_lds_dwordx4 v2, s[20:21]
	s_mov_b32 m0, s17
	v_add_u32_e32 v5, 0x14000, v4
	global_load_lds_dwordx4 v3, s[20:21]
	s_add_u32 s20, s0, 0x100
	v_readfirstlane_b32 s19, v5
	v_add_u32_e32 v5, 0x16000, v4
	s_addc_u32 s21, s1, 0
	s_mov_b32 m0, s19
	v_readfirstlane_b32 s19, v5
	v_add_u32_e32 v5, 0x18000, v4
	s_add_u32 s22, s2, 0x100
	global_load_lds_dwordx4 v1, s[20:21]
	s_mov_b32 m0, s19
	v_readfirstlane_b32 s19, v5
	v_add_u32_e32 v5, 0x1a000, v4
	s_addc_u32 s23, s3, 0
	global_load_lds_dwordx4 v2, s[20:21]
	s_mov_b32 m0, s19
	v_readfirstlane_b32 s19, v5
	v_add_u32_e32 v4, 0x1c000, v4
	global_load_lds_dwordx4 v1, s[22:23]
	s_mov_b32 m0, s19
	v_readfirstlane_b32 s19, v4
	global_load_lds_dwordx4 v2, s[22:23]
	s_mov_b32 m0, s19
	v_and_b32_e32 v8, 15, v0
	global_load_lds_dwordx4 v3, s[22:23]
	v_lshrrev_b32_e32 v11, 2, v0
	v_bfe_u32 v9, v0, 6, 2
	v_bfe_u32 v5, v0, 1, 3
	v_and_or_b32 v4, v11, 64, v8
	v_lshlrev_b32_e32 v123, 7, v4
	v_bitop3_b32 v4, v6, v5, 3 bitop3:0x6c
	v_mul_u32_u24_e32 v10, 48, v9
	v_lshlrev_b32_e32 v6, 4, v4
	v_or_b32_e32 v4, v10, v8
	v_lshlrev_b32_e32 v7, 7, v4
	v_add_u32_e32 v13, 0, v7
	s_waitcnt vmcnt(10)
	s_barrier
	v_add_u32_e32 v4, v13, v6
	ds_read_b128 v[14:17], v4 offset:16384
	v_add_u32_e32 v50, 0, v123
	v_add_u32_e32 v6, v50, v6
	ds_read_b128 v[18:21], v6
	ds_read_b128 v[22:25], v4 offset:18432
	ds_read_b128 v[26:29], v6 offset:2048
	ds_read_b128 v[30:33], v4 offset:20480
	ds_read_b128 v[42:45], v6 offset:4096
	ds_read_b128 v[46:49], v6 offset:6144
	v_bfe_u32 v12, v0, 4, 2
	v_bitop3_b32 v0, v12, v5, 4 bitop3:0x36
	v_lshlrev_b32_e32 v5, 4, v0
	s_add_i32 s19, 0, 0x14000
	v_add_u32_e32 v124, s19, v5
	s_waitcnt lgkmcnt(0)
	v_mfma_f32_16x16x32_f16 v[34:37], v[14:17], v[18:21], 0
	v_add_u32_e32 v7, v7, v124
	v_mfma_f32_16x16x32_f16 v[38:41], v[22:25], v[18:21], 0
	v_mfma_f32_16x16x32_f16 v[18:21], v[30:33], v[18:21], 0
	v_add_u32_e32 v0, v50, v5
	ds_read_b128 v[50:53], v0
	ds_read_b128 v[54:57], v0 offset:2048
	ds_read_b128 v[58:61], v0 offset:4096
	ds_read_b128 v[62:65], v0 offset:6144
	v_add_u32_e32 v5, v13, v5
	ds_read_b128 v[66:69], v5 offset:16384
	ds_read_b128 v[70:73], v5 offset:18432
	ds_read_b128 v[74:77], v5 offset:20480
	v_mfma_f32_16x16x32_f16 v[78:81], v[14:17], v[26:29], 0
	v_mfma_f32_16x16x32_f16 v[82:85], v[22:25], v[26:29], 0
	v_mfma_f32_16x16x32_f16 v[26:29], v[30:33], v[26:29], 0
	v_mfma_f32_16x16x32_f16 v[86:89], v[14:17], v[42:45], 0
	v_mfma_f32_16x16x32_f16 v[90:93], v[22:25], v[42:45], 0
	v_mfma_f32_16x16x32_f16 v[42:45], v[30:33], v[42:45], 0
	v_mfma_f32_16x16x32_f16 v[14:17], v[14:17], v[46:49], 0
	v_mfma_f32_16x16x32_f16 v[22:25], v[22:25], v[46:49], 0
	v_mfma_f32_16x16x32_f16 v[30:33], v[30:33], v[46:49], 0
	s_add_u32 s20, s0, 0x180
	s_mov_b32 m0, s13
	s_waitcnt vmcnt(5) lgkmcnt(0)
	s_barrier
	s_addc_u32 s21, s1, 0
	s_add_u32 s22, s2, 0x180
	global_load_lds_dwordx4 v1, s[20:21]
	s_mov_b32 m0, s4
	s_addc_u32 s23, s3, 0
	global_load_lds_dwordx4 v2, s[20:21]
	s_mov_b32 m0, s5
	s_nop 0
	global_load_lds_dwordx4 v1, s[22:23]
	s_mov_b32 m0, s6
	s_nop 0
	global_load_lds_dwordx4 v2, s[22:23]
	s_mov_b32 m0, s7
	s_nop 0
	global_load_lds_dwordx4 v3, s[22:23]
	s_waitcnt lgkmcnt(0)
	v_mfma_f32_16x16x32_f16 v[34:37], v[66:69], v[50:53], v[34:37]
	v_mfma_f32_16x16x32_f16 v[38:41], v[70:73], v[50:53], v[38:41]
	v_mfma_f32_16x16x32_f16 v[18:21], v[74:77], v[50:53], v[18:21]
	ds_read_b128 v[46:49], v6 offset:40960
	ds_read_b128 v[50:53], v6 offset:43008
	ds_read_b128 v[94:97], v6 offset:45056
	ds_read_b128 v[98:101], v6 offset:47104
	ds_read_b128 v[102:105], v4 offset:57344
	ds_read_b128 v[106:109], v4 offset:59392
	ds_read_b128 v[110:113], v4 offset:61440
	v_mfma_f32_16x16x32_f16 v[78:81], v[66:69], v[54:57], v[78:81]
	v_mfma_f32_16x16x32_f16 v[82:85], v[70:73], v[54:57], v[82:85]
	v_mfma_f32_16x16x32_f16 v[26:29], v[74:77], v[54:57], v[26:29]
	v_mfma_f32_16x16x32_f16 v[54:57], v[66:69], v[58:61], v[86:89]
	v_mfma_f32_16x16x32_f16 v[86:89], v[70:73], v[58:61], v[90:93]
	v_mfma_f32_16x16x32_f16 v[42:45], v[74:77], v[58:61], v[42:45]
	v_mfma_f32_16x16x32_f16 v[14:17], v[66:69], v[62:65], v[14:17]
	v_mfma_f32_16x16x32_f16 v[22:25], v[70:73], v[62:65], v[22:25]
	v_mfma_f32_16x16x32_f16 v[30:33], v[74:77], v[62:65], v[30:33]
	s_waitcnt lgkmcnt(0)
	v_mfma_f32_16x16x32_f16 v[34:37], v[102:105], v[46:49], v[34:37]
	v_mfma_f32_16x16x32_f16 v[38:41], v[106:109], v[46:49], v[38:41]
	v_mfma_f32_16x16x32_f16 v[18:21], v[110:113], v[46:49], v[18:21]
	ds_read_b128 v[46:49], v0 offset:40960
	ds_read_b128 v[58:61], v0 offset:43008
	ds_read_b128 v[62:65], v0 offset:45056
	ds_read_b128 v[66:69], v0 offset:47104
	ds_read_b128 v[70:73], v5 offset:57344
	ds_read_b128 v[74:77], v5 offset:59392
	ds_read_b128 v[90:93], v5 offset:61440
	v_mfma_f32_16x16x32_f16 v[78:81], v[102:105], v[50:53], v[78:81]
	v_mfma_f32_16x16x32_f16 v[82:85], v[106:109], v[50:53], v[82:85]
	v_mfma_f32_16x16x32_f16 v[26:29], v[110:113], v[50:53], v[26:29]
	v_mfma_f32_16x16x32_f16 v[50:53], v[102:105], v[94:97], v[54:57]
	v_mfma_f32_16x16x32_f16 v[54:57], v[106:109], v[94:97], v[86:89]
	v_mfma_f32_16x16x32_f16 v[42:45], v[110:113], v[94:97], v[42:45]
	v_mfma_f32_16x16x32_f16 v[86:89], v[102:105], v[98:101], v[14:17]
	v_mfma_f32_16x16x32_f16 v[22:25], v[106:109], v[98:101], v[22:25]
	v_mfma_f32_16x16x32_f16 v[30:33], v[110:113], v[98:101], v[30:33]
	s_add_u32 s20, s0, 0x200
	s_mov_b32 m0, s18
	s_waitcnt vmcnt(5) lgkmcnt(0)
	s_barrier
	s_addc_u32 s21, s1, 0
	s_add_u32 s22, s2, 0x200
	global_load_lds_dwordx4 v1, s[20:21]
	s_mov_b32 m0, s14
	s_addc_u32 s23, s3, 0
	global_load_lds_dwordx4 v2, s[20:21]
	s_mov_b32 m0, s15
	s_nop 0
	global_load_lds_dwordx4 v1, s[22:23]
	s_mov_b32 m0, s16
	s_nop 0
	global_load_lds_dwordx4 v2, s[22:23]
	s_mov_b32 m0, s17
	s_nop 0
	global_load_lds_dwordx4 v3, s[22:23]
	s_waitcnt lgkmcnt(0)
	v_mfma_f32_16x16x32_f16 v[34:37], v[70:73], v[46:49], v[34:37]
	v_mfma_f32_16x16x32_f16 v[38:41], v[74:77], v[46:49], v[38:41]
	v_mfma_f32_16x16x32_f16 v[46:49], v[90:93], v[46:49], v[18:21]
	v_add_u32_e32 v13, 0x14000, v6
	v_add_u32_e32 v15, 0x15000, v6
	s_nop 0
	v_add_u32_e32 v18, 0x18000, v4
	v_add_u32_e32 v14, 0x14800, v6
	ds_read_b128 v[94:97], v13
	ds_read_b128 v[98:101], v14
	v_add_u32_e32 v16, 0x15800, v6
	ds_read_b128 v[102:105], v15
	ds_read_b128 v[106:109], v16
	v_add_u32_e32 v19, 0x18800, v4
	ds_read_b128 v[110:113], v18
	ds_read_b128 v[114:117], v19
	v_add_u32_e32 v20, 0x19000, v4
	ds_read_b128 v[118:121], v20
	v_mfma_f32_16x16x32_f16 v[78:81], v[70:73], v[58:61], v[78:81]
	v_mfma_f32_16x16x32_f16 v[82:85], v[74:77], v[58:61], v[82:85]
	v_mfma_f32_16x16x32_f16 v[26:29], v[90:93], v[58:61], v[26:29]
	v_mfma_f32_16x16x32_f16 v[50:53], v[70:73], v[62:65], v[50:53]
	v_mfma_f32_16x16x32_f16 v[54:57], v[74:77], v[62:65], v[54:57]
	v_mfma_f32_16x16x32_f16 v[42:45], v[90:93], v[62:65], v[42:45]
	v_mfma_f32_16x16x32_f16 v[58:61], v[70:73], v[66:69], v[86:89]
	v_mfma_f32_16x16x32_f16 v[22:25], v[74:77], v[66:69], v[22:25]
	v_mfma_f32_16x16x32_f16 v[30:33], v[90:93], v[66:69], v[30:33]
	s_waitcnt lgkmcnt(0)
	v_mfma_f32_16x16x32_f16 v[34:37], v[110:113], v[94:97], v[34:37]
	v_mfma_f32_16x16x32_f16 v[38:41], v[114:117], v[94:97], v[38:41]
	v_mfma_f32_16x16x32_f16 v[46:49], v[118:121], v[94:97], v[46:49]
	v_add_u32_e32 v17, v124, v123
	ds_read_b128 v[62:65], v17 offset:2048
	ds_read_b128 v[66:69], v17 offset:4096
	ds_read_b128 v[70:73], v17 offset:6144
	ds_read_b128 v[74:77], v7 offset:16384
	ds_read_b128 v[86:89], v7 offset:18432
	ds_read_b128 v[90:93], v17
	ds_read_b128 v[94:97], v7 offset:20480
	v_mfma_f32_16x16x32_f16 v[78:81], v[110:113], v[98:101], v[78:81]
	v_mfma_f32_16x16x32_f16 v[82:85], v[114:117], v[98:101], v[82:85]
	v_mfma_f32_16x16x32_f16 v[26:29], v[118:121], v[98:101], v[26:29]
	v_mfma_f32_16x16x32_f16 v[50:53], v[110:113], v[102:105], v[50:53]
	v_mfma_f32_16x16x32_f16 v[54:57], v[114:117], v[102:105], v[54:57]
	v_mfma_f32_16x16x32_f16 v[42:45], v[118:121], v[102:105], v[42:45]
	v_mfma_f32_16x16x32_f16 v[58:61], v[110:113], v[106:109], v[58:61]
	v_mfma_f32_16x16x32_f16 v[22:25], v[114:117], v[106:109], v[22:25]
	v_mfma_f32_16x16x32_f16 v[30:33], v[118:121], v[106:109], v[30:33]
	v_add_u32_e32 v21, s19, v122
	s_add_u32 s20, s0, 0x280
	v_readfirstlane_b32 s23, v21
	v_add_u32_e32 v98, 0x2000, v21
	s_waitcnt vmcnt(5) lgkmcnt(0)
	s_barrier
	s_addc_u32 s21, s1, 0
	s_mov_b32 m0, s23
	v_readfirstlane_b32 s19, v98
	global_load_lds_dwordx4 v1, s[20:21]
	s_mov_b32 m0, s19
	v_add_u32_e32 v98, 0x4000, v21
	s_add_u32 s24, s2, 0x280
	global_load_lds_dwordx4 v2, s[20:21]
	v_readfirstlane_b32 s20, v98
	v_add_u32_e32 v98, 0x6000, v21
	s_addc_u32 s25, s3, 0
	s_mov_b32 m0, s20
	v_readfirstlane_b32 s21, v98
	v_add_u32_e32 v21, 0x8000, v21
	global_load_lds_dwordx4 v1, s[24:25]
	s_mov_b32 m0, s21
	v_readfirstlane_b32 s22, v21
	global_load_lds_dwordx4 v2, s[24:25]
	s_mov_b32 m0, s22
	s_nop 0
	global_load_lds_dwordx4 v3, s[24:25]
	s_waitcnt lgkmcnt(0)
	v_mfma_f32_16x16x32_f16 v[34:37], v[74:77], v[90:93], v[34:37]
	v_mfma_f32_16x16x32_f16 v[38:41], v[86:89], v[90:93], v[38:41]
	v_mfma_f32_16x16x32_f16 v[46:49], v[94:97], v[90:93], v[46:49]
	ds_read_b128 v[90:93], v6
	ds_read_b128 v[98:101], v6 offset:2048
	ds_read_b128 v[102:105], v6 offset:4096
	ds_read_b128 v[106:109], v6 offset:6144
	ds_read_b128 v[110:113], v4 offset:16384
	ds_read_b128 v[114:117], v4 offset:18432
	ds_read_b128 v[118:121], v4 offset:20480
	v_mfma_f32_16x16x32_f16 v[78:81], v[74:77], v[62:65], v[78:81]
	v_mfma_f32_16x16x32_f16 v[82:85], v[86:89], v[62:65], v[82:85]
	v_mfma_f32_16x16x32_f16 v[26:29], v[94:97], v[62:65], v[26:29]
	v_mfma_f32_16x16x32_f16 v[50:53], v[74:77], v[66:69], v[50:53]
	v_mfma_f32_16x16x32_f16 v[54:57], v[86:89], v[66:69], v[54:57]
	v_mfma_f32_16x16x32_f16 v[42:45], v[94:97], v[66:69], v[42:45]
	v_mfma_f32_16x16x32_f16 v[58:61], v[74:77], v[70:73], v[58:61]
	v_mfma_f32_16x16x32_f16 v[22:25], v[86:89], v[70:73], v[22:25]
	v_mfma_f32_16x16x32_f16 v[30:33], v[94:97], v[70:73], v[30:33]
	s_waitcnt lgkmcnt(0)
	v_mfma_f32_16x16x32_f16 v[34:37], v[110:113], v[90:93], v[34:37]
	v_mfma_f32_16x16x32_f16 v[38:41], v[114:117], v[90:93], v[38:41]
	v_mfma_f32_16x16x32_f16 v[46:49], v[118:121], v[90:93], v[46:49]
	ds_read_b128 v[62:65], v0
	ds_read_b128 v[66:69], v0 offset:2048
	ds_read_b128 v[70:73], v0 offset:4096
	ds_read_b128 v[74:77], v0 offset:6144
	ds_read_b128 v[86:89], v5 offset:16384
	ds_read_b128 v[90:93], v5 offset:18432
	ds_read_b128 v[94:97], v5 offset:20480
	v_mfma_f32_16x16x32_f16 v[78:81], v[110:113], v[98:101], v[78:81]
	v_mfma_f32_16x16x32_f16 v[82:85], v[114:117], v[98:101], v[82:85]
	v_mfma_f32_16x16x32_f16 v[26:29], v[118:121], v[98:101], v[26:29]
	v_mfma_f32_16x16x32_f16 v[50:53], v[110:113], v[102:105], v[50:53]
	v_mfma_f32_16x16x32_f16 v[54:57], v[114:117], v[102:105], v[54:57]
	v_mfma_f32_16x16x32_f16 v[42:45], v[118:121], v[102:105], v[42:45]
	v_mfma_f32_16x16x32_f16 v[58:61], v[110:113], v[106:109], v[58:61]
	v_mfma_f32_16x16x32_f16 v[22:25], v[114:117], v[106:109], v[22:25]
	v_mfma_f32_16x16x32_f16 v[30:33], v[118:121], v[106:109], v[30:33]
	s_add_u32 s24, s0, 0x300
	s_mov_b32 m0, s13
	s_waitcnt vmcnt(5) lgkmcnt(0)
	s_barrier
	s_addc_u32 s25, s1, 0
	s_add_u32 s26, s2, 0x300
	global_load_lds_dwordx4 v1, s[24:25]
	s_mov_b32 m0, s4
	s_addc_u32 s27, s3, 0
	global_load_lds_dwordx4 v2, s[24:25]
	s_mov_b32 m0, s5
	s_nop 0
	global_load_lds_dwordx4 v1, s[26:27]
	s_mov_b32 m0, s6
	s_nop 0
	global_load_lds_dwordx4 v2, s[26:27]
	s_mov_b32 m0, s7
	s_nop 0
	global_load_lds_dwordx4 v3, s[26:27]
	s_waitcnt lgkmcnt(0)
	v_mfma_f32_16x16x32_f16 v[34:37], v[86:89], v[62:65], v[34:37]
	v_mfma_f32_16x16x32_f16 v[38:41], v[90:93], v[62:65], v[38:41]
	v_mfma_f32_16x16x32_f16 v[46:49], v[94:97], v[62:65], v[46:49]
	ds_read_b128 v[62:65], v6 offset:40960
	ds_read_b128 v[98:101], v6 offset:43008
	ds_read_b128 v[102:105], v6 offset:45056
	ds_read_b128 v[106:109], v6 offset:47104
	ds_read_b128 v[110:113], v4 offset:57344
	ds_read_b128 v[114:117], v4 offset:59392
	ds_read_b128 v[118:121], v4 offset:61440
	v_mfma_f32_16x16x32_f16 v[78:81], v[86:89], v[66:69], v[78:81]
	v_mfma_f32_16x16x32_f16 v[82:85], v[90:93], v[66:69], v[82:85]
	v_mfma_f32_16x16x32_f16 v[26:29], v[94:97], v[66:69], v[26:29]
	v_mfma_f32_16x16x32_f16 v[50:53], v[86:89], v[70:73], v[50:53]
	v_mfma_f32_16x16x32_f16 v[54:57], v[90:93], v[70:73], v[54:57]
	v_mfma_f32_16x16x32_f16 v[42:45], v[94:97], v[70:73], v[42:45]
	v_mfma_f32_16x16x32_f16 v[58:61], v[86:89], v[74:77], v[58:61]
	v_mfma_f32_16x16x32_f16 v[22:25], v[90:93], v[74:77], v[22:25]
	v_mfma_f32_16x16x32_f16 v[30:33], v[94:97], v[74:77], v[30:33]
	s_waitcnt lgkmcnt(0)
	v_mfma_f32_16x16x32_f16 v[34:37], v[110:113], v[62:65], v[34:37]
	v_mfma_f32_16x16x32_f16 v[38:41], v[114:117], v[62:65], v[38:41]
	v_mfma_f32_16x16x32_f16 v[46:49], v[118:121], v[62:65], v[46:49]
	ds_read_b128 v[62:65], v0 offset:40960
	ds_read_b128 v[66:69], v0 offset:43008
	ds_read_b128 v[70:73], v0 offset:45056
	ds_read_b128 v[74:77], v0 offset:47104
	ds_read_b128 v[86:89], v5 offset:57344
	ds_read_b128 v[90:93], v5 offset:59392
	ds_read_b128 v[94:97], v5 offset:61440
	v_mfma_f32_16x16x32_f16 v[78:81], v[110:113], v[98:101], v[78:81]
	v_mfma_f32_16x16x32_f16 v[82:85], v[114:117], v[98:101], v[82:85]
	v_mfma_f32_16x16x32_f16 v[26:29], v[118:121], v[98:101], v[26:29]
	v_mfma_f32_16x16x32_f16 v[50:53], v[110:113], v[102:105], v[50:53]
	v_mfma_f32_16x16x32_f16 v[54:57], v[114:117], v[102:105], v[54:57]
	v_mfma_f32_16x16x32_f16 v[42:45], v[118:121], v[102:105], v[42:45]
	v_mfma_f32_16x16x32_f16 v[58:61], v[110:113], v[106:109], v[58:61]
	v_mfma_f32_16x16x32_f16 v[22:25], v[114:117], v[106:109], v[22:25]
	v_mfma_f32_16x16x32_f16 v[30:33], v[118:121], v[106:109], v[30:33]
	s_add_u32 s24, s0, 0x380
	s_mov_b32 m0, s18
	s_waitcnt vmcnt(5) lgkmcnt(0)
	s_barrier
	s_addc_u32 s25, s1, 0
	s_add_u32 s26, s2, 0x380
	global_load_lds_dwordx4 v1, s[24:25]
	s_mov_b32 m0, s14
	s_addc_u32 s27, s3, 0
	global_load_lds_dwordx4 v2, s[24:25]
	s_mov_b32 m0, s15
	s_nop 0
	global_load_lds_dwordx4 v1, s[26:27]
	s_mov_b32 m0, s16
	s_nop 0
	global_load_lds_dwordx4 v2, s[26:27]
	s_mov_b32 m0, s17
	s_nop 0
	global_load_lds_dwordx4 v3, s[26:27]
	s_waitcnt lgkmcnt(0)
	v_mfma_f32_16x16x32_f16 v[34:37], v[86:89], v[62:65], v[34:37]
	v_mfma_f32_16x16x32_f16 v[38:41], v[90:93], v[62:65], v[38:41]
	v_mfma_f32_16x16x32_f16 v[46:49], v[94:97], v[62:65], v[46:49]
	ds_read_b128 v[62:65], v13
	ds_read_b128 v[98:101], v14
	ds_read_b128 v[102:105], v15
	ds_read_b128 v[106:109], v16
	ds_read_b128 v[110:113], v18
	ds_read_b128 v[114:117], v19
	ds_read_b128 v[118:121], v20
	v_mfma_f32_16x16x32_f16 v[78:81], v[86:89], v[66:69], v[78:81]
	v_mfma_f32_16x16x32_f16 v[82:85], v[90:93], v[66:69], v[82:85]
	v_mfma_f32_16x16x32_f16 v[26:29], v[94:97], v[66:69], v[26:29]
	v_mfma_f32_16x16x32_f16 v[50:53], v[86:89], v[70:73], v[50:53]
	v_mfma_f32_16x16x32_f16 v[54:57], v[90:93], v[70:73], v[54:57]
	v_mfma_f32_16x16x32_f16 v[42:45], v[94:97], v[70:73], v[42:45]
	v_mfma_f32_16x16x32_f16 v[58:61], v[86:89], v[74:77], v[58:61]
	v_mfma_f32_16x16x32_f16 v[22:25], v[90:93], v[74:77], v[22:25]
	v_mfma_f32_16x16x32_f16 v[30:33], v[94:97], v[74:77], v[30:33]
	s_waitcnt lgkmcnt(0)
	v_mfma_f32_16x16x32_f16 v[34:37], v[110:113], v[62:65], v[34:37]
	v_mfma_f32_16x16x32_f16 v[38:41], v[114:117], v[62:65], v[38:41]
	v_mfma_f32_16x16x32_f16 v[46:49], v[118:121], v[62:65], v[46:49]
	ds_read_b128 v[62:65], v17 offset:2048
	ds_read_b128 v[66:69], v17 offset:4096
	ds_read_b128 v[70:73], v17 offset:6144
	ds_read_b128 v[74:77], v7 offset:16384
	ds_read_b128 v[86:89], v7 offset:18432
	ds_read_b128 v[90:93], v17
	ds_read_b128 v[94:97], v7 offset:20480
	v_mfma_f32_16x16x32_f16 v[78:81], v[110:113], v[98:101], v[78:81]
	v_mfma_f32_16x16x32_f16 v[82:85], v[114:117], v[98:101], v[82:85]
	v_mfma_f32_16x16x32_f16 v[26:29], v[118:121], v[98:101], v[26:29]
	v_mfma_f32_16x16x32_f16 v[50:53], v[110:113], v[102:105], v[50:53]
	v_mfma_f32_16x16x32_f16 v[54:57], v[114:117], v[102:105], v[54:57]
	v_mfma_f32_16x16x32_f16 v[42:45], v[118:121], v[102:105], v[42:45]
	v_mfma_f32_16x16x32_f16 v[58:61], v[110:113], v[106:109], v[58:61]
	v_mfma_f32_16x16x32_f16 v[22:25], v[114:117], v[106:109], v[22:25]
	v_mfma_f32_16x16x32_f16 v[30:33], v[118:121], v[106:109], v[30:33]
	s_add_u32 s24, s0, 0x400
	s_mov_b32 m0, s23
	s_waitcnt vmcnt(5) lgkmcnt(0)
	s_barrier
	s_addc_u32 s25, s1, 0
	s_add_u32 s26, s2, 0x400
	global_load_lds_dwordx4 v1, s[24:25]
	s_mov_b32 m0, s19
	s_addc_u32 s27, s3, 0
	global_load_lds_dwordx4 v2, s[24:25]
	s_mov_b32 m0, s20
	s_nop 0
	global_load_lds_dwordx4 v1, s[26:27]
	s_mov_b32 m0, s21
	s_nop 0
	global_load_lds_dwordx4 v2, s[26:27]
	s_mov_b32 m0, s22
	s_nop 0
	global_load_lds_dwordx4 v3, s[26:27]
	s_waitcnt lgkmcnt(0)
	v_mfma_f32_16x16x32_f16 v[34:37], v[74:77], v[90:93], v[34:37]
	v_mfma_f32_16x16x32_f16 v[38:41], v[86:89], v[90:93], v[38:41]
	v_mfma_f32_16x16x32_f16 v[46:49], v[94:97], v[90:93], v[46:49]
	ds_read_b128 v[90:93], v6
	ds_read_b128 v[98:101], v6 offset:2048
	ds_read_b128 v[102:105], v6 offset:4096
	ds_read_b128 v[106:109], v6 offset:6144
	ds_read_b128 v[110:113], v4 offset:16384
	ds_read_b128 v[114:117], v4 offset:18432
	ds_read_b128 v[118:121], v4 offset:20480
	v_mfma_f32_16x16x32_f16 v[78:81], v[74:77], v[62:65], v[78:81]
	v_mfma_f32_16x16x32_f16 v[82:85], v[86:89], v[62:65], v[82:85]
	v_mfma_f32_16x16x32_f16 v[26:29], v[94:97], v[62:65], v[26:29]
	v_mfma_f32_16x16x32_f16 v[50:53], v[74:77], v[66:69], v[50:53]
	v_mfma_f32_16x16x32_f16 v[54:57], v[86:89], v[66:69], v[54:57]
	v_mfma_f32_16x16x32_f16 v[42:45], v[94:97], v[66:69], v[42:45]
	v_mfma_f32_16x16x32_f16 v[58:61], v[74:77], v[70:73], v[58:61]
	v_mfma_f32_16x16x32_f16 v[22:25], v[86:89], v[70:73], v[22:25]
	v_mfma_f32_16x16x32_f16 v[30:33], v[94:97], v[70:73], v[30:33]
	s_waitcnt lgkmcnt(0)
	v_mfma_f32_16x16x32_f16 v[34:37], v[110:113], v[90:93], v[34:37]
	v_mfma_f32_16x16x32_f16 v[38:41], v[114:117], v[90:93], v[38:41]
	v_mfma_f32_16x16x32_f16 v[46:49], v[118:121], v[90:93], v[46:49]
	ds_read_b128 v[62:65], v0
	ds_read_b128 v[66:69], v0 offset:2048
	ds_read_b128 v[70:73], v0 offset:4096
	ds_read_b128 v[74:77], v0 offset:6144
	ds_read_b128 v[86:89], v5 offset:16384
	ds_read_b128 v[90:93], v5 offset:18432
	ds_read_b128 v[94:97], v5 offset:20480
	v_mfma_f32_16x16x32_f16 v[78:81], v[110:113], v[98:101], v[78:81]
	v_mfma_f32_16x16x32_f16 v[82:85], v[114:117], v[98:101], v[82:85]
	v_mfma_f32_16x16x32_f16 v[26:29], v[118:121], v[98:101], v[26:29]
	v_mfma_f32_16x16x32_f16 v[50:53], v[110:113], v[102:105], v[50:53]
	v_mfma_f32_16x16x32_f16 v[54:57], v[114:117], v[102:105], v[54:57]
	v_mfma_f32_16x16x32_f16 v[42:45], v[118:121], v[102:105], v[42:45]
	v_mfma_f32_16x16x32_f16 v[58:61], v[110:113], v[106:109], v[58:61]
	v_mfma_f32_16x16x32_f16 v[22:25], v[114:117], v[106:109], v[22:25]
	v_mfma_f32_16x16x32_f16 v[30:33], v[118:121], v[106:109], v[30:33]
	s_add_u32 s24, s0, 0x480
	s_mov_b32 m0, s13
	s_waitcnt vmcnt(5) lgkmcnt(0)
	s_barrier
	s_addc_u32 s25, s1, 0
	s_add_u32 s26, s2, 0x480
	global_load_lds_dwordx4 v1, s[24:25]
	s_mov_b32 m0, s4
	s_addc_u32 s27, s3, 0
	global_load_lds_dwordx4 v2, s[24:25]
	s_mov_b32 m0, s5
	s_nop 0
	global_load_lds_dwordx4 v1, s[26:27]
	s_mov_b32 m0, s6
	s_nop 0
	global_load_lds_dwordx4 v2, s[26:27]
	s_mov_b32 m0, s7
	s_nop 0
	global_load_lds_dwordx4 v3, s[26:27]
	s_waitcnt lgkmcnt(0)
	v_mfma_f32_16x16x32_f16 v[34:37], v[86:89], v[62:65], v[34:37]
	v_mfma_f32_16x16x32_f16 v[38:41], v[90:93], v[62:65], v[38:41]
	v_mfma_f32_16x16x32_f16 v[46:49], v[94:97], v[62:65], v[46:49]
	ds_read_b128 v[62:65], v6 offset:40960
	ds_read_b128 v[98:101], v6 offset:43008
	ds_read_b128 v[102:105], v6 offset:45056
	ds_read_b128 v[106:109], v6 offset:47104
	ds_read_b128 v[110:113], v4 offset:57344
	ds_read_b128 v[114:117], v4 offset:59392
	ds_read_b128 v[118:121], v4 offset:61440
	v_mfma_f32_16x16x32_f16 v[78:81], v[86:89], v[66:69], v[78:81]
	v_mfma_f32_16x16x32_f16 v[82:85], v[90:93], v[66:69], v[82:85]
	v_mfma_f32_16x16x32_f16 v[26:29], v[94:97], v[66:69], v[26:29]
	v_mfma_f32_16x16x32_f16 v[50:53], v[86:89], v[70:73], v[50:53]
	v_mfma_f32_16x16x32_f16 v[54:57], v[90:93], v[70:73], v[54:57]
	v_mfma_f32_16x16x32_f16 v[42:45], v[94:97], v[70:73], v[42:45]
	v_mfma_f32_16x16x32_f16 v[58:61], v[86:89], v[74:77], v[58:61]
	v_mfma_f32_16x16x32_f16 v[22:25], v[90:93], v[74:77], v[22:25]
	v_mfma_f32_16x16x32_f16 v[30:33], v[94:97], v[74:77], v[30:33]
	s_waitcnt lgkmcnt(0)
	v_mfma_f32_16x16x32_f16 v[34:37], v[110:113], v[62:65], v[34:37]
	v_mfma_f32_16x16x32_f16 v[38:41], v[114:117], v[62:65], v[38:41]
	v_mfma_f32_16x16x32_f16 v[46:49], v[118:121], v[62:65], v[46:49]
	ds_read_b128 v[62:65], v0 offset:40960
	ds_read_b128 v[66:69], v0 offset:43008
	ds_read_b128 v[70:73], v0 offset:45056
	ds_read_b128 v[74:77], v0 offset:47104
	ds_read_b128 v[86:89], v5 offset:57344
	ds_read_b128 v[90:93], v5 offset:59392
	ds_read_b128 v[94:97], v5 offset:61440
	v_mfma_f32_16x16x32_f16 v[78:81], v[110:113], v[98:101], v[78:81]
	v_mfma_f32_16x16x32_f16 v[82:85], v[114:117], v[98:101], v[82:85]
	v_mfma_f32_16x16x32_f16 v[26:29], v[118:121], v[98:101], v[26:29]
	v_mfma_f32_16x16x32_f16 v[50:53], v[110:113], v[102:105], v[50:53]
	v_mfma_f32_16x16x32_f16 v[54:57], v[114:117], v[102:105], v[54:57]
	v_mfma_f32_16x16x32_f16 v[42:45], v[118:121], v[102:105], v[42:45]
	v_mfma_f32_16x16x32_f16 v[58:61], v[110:113], v[106:109], v[58:61]
	v_mfma_f32_16x16x32_f16 v[22:25], v[114:117], v[106:109], v[22:25]
	v_mfma_f32_16x16x32_f16 v[30:33], v[118:121], v[106:109], v[30:33]
	s_add_u32 s24, s0, 0x500
	s_mov_b32 m0, s18
	s_waitcnt vmcnt(5) lgkmcnt(0)
	s_barrier
	s_addc_u32 s25, s1, 0
	s_add_u32 s26, s2, 0x500
	global_load_lds_dwordx4 v1, s[24:25]
	s_mov_b32 m0, s14
	s_addc_u32 s27, s3, 0
	global_load_lds_dwordx4 v2, s[24:25]
	s_mov_b32 m0, s15
	s_nop 0
	global_load_lds_dwordx4 v1, s[26:27]
	s_mov_b32 m0, s16
	s_nop 0
	global_load_lds_dwordx4 v2, s[26:27]
	s_mov_b32 m0, s17
	s_nop 0
	global_load_lds_dwordx4 v3, s[26:27]
	s_waitcnt lgkmcnt(0)
	v_mfma_f32_16x16x32_f16 v[34:37], v[86:89], v[62:65], v[34:37]
	v_mfma_f32_16x16x32_f16 v[38:41], v[90:93], v[62:65], v[38:41]
	v_mfma_f32_16x16x32_f16 v[46:49], v[94:97], v[62:65], v[46:49]
	ds_read_b128 v[62:65], v13
	ds_read_b128 v[98:101], v14
	ds_read_b128 v[102:105], v15
	ds_read_b128 v[106:109], v16
	ds_read_b128 v[110:113], v18
	ds_read_b128 v[114:117], v19
	ds_read_b128 v[118:121], v20
	v_mfma_f32_16x16x32_f16 v[78:81], v[86:89], v[66:69], v[78:81]
	v_mfma_f32_16x16x32_f16 v[82:85], v[90:93], v[66:69], v[82:85]
	v_mfma_f32_16x16x32_f16 v[26:29], v[94:97], v[66:69], v[26:29]
	v_mfma_f32_16x16x32_f16 v[50:53], v[86:89], v[70:73], v[50:53]
	v_mfma_f32_16x16x32_f16 v[54:57], v[90:93], v[70:73], v[54:57]
	v_mfma_f32_16x16x32_f16 v[42:45], v[94:97], v[70:73], v[42:45]
	v_mfma_f32_16x16x32_f16 v[58:61], v[86:89], v[74:77], v[58:61]
	v_mfma_f32_16x16x32_f16 v[22:25], v[90:93], v[74:77], v[22:25]
	v_mfma_f32_16x16x32_f16 v[30:33], v[94:97], v[74:77], v[30:33]
	s_waitcnt lgkmcnt(0)
	v_mfma_f32_16x16x32_f16 v[34:37], v[110:113], v[62:65], v[34:37]
	v_mfma_f32_16x16x32_f16 v[38:41], v[114:117], v[62:65], v[38:41]
	v_mfma_f32_16x16x32_f16 v[46:49], v[118:121], v[62:65], v[46:49]
	ds_read_b128 v[62:65], v17 offset:2048
	ds_read_b128 v[66:69], v17 offset:4096
	ds_read_b128 v[70:73], v17 offset:6144
	ds_read_b128 v[74:77], v7 offset:16384
	ds_read_b128 v[86:89], v7 offset:18432
	ds_read_b128 v[90:93], v17
	ds_read_b128 v[94:97], v7 offset:20480
	v_mfma_f32_16x16x32_f16 v[78:81], v[110:113], v[98:101], v[78:81]
	v_mfma_f32_16x16x32_f16 v[82:85], v[114:117], v[98:101], v[82:85]
	v_mfma_f32_16x16x32_f16 v[26:29], v[118:121], v[98:101], v[26:29]
	v_mfma_f32_16x16x32_f16 v[50:53], v[110:113], v[102:105], v[50:53]
	v_mfma_f32_16x16x32_f16 v[54:57], v[114:117], v[102:105], v[54:57]
	v_mfma_f32_16x16x32_f16 v[42:45], v[118:121], v[102:105], v[42:45]
	v_mfma_f32_16x16x32_f16 v[58:61], v[110:113], v[106:109], v[58:61]
	v_mfma_f32_16x16x32_f16 v[22:25], v[114:117], v[106:109], v[22:25]
	v_mfma_f32_16x16x32_f16 v[30:33], v[118:121], v[106:109], v[30:33]
	s_add_u32 s24, s0, 0x580
	s_mov_b32 m0, s23
	s_waitcnt vmcnt(5) lgkmcnt(0)
	s_barrier
	s_addc_u32 s25, s1, 0
	s_add_u32 s26, s2, 0x580
	global_load_lds_dwordx4 v1, s[24:25]
	s_mov_b32 m0, s19
	s_addc_u32 s27, s3, 0
	global_load_lds_dwordx4 v2, s[24:25]
	s_mov_b32 m0, s20
	s_nop 0
	global_load_lds_dwordx4 v1, s[26:27]
	s_mov_b32 m0, s21
	s_nop 0
	global_load_lds_dwordx4 v2, s[26:27]
	s_mov_b32 m0, s22
	s_nop 0
	global_load_lds_dwordx4 v3, s[26:27]
	s_waitcnt lgkmcnt(0)
	v_mfma_f32_16x16x32_f16 v[34:37], v[74:77], v[90:93], v[34:37]
	v_mfma_f32_16x16x32_f16 v[38:41], v[86:89], v[90:93], v[38:41]
	v_mfma_f32_16x16x32_f16 v[46:49], v[94:97], v[90:93], v[46:49]
	ds_read_b128 v[90:93], v6
	ds_read_b128 v[98:101], v6 offset:2048
	ds_read_b128 v[102:105], v6 offset:4096
	ds_read_b128 v[106:109], v6 offset:6144
	ds_read_b128 v[110:113], v4 offset:16384
	ds_read_b128 v[114:117], v4 offset:18432
	ds_read_b128 v[118:121], v4 offset:20480
	v_mfma_f32_16x16x32_f16 v[78:81], v[74:77], v[62:65], v[78:81]
	v_mfma_f32_16x16x32_f16 v[82:85], v[86:89], v[62:65], v[82:85]
	v_mfma_f32_16x16x32_f16 v[26:29], v[94:97], v[62:65], v[26:29]
	v_mfma_f32_16x16x32_f16 v[50:53], v[74:77], v[66:69], v[50:53]
	v_mfma_f32_16x16x32_f16 v[54:57], v[86:89], v[66:69], v[54:57]
	v_mfma_f32_16x16x32_f16 v[42:45], v[94:97], v[66:69], v[42:45]
	v_mfma_f32_16x16x32_f16 v[58:61], v[74:77], v[70:73], v[58:61]
	v_mfma_f32_16x16x32_f16 v[22:25], v[86:89], v[70:73], v[22:25]
	v_mfma_f32_16x16x32_f16 v[30:33], v[94:97], v[70:73], v[30:33]
	s_waitcnt lgkmcnt(0)
	v_mfma_f32_16x16x32_f16 v[34:37], v[110:113], v[90:93], v[34:37]
	v_mfma_f32_16x16x32_f16 v[38:41], v[114:117], v[90:93], v[38:41]
	v_mfma_f32_16x16x32_f16 v[46:49], v[118:121], v[90:93], v[46:49]
	ds_read_b128 v[62:65], v0
	ds_read_b128 v[66:69], v0 offset:2048
	ds_read_b128 v[70:73], v0 offset:4096
	ds_read_b128 v[74:77], v0 offset:6144
	ds_read_b128 v[86:89], v5 offset:16384
	ds_read_b128 v[90:93], v5 offset:18432
	ds_read_b128 v[94:97], v5 offset:20480
	v_mfma_f32_16x16x32_f16 v[78:81], v[110:113], v[98:101], v[78:81]
	v_mfma_f32_16x16x32_f16 v[82:85], v[114:117], v[98:101], v[82:85]
	v_mfma_f32_16x16x32_f16 v[26:29], v[118:121], v[98:101], v[26:29]
	v_mfma_f32_16x16x32_f16 v[50:53], v[110:113], v[102:105], v[50:53]
	v_mfma_f32_16x16x32_f16 v[54:57], v[114:117], v[102:105], v[54:57]
	v_mfma_f32_16x16x32_f16 v[42:45], v[118:121], v[102:105], v[42:45]
	v_mfma_f32_16x16x32_f16 v[58:61], v[110:113], v[106:109], v[58:61]
	v_mfma_f32_16x16x32_f16 v[22:25], v[114:117], v[106:109], v[22:25]
	v_mfma_f32_16x16x32_f16 v[30:33], v[118:121], v[106:109], v[30:33]
	s_add_u32 s24, s0, 0x600
	s_mov_b32 m0, s13
	s_waitcnt vmcnt(5) lgkmcnt(0)
	s_barrier
	s_addc_u32 s25, s1, 0
	s_add_u32 s26, s2, 0x600
	global_load_lds_dwordx4 v1, s[24:25]
	s_mov_b32 m0, s4
	s_addc_u32 s27, s3, 0
	global_load_lds_dwordx4 v2, s[24:25]
	s_mov_b32 m0, s5
	s_nop 0
	global_load_lds_dwordx4 v1, s[26:27]
	s_mov_b32 m0, s6
	s_nop 0
	global_load_lds_dwordx4 v2, s[26:27]
	s_mov_b32 m0, s7
	s_nop 0
	global_load_lds_dwordx4 v3, s[26:27]
	s_waitcnt lgkmcnt(0)
	v_mfma_f32_16x16x32_f16 v[34:37], v[86:89], v[62:65], v[34:37]
	v_mfma_f32_16x16x32_f16 v[38:41], v[90:93], v[62:65], v[38:41]
	v_mfma_f32_16x16x32_f16 v[46:49], v[94:97], v[62:65], v[46:49]
	ds_read_b128 v[62:65], v6 offset:40960
	ds_read_b128 v[98:101], v6 offset:43008
	ds_read_b128 v[102:105], v6 offset:45056
	ds_read_b128 v[106:109], v6 offset:47104
	ds_read_b128 v[110:113], v4 offset:57344
	ds_read_b128 v[114:117], v4 offset:59392
	ds_read_b128 v[118:121], v4 offset:61440
	v_mfma_f32_16x16x32_f16 v[78:81], v[86:89], v[66:69], v[78:81]
	v_mfma_f32_16x16x32_f16 v[82:85], v[90:93], v[66:69], v[82:85]
	v_mfma_f32_16x16x32_f16 v[26:29], v[94:97], v[66:69], v[26:29]
	v_mfma_f32_16x16x32_f16 v[50:53], v[86:89], v[70:73], v[50:53]
	v_mfma_f32_16x16x32_f16 v[54:57], v[90:93], v[70:73], v[54:57]
	v_mfma_f32_16x16x32_f16 v[42:45], v[94:97], v[70:73], v[42:45]
	v_mfma_f32_16x16x32_f16 v[58:61], v[86:89], v[74:77], v[58:61]
	v_mfma_f32_16x16x32_f16 v[22:25], v[90:93], v[74:77], v[22:25]
	v_mfma_f32_16x16x32_f16 v[30:33], v[94:97], v[74:77], v[30:33]
	s_waitcnt lgkmcnt(0)
	v_mfma_f32_16x16x32_f16 v[34:37], v[110:113], v[62:65], v[34:37]
	v_mfma_f32_16x16x32_f16 v[38:41], v[114:117], v[62:65], v[38:41]
	v_mfma_f32_16x16x32_f16 v[46:49], v[118:121], v[62:65], v[46:49]
	ds_read_b128 v[62:65], v0 offset:40960
	ds_read_b128 v[66:69], v0 offset:43008
	ds_read_b128 v[70:73], v0 offset:45056
	ds_read_b128 v[74:77], v0 offset:47104
	ds_read_b128 v[86:89], v5 offset:57344
	ds_read_b128 v[90:93], v5 offset:59392
	ds_read_b128 v[94:97], v5 offset:61440
	v_mfma_f32_16x16x32_f16 v[78:81], v[110:113], v[98:101], v[78:81]
	v_mfma_f32_16x16x32_f16 v[82:85], v[114:117], v[98:101], v[82:85]
	v_mfma_f32_16x16x32_f16 v[26:29], v[118:121], v[98:101], v[26:29]
	v_mfma_f32_16x16x32_f16 v[50:53], v[110:113], v[102:105], v[50:53]
	v_mfma_f32_16x16x32_f16 v[54:57], v[114:117], v[102:105], v[54:57]
	v_mfma_f32_16x16x32_f16 v[42:45], v[118:121], v[102:105], v[42:45]
	v_mfma_f32_16x16x32_f16 v[58:61], v[110:113], v[106:109], v[58:61]
	v_mfma_f32_16x16x32_f16 v[22:25], v[114:117], v[106:109], v[22:25]
	v_mfma_f32_16x16x32_f16 v[30:33], v[118:121], v[106:109], v[30:33]
	s_add_u32 s24, s0, 0x680
	s_mov_b32 m0, s18
	s_waitcnt vmcnt(5) lgkmcnt(0)
	s_barrier
	s_addc_u32 s25, s1, 0
	s_add_u32 s26, s2, 0x680
	global_load_lds_dwordx4 v1, s[24:25]
	s_mov_b32 m0, s14
	s_addc_u32 s27, s3, 0
	global_load_lds_dwordx4 v2, s[24:25]
	s_mov_b32 m0, s15
	s_nop 0
	global_load_lds_dwordx4 v1, s[26:27]
	s_mov_b32 m0, s16
	s_nop 0
	global_load_lds_dwordx4 v2, s[26:27]
	s_mov_b32 m0, s17
	s_nop 0
	global_load_lds_dwordx4 v3, s[26:27]
	s_waitcnt lgkmcnt(0)
	v_mfma_f32_16x16x32_f16 v[34:37], v[86:89], v[62:65], v[34:37]
	v_mfma_f32_16x16x32_f16 v[38:41], v[90:93], v[62:65], v[38:41]
	v_mfma_f32_16x16x32_f16 v[46:49], v[94:97], v[62:65], v[46:49]
	ds_read_b128 v[62:65], v13
	ds_read_b128 v[98:101], v14
	ds_read_b128 v[102:105], v15
	ds_read_b128 v[106:109], v16
	ds_read_b128 v[110:113], v18
	ds_read_b128 v[114:117], v19
	ds_read_b128 v[118:121], v20
	v_mfma_f32_16x16x32_f16 v[78:81], v[86:89], v[66:69], v[78:81]
	v_mfma_f32_16x16x32_f16 v[82:85], v[90:93], v[66:69], v[82:85]
	v_mfma_f32_16x16x32_f16 v[26:29], v[94:97], v[66:69], v[26:29]
	v_mfma_f32_16x16x32_f16 v[50:53], v[86:89], v[70:73], v[50:53]
	v_mfma_f32_16x16x32_f16 v[54:57], v[90:93], v[70:73], v[54:57]
	v_mfma_f32_16x16x32_f16 v[42:45], v[94:97], v[70:73], v[42:45]
	v_mfma_f32_16x16x32_f16 v[58:61], v[86:89], v[74:77], v[58:61]
	v_mfma_f32_16x16x32_f16 v[22:25], v[90:93], v[74:77], v[22:25]
	v_mfma_f32_16x16x32_f16 v[30:33], v[94:97], v[74:77], v[30:33]
	s_waitcnt lgkmcnt(0)
	v_mfma_f32_16x16x32_f16 v[34:37], v[110:113], v[62:65], v[34:37]
	v_mfma_f32_16x16x32_f16 v[38:41], v[114:117], v[62:65], v[38:41]
	v_mfma_f32_16x16x32_f16 v[46:49], v[118:121], v[62:65], v[46:49]
	ds_read_b128 v[62:65], v17 offset:2048
	ds_read_b128 v[66:69], v17 offset:4096
	ds_read_b128 v[70:73], v17 offset:6144
	ds_read_b128 v[74:77], v7 offset:16384
	ds_read_b128 v[86:89], v7 offset:18432
	ds_read_b128 v[90:93], v17
	ds_read_b128 v[94:97], v7 offset:20480
	v_mfma_f32_16x16x32_f16 v[78:81], v[110:113], v[98:101], v[78:81]
	v_mfma_f32_16x16x32_f16 v[82:85], v[114:117], v[98:101], v[82:85]
	v_mfma_f32_16x16x32_f16 v[26:29], v[118:121], v[98:101], v[26:29]
	v_mfma_f32_16x16x32_f16 v[50:53], v[110:113], v[102:105], v[50:53]
	v_mfma_f32_16x16x32_f16 v[54:57], v[114:117], v[102:105], v[54:57]
	v_mfma_f32_16x16x32_f16 v[42:45], v[118:121], v[102:105], v[42:45]
	v_mfma_f32_16x16x32_f16 v[58:61], v[110:113], v[106:109], v[58:61]
	v_mfma_f32_16x16x32_f16 v[22:25], v[114:117], v[106:109], v[22:25]
	v_mfma_f32_16x16x32_f16 v[30:33], v[118:121], v[106:109], v[30:33]
	s_add_u32 s14, s0, 0x700
	s_mov_b32 m0, s23
	s_waitcnt vmcnt(5) lgkmcnt(0)
	s_barrier
	s_addc_u32 s15, s1, 0
	s_add_u32 s16, s2, 0x700
	global_load_lds_dwordx4 v1, s[14:15]
	s_mov_b32 m0, s19
	s_addc_u32 s17, s3, 0
	global_load_lds_dwordx4 v2, s[14:15]
	s_mov_b32 m0, s20
	s_nop 0
	global_load_lds_dwordx4 v1, s[16:17]
	s_mov_b32 m0, s21
	s_nop 0
	global_load_lds_dwordx4 v2, s[16:17]
	s_mov_b32 m0, s22
	s_nop 0
	global_load_lds_dwordx4 v3, s[16:17]
	s_waitcnt lgkmcnt(0)
	v_mfma_f32_16x16x32_f16 v[34:37], v[74:77], v[90:93], v[34:37]
	v_mfma_f32_16x16x32_f16 v[38:41], v[86:89], v[90:93], v[38:41]
	v_mfma_f32_16x16x32_f16 v[46:49], v[94:97], v[90:93], v[46:49]
	ds_read_b128 v[90:93], v6
	ds_read_b128 v[98:101], v6 offset:2048
	ds_read_b128 v[102:105], v6 offset:4096
	ds_read_b128 v[106:109], v6 offset:6144
	ds_read_b128 v[110:113], v4 offset:16384
	ds_read_b128 v[114:117], v4 offset:18432
	ds_read_b128 v[118:121], v4 offset:20480
	v_mfma_f32_16x16x32_f16 v[78:81], v[74:77], v[62:65], v[78:81]
	v_mfma_f32_16x16x32_f16 v[82:85], v[86:89], v[62:65], v[82:85]
	v_mfma_f32_16x16x32_f16 v[26:29], v[94:97], v[62:65], v[26:29]
	v_mfma_f32_16x16x32_f16 v[50:53], v[74:77], v[66:69], v[50:53]
	v_mfma_f32_16x16x32_f16 v[54:57], v[86:89], v[66:69], v[54:57]
	v_mfma_f32_16x16x32_f16 v[42:45], v[94:97], v[66:69], v[42:45]
	v_mfma_f32_16x16x32_f16 v[58:61], v[74:77], v[70:73], v[58:61]
	v_mfma_f32_16x16x32_f16 v[22:25], v[86:89], v[70:73], v[22:25]
	v_mfma_f32_16x16x32_f16 v[30:33], v[94:97], v[70:73], v[30:33]
	s_waitcnt lgkmcnt(0)
	v_mfma_f32_16x16x32_f16 v[34:37], v[110:113], v[90:93], v[34:37]
	v_mfma_f32_16x16x32_f16 v[38:41], v[114:117], v[90:93], v[38:41]
	v_mfma_f32_16x16x32_f16 v[46:49], v[118:121], v[90:93], v[46:49]
	ds_read_b128 v[62:65], v0
	ds_read_b128 v[66:69], v0 offset:2048
	ds_read_b128 v[70:73], v0 offset:4096
	ds_read_b128 v[74:77], v0 offset:6144
	ds_read_b128 v[86:89], v5 offset:16384
	ds_read_b128 v[90:93], v5 offset:18432
	ds_read_b128 v[94:97], v5 offset:20480
	v_mfma_f32_16x16x32_f16 v[78:81], v[110:113], v[98:101], v[78:81]
	v_mfma_f32_16x16x32_f16 v[82:85], v[114:117], v[98:101], v[82:85]
	v_mfma_f32_16x16x32_f16 v[26:29], v[118:121], v[98:101], v[26:29]
	v_mfma_f32_16x16x32_f16 v[50:53], v[110:113], v[102:105], v[50:53]
	v_mfma_f32_16x16x32_f16 v[54:57], v[114:117], v[102:105], v[54:57]
	v_mfma_f32_16x16x32_f16 v[42:45], v[118:121], v[102:105], v[42:45]
	v_mfma_f32_16x16x32_f16 v[58:61], v[110:113], v[106:109], v[58:61]
	v_mfma_f32_16x16x32_f16 v[22:25], v[114:117], v[106:109], v[22:25]
	v_mfma_f32_16x16x32_f16 v[30:33], v[118:121], v[106:109], v[30:33]
	s_add_u32 s0, s0, 0x780
	s_mov_b32 m0, s13
	s_waitcnt vmcnt(5) lgkmcnt(0)
	s_barrier
	s_addc_u32 s1, s1, 0
	s_add_u32 s2, s2, 0x780
	global_load_lds_dwordx4 v1, s[0:1]
	s_mov_b32 m0, s4
	s_addc_u32 s3, s3, 0
	global_load_lds_dwordx4 v2, s[0:1]
	s_mov_b32 m0, s5
	s_nop 0
	global_load_lds_dwordx4 v1, s[2:3]
	s_mov_b32 m0, s6
	s_nop 0
	global_load_lds_dwordx4 v2, s[2:3]
	s_mov_b32 m0, s7
	s_nop 0
	global_load_lds_dwordx4 v3, s[2:3]
	s_waitcnt lgkmcnt(0)
	v_mfma_f32_16x16x32_f16 v[34:37], v[86:89], v[62:65], v[34:37]
	v_mfma_f32_16x16x32_f16 v[38:41], v[90:93], v[62:65], v[38:41]
	v_mfma_f32_16x16x32_f16 v[46:49], v[94:97], v[62:65], v[46:49]
	ds_read_b128 v[62:65], v6 offset:40960
	ds_read_b128 v[98:101], v6 offset:43008
	ds_read_b128 v[102:105], v6 offset:45056
	ds_read_b128 v[106:109], v6 offset:47104
	ds_read_b128 v[110:113], v4 offset:57344
	ds_read_b128 v[114:117], v4 offset:59392
	ds_read_b128 v[118:121], v4 offset:61440
	v_mfma_f32_16x16x32_f16 v[78:81], v[86:89], v[66:69], v[78:81]
	v_mfma_f32_16x16x32_f16 v[82:85], v[90:93], v[66:69], v[82:85]
	v_mfma_f32_16x16x32_f16 v[26:29], v[94:97], v[66:69], v[26:29]
	v_mfma_f32_16x16x32_f16 v[50:53], v[86:89], v[70:73], v[50:53]
	v_mfma_f32_16x16x32_f16 v[54:57], v[90:93], v[70:73], v[54:57]
	v_mfma_f32_16x16x32_f16 v[42:45], v[94:97], v[70:73], v[42:45]
	v_mfma_f32_16x16x32_f16 v[58:61], v[86:89], v[74:77], v[58:61]
	v_mfma_f32_16x16x32_f16 v[22:25], v[90:93], v[74:77], v[22:25]
	v_mfma_f32_16x16x32_f16 v[30:33], v[94:97], v[74:77], v[30:33]
	s_waitcnt lgkmcnt(0)
	v_mfma_f32_16x16x32_f16 v[34:37], v[110:113], v[62:65], v[34:37]
	v_mfma_f32_16x16x32_f16 v[38:41], v[114:117], v[62:65], v[38:41]
	v_mfma_f32_16x16x32_f16 v[46:49], v[118:121], v[62:65], v[46:49]
	ds_read_b128 v[62:65], v0 offset:40960
	ds_read_b128 v[66:69], v0 offset:43008
	ds_read_b128 v[70:73], v0 offset:45056
	ds_read_b128 v[74:77], v0 offset:47104
	ds_read_b128 v[86:89], v5 offset:57344
	ds_read_b128 v[90:93], v5 offset:59392
	ds_read_b128 v[94:97], v5 offset:61440
	v_mfma_f32_16x16x32_f16 v[78:81], v[110:113], v[98:101], v[78:81]
	v_mfma_f32_16x16x32_f16 v[82:85], v[114:117], v[98:101], v[82:85]
	v_mfma_f32_16x16x32_f16 v[26:29], v[118:121], v[98:101], v[26:29]
	v_mfma_f32_16x16x32_f16 v[50:53], v[110:113], v[102:105], v[50:53]
	v_mfma_f32_16x16x32_f16 v[54:57], v[114:117], v[102:105], v[54:57]
	v_mfma_f32_16x16x32_f16 v[42:45], v[118:121], v[102:105], v[42:45]
	v_mfma_f32_16x16x32_f16 v[58:61], v[110:113], v[106:109], v[58:61]
	v_mfma_f32_16x16x32_f16 v[22:25], v[114:117], v[106:109], v[22:25]
	v_mfma_f32_16x16x32_f16 v[30:33], v[118:121], v[106:109], v[30:33]
	s_waitcnt vmcnt(5) lgkmcnt(0)
	s_barrier
	s_waitcnt lgkmcnt(0)
	v_mfma_f32_16x16x32_f16 v[34:37], v[86:89], v[62:65], v[34:37]
	v_mfma_f32_16x16x32_f16 v[38:41], v[90:93], v[62:65], v[38:41]
	v_mfma_f32_16x16x32_f16 v[46:49], v[94:97], v[62:65], v[46:49]
	ds_read_b128 v[62:65], v13
	ds_read_b128 v[98:101], v14
	ds_read_b128 v[102:105], v15
	ds_read_b128 v[106:109], v16
	ds_read_b128 v[110:113], v18
	ds_read_b128 v[114:117], v19
	ds_read_b128 v[18:21], v20
	v_mfma_f32_16x16x32_f16 v[78:81], v[86:89], v[66:69], v[78:81]
	v_mfma_f32_16x16x32_f16 v[82:85], v[90:93], v[66:69], v[82:85]
	v_mfma_f32_16x16x32_f16 v[26:29], v[94:97], v[66:69], v[26:29]
	v_mfma_f32_16x16x32_f16 v[50:53], v[86:89], v[70:73], v[50:53]
	v_mfma_f32_16x16x32_f16 v[54:57], v[90:93], v[70:73], v[54:57]
	v_mfma_f32_16x16x32_f16 v[42:45], v[94:97], v[70:73], v[42:45]
	v_mfma_f32_16x16x32_f16 v[58:61], v[86:89], v[74:77], v[58:61]
	v_mfma_f32_16x16x32_f16 v[22:25], v[90:93], v[74:77], v[22:25]
	v_mfma_f32_16x16x32_f16 v[30:33], v[94:97], v[74:77], v[30:33]
	s_waitcnt lgkmcnt(0)
	v_mfma_f32_16x16x32_f16 v[34:37], v[110:113], v[62:65], v[34:37]
	v_mfma_f32_16x16x32_f16 v[38:41], v[114:117], v[62:65], v[38:41]
	v_mfma_f32_16x16x32_f16 v[46:49], v[18:21], v[62:65], v[46:49]
	ds_read_b128 v[62:65], v17 offset:2048
	ds_read_b128 v[66:69], v17 offset:4096
	ds_read_b128 v[70:73], v17 offset:6144
	ds_read_b128 v[74:77], v7 offset:16384
	ds_read_b128 v[86:89], v7 offset:18432
	ds_read_b128 v[14:17], v17
	ds_read_b128 v[90:93], v7 offset:20480
	v_mfma_f32_16x16x32_f16 v[78:81], v[110:113], v[98:101], v[78:81]
	v_mfma_f32_16x16x32_f16 v[82:85], v[114:117], v[98:101], v[82:85]
	v_mfma_f32_16x16x32_f16 v[26:29], v[18:21], v[98:101], v[26:29]
	v_mfma_f32_16x16x32_f16 v[50:53], v[110:113], v[102:105], v[50:53]
	v_mfma_f32_16x16x32_f16 v[54:57], v[114:117], v[102:105], v[54:57]
	v_mfma_f32_16x16x32_f16 v[42:45], v[18:21], v[102:105], v[42:45]
	v_mfma_f32_16x16x32_f16 v[58:61], v[110:113], v[106:109], v[58:61]
	v_mfma_f32_16x16x32_f16 v[22:25], v[114:117], v[106:109], v[22:25]
	v_mfma_f32_16x16x32_f16 v[18:21], v[18:21], v[106:109], v[30:33]
	s_waitcnt vmcnt(0) lgkmcnt(0)
	s_barrier
	s_waitcnt lgkmcnt(0)
	v_mfma_f32_16x16x32_f16 v[30:33], v[74:77], v[14:17], v[34:37]
	v_mfma_f32_16x16x32_f16 v[34:37], v[86:89], v[14:17], v[38:41]
	v_mfma_f32_16x16x32_f16 v[14:17], v[90:93], v[14:17], v[46:49]
	s_nop 1
	ds_read_b128 v[38:41], v6
	ds_read_b128 v[46:49], v6 offset:2048
	ds_read_b128 v[94:97], v6 offset:4096
	ds_read_b128 v[98:101], v6 offset:6144
	ds_read_b128 v[102:105], v4 offset:16384
	ds_read_b128 v[106:109], v4 offset:18432
	ds_read_b128 v[110:113], v4 offset:20480
	v_mfma_f32_16x16x32_f16 v[78:81], v[74:77], v[62:65], v[78:81]
	v_mfma_f32_16x16x32_f16 v[82:85], v[86:89], v[62:65], v[82:85]
	v_mfma_f32_16x16x32_f16 v[26:29], v[90:93], v[62:65], v[26:29]
	v_mfma_f32_16x16x32_f16 v[50:53], v[74:77], v[66:69], v[50:53]
	v_mfma_f32_16x16x32_f16 v[54:57], v[86:89], v[66:69], v[54:57]
	v_mfma_f32_16x16x32_f16 v[42:45], v[90:93], v[66:69], v[42:45]
	v_mfma_f32_16x16x32_f16 v[58:61], v[74:77], v[70:73], v[58:61]
	v_mfma_f32_16x16x32_f16 v[22:25], v[86:89], v[70:73], v[22:25]
	v_mfma_f32_16x16x32_f16 v[18:21], v[90:93], v[70:73], v[18:21]
	s_waitcnt lgkmcnt(0)
	v_mfma_f32_16x16x32_f16 v[30:33], v[102:105], v[38:41], v[30:33]
	v_mfma_f32_16x16x32_f16 v[34:37], v[106:109], v[38:41], v[34:37]
	v_mfma_f32_16x16x32_f16 v[14:17], v[110:113], v[38:41], v[14:17]
	ds_read_b128 v[38:41], v0
	ds_read_b128 v[62:65], v0 offset:2048
	ds_read_b128 v[66:69], v0 offset:4096
	ds_read_b128 v[0:3], v0 offset:6144
	ds_read_b128 v[70:73], v5 offset:16384
	ds_read_b128 v[74:77], v5 offset:18432
	ds_read_b128 v[86:89], v5 offset:20480
	v_mfma_f32_16x16x32_f16 v[4:7], v[102:105], v[46:49], v[78:81]
	v_mfma_f32_16x16x32_f16 v[78:81], v[106:109], v[46:49], v[82:85]
	v_mfma_f32_16x16x32_f16 v[26:29], v[110:113], v[46:49], v[26:29]
	v_mfma_f32_16x16x32_f16 v[46:49], v[102:105], v[94:97], v[50:53]
	v_mfma_f32_16x16x32_f16 v[50:53], v[106:109], v[94:97], v[54:57]
	v_mfma_f32_16x16x32_f16 v[42:45], v[110:113], v[94:97], v[42:45]
	v_mfma_f32_16x16x32_f16 v[54:57], v[102:105], v[98:101], v[58:61]
	v_mfma_f32_16x16x32_f16 v[22:25], v[106:109], v[98:101], v[22:25]
	v_mfma_f32_16x16x32_f16 v[18:21], v[110:113], v[98:101], v[18:21]
	s_waitcnt lgkmcnt(0)
	v_mfma_f32_16x16x32_f16 v[30:33], v[70:73], v[38:41], v[30:33]
	v_mfma_f32_16x16x32_f16 v[34:37], v[74:77], v[38:41], v[34:37]
	v_mfma_f32_16x16x32_f16 v[14:17], v[86:89], v[38:41], v[14:17]
	v_mfma_f32_16x16x32_f16 v[38:41], v[70:73], v[62:65], v[4:7]
	v_mfma_f32_16x16x32_f16 v[58:61], v[74:77], v[62:65], v[78:81]
	v_mfma_f32_16x16x32_f16 v[26:29], v[86:89], v[62:65], v[26:29]
	v_mfma_f32_16x16x32_f16 v[46:49], v[70:73], v[66:69], v[46:49]
	v_mfma_f32_16x16x32_f16 v[50:53], v[74:77], v[66:69], v[50:53]
	v_mfma_f32_16x16x32_f16 v[42:45], v[86:89], v[66:69], v[42:45]
	v_mfma_f32_16x16x32_f16 v[54:57], v[70:73], v[0:3], v[54:57]
	v_mfma_f32_16x16x32_f16 v[4:7], v[74:77], v[0:3], v[22:25]
	v_mfma_f32_16x16x32_f16 v[0:3], v[86:89], v[0:3], v[18:21]
	s_lshl_b32 s0, s12, 1
	v_or_b32_e32 v11, s10, v11
	s_and_b32 s5, s0, 0x3fffff0
	s_movk_i32 s0, 0x3c0
	v_mad_u32_u24 v62, v9, 48, s11
	v_lshlrev_b32_e32 v24, 2, v12
	v_and_or_b32 v63, v11, s0, v8
	s_movk_i32 s0, 0x400
	s_mov_b32 s4, 0x3e38aa3b
	v_and_or_b32 v20, v10, 48, v24
	v_pk_mul_f32 v[10:11], v[32:33], s[4:5] op_sel_hi:[1,0]
	v_cmp_gt_u32_e32 vcc, s0, v62
	v_pk_mul_f32 v[12:13], v[30:31], s[4:5] op_sel_hi:[1,0]
	v_lshrrev_b32_e32 v8, 10, v62
	v_cndmask_b32_e32 v9, v33, v11, vcc
	v_cndmask_b32_e32 v11, v32, v10, vcc
	v_lshrrev_b32_e32 v18, 6, v62
	v_cndmask_b32_e32 v10, v31, v13, vcc
	v_cndmask_b32_e32 v12, v30, v12, vcc
	v_cvt_pk_f16_f32 v11, v11, v9
	v_mov_b32_e32 v9, 0
	v_cvt_pk_f16_f32 v10, v12, v10
	v_lshlrev_b64 v[12:13], 22, v[8:9]
	v_and_or_b32 v8, v18, 15, s5
	v_lshlrev_b32_e32 v30, 10, v8
	v_or_b32_e32 v8, v30, v63
	v_lshl_add_u64 v[12:13], s[8:9], 0, v[12:13]
	v_lshlrev_b64 v[18:19], 7, v[8:9]
	v_lshl_add_u64 v[18:19], v[12:13], 0, v[18:19]
	v_lshlrev_b32_e32 v8, 1, v20
	v_lshl_add_u64 v[18:19], v[18:19], 0, v[8:9]
	s_movk_i32 s0, 0x3f0
	global_store_dwordx2 v[18:19], v[10:11], off
	v_add_u32_e32 v11, 16, v62
	v_pk_mul_f32 v[18:19], v[36:37], s[4:5] op_sel_hi:[1,0]
	v_pk_mul_f32 v[20:21], v[34:35], s[4:5] op_sel_hi:[1,0]
	v_cmp_gt_u32_e64 s[0:1], s0, v62
	v_lshrrev_b32_e32 v10, 10, v11
	v_and_or_b32 v23, v11, 48, v24
	v_cndmask_b32_e64 v22, v36, v18, s[0:1]
	v_cndmask_b32_e64 v18, v35, v21, s[0:1]
	v_cndmask_b32_e64 v20, v34, v20, s[0:1]
	v_lshrrev_b32_e32 v21, 6, v11
	v_cvt_pk_f16_f32 v18, v20, v18
	v_and_or_b32 v20, v21, 15, s5
	v_mov_b32_e32 v11, v9
	v_lshlrev_b32_e32 v31, 10, v20
	v_lshlrev_b64 v[10:11], 22, v[10:11]
	v_or_b32_e32 v20, v31, v63
	v_mov_b32_e32 v21, v9
	v_cndmask_b32_e64 v19, v37, v19, s[0:1]
	v_lshl_add_u64 v[10:11], s[8:9], 0, v[10:11]
	v_lshlrev_b64 v[20:21], 7, v[20:21]
	v_cvt_pk_f16_f32 v19, v22, v19
	v_lshl_add_u64 v[20:21], v[10:11], 0, v[20:21]
	v_lshlrev_b32_e32 v22, 1, v23
	v_mov_b32_e32 v23, v9
	v_lshl_add_u64 v[20:21], v[20:21], 0, v[22:23]
	global_store_dwordx2 v[20:21], v[18:19], off
	v_add_u32_e32 v19, 32, v62
	s_movk_i32 s2, 0x3e0
	v_and_or_b32 v33, v19, 48, v24
	v_pk_mul_f32 v[20:21], v[16:17], s[4:5] op_sel_hi:[1,0]
	v_pk_mul_f32 v[24:25], v[14:15], s[4:5] op_sel_hi:[1,0]
	v_cmp_gt_u32_e64 s[2:3], s2, v62
	v_lshrrev_b32_e32 v18, 10, v19
	v_lshrrev_b32_e32 v32, 6, v19
	v_cndmask_b32_e64 v17, v17, v21, s[2:3]
	v_cndmask_b32_e64 v16, v16, v20, s[2:3]
	v_cndmask_b32_e64 v15, v15, v25, s[2:3]
	v_cndmask_b32_e64 v14, v14, v24, s[2:3]
	v_mov_b32_e32 v19, v9
	v_cvt_pk_f16_f32 v14, v14, v15
	v_cvt_pk_f16_f32 v15, v16, v17
	v_lshlrev_b64 v[16:17], 22, v[18:19]
	v_and_or_b32 v18, v32, 15, s5
	v_lshlrev_b32_e32 v24, 10, v18
	v_or_b32_e32 v18, v24, v63
	v_lshl_add_u64 v[16:17], s[8:9], 0, v[16:17]
	v_lshlrev_b64 v[18:19], 7, v[18:19]
	v_lshl_add_u64 v[18:19], v[16:17], 0, v[18:19]
	v_lshlrev_b32_e32 v20, 1, v33
	v_mov_b32_e32 v21, v9
	v_lshl_add_u64 v[18:19], v[18:19], 0, v[20:21]
	global_store_dwordx2 v[18:19], v[14:15], off
	v_pk_mul_f32 v[14:15], v[40:41], s[4:5] op_sel_hi:[1,0]
	v_pk_mul_f32 v[18:19], v[38:39], s[4:5] op_sel_hi:[1,0]
	v_or_b32_e32 v25, 16, v63
	v_cndmask_b32_e32 v32, v40, v14, vcc
	v_cndmask_b32_e32 v14, v39, v19, vcc
	v_cndmask_b32_e32 v18, v38, v18, vcc
	v_cvt_pk_f16_f32 v14, v18, v14
	v_or_b32_e32 v18, v30, v25
	v_mov_b32_e32 v19, v9
	v_lshlrev_b64 v[18:19], 7, v[18:19]
	v_cndmask_b32_e32 v15, v41, v15, vcc
	v_lshl_add_u64 v[18:19], v[12:13], 0, v[18:19]
	v_cvt_pk_f16_f32 v15, v32, v15
	v_lshl_add_u64 v[18:19], v[18:19], 0, v[8:9]
	global_store_dwordx2 v[18:19], v[14:15], off
	v_pk_mul_f32 v[14:15], v[60:61], s[4:5] op_sel_hi:[1,0]
	v_pk_mul_f32 v[18:19], v[58:59], s[4:5] op_sel_hi:[1,0]
	v_cndmask_b32_e64 v32, v60, v14, s[0:1]
	v_cndmask_b32_e64 v14, v59, v19, s[0:1]
	v_cndmask_b32_e64 v18, v58, v18, s[0:1]
	v_cvt_pk_f16_f32 v14, v18, v14
	v_or_b32_e32 v18, v31, v25
	v_mov_b32_e32 v19, v9
	v_lshlrev_b64 v[18:19], 7, v[18:19]
	v_cndmask_b32_e64 v15, v61, v15, s[0:1]
	v_lshl_add_u64 v[18:19], v[10:11], 0, v[18:19]
	v_cvt_pk_f16_f32 v15, v32, v15
	v_lshl_add_u64 v[18:19], v[18:19], 0, v[22:23]
	global_store_dwordx2 v[18:19], v[14:15], off
	v_pk_mul_f32 v[14:15], v[28:29], s[4:5] op_sel_hi:[1,0]
	v_pk_mul_f32 v[18:19], v[26:27], s[4:5] op_sel_hi:[1,0]
	v_cndmask_b32_e64 v28, v28, v14, s[2:3]
	v_cndmask_b32_e64 v14, v27, v19, s[2:3]
	v_cndmask_b32_e64 v18, v26, v18, s[2:3]
	v_cvt_pk_f16_f32 v14, v18, v14
	v_or_b32_e32 v18, v24, v25
	v_mov_b32_e32 v19, v9
	v_lshlrev_b64 v[18:19], 7, v[18:19]
	v_cndmask_b32_e64 v15, v29, v15, s[2:3]
	v_lshl_add_u64 v[18:19], v[16:17], 0, v[18:19]
	v_cvt_pk_f16_f32 v15, v28, v15
	v_lshl_add_u64 v[18:19], v[18:19], 0, v[20:21]
	global_store_dwordx2 v[18:19], v[14:15], off
	v_pk_mul_f32 v[14:15], v[48:49], s[4:5] op_sel_hi:[1,0]
	v_pk_mul_f32 v[18:19], v[46:47], s[4:5] op_sel_hi:[1,0]
	v_or_b32_e32 v25, 32, v63
	v_cndmask_b32_e32 v26, v48, v14, vcc
	v_cndmask_b32_e32 v14, v47, v19, vcc
	v_cndmask_b32_e32 v18, v46, v18, vcc
	v_cvt_pk_f16_f32 v14, v18, v14
	v_or_b32_e32 v18, v30, v25
	v_mov_b32_e32 v19, v9
	v_lshlrev_b64 v[18:19], 7, v[18:19]
	v_cndmask_b32_e32 v15, v49, v15, vcc
	v_lshl_add_u64 v[18:19], v[12:13], 0, v[18:19]
	v_cvt_pk_f16_f32 v15, v26, v15
	v_lshl_add_u64 v[18:19], v[18:19], 0, v[8:9]
	global_store_dwordx2 v[18:19], v[14:15], off
	v_pk_mul_f32 v[14:15], v[52:53], s[4:5] op_sel_hi:[1,0]
	v_pk_mul_f32 v[18:19], v[50:51], s[4:5] op_sel_hi:[1,0]
	v_cndmask_b32_e64 v26, v52, v14, s[0:1]
	v_cndmask_b32_e64 v14, v51, v19, s[0:1]
	v_cndmask_b32_e64 v18, v50, v18, s[0:1]
	v_cvt_pk_f16_f32 v14, v18, v14
	v_or_b32_e32 v18, v31, v25
	v_mov_b32_e32 v19, v9
	v_lshlrev_b64 v[18:19], 7, v[18:19]
	v_cndmask_b32_e64 v15, v53, v15, s[0:1]
	v_lshl_add_u64 v[18:19], v[10:11], 0, v[18:19]
	v_cvt_pk_f16_f32 v15, v26, v15
	v_lshl_add_u64 v[18:19], v[18:19], 0, v[22:23]
	global_store_dwordx2 v[18:19], v[14:15], off
	v_pk_mul_f32 v[14:15], v[44:45], s[4:5] op_sel_hi:[1,0]
	v_pk_mul_f32 v[18:19], v[42:43], s[4:5] op_sel_hi:[1,0]
	v_cndmask_b32_e64 v26, v44, v14, s[2:3]
	v_cndmask_b32_e64 v14, v43, v19, s[2:3]
	v_cndmask_b32_e64 v18, v42, v18, s[2:3]
	v_cvt_pk_f16_f32 v14, v18, v14
	v_or_b32_e32 v18, v24, v25
	v_mov_b32_e32 v19, v9
	v_lshlrev_b64 v[18:19], 7, v[18:19]
	v_cndmask_b32_e64 v15, v45, v15, s[2:3]
	v_lshl_add_u64 v[18:19], v[16:17], 0, v[18:19]
	v_cvt_pk_f16_f32 v15, v26, v15
	v_lshl_add_u64 v[18:19], v[18:19], 0, v[20:21]
	global_store_dwordx2 v[18:19], v[14:15], off
	v_pk_mul_f32 v[14:15], v[56:57], s[4:5] op_sel_hi:[1,0]
	v_pk_mul_f32 v[18:19], v[54:55], s[4:5] op_sel_hi:[1,0]
	v_or_b32_e32 v25, 48, v63
	v_cndmask_b32_e32 v26, v56, v14, vcc
	v_cndmask_b32_e32 v14, v55, v19, vcc
	v_cndmask_b32_e32 v18, v54, v18, vcc
	v_cvt_pk_f16_f32 v14, v18, v14
	v_or_b32_e32 v18, v30, v25
	v_mov_b32_e32 v19, v9
	v_lshlrev_b64 v[18:19], 7, v[18:19]
	v_cndmask_b32_e32 v15, v57, v15, vcc
	v_lshl_add_u64 v[12:13], v[12:13], 0, v[18:19]
	v_cvt_pk_f16_f32 v15, v26, v15
	v_lshl_add_u64 v[12:13], v[12:13], 0, v[8:9]
	global_store_dwordx2 v[12:13], v[14:15], off
	v_pk_mul_f32 v[12:13], v[6:7], s[4:5] op_sel_hi:[1,0]
	v_pk_mul_f32 v[14:15], v[4:5], s[4:5] op_sel_hi:[1,0]
	v_cndmask_b32_e64 v7, v7, v13, s[0:1]
	v_cndmask_b32_e64 v6, v6, v12, s[0:1]
	v_cndmask_b32_e64 v5, v5, v15, s[0:1]
	v_cndmask_b32_e64 v4, v4, v14, s[0:1]
	v_or_b32_e32 v8, v31, v25
	v_cvt_pk_f16_f32 v4, v4, v5
	v_cvt_pk_f16_f32 v5, v6, v7
	v_lshlrev_b64 v[6:7], 7, v[8:9]
	v_lshl_add_u64 v[6:7], v[10:11], 0, v[6:7]
	v_lshl_add_u64 v[6:7], v[6:7], 0, v[22:23]
	global_store_dwordx2 v[6:7], v[4:5], off
	v_pk_mul_f32 v[4:5], v[2:3], s[4:5] op_sel_hi:[1,0]
	v_pk_mul_f32 v[6:7], v[0:1], s[4:5] op_sel_hi:[1,0]
	v_cndmask_b32_e64 v3, v3, v5, s[2:3]
	v_cndmask_b32_e64 v2, v2, v4, s[2:3]
	v_cndmask_b32_e64 v1, v1, v7, s[2:3]
	v_cndmask_b32_e64 v0, v0, v6, s[2:3]
	v_or_b32_e32 v8, v24, v25
	v_cvt_pk_f16_f32 v0, v0, v1
	v_cvt_pk_f16_f32 v1, v2, v3
	v_lshlrev_b64 v[2:3], 7, v[8:9]
	v_lshl_add_u64 v[2:3], v[16:17], 0, v[2:3]
	v_lshl_add_u64 v[2:3], v[2:3], 0, v[20:21]
	global_store_dwordx2 v[2:3], v[0:1], off
	s_endpgm
	s_endpgm
	s_endpgm
	s_endpgm
	s_endpgm
	s_endpgm
	s_endpgm
	s_endpgm
	s_endpgm
	s_endpgm
	s_endpgm
	s_endpgm
	s_endpgm
	s_endpgm
	s_endpgm
	s_endpgm
	s_endpgm
	s_endpgm
	s_endpgm
	s_endpgm
	s_endpgm
	s_endpgm
	s_endpgm
	s_endpgm
	s_endpgm
	s_endpgm
	s_endpgm
	s_endpgm
	s_endpgm
	s_endpgm
	s_endpgm
	s_endpgm
	s_endpgm
	s_endpgm
	s_endpgm
	s_endpgm
	s_endpgm
	s_endpgm
	s_endpgm
	s_endpgm
	s_endpgm
	s_endpgm
	s_endpgm
	s_endpgm
	s_endpgm
	s_endpgm
	s_endpgm
	s_endpgm
	s_endpgm
	s_endpgm
	s_endpgm
	s_endpgm
	s_endpgm
	s_endpgm
	s_endpgm
	s_endpgm
	s_endpgm
	s_endpgm

.LBB5_4:
	s_load_dwordx2 s[2:3], s[0:1], 0x14
	v_lshrrev_b32_e32 v3, 4, v0
	s_lshl_b32 s12, s15, 7
	s_lshl_b32 s13, s14, 7
	v_xor_b32_e32 v1, v3, v0
	s_waitcnt lgkmcnt(0)
	s_ashr_i32 s14, s3, 31
	s_mul_i32 s0, s12, s14
	s_mul_hi_u32 s1, s12, s3
	v_lshlrev_b32_e32 v1, 3, v1
	v_or_b32_e32 v4, 0x200, v0
	s_add_i32 s1, s1, s0
	s_mul_i32 s0, s12, s3
	v_and_b32_e32 v2, 56, v1
	v_lshrrev_b32_e32 v1, 3, v0
	v_lshrrev_b32_e32 v4, 3, v4
	s_lshl_b64 s[0:1], s[0:1], 1
	v_mul_lo_u32 v1, v1, s3
	v_mul_lo_u32 v4, v4, s3
	s_add_u32 s0, s4, s0
	v_add_lshl_u32 v1, v1, v2, 1
	v_add_lshl_u32 v2, v4, v2, 1
	s_addc_u32 s1, s5, s1
	s_mul_i32 s4, s13, s14
	s_mul_hi_u32 s5, s13, s3
	v_lshl_add_u32 v4, v0, 4, 0
	s_add_i32 s5, s5, s4
	s_mul_i32 s4, s13, s3
	v_readfirstlane_b32 s18, v4
	v_add_u32_e32 v5, 0x2000, v4
	s_lshl_b64 s[4:5], s[4:5], 1
	s_mov_b32 m0, s18
	v_readfirstlane_b32 s15, v5
	v_add_u32_e32 v5, 0x4000, v4
	s_add_u32 s4, s6, s4
	global_load_lds_dwordx4 v1, s[0:1]
	s_mov_b32 m0, s15
	v_readfirstlane_b32 s16, v5
	v_add_u32_e32 v5, 0x6000, v4
	s_addc_u32 s5, s7, s5
	global_load_lds_dwordx4 v2, s[0:1]
	s_mov_b32 m0, s16
	v_readfirstlane_b32 s17, v5
	v_add_u32_e32 v5, 0x8000, v4
	global_load_lds_dwordx4 v1, s[4:5]
	s_mov_b32 m0, s17
	s_add_u32 s6, s0, 0x80
	v_readfirstlane_b32 s14, v5
	v_add_u32_e32 v5, 0xa000, v4
	global_load_lds_dwordx4 v2, s[4:5]
	s_addc_u32 s7, s1, 0
	s_mov_b32 m0, s14
	v_readfirstlane_b32 s3, v5
	global_load_lds_dwordx4 v1, s[6:7]
	s_mov_b32 m0, s3
	v_add_u32_e32 v5, 0xc000, v4
	s_add_u32 s20, s4, 0x80
	global_load_lds_dwordx4 v2, s[6:7]
	v_readfirstlane_b32 s6, v5
	v_add_u32_e32 v4, 0xe000, v4
	s_addc_u32 s21, s5, 0
	s_mov_b32 m0, s6
	v_readfirstlane_b32 s7, v4
	global_load_lds_dwordx4 v1, s[20:21]
	s_mov_b32 m0, s7
	v_lshrrev_b32_e32 v5, 1, v0
	global_load_lds_dwordx4 v2, s[20:21]
	v_bfe_u32 v6, v0, 1, 3
	v_and_b32_e32 v4, 15, v0
	v_lshrrev_b32_e32 v7, 2, v0
	v_bitop3_b32 v3, v3, v6, 3 bitop3:0x6c
	v_and_b32_e32 v8, 0x60, v5
	v_and_or_b32 v32, v7, 64, v4
	v_lshlrev_b32_e32 v7, 4, v3
	v_or_b32_e32 v3, v8, v4
	v_lshl_add_u32 v4, v3, 7, 0
	s_waitcnt vmcnt(4)
	s_barrier
	v_add_u32_e32 v3, v4, v7
	ds_read_b128 v[10:13], v3 offset:16384
	v_lshl_add_u32 v30, v32, 7, 0
	v_add_u32_e32 v5, v30, v7
	ds_read_b128 v[14:17], v5
	ds_read_b128 v[18:21], v3 offset:18432
	ds_read_b128 v[22:25], v5 offset:2048
	ds_read_b128 v[34:37], v5 offset:4096
	ds_read_b128 v[38:41], v5 offset:6144
	v_bfe_u32 v9, v0, 4, 2
	v_bitop3_b32 v0, v9, v6, 4 bitop3:0x36
	s_waitcnt lgkmcnt(0)
	v_mfma_f32_16x16x32_f16 v[26:29], v[10:13], v[14:17], 0
	v_lshlrev_b32_e32 v6, 4, v0
	v_mfma_f32_16x16x32_f16 v[14:17], v[18:21], v[14:17], 0
	v_add_u32_e32 v0, v30, v6
	ds_read_b128 v[42:45], v0
	ds_read_b128 v[46:49], v0 offset:2048
	ds_read_b128 v[50:53], v0 offset:4096
	ds_read_b128 v[54:57], v0 offset:6144
	v_add_u32_e32 v4, v4, v6
	ds_read_b128 v[58:61], v4 offset:16384
	ds_read_b128 v[62:65], v4 offset:18432
	v_mfma_f32_16x16x32_f16 v[66:69], v[10:13], v[22:25], 0
	v_mfma_f32_16x16x32_f16 v[22:25], v[18:21], v[22:25], 0
	v_mfma_f32_16x16x32_f16 v[70:73], v[10:13], v[34:37], 0
	v_mfma_f32_16x16x32_f16 v[34:37], v[18:21], v[34:37], 0
	v_mfma_f32_16x16x32_f16 v[10:13], v[10:13], v[38:41], 0
	v_mfma_f32_16x16x32_f16 v[18:21], v[18:21], v[38:41], 0
	s_add_u32 s20, s0, 0x100
	s_mov_b32 m0, s18
	s_waitcnt vmcnt(0) lgkmcnt(0)
	s_barrier
	s_addc_u32 s21, s1, 0
	s_add_u32 s22, s4, 0x100
	global_load_lds_dwordx4 v1, s[20:21]
	s_mov_b32 m0, s15
	s_addc_u32 s23, s5, 0
	global_load_lds_dwordx4 v2, s[20:21]
	s_mov_b32 m0, s16
	s_nop 0
	global_load_lds_dwordx4 v1, s[22:23]
	s_mov_b32 m0, s17
	s_nop 0
	global_load_lds_dwordx4 v2, s[22:23]
	s_waitcnt lgkmcnt(0)
	v_mfma_f32_16x16x32_f16 v[26:29], v[58:61], v[42:45], v[26:29]
	v_mfma_f32_16x16x32_f16 v[14:17], v[62:65], v[42:45], v[14:17]
	ds_read_b128 v[38:41], v5 offset:32768
	ds_read_b128 v[42:45], v5 offset:34816
	ds_read_b128 v[74:77], v5 offset:36864
	ds_read_b128 v[78:81], v5 offset:38912
	ds_read_b128 v[82:85], v3 offset:49152
	ds_read_b128 v[86:89], v3 offset:51200
	v_mfma_f32_16x16x32_f16 v[66:69], v[58:61], v[46:49], v[66:69]
	v_mfma_f32_16x16x32_f16 v[22:25], v[62:65], v[46:49], v[22:25]
	v_mfma_f32_16x16x32_f16 v[46:49], v[58:61], v[50:53], v[70:73]
	v_mfma_f32_16x16x32_f16 v[34:37], v[62:65], v[50:53], v[34:37]
	v_mfma_f32_16x16x32_f16 v[10:13], v[58:61], v[54:57], v[10:13]
	v_mfma_f32_16x16x32_f16 v[18:21], v[62:65], v[54:57], v[18:21]
	s_waitcnt lgkmcnt(0)
	v_mfma_f32_16x16x32_f16 v[26:29], v[82:85], v[38:41], v[26:29]
	v_mfma_f32_16x16x32_f16 v[14:17], v[86:89], v[38:41], v[14:17]
	ds_read_b128 v[38:41], v0 offset:32768
	ds_read_b128 v[50:53], v0 offset:34816
	ds_read_b128 v[54:57], v0 offset:36864
	ds_read_b128 v[58:61], v0 offset:38912
	ds_read_b128 v[62:65], v4 offset:49152
	ds_read_b128 v[70:73], v4 offset:51200
	v_mfma_f32_16x16x32_f16 v[66:69], v[82:85], v[42:45], v[66:69]
	v_mfma_f32_16x16x32_f16 v[22:25], v[86:89], v[42:45], v[22:25]
	v_mfma_f32_16x16x32_f16 v[42:45], v[82:85], v[74:77], v[46:49]
	v_mfma_f32_16x16x32_f16 v[34:37], v[86:89], v[74:77], v[34:37]
	v_mfma_f32_16x16x32_f16 v[10:13], v[82:85], v[78:81], v[10:13]
	v_mfma_f32_16x16x32_f16 v[18:21], v[86:89], v[78:81], v[18:21]
	s_add_u32 s20, s0, 0x180
	s_mov_b32 m0, s14
	s_waitcnt vmcnt(0) lgkmcnt(0)
	s_barrier
	s_addc_u32 s21, s1, 0
	s_add_u32 s22, s4, 0x180
	global_load_lds_dwordx4 v1, s[20:21]
	s_mov_b32 m0, s3
	s_addc_u32 s23, s5, 0
	global_load_lds_dwordx4 v2, s[20:21]
	s_mov_b32 m0, s6
	s_nop 0
	global_load_lds_dwordx4 v1, s[22:23]
	s_mov_b32 m0, s7
	s_nop 0
	global_load_lds_dwordx4 v2, s[22:23]
	s_waitcnt lgkmcnt(0)
	v_mfma_f32_16x16x32_f16 v[26:29], v[62:65], v[38:41], v[26:29]
	v_mfma_f32_16x16x32_f16 v[14:17], v[70:73], v[38:41], v[14:17]
	ds_read_b128 v[38:41], v5
	ds_read_b128 v[46:49], v5 offset:2048
	ds_read_b128 v[74:77], v5 offset:4096
	ds_read_b128 v[78:81], v5 offset:6144
	ds_read_b128 v[82:85], v3 offset:16384
	ds_read_b128 v[86:89], v3 offset:18432
	v_mfma_f32_16x16x32_f16 v[66:69], v[62:65], v[50:53], v[66:69]
	v_mfma_f32_16x16x32_f16 v[22:25], v[70:73], v[50:53], v[22:25]
	v_mfma_f32_16x16x32_f16 v[42:45], v[62:65], v[54:57], v[42:45]
	v_mfma_f32_16x16x32_f16 v[34:37], v[70:73], v[54:57], v[34:37]
	v_mfma_f32_16x16x32_f16 v[10:13], v[62:65], v[58:61], v[10:13]
	v_mfma_f32_16x16x32_f16 v[18:21], v[70:73], v[58:61], v[18:21]
	s_waitcnt lgkmcnt(0)
	v_mfma_f32_16x16x32_f16 v[26:29], v[82:85], v[38:41], v[26:29]
	v_mfma_f32_16x16x32_f16 v[14:17], v[86:89], v[38:41], v[14:17]
	ds_read_b128 v[38:41], v0
	ds_read_b128 v[50:53], v0 offset:2048
	ds_read_b128 v[54:57], v0 offset:4096
	ds_read_b128 v[58:61], v0 offset:6144
	ds_read_b128 v[62:65], v4 offset:16384
	ds_read_b128 v[70:73], v4 offset:18432
	v_mfma_f32_16x16x32_f16 v[66:69], v[82:85], v[46:49], v[66:69]
	v_mfma_f32_16x16x32_f16 v[22:25], v[86:89], v[46:49], v[22:25]
	v_mfma_f32_16x16x32_f16 v[42:45], v[82:85], v[74:77], v[42:45]
	v_mfma_f32_16x16x32_f16 v[34:37], v[86:89], v[74:77], v[34:37]
	v_mfma_f32_16x16x32_f16 v[10:13], v[82:85], v[78:81], v[10:13]
	v_mfma_f32_16x16x32_f16 v[18:21], v[86:89], v[78:81], v[18:21]
	s_add_u32 s20, s0, 0x200
	s_mov_b32 m0, s18
	s_waitcnt vmcnt(0) lgkmcnt(0)
	s_barrier
	s_addc_u32 s21, s1, 0
	s_add_u32 s22, s4, 0x200
	global_load_lds_dwordx4 v1, s[20:21]
	s_mov_b32 m0, s15
	s_addc_u32 s23, s5, 0
	global_load_lds_dwordx4 v2, s[20:21]
	s_mov_b32 m0, s16
	s_nop 0
	global_load_lds_dwordx4 v1, s[22:23]
	s_mov_b32 m0, s17
	s_nop 0
	global_load_lds_dwordx4 v2, s[22:23]
	s_waitcnt lgkmcnt(0)
	v_mfma_f32_16x16x32_f16 v[26:29], v[62:65], v[38:41], v[26:29]
	v_mfma_f32_16x16x32_f16 v[14:17], v[70:73], v[38:41], v[14:17]
	ds_read_b128 v[38:41], v5 offset:32768
	ds_read_b128 v[46:49], v5 offset:34816
	ds_read_b128 v[74:77], v5 offset:36864
	ds_read_b128 v[78:81], v5 offset:38912
	ds_read_b128 v[82:85], v3 offset:49152
	ds_read_b128 v[86:89], v3 offset:51200
	v_mfma_f32_16x16x32_f16 v[66:69], v[62:65], v[50:53], v[66:69]
	v_mfma_f32_16x16x32_f16 v[22:25], v[70:73], v[50:53], v[22:25]
	v_mfma_f32_16x16x32_f16 v[42:45], v[62:65], v[54:57], v[42:45]
	v_mfma_f32_16x16x32_f16 v[34:37], v[70:73], v[54:57], v[34:37]
	v_mfma_f32_16x16x32_f16 v[10:13], v[62:65], v[58:61], v[10:13]
	v_mfma_f32_16x16x32_f16 v[18:21], v[70:73], v[58:61], v[18:21]
	s_waitcnt lgkmcnt(0)
	v_mfma_f32_16x16x32_f16 v[26:29], v[82:85], v[38:41], v[26:29]
	v_mfma_f32_16x16x32_f16 v[14:17], v[86:89], v[38:41], v[14:17]
	ds_read_b128 v[38:41], v0 offset:32768
	ds_read_b128 v[50:53], v0 offset:34816
	ds_read_b128 v[54:57], v0 offset:36864
	ds_read_b128 v[58:61], v0 offset:38912
	ds_read_b128 v[62:65], v4 offset:49152
	ds_read_b128 v[70:73], v4 offset:51200
	v_mfma_f32_16x16x32_f16 v[66:69], v[82:85], v[46:49], v[66:69]
	v_mfma_f32_16x16x32_f16 v[22:25], v[86:89], v[46:49], v[22:25]
	v_mfma_f32_16x16x32_f16 v[42:45], v[82:85], v[74:77], v[42:45]
	v_mfma_f32_16x16x32_f16 v[34:37], v[86:89], v[74:77], v[34:37]
	v_mfma_f32_16x16x32_f16 v[10:13], v[82:85], v[78:81], v[10:13]
	v_mfma_f32_16x16x32_f16 v[18:21], v[86:89], v[78:81], v[18:21]
	s_add_u32 s20, s0, 0x280
	s_mov_b32 m0, s14
	s_waitcnt vmcnt(0) lgkmcnt(0)
	s_barrier
	s_addc_u32 s21, s1, 0
	s_add_u32 s22, s4, 0x280
	global_load_lds_dwordx4 v1, s[20:21]
	s_mov_b32 m0, s3
	s_addc_u32 s23, s5, 0
	global_load_lds_dwordx4 v2, s[20:21]
	s_mov_b32 m0, s6
	s_nop 0
	global_load_lds_dwordx4 v1, s[22:23]
	s_mov_b32 m0, s7
	s_nop 0
	global_load_lds_dwordx4 v2, s[22:23]
	s_waitcnt lgkmcnt(0)
	v_mfma_f32_16x16x32_f16 v[26:29], v[62:65], v[38:41], v[26:29]
	v_mfma_f32_16x16x32_f16 v[14:17], v[70:73], v[38:41], v[14:17]
	ds_read_b128 v[38:41], v5
	ds_read_b128 v[46:49], v5 offset:2048
	ds_read_b128 v[74:77], v5 offset:4096
	ds_read_b128 v[78:81], v5 offset:6144
	ds_read_b128 v[82:85], v3 offset:16384
	ds_read_b128 v[86:89], v3 offset:18432
	v_mfma_f32_16x16x32_f16 v[66:69], v[62:65], v[50:53], v[66:69]
	v_mfma_f32_16x16x32_f16 v[22:25], v[70:73], v[50:53], v[22:25]
	v_mfma_f32_16x16x32_f16 v[42:45], v[62:65], v[54:57], v[42:45]
	v_mfma_f32_16x16x32_f16 v[34:37], v[70:73], v[54:57], v[34:37]
	v_mfma_f32_16x16x32_f16 v[10:13], v[62:65], v[58:61], v[10:13]
	v_mfma_f32_16x16x32_f16 v[18:21], v[70:73], v[58:61], v[18:21]
	s_waitcnt lgkmcnt(0)
	v_mfma_f32_16x16x32_f16 v[26:29], v[82:85], v[38:41], v[26:29]
	v_mfma_f32_16x16x32_f16 v[14:17], v[86:89], v[38:41], v[14:17]
	ds_read_b128 v[38:41], v0
	ds_read_b128 v[50:53], v0 offset:2048
	ds_read_b128 v[54:57], v0 offset:4096
	ds_read_b128 v[58:61], v0 offset:6144
	ds_read_b128 v[62:65], v4 offset:16384
	ds_read_b128 v[70:73], v4 offset:18432
	v_mfma_f32_16x16x32_f16 v[66:69], v[82:85], v[46:49], v[66:69]
	v_mfma_f32_16x16x32_f16 v[22:25], v[86:89], v[46:49], v[22:25]
	v_mfma_f32_16x16x32_f16 v[42:45], v[82:85], v[74:77], v[42:45]
	v_mfma_f32_16x16x32_f16 v[34:37], v[86:89], v[74:77], v[34:37]
	v_mfma_f32_16x16x32_f16 v[10:13], v[82:85], v[78:81], v[10:13]
	v_mfma_f32_16x16x32_f16 v[18:21], v[86:89], v[78:81], v[18:21]
	s_add_u32 s20, s0, 0x300
	s_mov_b32 m0, s18
	s_waitcnt vmcnt(0) lgkmcnt(0)
	s_barrier
	s_addc_u32 s21, s1, 0
	s_add_u32 s22, s4, 0x300
	global_load_lds_dwordx4 v1, s[20:21]
	s_mov_b32 m0, s15
	s_addc_u32 s23, s5, 0
	global_load_lds_dwordx4 v2, s[20:21]
	s_mov_b32 m0, s16
	s_nop 0
	global_load_lds_dwordx4 v1, s[22:23]
	s_mov_b32 m0, s17
	s_nop 0
	global_load_lds_dwordx4 v2, s[22:23]
	s_waitcnt lgkmcnt(0)
	v_mfma_f32_16x16x32_f16 v[26:29], v[62:65], v[38:41], v[26:29]
	v_mfma_f32_16x16x32_f16 v[14:17], v[70:73], v[38:41], v[14:17]
	ds_read_b128 v[38:41], v5 offset:32768
	ds_read_b128 v[46:49], v5 offset:34816
	ds_read_b128 v[74:77], v5 offset:36864
	ds_read_b128 v[78:81], v5 offset:38912
	ds_read_b128 v[82:85], v3 offset:49152
	ds_read_b128 v[86:89], v3 offset:51200
	v_mfma_f32_16x16x32_f16 v[66:69], v[62:65], v[50:53], v[66:69]
	v_mfma_f32_16x16x32_f16 v[22:25], v[70:73], v[50:53], v[22:25]
	v_mfma_f32_16x16x32_f16 v[42:45], v[62:65], v[54:57], v[42:45]
	v_mfma_f32_16x16x32_f16 v[34:37], v[70:73], v[54:57], v[34:37]
	v_mfma_f32_16x16x32_f16 v[10:13], v[62:65], v[58:61], v[10:13]
	v_mfma_f32_16x16x32_f16 v[18:21], v[70:73], v[58:61], v[18:21]
	s_waitcnt lgkmcnt(0)
	v_mfma_f32_16x16x32_f16 v[26:29], v[82:85], v[38:41], v[26:29]
	v_mfma_f32_16x16x32_f16 v[14:17], v[86:89], v[38:41], v[14:17]
	ds_read_b128 v[38:41], v0 offset:32768
	ds_read_b128 v[50:53], v0 offset:34816
	ds_read_b128 v[54:57], v0 offset:36864
	ds_read_b128 v[58:61], v0 offset:38912
	ds_read_b128 v[62:65], v4 offset:49152
	ds_read_b128 v[70:73], v4 offset:51200
	v_mfma_f32_16x16x32_f16 v[66:69], v[82:85], v[46:49], v[66:69]
	v_mfma_f32_16x16x32_f16 v[22:25], v[86:89], v[46:49], v[22:25]
	v_mfma_f32_16x16x32_f16 v[42:45], v[82:85], v[74:77], v[42:45]
	v_mfma_f32_16x16x32_f16 v[34:37], v[86:89], v[74:77], v[34:37]
	v_mfma_f32_16x16x32_f16 v[10:13], v[82:85], v[78:81], v[10:13]
	v_mfma_f32_16x16x32_f16 v[18:21], v[86:89], v[78:81], v[18:21]
	s_add_u32 s20, s0, 0x380
	s_mov_b32 m0, s14
	s_waitcnt vmcnt(0) lgkmcnt(0)
	s_barrier
	s_addc_u32 s21, s1, 0
	s_add_u32 s22, s4, 0x380
	global_load_lds_dwordx4 v1, s[20:21]
	s_mov_b32 m0, s3
	s_addc_u32 s23, s5, 0
	global_load_lds_dwordx4 v2, s[20:21]
	s_mov_b32 m0, s6
	s_nop 0
	global_load_lds_dwordx4 v1, s[22:23]
	s_mov_b32 m0, s7
	s_nop 0
	global_load_lds_dwordx4 v2, s[22:23]
	s_waitcnt lgkmcnt(0)
	v_mfma_f32_16x16x32_f16 v[26:29], v[62:65], v[38:41], v[26:29]
	v_mfma_f32_16x16x32_f16 v[14:17], v[70:73], v[38:41], v[14:17]
	ds_read_b128 v[38:41], v5
	ds_read_b128 v[46:49], v5 offset:2048
	ds_read_b128 v[74:77], v5 offset:4096
	ds_read_b128 v[78:81], v5 offset:6144
	ds_read_b128 v[82:85], v3 offset:16384
	ds_read_b128 v[86:89], v3 offset:18432
	v_mfma_f32_16x16x32_f16 v[66:69], v[62:65], v[50:53], v[66:69]
	v_mfma_f32_16x16x32_f16 v[22:25], v[70:73], v[50:53], v[22:25]
	v_mfma_f32_16x16x32_f16 v[42:45], v[62:65], v[54:57], v[42:45]
	v_mfma_f32_16x16x32_f16 v[34:37], v[70:73], v[54:57], v[34:37]
	v_mfma_f32_16x16x32_f16 v[10:13], v[62:65], v[58:61], v[10:13]
	v_mfma_f32_16x16x32_f16 v[18:21], v[70:73], v[58:61], v[18:21]
	s_waitcnt lgkmcnt(0)
	v_mfma_f32_16x16x32_f16 v[26:29], v[82:85], v[38:41], v[26:29]
	v_mfma_f32_16x16x32_f16 v[14:17], v[86:89], v[38:41], v[14:17]
	ds_read_b128 v[38:41], v0
	ds_read_b128 v[50:53], v0 offset:2048
	ds_read_b128 v[54:57], v0 offset:4096
	ds_read_b128 v[58:61], v0 offset:6144
	ds_read_b128 v[62:65], v4 offset:16384
	ds_read_b128 v[70:73], v4 offset:18432
	v_mfma_f32_16x16x32_f16 v[66:69], v[82:85], v[46:49], v[66:69]
	v_mfma_f32_16x16x32_f16 v[22:25], v[86:89], v[46:49], v[22:25]
	v_mfma_f32_16x16x32_f16 v[42:45], v[82:85], v[74:77], v[42:45]
	v_mfma_f32_16x16x32_f16 v[34:37], v[86:89], v[74:77], v[34:37]
	v_mfma_f32_16x16x32_f16 v[10:13], v[82:85], v[78:81], v[10:13]
	v_mfma_f32_16x16x32_f16 v[18:21], v[86:89], v[78:81], v[18:21]
	s_add_u32 s20, s0, 0x400
	s_mov_b32 m0, s18
	s_waitcnt vmcnt(0) lgkmcnt(0)
	s_barrier
	s_addc_u32 s21, s1, 0
	s_add_u32 s22, s4, 0x400
	global_load_lds_dwordx4 v1, s[20:21]
	s_mov_b32 m0, s15
	s_addc_u32 s23, s5, 0
	global_load_lds_dwordx4 v2, s[20:21]
	s_mov_b32 m0, s16
	s_nop 0
	global_load_lds_dwordx4 v1, s[22:23]
	s_mov_b32 m0, s17
	s_nop 0
	global_load_lds_dwordx4 v2, s[22:23]
	s_waitcnt lgkmcnt(0)
	v_mfma_f32_16x16x32_f16 v[26:29], v[62:65], v[38:41], v[26:29]
	v_mfma_f32_16x16x32_f16 v[14:17], v[70:73], v[38:41], v[14:17]
	ds_read_b128 v[38:41], v5 offset:32768
	ds_read_b128 v[46:49], v5 offset:34816
	ds_read_b128 v[74:77], v5 offset:36864
	ds_read_b128 v[78:81], v5 offset:38912
	ds_read_b128 v[82:85], v3 offset:49152
	ds_read_b128 v[86:89], v3 offset:51200
	v_mfma_f32_16x16x32_f16 v[66:69], v[62:65], v[50:53], v[66:69]
	v_mfma_f32_16x16x32_f16 v[22:25], v[70:73], v[50:53], v[22:25]
	v_mfma_f32_16x16x32_f16 v[42:45], v[62:65], v[54:57], v[42:45]
	v_mfma_f32_16x16x32_f16 v[34:37], v[70:73], v[54:57], v[34:37]
	v_mfma_f32_16x16x32_f16 v[10:13], v[62:65], v[58:61], v[10:13]
	v_mfma_f32_16x16x32_f16 v[18:21], v[70:73], v[58:61], v[18:21]
	s_waitcnt lgkmcnt(0)
	v_mfma_f32_16x16x32_f16 v[26:29], v[82:85], v[38:41], v[26:29]
	v_mfma_f32_16x16x32_f16 v[14:17], v[86:89], v[38:41], v[14:17]
	ds_read_b128 v[38:41], v0 offset:32768
	ds_read_b128 v[50:53], v0 offset:34816
	ds_read_b128 v[54:57], v0 offset:36864
	ds_read_b128 v[58:61], v0 offset:38912
	ds_read_b128 v[62:65], v4 offset:49152
	ds_read_b128 v[70:73], v4 offset:51200
	v_mfma_f32_16x16x32_f16 v[66:69], v[82:85], v[46:49], v[66:69]
	v_mfma_f32_16x16x32_f16 v[22:25], v[86:89], v[46:49], v[22:25]
	v_mfma_f32_16x16x32_f16 v[42:45], v[82:85], v[74:77], v[42:45]
	v_mfma_f32_16x16x32_f16 v[34:37], v[86:89], v[74:77], v[34:37]
	v_mfma_f32_16x16x32_f16 v[10:13], v[82:85], v[78:81], v[10:13]
	v_mfma_f32_16x16x32_f16 v[18:21], v[86:89], v[78:81], v[18:21]
	s_add_u32 s20, s0, 0x480
	s_mov_b32 m0, s14
	s_waitcnt vmcnt(0) lgkmcnt(0)
	s_barrier
	s_addc_u32 s21, s1, 0
	s_add_u32 s22, s4, 0x480
	global_load_lds_dwordx4 v1, s[20:21]
	s_mov_b32 m0, s3
	s_addc_u32 s23, s5, 0
	global_load_lds_dwordx4 v2, s[20:21]
	s_mov_b32 m0, s6
	s_nop 0
	global_load_lds_dwordx4 v1, s[22:23]
	s_mov_b32 m0, s7
	s_nop 0
	global_load_lds_dwordx4 v2, s[22:23]
	s_waitcnt lgkmcnt(0)
	v_mfma_f32_16x16x32_f16 v[26:29], v[62:65], v[38:41], v[26:29]
	v_mfma_f32_16x16x32_f16 v[14:17], v[70:73], v[38:41], v[14:17]
	ds_read_b128 v[38:41], v5
	ds_read_b128 v[46:49], v5 offset:2048
	ds_read_b128 v[74:77], v5 offset:4096
	ds_read_b128 v[78:81], v5 offset:6144
	ds_read_b128 v[82:85], v3 offset:16384
	ds_read_b128 v[86:89], v3 offset:18432
	v_mfma_f32_16x16x32_f16 v[66:69], v[62:65], v[50:53], v[66:69]
	v_mfma_f32_16x16x32_f16 v[22:25], v[70:73], v[50:53], v[22:25]
	v_mfma_f32_16x16x32_f16 v[42:45], v[62:65], v[54:57], v[42:45]
	v_mfma_f32_16x16x32_f16 v[34:37], v[70:73], v[54:57], v[34:37]
	v_mfma_f32_16x16x32_f16 v[10:13], v[62:65], v[58:61], v[10:13]
	v_mfma_f32_16x16x32_f16 v[18:21], v[70:73], v[58:61], v[18:21]
	s_waitcnt lgkmcnt(0)
	v_mfma_f32_16x16x32_f16 v[26:29], v[82:85], v[38:41], v[26:29]
	v_mfma_f32_16x16x32_f16 v[14:17], v[86:89], v[38:41], v[14:17]
	ds_read_b128 v[38:41], v0
	ds_read_b128 v[50:53], v0 offset:2048
	ds_read_b128 v[54:57], v0 offset:4096
	ds_read_b128 v[58:61], v0 offset:6144
	ds_read_b128 v[62:65], v4 offset:16384
	ds_read_b128 v[70:73], v4 offset:18432
	v_mfma_f32_16x16x32_f16 v[66:69], v[82:85], v[46:49], v[66:69]
	v_mfma_f32_16x16x32_f16 v[22:25], v[86:89], v[46:49], v[22:25]
	v_mfma_f32_16x16x32_f16 v[42:45], v[82:85], v[74:77], v[42:45]
	v_mfma_f32_16x16x32_f16 v[34:37], v[86:89], v[74:77], v[34:37]
	v_mfma_f32_16x16x32_f16 v[10:13], v[82:85], v[78:81], v[10:13]
	v_mfma_f32_16x16x32_f16 v[18:21], v[86:89], v[78:81], v[18:21]
	s_add_u32 s20, s0, 0x500
	s_mov_b32 m0, s18
	s_waitcnt vmcnt(0) lgkmcnt(0)
	s_barrier
	s_addc_u32 s21, s1, 0
	s_add_u32 s22, s4, 0x500
	global_load_lds_dwordx4 v1, s[20:21]
	s_mov_b32 m0, s15
	s_addc_u32 s23, s5, 0
	global_load_lds_dwordx4 v2, s[20:21]
	s_mov_b32 m0, s16
	s_nop 0
	global_load_lds_dwordx4 v1, s[22:23]
	s_mov_b32 m0, s17
	s_nop 0
	global_load_lds_dwordx4 v2, s[22:23]
	s_waitcnt lgkmcnt(0)
	v_mfma_f32_16x16x32_f16 v[26:29], v[62:65], v[38:41], v[26:29]
	v_mfma_f32_16x16x32_f16 v[14:17], v[70:73], v[38:41], v[14:17]
	ds_read_b128 v[38:41], v5 offset:32768
	ds_read_b128 v[46:49], v5 offset:34816
	ds_read_b128 v[74:77], v5 offset:36864
	ds_read_b128 v[78:81], v5 offset:38912
	ds_read_b128 v[82:85], v3 offset:49152
	ds_read_b128 v[86:89], v3 offset:51200
	v_mfma_f32_16x16x32_f16 v[66:69], v[62:65], v[50:53], v[66:69]
	v_mfma_f32_16x16x32_f16 v[22:25], v[70:73], v[50:53], v[22:25]
	v_mfma_f32_16x16x32_f16 v[42:45], v[62:65], v[54:57], v[42:45]
	v_mfma_f32_16x16x32_f16 v[34:37], v[70:73], v[54:57], v[34:37]
	v_mfma_f32_16x16x32_f16 v[10:13], v[62:65], v[58:61], v[10:13]
	v_mfma_f32_16x16x32_f16 v[18:21], v[70:73], v[58:61], v[18:21]
	s_waitcnt lgkmcnt(0)
	v_mfma_f32_16x16x32_f16 v[26:29], v[82:85], v[38:41], v[26:29]
	v_mfma_f32_16x16x32_f16 v[14:17], v[86:89], v[38:41], v[14:17]
	ds_read_b128 v[38:41], v0 offset:32768
	ds_read_b128 v[50:53], v0 offset:34816
	ds_read_b128 v[54:57], v0 offset:36864
	ds_read_b128 v[58:61], v0 offset:38912
	ds_read_b128 v[62:65], v4 offset:49152
	ds_read_b128 v[70:73], v4 offset:51200
	v_mfma_f32_16x16x32_f16 v[66:69], v[82:85], v[46:49], v[66:69]
	v_mfma_f32_16x16x32_f16 v[22:25], v[86:89], v[46:49], v[22:25]
	v_mfma_f32_16x16x32_f16 v[42:45], v[82:85], v[74:77], v[42:45]
	v_mfma_f32_16x16x32_f16 v[34:37], v[86:89], v[74:77], v[34:37]
	v_mfma_f32_16x16x32_f16 v[10:13], v[82:85], v[78:81], v[10:13]
	v_mfma_f32_16x16x32_f16 v[18:21], v[86:89], v[78:81], v[18:21]
	s_add_u32 s20, s0, 0x580
	s_mov_b32 m0, s14
	s_waitcnt vmcnt(0) lgkmcnt(0)
	s_barrier
	s_addc_u32 s21, s1, 0
	s_add_u32 s22, s4, 0x580
	global_load_lds_dwordx4 v1, s[20:21]
	s_mov_b32 m0, s3
	s_addc_u32 s23, s5, 0
	global_load_lds_dwordx4 v2, s[20:21]
	s_mov_b32 m0, s6
	s_nop 0
	global_load_lds_dwordx4 v1, s[22:23]
	s_mov_b32 m0, s7
	s_nop 0
	global_load_lds_dwordx4 v2, s[22:23]
	s_waitcnt lgkmcnt(0)
	v_mfma_f32_16x16x32_f16 v[26:29], v[62:65], v[38:41], v[26:29]
	v_mfma_f32_16x16x32_f16 v[14:17], v[70:73], v[38:41], v[14:17]
	ds_read_b128 v[38:41], v5
	ds_read_b128 v[46:49], v5 offset:2048
	ds_read_b128 v[74:77], v5 offset:4096
	ds_read_b128 v[78:81], v5 offset:6144
	ds_read_b128 v[82:85], v3 offset:16384
	ds_read_b128 v[86:89], v3 offset:18432
	v_mfma_f32_16x16x32_f16 v[66:69], v[62:65], v[50:53], v[66:69]
	v_mfma_f32_16x16x32_f16 v[22:25], v[70:73], v[50:53], v[22:25]
	v_mfma_f32_16x16x32_f16 v[42:45], v[62:65], v[54:57], v[42:45]
	v_mfma_f32_16x16x32_f16 v[34:37], v[70:73], v[54:57], v[34:37]
	v_mfma_f32_16x16x32_f16 v[10:13], v[62:65], v[58:61], v[10:13]
	v_mfma_f32_16x16x32_f16 v[18:21], v[70:73], v[58:61], v[18:21]
	s_waitcnt lgkmcnt(0)
	v_mfma_f32_16x16x32_f16 v[26:29], v[82:85], v[38:41], v[26:29]
	v_mfma_f32_16x16x32_f16 v[14:17], v[86:89], v[38:41], v[14:17]
	ds_read_b128 v[38:41], v0
	ds_read_b128 v[50:53], v0 offset:2048
	ds_read_b128 v[54:57], v0 offset:4096
	ds_read_b128 v[58:61], v0 offset:6144
	ds_read_b128 v[62:65], v4 offset:16384
	ds_read_b128 v[70:73], v4 offset:18432
	v_mfma_f32_16x16x32_f16 v[66:69], v[82:85], v[46:49], v[66:69]
	v_mfma_f32_16x16x32_f16 v[22:25], v[86:89], v[46:49], v[22:25]
	v_mfma_f32_16x16x32_f16 v[42:45], v[82:85], v[74:77], v[42:45]
	v_mfma_f32_16x16x32_f16 v[34:37], v[86:89], v[74:77], v[34:37]
	v_mfma_f32_16x16x32_f16 v[10:13], v[82:85], v[78:81], v[10:13]
	v_mfma_f32_16x16x32_f16 v[18:21], v[86:89], v[78:81], v[18:21]
	s_add_u32 s20, s0, 0x600
	s_mov_b32 m0, s18
	s_waitcnt vmcnt(0) lgkmcnt(0)
	s_barrier
	s_addc_u32 s21, s1, 0
	s_add_u32 s22, s4, 0x600
	global_load_lds_dwordx4 v1, s[20:21]
	s_mov_b32 m0, s15
	s_addc_u32 s23, s5, 0
	global_load_lds_dwordx4 v2, s[20:21]
	s_mov_b32 m0, s16
	s_nop 0
	global_load_lds_dwordx4 v1, s[22:23]
	s_mov_b32 m0, s17
	s_nop 0
	global_load_lds_dwordx4 v2, s[22:23]
	s_waitcnt lgkmcnt(0)
	v_mfma_f32_16x16x32_f16 v[26:29], v[62:65], v[38:41], v[26:29]
	v_mfma_f32_16x16x32_f16 v[14:17], v[70:73], v[38:41], v[14:17]
	ds_read_b128 v[38:41], v5 offset:32768
	ds_read_b128 v[46:49], v5 offset:34816
	ds_read_b128 v[74:77], v5 offset:36864
	ds_read_b128 v[78:81], v5 offset:38912
	ds_read_b128 v[82:85], v3 offset:49152
	ds_read_b128 v[86:89], v3 offset:51200
	v_mfma_f32_16x16x32_f16 v[66:69], v[62:65], v[50:53], v[66:69]
	v_mfma_f32_16x16x32_f16 v[22:25], v[70:73], v[50:53], v[22:25]
	v_mfma_f32_16x16x32_f16 v[42:45], v[62:65], v[54:57], v[42:45]
	v_mfma_f32_16x16x32_f16 v[34:37], v[70:73], v[54:57], v[34:37]
	v_mfma_f32_16x16x32_f16 v[10:13], v[62:65], v[58:61], v[10:13]
	v_mfma_f32_16x16x32_f16 v[18:21], v[70:73], v[58:61], v[18:21]
	s_waitcnt lgkmcnt(0)
	v_mfma_f32_16x16x32_f16 v[26:29], v[82:85], v[38:41], v[26:29]
	v_mfma_f32_16x16x32_f16 v[14:17], v[86:89], v[38:41], v[14:17]
	ds_read_b128 v[38:41], v0 offset:32768
	ds_read_b128 v[50:53], v0 offset:34816
	ds_read_b128 v[54:57], v0 offset:36864
	ds_read_b128 v[58:61], v0 offset:38912
	ds_read_b128 v[62:65], v4 offset:49152
	ds_read_b128 v[70:73], v4 offset:51200
	v_mfma_f32_16x16x32_f16 v[66:69], v[82:85], v[46:49], v[66:69]
	v_mfma_f32_16x16x32_f16 v[22:25], v[86:89], v[46:49], v[22:25]
	v_mfma_f32_16x16x32_f16 v[42:45], v[82:85], v[74:77], v[42:45]
	v_mfma_f32_16x16x32_f16 v[34:37], v[86:89], v[74:77], v[34:37]
	v_mfma_f32_16x16x32_f16 v[10:13], v[82:85], v[78:81], v[10:13]
	v_mfma_f32_16x16x32_f16 v[18:21], v[86:89], v[78:81], v[18:21]
	s_add_u32 s20, s0, 0x680
	s_mov_b32 m0, s14
	s_waitcnt vmcnt(0) lgkmcnt(0)
	s_barrier
	s_addc_u32 s21, s1, 0
	s_add_u32 s22, s4, 0x680
	global_load_lds_dwordx4 v1, s[20:21]
	s_mov_b32 m0, s3
	s_addc_u32 s23, s5, 0
	global_load_lds_dwordx4 v2, s[20:21]
	s_mov_b32 m0, s6
	s_nop 0
	global_load_lds_dwordx4 v1, s[22:23]
	s_mov_b32 m0, s7
	s_nop 0
	global_load_lds_dwordx4 v2, s[22:23]
	s_waitcnt lgkmcnt(0)
	v_mfma_f32_16x16x32_f16 v[26:29], v[62:65], v[38:41], v[26:29]
	v_mfma_f32_16x16x32_f16 v[14:17], v[70:73], v[38:41], v[14:17]
	ds_read_b128 v[38:41], v5
	ds_read_b128 v[46:49], v5 offset:2048
	ds_read_b128 v[74:77], v5 offset:4096
	ds_read_b128 v[78:81], v5 offset:6144
	ds_read_b128 v[82:85], v3 offset:16384
	ds_read_b128 v[86:89], v3 offset:18432
	v_mfma_f32_16x16x32_f16 v[66:69], v[62:65], v[50:53], v[66:69]
	v_mfma_f32_16x16x32_f16 v[22:25], v[70:73], v[50:53], v[22:25]
	v_mfma_f32_16x16x32_f16 v[42:45], v[62:65], v[54:57], v[42:45]
	v_mfma_f32_16x16x32_f16 v[34:37], v[70:73], v[54:57], v[34:37]
	v_mfma_f32_16x16x32_f16 v[10:13], v[62:65], v[58:61], v[10:13]
	v_mfma_f32_16x16x32_f16 v[18:21], v[70:73], v[58:61], v[18:21]
	s_waitcnt lgkmcnt(0)
	v_mfma_f32_16x16x32_f16 v[26:29], v[82:85], v[38:41], v[26:29]
	v_mfma_f32_16x16x32_f16 v[14:17], v[86:89], v[38:41], v[14:17]
	ds_read_b128 v[38:41], v0
	ds_read_b128 v[50:53], v0 offset:2048
	ds_read_b128 v[54:57], v0 offset:4096
	ds_read_b128 v[58:61], v0 offset:6144
	ds_read_b128 v[62:65], v4 offset:16384
	ds_read_b128 v[70:73], v4 offset:18432
	v_mfma_f32_16x16x32_f16 v[66:69], v[82:85], v[46:49], v[66:69]
	v_mfma_f32_16x16x32_f16 v[22:25], v[86:89], v[46:49], v[22:25]
	v_mfma_f32_16x16x32_f16 v[42:45], v[82:85], v[74:77], v[42:45]
	v_mfma_f32_16x16x32_f16 v[34:37], v[86:89], v[74:77], v[34:37]
	v_mfma_f32_16x16x32_f16 v[10:13], v[82:85], v[78:81], v[10:13]
	v_mfma_f32_16x16x32_f16 v[18:21], v[86:89], v[78:81], v[18:21]
	s_mov_b32 m0, s18
	s_add_u32 s18, s0, 0x700
	s_waitcnt vmcnt(0) lgkmcnt(0)
	s_barrier
	s_addc_u32 s19, s1, 0
	s_add_u32 s20, s4, 0x700
	global_load_lds_dwordx4 v1, s[18:19]
	s_mov_b32 m0, s15
	s_addc_u32 s21, s5, 0
	global_load_lds_dwordx4 v2, s[18:19]
	s_mov_b32 m0, s16
	s_nop 0
	global_load_lds_dwordx4 v1, s[20:21]
	s_mov_b32 m0, s17
	s_nop 0
	global_load_lds_dwordx4 v2, s[20:21]
	s_waitcnt lgkmcnt(0)
	v_mfma_f32_16x16x32_f16 v[26:29], v[62:65], v[38:41], v[26:29]
	v_mfma_f32_16x16x32_f16 v[14:17], v[70:73], v[38:41], v[14:17]
	ds_read_b128 v[38:41], v5 offset:32768
	ds_read_b128 v[46:49], v5 offset:34816
	ds_read_b128 v[74:77], v5 offset:36864
	ds_read_b128 v[78:81], v5 offset:38912
	ds_read_b128 v[82:85], v3 offset:49152
	ds_read_b128 v[86:89], v3 offset:51200
	v_mfma_f32_16x16x32_f16 v[66:69], v[62:65], v[50:53], v[66:69]
	v_mfma_f32_16x16x32_f16 v[22:25], v[70:73], v[50:53], v[22:25]
	v_mfma_f32_16x16x32_f16 v[42:45], v[62:65], v[54:57], v[42:45]
	v_mfma_f32_16x16x32_f16 v[34:37], v[70:73], v[54:57], v[34:37]
	v_mfma_f32_16x16x32_f16 v[10:13], v[62:65], v[58:61], v[10:13]
	v_mfma_f32_16x16x32_f16 v[18:21], v[70:73], v[58:61], v[18:21]
	s_waitcnt lgkmcnt(0)
	v_mfma_f32_16x16x32_f16 v[26:29], v[82:85], v[38:41], v[26:29]
	v_mfma_f32_16x16x32_f16 v[14:17], v[86:89], v[38:41], v[14:17]
	ds_read_b128 v[38:41], v0 offset:32768
	ds_read_b128 v[50:53], v0 offset:34816
	ds_read_b128 v[54:57], v0 offset:36864
	ds_read_b128 v[58:61], v0 offset:38912
	ds_read_b128 v[62:65], v4 offset:49152
	ds_read_b128 v[70:73], v4 offset:51200
	v_mfma_f32_16x16x32_f16 v[66:69], v[82:85], v[46:49], v[66:69]
	v_mfma_f32_16x16x32_f16 v[22:25], v[86:89], v[46:49], v[22:25]
	v_mfma_f32_16x16x32_f16 v[42:45], v[82:85], v[74:77], v[42:45]
	v_mfma_f32_16x16x32_f16 v[34:37], v[86:89], v[74:77], v[34:37]
	v_mfma_f32_16x16x32_f16 v[10:13], v[82:85], v[78:81], v[10:13]
	v_mfma_f32_16x16x32_f16 v[18:21], v[86:89], v[78:81], v[18:21]
	s_add_u32 s0, s0, 0x780
	s_mov_b32 m0, s14
	s_waitcnt vmcnt(0) lgkmcnt(0)
	s_barrier
	s_addc_u32 s1, s1, 0
	s_add_u32 s4, s4, 0x780
	global_load_lds_dwordx4 v1, s[0:1]
	s_mov_b32 m0, s3
	s_addc_u32 s5, s5, 0
	global_load_lds_dwordx4 v2, s[0:1]
	s_mov_b32 m0, s6
	s_nop 0
	global_load_lds_dwordx4 v1, s[4:5]
	s_mov_b32 m0, s7
	s_nop 0
	global_load_lds_dwordx4 v2, s[4:5]
	s_waitcnt lgkmcnt(0)
	v_mfma_f32_16x16x32_f16 v[26:29], v[62:65], v[38:41], v[26:29]
	v_mfma_f32_16x16x32_f16 v[14:17], v[70:73], v[38:41], v[14:17]
	ds_read_b128 v[38:41], v5
	ds_read_b128 v[46:49], v5 offset:2048
	ds_read_b128 v[74:77], v5 offset:4096
	ds_read_b128 v[78:81], v5 offset:6144
	ds_read_b128 v[82:85], v3 offset:16384
	ds_read_b128 v[86:89], v3 offset:18432
	v_mfma_f32_16x16x32_f16 v[66:69], v[62:65], v[50:53], v[66:69]
	v_mfma_f32_16x16x32_f16 v[22:25], v[70:73], v[50:53], v[22:25]
	v_mfma_f32_16x16x32_f16 v[42:45], v[62:65], v[54:57], v[42:45]
	v_mfma_f32_16x16x32_f16 v[34:37], v[70:73], v[54:57], v[34:37]
	v_mfma_f32_16x16x32_f16 v[10:13], v[62:65], v[58:61], v[10:13]
	v_mfma_f32_16x16x32_f16 v[18:21], v[70:73], v[58:61], v[18:21]
	s_waitcnt lgkmcnt(0)
	v_mfma_f32_16x16x32_f16 v[26:29], v[82:85], v[38:41], v[26:29]
	v_mfma_f32_16x16x32_f16 v[14:17], v[86:89], v[38:41], v[14:17]
	ds_read_b128 v[38:41], v0
	ds_read_b128 v[50:53], v0 offset:2048
	ds_read_b128 v[54:57], v0 offset:4096
	ds_read_b128 v[58:61], v0 offset:6144
	ds_read_b128 v[62:65], v4 offset:16384
	ds_read_b128 v[70:73], v4 offset:18432
	v_mfma_f32_16x16x32_f16 v[66:69], v[82:85], v[46:49], v[66:69]
	v_mfma_f32_16x16x32_f16 v[22:25], v[86:89], v[46:49], v[22:25]
	v_mfma_f32_16x16x32_f16 v[42:45], v[82:85], v[74:77], v[42:45]
	v_mfma_f32_16x16x32_f16 v[34:37], v[86:89], v[74:77], v[34:37]
	v_mfma_f32_16x16x32_f16 v[10:13], v[82:85], v[78:81], v[10:13]
	v_mfma_f32_16x16x32_f16 v[18:21], v[86:89], v[78:81], v[18:21]
	s_waitcnt vmcnt(0) lgkmcnt(0)
	s_barrier
	s_waitcnt lgkmcnt(0)
	v_mfma_f32_16x16x32_f16 v[26:29], v[62:65], v[38:41], v[26:29]
	v_mfma_f32_16x16x32_f16 v[14:17], v[70:73], v[38:41], v[14:17]
	ds_read_b128 v[38:41], v5 offset:32768
	ds_read_b128 v[46:49], v5 offset:34816
	ds_read_b128 v[74:77], v5 offset:36864
	ds_read_b128 v[78:81], v5 offset:38912
	ds_read_b128 v[82:85], v3 offset:49152
	ds_read_b128 v[86:89], v3 offset:51200
	v_mfma_f32_16x16x32_f16 v[66:69], v[62:65], v[50:53], v[66:69]
	v_mfma_f32_16x16x32_f16 v[22:25], v[70:73], v[50:53], v[22:25]
	v_mfma_f32_16x16x32_f16 v[42:45], v[62:65], v[54:57], v[42:45]
	v_mfma_f32_16x16x32_f16 v[34:37], v[70:73], v[54:57], v[34:37]
	v_mfma_f32_16x16x32_f16 v[10:13], v[62:65], v[58:61], v[10:13]
	v_mfma_f32_16x16x32_f16 v[18:21], v[70:73], v[58:61], v[18:21]
	s_waitcnt lgkmcnt(0)
	v_mfma_f32_16x16x32_f16 v[26:29], v[82:85], v[38:41], v[26:29]
	v_mfma_f32_16x16x32_f16 v[14:17], v[86:89], v[38:41], v[14:17]
	ds_read_b128 v[38:41], v0 offset:32768
	ds_read_b128 v[50:53], v0 offset:34816
	ds_read_b128 v[54:57], v0 offset:36864
	ds_read_b128 v[0:3], v0 offset:38912
	ds_read_b128 v[58:61], v4 offset:49152
	ds_read_b128 v[62:65], v4 offset:51200
	v_mfma_f32_16x16x32_f16 v[4:7], v[82:85], v[46:49], v[66:69]
	v_mfma_f32_16x16x32_f16 v[22:25], v[86:89], v[46:49], v[22:25]
	v_mfma_f32_16x16x32_f16 v[42:45], v[82:85], v[74:77], v[42:45]
	v_mfma_f32_16x16x32_f16 v[34:37], v[86:89], v[74:77], v[34:37]
	v_mfma_f32_16x16x32_f16 v[10:13], v[82:85], v[78:81], v[10:13]
	v_mfma_f32_16x16x32_f16 v[46:49], v[86:89], v[78:81], v[18:21]
	s_waitcnt lgkmcnt(0)
	v_mfma_f32_16x16x32_f16 v[66:69], v[58:61], v[38:41], v[26:29]
	v_mfma_f32_16x16x32_f16 v[38:41], v[62:65], v[38:41], v[14:17]
	v_mfma_f32_16x16x32_f16 v[28:31], v[58:61], v[50:53], v[4:7]
	v_mfma_f32_16x16x32_f16 v[24:27], v[62:65], v[50:53], v[22:25]
	v_mfma_f32_16x16x32_f16 v[20:23], v[58:61], v[54:57], v[42:45]
	v_mfma_f32_16x16x32_f16 v[16:19], v[62:65], v[54:57], v[34:37]
	v_mfma_f32_16x16x32_f16 v[4:7], v[58:61], v[0:3], v[10:13]
	v_mfma_f32_16x16x32_f16 v[0:3], v[62:65], v[0:3], v[46:49]
	v_lshlrev_b32_e32 v9, 2, v9
	v_or3_b32 v34, v9, v8, s13
	v_mov_b32_e32 v35, 0
	v_lshl_add_u64 v[36:37], v[34:35], 2, s[10:11]
	global_load_dwordx4 v[8:11], v[36:37], off
	global_load_dwordx4 v[12:15], v[36:37], off offset:64
	v_or_b32_e32 v36, s12, v32
	v_mad_u64_u32 v[42:43], s[18:19], v36, s2, 0
	s_ashr_i32 s1, s2, 31
	s_mov_b32 s16, 0xbf3a00e3
	v_mov_b32_e32 v44, v43
	v_mov_b64_e32 v[32:33], s[16:17]
	v_mad_u64_u32 v[44:45], s[16:17], v36, s1, v[44:45]
	s_mov_b32 s14, 0x3e6d3388
	v_mov_b32_e32 v43, v44
	s_mov_b32 s10, 0x3f07dc22
	s_mov_b32 s6, 0xbf38aa3b
	s_mov_b32 s12, 0x3f35f0e3
	s_mov_b32 s0, 0xbe11a98e
	s_mov_b32 s4, 0x3e027906
	v_lshlrev_b64 v[34:35], 1, v[34:35]
	v_lshl_add_u64 v[42:43], v[42:43], 1, s[8:9]
	v_lshl_add_u64 v[42:43], v[42:43], 0, v[34:35]
	s_waitcnt vmcnt(0)
	v_pk_add_f32 v[46:47], v[66:67], v[8:9]
	v_pk_add_f32 v[44:45], v[68:69], v[10:11]
	v_and_b32_e32 v49, 0x7fffffff, v47
	v_and_b32_e32 v48, 0x7fffffff, v46
	v_and_b32_e32 v55, 0x7fffffff, v45
	v_and_b32_e32 v54, 0x7fffffff, v44
	v_pk_fma_f32 v[48:49], v[48:49], s[14:15], 1.0 op_sel_hi:[1,0,0]
	v_pk_add_f32 v[38:39], v[38:39], v[12:13]
	v_pk_fma_f32 v[54:55], v[54:55], s[14:15], 1.0 op_sel_hi:[1,0,0]
	v_rcp_f32_e32 v48, v48
	v_rcp_f32_e32 v49, v49
	v_and_b32_e32 v57, 0x7fffffff, v39
	v_and_b32_e32 v56, 0x7fffffff, v38
	v_rcp_f32_e32 v54, v54
	v_rcp_f32_e32 v55, v55
	v_pk_fma_f32 v[56:57], v[56:57], s[14:15], 1.0 op_sel_hi:[1,0,0]
	v_pk_mul_f32 v[52:53], v[46:47], v[46:47]
	v_rcp_f32_e32 v56, v56
	v_rcp_f32_e32 v57, v57
	v_pk_mul_f32 v[50:51], v[44:45], v[44:45]
	v_pk_mul_f32 v[52:53], v[52:53], s[6:7] op_sel_hi:[1,0]
	v_pk_fma_f32 v[64:65], v[48:49], s[10:11], v[32:33] op_sel_hi:[1,0,0]
	v_pk_mul_f32 v[50:51], v[50:51], s[6:7] op_sel_hi:[1,0]
	v_exp_f32_e32 v52, v52
	v_exp_f32_e32 v53, v53
	v_pk_fma_f32 v[66:67], v[54:55], s[10:11], v[32:33] op_sel_hi:[1,0,0]
	v_pk_fma_f32 v[64:65], v[48:49], v[64:65], s[12:13] op_sel_hi:[1,1,0]
	v_pk_mul_f32 v[60:61], v[38:39], v[38:39]
	v_exp_f32_e32 v50, v50
	v_exp_f32_e32 v51, v51
	v_pk_fma_f32 v[66:67], v[54:55], v[66:67], s[12:13] op_sel_hi:[1,1,0]
	v_pk_fma_f32 v[64:65], v[48:49], v[64:65], s[0:1] op_sel_hi:[1,1,0]
	v_pk_mul_f32 v[60:61], v[60:61], s[6:7] op_sel_hi:[1,0]
	v_pk_fma_f32 v[68:69], v[56:57], s[10:11], v[32:33] op_sel_hi:[1,0,0]
	v_pk_fma_f32 v[66:67], v[54:55], v[66:67], s[0:1] op_sel_hi:[1,1,0]
	v_pk_fma_f32 v[64:65], v[48:49], v[64:65], s[4:5] op_sel_hi:[1,1,0]
	v_exp_f32_e32 v60, v60
	v_exp_f32_e32 v61, v61
	v_pk_fma_f32 v[68:69], v[56:57], v[68:69], s[12:13] op_sel_hi:[1,1,0]
	v_pk_fma_f32 v[66:67], v[54:55], v[66:67], s[4:5] op_sel_hi:[1,1,0]
	v_pk_mul_f32 v[48:49], v[48:49], v[64:65]
	v_pk_add_f32 v[40:41], v[40:41], v[14:15]
	v_pk_fma_f32 v[68:69], v[56:57], v[68:69], s[0:1] op_sel_hi:[1,1,0]
	v_pk_mul_f32 v[54:55], v[54:55], v[66:67]
	v_pk_mul_f32 v[48:49], v[52:53], v[48:49]
	v_and_b32_e32 v63, 0x7fffffff, v41
	v_and_b32_e32 v62, 0x7fffffff, v40
	v_pk_fma_f32 v[68:69], v[56:57], v[68:69], s[4:5] op_sel_hi:[1,1,0]
	v_pk_mul_f32 v[50:51], v[50:51], v[54:55]
	v_pk_mul_f32 v[54:55], v[46:47], v[48:49]
	v_pk_fma_f32 v[48:49], v[46:47], v[48:49], v[46:47] neg_lo:[1,0,0] neg_hi:[1,0,0]
	v_cmp_gt_f32_e32 vcc, 0, v46
	v_pk_fma_f32 v[62:63], v[62:63], s[14:15], 1.0 op_sel_hi:[1,0,0]
	v_pk_mul_f32 v[56:57], v[56:57], v[68:69]
	v_cndmask_b32_e32 v37, v48, v54, vcc
	v_cmp_gt_f32_e32 vcc, 0, v47
	v_rcp_f32_e32 v62, v62
	v_rcp_f32_e32 v63, v63
	v_pk_mul_f32 v[52:53], v[60:61], v[56:57]
	v_pk_mul_f32 v[56:57], v[44:45], v[50:51]
	v_pk_fma_f32 v[50:51], v[44:45], v[50:51], v[44:45] neg_lo:[1,0,0] neg_hi:[1,0,0]
	v_cndmask_b32_e32 v46, v49, v55, vcc
	v_cmp_gt_f32_e32 vcc, 0, v44
	v_pk_mul_f32 v[58:59], v[40:41], v[40:41]
	v_pk_mul_f32 v[60:61], v[38:39], v[52:53]
	v_cndmask_b32_e32 v44, v50, v56, vcc
	v_cmp_gt_f32_e32 vcc, 0, v45
	v_pk_fma_f32 v[52:53], v[38:39], v[52:53], v[38:39] neg_lo:[1,0,0] neg_hi:[1,0,0]
	v_pk_add_f32 v[28:29], v[28:29], v[8:9]
	v_cndmask_b32_e32 v45, v51, v57, vcc
	v_cmp_gt_f32_e32 vcc, 0, v38
	v_cvt_pk_f16_f32 v45, v44, v45
	v_cvt_pk_f16_f32 v44, v37, v46
	v_cndmask_b32_e32 v47, v52, v60, vcc
	global_store_dwordx2 v[42:43], v[44:45], off
	v_cmp_gt_f32_e32 vcc, 0, v39
	v_pk_fma_f32 v[38:39], v[62:63], s[10:11], v[32:33] op_sel_hi:[1,0,0]
	v_pk_mul_f32 v[44:45], v[58:59], s[6:7] op_sel_hi:[1,0]
	v_pk_fma_f32 v[38:39], v[62:63], v[38:39], s[12:13] op_sel_hi:[1,1,0]
	v_exp_f32_e32 v44, v44
	v_exp_f32_e32 v45, v45
	v_pk_fma_f32 v[38:39], v[62:63], v[38:39], s[0:1] op_sel_hi:[1,1,0]
	v_cndmask_b32_e32 v37, v53, v61, vcc
	v_pk_fma_f32 v[38:39], v[62:63], v[38:39], s[4:5] op_sel_hi:[1,1,0]
	v_cmp_gt_f32_e32 vcc, 0, v40
	v_pk_mul_f32 v[38:39], v[62:63], v[38:39]
	v_pk_add_f32 v[30:31], v[30:31], v[10:11]
	v_pk_mul_f32 v[38:39], v[44:45], v[38:39]
	v_and_b32_e32 v46, 0x7fffffff, v30
	v_pk_mul_f32 v[44:45], v[40:41], v[38:39]
	v_pk_fma_f32 v[38:39], v[40:41], v[38:39], v[40:41] neg_lo:[1,0,0] neg_hi:[1,0,0]
	v_pk_add_f32 v[24:25], v[24:25], v[12:13]
	v_cndmask_b32_e32 v38, v38, v44, vcc
	v_cmp_gt_f32_e32 vcc, 0, v41
	v_pk_add_f32 v[26:27], v[26:27], v[14:15]
	v_pk_add_f32 v[20:21], v[20:21], v[8:9]
	v_cndmask_b32_e32 v39, v39, v45, vcc
	v_cvt_pk_f16_f32 v39, v38, v39
	v_cvt_pk_f16_f32 v38, v47, v37
	global_store_dwordx2 v[42:43], v[38:39], off offset:32
	v_and_b32_e32 v43, 0x7fffffff, v29
	v_and_b32_e32 v42, 0x7fffffff, v28
	v_pk_fma_f32 v[42:43], v[42:43], s[14:15], 1.0 op_sel_hi:[1,0,0]
	v_or_b32_e32 v37, 16, v36
	v_rcp_f32_e32 v42, v42
	v_rcp_f32_e32 v43, v43
	v_mad_u64_u32 v[38:39], s[16:17], v37, s2, 0
	v_mov_b32_e32 v40, v39
	v_mad_u64_u32 v[40:41], s[16:17], v37, s1, v[40:41]
	v_pk_mul_f32 v[44:45], v[28:29], v[28:29]
	v_mov_b32_e32 v39, v40
	v_pk_fma_f32 v[40:41], v[42:43], s[10:11], v[32:33] op_sel_hi:[1,0,0]
	v_pk_mul_f32 v[44:45], v[44:45], s[6:7] op_sel_hi:[1,0]
	v_pk_fma_f32 v[40:41], v[42:43], v[40:41], s[12:13] op_sel_hi:[1,1,0]
	v_exp_f32_e32 v44, v44
	v_exp_f32_e32 v45, v45
	v_pk_fma_f32 v[40:41], v[42:43], v[40:41], s[0:1] op_sel_hi:[1,1,0]
	v_and_b32_e32 v47, 0x7fffffff, v31
	v_pk_fma_f32 v[40:41], v[42:43], v[40:41], s[4:5] op_sel_hi:[1,1,0]
	v_pk_fma_f32 v[46:47], v[46:47], s[14:15], 1.0 op_sel_hi:[1,0,0]
	v_pk_mul_f32 v[40:41], v[42:43], v[40:41]
	v_rcp_f32_e32 v46, v46
	v_rcp_f32_e32 v47, v47
	v_pk_mul_f32 v[40:41], v[44:45], v[40:41]
	v_cmp_gt_f32_e32 vcc, 0, v28
	v_pk_mul_f32 v[44:45], v[28:29], v[40:41]
	v_pk_fma_f32 v[40:41], v[28:29], v[40:41], v[28:29] neg_lo:[1,0,0] neg_hi:[1,0,0]
	v_pk_mul_f32 v[42:43], v[30:31], v[30:31]
	v_cndmask_b32_e32 v37, v40, v44, vcc
	v_cmp_gt_f32_e32 vcc, 0, v29
	v_pk_fma_f32 v[28:29], v[46:47], s[10:11], v[32:33] op_sel_hi:[1,0,0]
	v_lshl_add_u64 v[38:39], v[38:39], 1, s[8:9]
	v_cndmask_b32_e32 v44, v41, v45, vcc
	v_pk_mul_f32 v[40:41], v[42:43], s[6:7] op_sel_hi:[1,0]
	v_pk_fma_f32 v[28:29], v[46:47], v[28:29], s[12:13] op_sel_hi:[1,1,0]
	v_exp_f32_e32 v40, v40
	v_exp_f32_e32 v41, v41
	v_pk_fma_f32 v[28:29], v[46:47], v[28:29], s[0:1] op_sel_hi:[1,1,0]
	v_cmp_gt_f32_e32 vcc, 0, v30
	v_pk_fma_f32 v[28:29], v[46:47], v[28:29], s[4:5] op_sel_hi:[1,1,0]
	v_lshl_add_u64 v[38:39], v[38:39], 0, v[34:35]
	v_pk_mul_f32 v[28:29], v[46:47], v[28:29]
	v_and_b32_e32 v43, 0x7fffffff, v27
	v_pk_mul_f32 v[28:29], v[40:41], v[28:29]
	v_and_b32_e32 v42, 0x7fffffff, v26
	v_pk_mul_f32 v[40:41], v[30:31], v[28:29]
	v_pk_fma_f32 v[28:29], v[30:31], v[28:29], v[30:31] neg_lo:[1,0,0] neg_hi:[1,0,0]
	v_and_b32_e32 v30, 0x7fffffff, v24
	v_cndmask_b32_e32 v28, v28, v40, vcc
	v_cmp_gt_f32_e32 vcc, 0, v31
	v_and_b32_e32 v31, 0x7fffffff, v25
	v_pk_fma_f32 v[30:31], v[30:31], s[14:15], 1.0 op_sel_hi:[1,0,0]
	v_cndmask_b32_e32 v29, v29, v41, vcc
	v_rcp_f32_e32 v30, v30
	v_rcp_f32_e32 v31, v31
	v_cvt_pk_f16_f32 v29, v28, v29
	v_cvt_pk_f16_f32 v28, v37, v44
	v_pk_mul_f32 v[40:41], v[24:25], v[24:25]
	global_store_dwordx2 v[38:39], v[28:29], off
	v_pk_fma_f32 v[28:29], v[30:31], s[10:11], v[32:33] op_sel_hi:[1,0,0]
	v_pk_mul_f32 v[40:41], v[40:41], s[6:7] op_sel_hi:[1,0]
	v_pk_fma_f32 v[28:29], v[30:31], v[28:29], s[12:13] op_sel_hi:[1,1,0]
	v_exp_f32_e32 v40, v40
	v_exp_f32_e32 v41, v41
	v_pk_fma_f32 v[28:29], v[30:31], v[28:29], s[0:1] op_sel_hi:[1,1,0]
	v_pk_fma_f32 v[42:43], v[42:43], s[14:15], 1.0 op_sel_hi:[1,0,0]
	v_pk_fma_f32 v[28:29], v[30:31], v[28:29], s[4:5] op_sel_hi:[1,1,0]
	v_rcp_f32_e32 v42, v42
	v_pk_mul_f32 v[28:29], v[30:31], v[28:29]
	v_rcp_f32_e32 v43, v43
	v_pk_mul_f32 v[28:29], v[40:41], v[28:29]
	v_cmp_gt_f32_e32 vcc, 0, v24
	v_pk_mul_f32 v[40:41], v[24:25], v[28:29]
	v_pk_fma_f32 v[28:29], v[24:25], v[28:29], v[24:25] neg_lo:[1,0,0] neg_hi:[1,0,0]
	v_pk_mul_f32 v[30:31], v[26:27], v[26:27]
	v_cndmask_b32_e32 v37, v28, v40, vcc
	v_cmp_gt_f32_e32 vcc, 0, v25
	v_pk_fma_f32 v[24:25], v[42:43], s[10:11], v[32:33] op_sel_hi:[1,0,0]
	v_pk_add_f32 v[22:23], v[22:23], v[10:11]
	v_cndmask_b32_e32 v40, v29, v41, vcc
	v_pk_mul_f32 v[28:29], v[30:31], s[6:7] op_sel_hi:[1,0]
	v_pk_fma_f32 v[24:25], v[42:43], v[24:25], s[12:13] op_sel_hi:[1,1,0]
	v_exp_f32_e32 v28, v28
	v_exp_f32_e32 v29, v29
	v_pk_fma_f32 v[24:25], v[42:43], v[24:25], s[0:1] op_sel_hi:[1,1,0]
	v_cmp_gt_f32_e32 vcc, 0, v26
	v_pk_fma_f32 v[24:25], v[42:43], v[24:25], s[4:5] op_sel_hi:[1,1,0]
	v_pk_mul_f32 v[30:31], v[20:21], v[20:21]
	v_pk_mul_f32 v[24:25], v[42:43], v[24:25]
	v_pk_mul_f32 v[30:31], v[30:31], s[6:7] op_sel_hi:[1,0]
	v_pk_mul_f32 v[24:25], v[28:29], v[24:25]
	v_exp_f32_e32 v30, v30
	v_pk_mul_f32 v[28:29], v[26:27], v[24:25]
	v_pk_fma_f32 v[24:25], v[26:27], v[24:25], v[26:27] neg_lo:[1,0,0] neg_hi:[1,0,0]
	v_exp_f32_e32 v31, v31
	v_cndmask_b32_e32 v24, v24, v28, vcc
	v_cmp_gt_f32_e32 vcc, 0, v27
	v_and_b32_e32 v28, 0x7fffffff, v20
	v_or_b32_e32 v27, 32, v36
	v_cndmask_b32_e32 v25, v25, v29, vcc
	v_and_b32_e32 v29, 0x7fffffff, v21
	v_pk_fma_f32 v[28:29], v[28:29], s[14:15], 1.0 op_sel_hi:[1,0,0]
	v_cvt_pk_f16_f32 v25, v24, v25
	v_cvt_pk_f16_f32 v24, v37, v40
	v_rcp_f32_e32 v28, v28
	v_rcp_f32_e32 v29, v29
	global_store_dwordx2 v[38:39], v[24:25], off offset:32
	v_mad_u64_u32 v[24:25], s[16:17], v27, s2, 0
	v_mov_b32_e32 v26, v25
	v_mad_u64_u32 v[26:27], s[16:17], v27, s1, v[26:27]
	v_mov_b32_e32 v25, v26
	v_pk_fma_f32 v[26:27], v[28:29], s[10:11], v[32:33] op_sel_hi:[1,0,0]
	v_and_b32_e32 v39, 0x7fffffff, v23
	v_pk_fma_f32 v[26:27], v[28:29], v[26:27], s[12:13] op_sel_hi:[1,1,0]
	v_and_b32_e32 v38, 0x7fffffff, v22
	v_pk_fma_f32 v[26:27], v[28:29], v[26:27], s[0:1] op_sel_hi:[1,1,0]
	v_pk_fma_f32 v[38:39], v[38:39], s[14:15], 1.0 op_sel_hi:[1,0,0]
	v_pk_fma_f32 v[26:27], v[28:29], v[26:27], s[4:5] op_sel_hi:[1,1,0]
	v_rcp_f32_e32 v38, v38
	v_pk_mul_f32 v[26:27], v[28:29], v[26:27]
	v_rcp_f32_e32 v39, v39
	v_pk_mul_f32 v[26:27], v[30:31], v[26:27]
	v_cmp_gt_f32_e32 vcc, 0, v20
	v_pk_mul_f32 v[30:31], v[20:21], v[26:27]
	v_pk_fma_f32 v[26:27], v[20:21], v[26:27], v[20:21] neg_lo:[1,0,0] neg_hi:[1,0,0]
	v_pk_mul_f32 v[28:29], v[22:23], v[22:23]
	v_cndmask_b32_e32 v30, v26, v30, vcc
	v_cmp_gt_f32_e32 vcc, 0, v21
	v_pk_fma_f32 v[20:21], v[38:39], s[10:11], v[32:33] op_sel_hi:[1,0,0]
	v_pk_add_f32 v[16:17], v[16:17], v[12:13]
	v_cndmask_b32_e32 v31, v27, v31, vcc
	v_pk_mul_f32 v[26:27], v[28:29], s[6:7] op_sel_hi:[1,0]
	v_pk_fma_f32 v[20:21], v[38:39], v[20:21], s[12:13] op_sel_hi:[1,1,0]
	v_exp_f32_e32 v26, v26
	v_exp_f32_e32 v27, v27
	v_pk_fma_f32 v[20:21], v[38:39], v[20:21], s[0:1] op_sel_hi:[1,1,0]
	v_cmp_gt_f32_e32 vcc, 0, v22
	v_pk_fma_f32 v[20:21], v[38:39], v[20:21], s[4:5] op_sel_hi:[1,1,0]
	v_lshl_add_u64 v[24:25], v[24:25], 1, s[8:9]
	v_pk_mul_f32 v[20:21], v[38:39], v[20:21]
	v_lshl_add_u64 v[24:25], v[24:25], 0, v[34:35]
	v_pk_mul_f32 v[20:21], v[26:27], v[20:21]
	v_pk_add_f32 v[18:19], v[18:19], v[14:15]
	v_pk_mul_f32 v[26:27], v[22:23], v[20:21]
	v_pk_fma_f32 v[20:21], v[22:23], v[20:21], v[22:23] neg_lo:[1,0,0] neg_hi:[1,0,0]
	v_and_b32_e32 v22, 0x7fffffff, v16
	v_cndmask_b32_e32 v20, v20, v26, vcc
	v_cmp_gt_f32_e32 vcc, 0, v23
	v_and_b32_e32 v23, 0x7fffffff, v17
	v_pk_fma_f32 v[22:23], v[22:23], s[14:15], 1.0 op_sel_hi:[1,0,0]
	v_cndmask_b32_e32 v21, v21, v27, vcc
	v_rcp_f32_e32 v22, v22
	v_rcp_f32_e32 v23, v23
	v_cvt_pk_f16_f32 v21, v20, v21
	v_cvt_pk_f16_f32 v20, v30, v31
	v_pk_mul_f32 v[26:27], v[16:17], v[16:17]
	global_store_dwordx2 v[24:25], v[20:21], off
	v_pk_fma_f32 v[20:21], v[22:23], s[10:11], v[32:33] op_sel_hi:[1,0,0]
	v_pk_mul_f32 v[26:27], v[26:27], s[6:7] op_sel_hi:[1,0]
	v_pk_fma_f32 v[20:21], v[22:23], v[20:21], s[12:13] op_sel_hi:[1,1,0]
	v_exp_f32_e32 v26, v26
	v_exp_f32_e32 v27, v27
	v_pk_fma_f32 v[20:21], v[22:23], v[20:21], s[0:1] op_sel_hi:[1,1,0]
	v_and_b32_e32 v29, 0x7fffffff, v19
	v_and_b32_e32 v28, 0x7fffffff, v18
	v_pk_fma_f32 v[20:21], v[22:23], v[20:21], s[4:5] op_sel_hi:[1,1,0]
	v_pk_fma_f32 v[28:29], v[28:29], s[14:15], 1.0 op_sel_hi:[1,0,0]
	v_pk_mul_f32 v[20:21], v[22:23], v[20:21]
	v_rcp_f32_e32 v28, v28
	v_rcp_f32_e32 v29, v29
	v_pk_mul_f32 v[20:21], v[26:27], v[20:21]
	v_cmp_gt_f32_e32 vcc, 0, v16
	v_pk_mul_f32 v[26:27], v[16:17], v[20:21]
	v_pk_fma_f32 v[20:21], v[16:17], v[20:21], v[16:17] neg_lo:[1,0,0] neg_hi:[1,0,0]
	v_pk_mul_f32 v[22:23], v[18:19], v[18:19]
	v_cndmask_b32_e32 v26, v20, v26, vcc
	v_cmp_gt_f32_e32 vcc, 0, v17
	v_pk_fma_f32 v[16:17], v[28:29], s[10:11], v[32:33] op_sel_hi:[1,0,0]
	v_pk_add_f32 v[4:5], v[4:5], v[8:9]
	v_cndmask_b32_e32 v27, v21, v27, vcc
	v_pk_mul_f32 v[20:21], v[22:23], s[6:7] op_sel_hi:[1,0]
	v_pk_fma_f32 v[16:17], v[28:29], v[16:17], s[12:13] op_sel_hi:[1,1,0]
	v_exp_f32_e32 v20, v20
	v_exp_f32_e32 v21, v21
	v_pk_fma_f32 v[16:17], v[28:29], v[16:17], s[0:1] op_sel_hi:[1,1,0]
	v_cmp_gt_f32_e32 vcc, 0, v18
	v_pk_fma_f32 v[16:17], v[28:29], v[16:17], s[4:5] op_sel_hi:[1,1,0]
	v_and_b32_e32 v9, 0x7fffffff, v5
	v_pk_mul_f32 v[16:17], v[28:29], v[16:17]
	v_and_b32_e32 v8, 0x7fffffff, v4
	v_pk_mul_f32 v[16:17], v[20:21], v[16:17]
	v_pk_fma_f32 v[8:9], v[8:9], s[14:15], 1.0 op_sel_hi:[1,0,0]
	v_pk_mul_f32 v[20:21], v[18:19], v[16:17]
	v_pk_fma_f32 v[16:17], v[18:19], v[16:17], v[18:19] neg_lo:[1,0,0] neg_hi:[1,0,0]
	v_rcp_f32_e32 v8, v8
	v_cndmask_b32_e32 v16, v16, v20, vcc
	v_cmp_gt_f32_e32 vcc, 0, v19
	v_or_b32_e32 v19, 48, v36
	v_rcp_f32_e32 v9, v9
	v_cndmask_b32_e32 v17, v17, v21, vcc
	v_cvt_pk_f16_f32 v17, v16, v17
	v_cvt_pk_f16_f32 v16, v26, v27
	global_store_dwordx2 v[24:25], v[16:17], off offset:32
	v_mad_u64_u32 v[16:17], s[2:3], v19, s2, 0
	v_mov_b32_e32 v18, v17
	v_mad_u64_u32 v[18:19], s[2:3], v19, s1, v[18:19]
	v_mov_b32_e32 v17, v18
	v_pk_mul_f32 v[18:19], v[4:5], v[4:5]
	v_pk_add_f32 v[6:7], v[6:7], v[10:11]
	v_pk_fma_f32 v[10:11], v[8:9], s[10:11], v[32:33] op_sel_hi:[1,0,0]
	v_pk_mul_f32 v[18:19], v[18:19], s[6:7] op_sel_hi:[1,0]
	v_pk_fma_f32 v[10:11], v[8:9], v[10:11], s[12:13] op_sel_hi:[1,1,0]
	v_exp_f32_e32 v18, v18
	v_exp_f32_e32 v19, v19
	v_pk_fma_f32 v[10:11], v[8:9], v[10:11], s[0:1] op_sel_hi:[1,1,0]
	v_and_b32_e32 v21, 0x7fffffff, v7
	v_and_b32_e32 v20, 0x7fffffff, v6
	v_pk_fma_f32 v[10:11], v[8:9], v[10:11], s[4:5] op_sel_hi:[1,1,0]
	v_pk_fma_f32 v[20:21], v[20:21], s[14:15], 1.0 op_sel_hi:[1,0,0]
	v_pk_mul_f32 v[8:9], v[8:9], v[10:11]
	v_rcp_f32_e32 v20, v20
	v_rcp_f32_e32 v21, v21
	v_pk_mul_f32 v[8:9], v[18:19], v[8:9]
	v_cmp_gt_f32_e32 vcc, 0, v4
	v_pk_mul_f32 v[18:19], v[4:5], v[8:9]
	v_pk_fma_f32 v[8:9], v[4:5], v[8:9], v[4:5] neg_lo:[1,0,0] neg_hi:[1,0,0]
	v_pk_mul_f32 v[10:11], v[6:7], v[6:7]
	v_cndmask_b32_e32 v18, v8, v18, vcc
	v_cmp_gt_f32_e32 vcc, 0, v5
	v_pk_fma_f32 v[4:5], v[20:21], s[10:11], v[32:33] op_sel_hi:[1,0,0]
	v_pk_add_f32 v[0:1], v[0:1], v[12:13]
	v_cndmask_b32_e32 v19, v9, v19, vcc
	v_pk_mul_f32 v[8:9], v[10:11], s[6:7] op_sel_hi:[1,0]
	v_pk_fma_f32 v[4:5], v[20:21], v[4:5], s[12:13] op_sel_hi:[1,1,0]
	v_exp_f32_e32 v8, v8
	v_exp_f32_e32 v9, v9
	v_pk_fma_f32 v[4:5], v[20:21], v[4:5], s[0:1] op_sel_hi:[1,1,0]
	v_cmp_gt_f32_e32 vcc, 0, v6
	v_pk_fma_f32 v[4:5], v[20:21], v[4:5], s[4:5] op_sel_hi:[1,1,0]
	v_lshl_add_u64 v[16:17], v[16:17], 1, s[8:9]
	v_pk_mul_f32 v[4:5], v[20:21], v[4:5]
	v_pk_mul_f32 v[10:11], v[0:1], v[0:1]
	v_pk_mul_f32 v[4:5], v[8:9], v[4:5]
	v_pk_mul_f32 v[10:11], v[10:11], s[6:7] op_sel_hi:[1,0]
	v_pk_mul_f32 v[8:9], v[6:7], v[4:5]
	v_pk_fma_f32 v[4:5], v[6:7], v[4:5], v[6:7] neg_lo:[1,0,0] neg_hi:[1,0,0]
	v_and_b32_e32 v6, 0x7fffffff, v0
	v_cndmask_b32_e32 v4, v4, v8, vcc
	v_cmp_gt_f32_e32 vcc, 0, v7
	v_and_b32_e32 v7, 0x7fffffff, v1
	v_pk_fma_f32 v[6:7], v[6:7], s[14:15], 1.0 op_sel_hi:[1,0,0]
	v_cndmask_b32_e32 v5, v5, v9, vcc
	v_rcp_f32_e32 v6, v6
	v_rcp_f32_e32 v7, v7
	v_cvt_pk_f16_f32 v5, v4, v5
	v_cvt_pk_f16_f32 v4, v18, v19
	v_lshl_add_u64 v[8:9], v[16:17], 0, v[34:35]
	global_store_dwordx2 v[8:9], v[4:5], off
	v_pk_fma_f32 v[4:5], v[6:7], s[10:11], v[32:33] op_sel_hi:[1,0,0]
	v_pk_add_f32 v[2:3], v[2:3], v[14:15]
	v_pk_fma_f32 v[4:5], v[6:7], v[4:5], s[12:13] op_sel_hi:[1,1,0]
	v_exp_f32_e32 v10, v10
	v_exp_f32_e32 v11, v11
	v_pk_fma_f32 v[4:5], v[6:7], v[4:5], s[0:1] op_sel_hi:[1,1,0]
	v_and_b32_e32 v13, 0x7fffffff, v3
	v_and_b32_e32 v12, 0x7fffffff, v2
	v_pk_fma_f32 v[4:5], v[6:7], v[4:5], s[4:5] op_sel_hi:[1,1,0]
	v_pk_fma_f32 v[12:13], v[12:13], s[14:15], 1.0 op_sel_hi:[1,0,0]
	v_pk_mul_f32 v[4:5], v[6:7], v[4:5]
	v_rcp_f32_e32 v12, v12
	v_rcp_f32_e32 v13, v13
	v_pk_mul_f32 v[4:5], v[10:11], v[4:5]
	v_cmp_gt_f32_e32 vcc, 0, v0
	v_pk_mul_f32 v[10:11], v[0:1], v[4:5]
	v_pk_fma_f32 v[4:5], v[0:1], v[4:5], v[0:1] neg_lo:[1,0,0] neg_hi:[1,0,0]
	v_pk_mul_f32 v[6:7], v[2:3], v[2:3]
	v_cndmask_b32_e32 v10, v4, v10, vcc
	v_cmp_gt_f32_e32 vcc, 0, v1
	v_pk_fma_f32 v[0:1], v[12:13], s[10:11], v[32:33] op_sel_hi:[1,0,0]
	s_nop 0
	v_cndmask_b32_e32 v11, v5, v11, vcc
	v_pk_mul_f32 v[4:5], v[6:7], s[6:7] op_sel_hi:[1,0]
	v_pk_fma_f32 v[0:1], v[12:13], v[0:1], s[12:13] op_sel_hi:[1,1,0]
	v_exp_f32_e32 v4, v4
	v_exp_f32_e32 v5, v5
	v_pk_fma_f32 v[0:1], v[12:13], v[0:1], s[0:1] op_sel_hi:[1,1,0]
	v_cmp_gt_f32_e32 vcc, 0, v2
	v_pk_fma_f32 v[0:1], v[12:13], v[0:1], s[4:5] op_sel_hi:[1,1,0]
	s_nop 0
	v_pk_mul_f32 v[0:1], v[12:13], v[0:1]
	s_nop 0
	v_pk_mul_f32 v[0:1], v[4:5], v[0:1]
	s_nop 0
	v_pk_mul_f32 v[4:5], v[2:3], v[0:1]
	v_pk_fma_f32 v[0:1], v[2:3], v[0:1], v[2:3] neg_lo:[1,0,0] neg_hi:[1,0,0]
	s_nop 0
	v_cndmask_b32_e32 v0, v0, v4, vcc
	v_cmp_gt_f32_e32 vcc, 0, v3
	s_nop 1
	v_cndmask_b32_e32 v1, v1, v5, vcc
	v_cvt_pk_f16_f32 v1, v0, v1
	v_cvt_pk_f16_f32 v0, v10, v11
	global_store_dwordx2 v[8:9], v[0:1], off offset:32
	s_endpgm
	s_endpgm
	s_endpgm
	s_endpgm
	s_endpgm
	s_endpgm
	s_endpgm
	s_endpgm
	s_endpgm
	s_endpgm
	s_endpgm
	s_endpgm
	s_endpgm
	s_endpgm
	s_endpgm
	s_endpgm
	s_endpgm
	s_endpgm
	s_endpgm
	s_endpgm
	s_endpgm

.LBB6_4:
	s_load_dwordx2 s[2:3], s[0:1], 0x14
	s_lshl_b32 s12, s15, 7
	s_lshl_b32 s13, s14, 6
	v_lshrrev_b32_e32 v2, 4, v0
	v_xor_b32_e32 v1, v2, v0
	s_waitcnt lgkmcnt(0)
	s_ashr_i32 s14, s3, 31
	s_mul_i32 s0, s12, s14
	s_mul_hi_u32 s1, s12, s3
	s_add_i32 s1, s1, s0
	s_mul_i32 s0, s12, s3
	v_or_b32_e32 v4, 0x200, v0
	s_lshl_b64 s[0:1], s[0:1], 1
	v_lshlrev_b32_e32 v1, 3, v1
	v_lshrrev_b32_e32 v3, 3, v0
	v_lshrrev_b32_e32 v4, 3, v4
	s_add_u32 s0, s4, s0
	v_and_b32_e32 v1, 56, v1
	v_mul_lo_u32 v3, v3, s3
	v_mul_lo_u32 v4, v4, s3
	s_addc_u32 s1, s5, s1
	s_mul_i32 s4, s13, s14
	s_mul_hi_u32 s5, s13, s3
	v_lshlrev_b32_e32 v54, 4, v0
	v_add_lshl_u32 v3, v3, v1, 1
	v_add_lshl_u32 v4, v4, v1, 1
	s_add_i32 s5, s5, s4
	s_mul_i32 s4, s13, s3
	v_add_u32_e32 v1, 0, v54
	s_lshl_b64 s[4:5], s[4:5], 1
	v_readfirstlane_b32 s19, v1
	v_add_u32_e32 v5, 0x2000, v1
	s_add_u32 s4, s6, s4
	s_mov_b32 m0, s19
	v_readfirstlane_b32 s17, v5
	v_add_u32_e32 v5, 0x4000, v1
	s_addc_u32 s5, s7, s5
	global_load_lds_dwordx4 v3, s[0:1]
	s_mov_b32 m0, s17
	v_readfirstlane_b32 s18, v5
	v_add_u32_e32 v5, 0x6000, v1
	global_load_lds_dwordx4 v4, s[0:1]
	s_mov_b32 m0, s18
	s_add_u32 s6, s0, 0x80
	v_readfirstlane_b32 s16, v5
	v_add_u32_e32 v5, 0x8000, v1
	global_load_lds_dwordx4 v3, s[4:5]
	s_addc_u32 s7, s1, 0
	s_mov_b32 m0, s16
	v_readfirstlane_b32 s14, v5
	v_add_u32_e32 v5, 0xa000, v1
	s_add_u32 s20, s4, 0x80
	global_load_lds_dwordx4 v3, s[6:7]
	s_mov_b32 m0, s14
	v_readfirstlane_b32 s15, v5
	s_addc_u32 s21, s5, 0
	global_load_lds_dwordx4 v4, s[6:7]
	s_mov_b32 m0, s15
	v_add_u32_e32 v5, 0xc000, v1
	global_load_lds_dwordx4 v3, s[20:21]
	s_add_u32 s20, s0, 0x100
	s_addc_u32 s21, s1, 0
	v_readfirstlane_b32 s7, v5
	v_add_u32_e32 v5, 0xe000, v1
	s_add_u32 s22, s4, 0x100
	s_mov_b32 m0, s7
	v_readfirstlane_b32 s3, v5
	v_add_u32_e32 v5, 0x10000, v1
	s_addc_u32 s23, s5, 0
	global_load_lds_dwordx4 v3, s[20:21]
	s_mov_b32 m0, s3
	v_readfirstlane_b32 s6, v5
	v_add_u32_e32 v5, 0x12000, v1
	global_load_lds_dwordx4 v4, s[20:21]
	s_mov_b32 m0, s6
	s_add_u32 s20, s0, 0x180
	v_readfirstlane_b32 s24, v5
	v_add_u32_e32 v5, 0x14000, v1
	global_load_lds_dwordx4 v3, s[22:23]
	s_addc_u32 s21, s1, 0
	s_mov_b32 m0, s24
	v_readfirstlane_b32 s24, v5
	s_add_u32 s22, s4, 0x180
	global_load_lds_dwordx4 v3, s[20:21]
	s_mov_b32 m0, s24
	v_add_u32_e32 v5, 0x16000, v1
	s_addc_u32 s23, s5, 0
	global_load_lds_dwordx4 v4, s[20:21]
	v_readfirstlane_b32 s20, v5
	v_add_u32_e32 v5, 0x18000, v1
	s_mov_b32 m0, s20
	s_add_u32 s20, s0, 0x200
	v_readfirstlane_b32 s24, v5
	v_add_u32_e32 v5, 0x1a000, v1
	global_load_lds_dwordx4 v3, s[22:23]
	s_addc_u32 s21, s1, 0
	s_mov_b32 m0, s24
	v_readfirstlane_b32 s24, v5
	s_add_u32 s22, s4, 0x200
	global_load_lds_dwordx4 v3, s[20:21]
	s_mov_b32 m0, s24
	v_add_u32_e32 v5, 0x1c000, v1
	s_addc_u32 s23, s5, 0
	global_load_lds_dwordx4 v4, s[20:21]
	v_readfirstlane_b32 s20, v5
	v_add_u32_e32 v5, 0x1e000, v1
	s_mov_b32 m0, s20
	s_add_u32 s20, s0, 0x280
	v_readfirstlane_b32 s24, v5
	v_add_u32_e32 v5, 0x20000, v1
	global_load_lds_dwordx4 v3, s[22:23]
	s_addc_u32 s21, s1, 0
	s_mov_b32 m0, s24
	v_readfirstlane_b32 s24, v5
	global_load_lds_dwordx4 v3, s[20:21]
	s_mov_b32 m0, s24
	v_add_u32_e32 v1, 0x22000, v1
	s_add_u32 s22, s4, 0x280
	global_load_lds_dwordx4 v4, s[20:21]
	v_readfirstlane_b32 s20, v1
	s_addc_u32 s23, s5, 0
	s_mov_b32 m0, s20
	v_bfe_u32 v7, v0, 1, 3
	global_load_lds_dwordx4 v3, s[22:23]
	v_lshrrev_b32_e32 v6, 1, v0
	v_bitop3_b32 v2, v2, v7, 3 bitop3:0x6c
	v_and_b32_e32 v5, 15, v0
	v_lshrrev_b32_e32 v1, 2, v0
	s_movk_i32 s20, 0x60
	v_lshlrev_b32_e32 v9, 4, v2
	v_and_b32_e32 v2, 32, v6
	v_and_or_b32 v1, v1, s20, v5
	v_or_b32_e32 v5, v2, v5
	v_lshlrev_b32_e32 v6, 7, v5
	v_add_u32_e32 v38, 0, v6
	s_waitcnt vmcnt(15)
	s_barrier
	v_add_u32_e32 v8, v38, v9
	ds_read_b128 v[10:13], v8 offset:16384
	v_lshlrev_b32_e32 v55, 7, v1
	v_add_u32_e32 v30, 0, v55
	v_add_u32_e32 v5, v30, v9
	ds_read_b128 v[14:17], v5
	ds_read_b128 v[18:21], v8 offset:18432
	ds_read_b128 v[22:25], v5 offset:2048
	v_bfe_u32 v0, v0, 4, 2
	v_bitop3_b32 v9, v0, v7, 4 bitop3:0x36
	s_waitcnt lgkmcnt(0)
	v_mfma_f32_16x16x32_f16 v[26:29], v[10:13], v[14:17], 0
	v_or_b32_e32 v56, 0x4000, v6
	v_add_u32_e32 v7, 0x4000, v8
	v_lshlrev_b32_e32 v57, 4, v9
	v_mfma_f32_16x16x32_f16 v[14:17], v[18:21], v[14:17], 0
	v_add_u32_e32 v6, v30, v57
	v_add_u32_e32 v9, v38, v57
	ds_read_b128 v[30:33], v6
	ds_read_b128 v[34:37], v6 offset:2048
	ds_read_b128 v[38:41], v9 offset:16384
	ds_read_b128 v[42:45], v9 offset:18432
	v_mfma_f32_16x16x32_f16 v[10:13], v[10:13], v[22:25], 0
	v_mfma_f32_16x16x32_f16 v[18:21], v[18:21], v[22:25], 0
	s_add_u32 s20, s0, 0x300
	s_mov_b32 m0, s19
	s_waitcnt vmcnt(12) lgkmcnt(0)
	s_barrier
	s_addc_u32 s21, s1, 0
	s_add_u32 s22, s4, 0x300
	global_load_lds_dwordx4 v3, s[20:21]
	s_mov_b32 m0, s17
	s_addc_u32 s23, s5, 0
	global_load_lds_dwordx4 v4, s[20:21]
	s_mov_b32 m0, s18
	s_nop 0
	global_load_lds_dwordx4 v3, s[22:23]
	s_waitcnt lgkmcnt(0)
	v_mfma_f32_16x16x32_f16 v[22:25], v[38:41], v[30:33], v[26:29]
	v_mfma_f32_16x16x32_f16 v[14:17], v[42:45], v[30:33], v[14:17]
	s_nop 1
	ds_read_b128 v[26:29], v5 offset:24576
	ds_read_b128 v[30:33], v5 offset:26624
	ds_read_b128 v[46:49], v8 offset:40960
	ds_read_b128 v[50:53], v8 offset:43008
	v_mfma_f32_16x16x32_f16 v[10:13], v[38:41], v[34:37], v[10:13]
	v_mfma_f32_16x16x32_f16 v[18:21], v[42:45], v[34:37], v[18:21]
	s_waitcnt lgkmcnt(0)
	v_mfma_f32_16x16x32_f16 v[22:25], v[46:49], v[26:29], v[22:25]
	v_mfma_f32_16x16x32_f16 v[14:17], v[50:53], v[26:29], v[14:17]
	ds_read_b128 v[26:29], v6 offset:24576
	ds_read_b128 v[34:37], v6 offset:26624
	ds_read_b128 v[38:41], v9 offset:40960
	ds_read_b128 v[42:45], v9 offset:43008
	v_mfma_f32_16x16x32_f16 v[10:13], v[46:49], v[30:33], v[10:13]
	v_mfma_f32_16x16x32_f16 v[18:21], v[50:53], v[30:33], v[18:21]
	s_add_u32 s20, s0, 0x380
	s_mov_b32 m0, s16
	s_waitcnt vmcnt(12) lgkmcnt(0)
	s_barrier
	s_addc_u32 s21, s1, 0
	s_add_u32 s22, s4, 0x380
	global_load_lds_dwordx4 v3, s[20:21]
	s_mov_b32 m0, s14
	s_addc_u32 s23, s5, 0
	global_load_lds_dwordx4 v4, s[20:21]
	s_mov_b32 m0, s15
	s_nop 0
	global_load_lds_dwordx4 v3, s[22:23]
	s_waitcnt lgkmcnt(0)
	v_mfma_f32_16x16x32_f16 v[22:25], v[38:41], v[26:29], v[22:25]
	v_mfma_f32_16x16x32_f16 v[14:17], v[42:45], v[26:29], v[14:17]
	ds_read_b128 v[26:29], v5 offset:49152
	ds_read_b128 v[30:33], v5 offset:51200
	ds_read_b128 v[46:49], v7 offset:49152
	ds_read_b128 v[50:53], v7 offset:51200
	v_mfma_f32_16x16x32_f16 v[10:13], v[38:41], v[34:37], v[10:13]
	v_mfma_f32_16x16x32_f16 v[18:21], v[42:45], v[34:37], v[18:21]
	s_waitcnt lgkmcnt(0)
	v_mfma_f32_16x16x32_f16 v[22:25], v[46:49], v[26:29], v[22:25]
	v_mfma_f32_16x16x32_f16 v[14:17], v[50:53], v[26:29], v[14:17]
	s_add_i32 s20, 0, 0xc000
	v_add3_u32 v58, s20, v57, v56
	ds_read_b128 v[26:29], v6 offset:49152
	ds_read_b128 v[34:37], v6 offset:51200
	ds_read_b128 v[38:41], v58
	ds_read_b128 v[42:45], v58 offset:2048
	v_mfma_f32_16x16x32_f16 v[10:13], v[46:49], v[30:33], v[10:13]
	v_mfma_f32_16x16x32_f16 v[18:21], v[50:53], v[30:33], v[18:21]
	s_add_u32 s20, s0, 0x400
	s_mov_b32 m0, s7
	s_waitcnt vmcnt(12) lgkmcnt(0)
	s_barrier
	s_addc_u32 s21, s1, 0
	s_add_u32 s22, s4, 0x400
	global_load_lds_dwordx4 v3, s[20:21]
	s_mov_b32 m0, s3
	s_addc_u32 s23, s5, 0
	global_load_lds_dwordx4 v4, s[20:21]
	s_mov_b32 m0, s6
	s_nop 0
	global_load_lds_dwordx4 v3, s[22:23]
	s_waitcnt lgkmcnt(0)
	v_mfma_f32_16x16x32_f16 v[22:25], v[38:41], v[26:29], v[22:25]
	v_mfma_f32_16x16x32_f16 v[14:17], v[42:45], v[26:29], v[14:17]
	v_add_u32_e32 v59, 0x12000, v5
	v_add_u32_e32 v61, 0x16000, v8
	v_add_u32_e32 v60, 0x12800, v5
	ds_read_b128 v[26:29], v59
	ds_read_b128 v[30:33], v60
	v_add_u32_e32 v62, 0x16800, v8
	ds_read_b128 v[46:49], v61
	ds_read_b128 v[50:53], v62
	v_mfma_f32_16x16x32_f16 v[10:13], v[38:41], v[34:37], v[10:13]
	v_mfma_f32_16x16x32_f16 v[18:21], v[42:45], v[34:37], v[18:21]
	s_waitcnt lgkmcnt(0)
	v_mfma_f32_16x16x32_f16 v[22:25], v[46:49], v[26:29], v[22:25]
	v_mfma_f32_16x16x32_f16 v[14:17], v[50:53], v[26:29], v[14:17]
	s_add_i32 s20, 0, 0x12000
	v_add_u32_e32 v38, s20, v57
	v_add_u32_e32 v63, v38, v55
	v_add_u32_e32 v64, v38, v56
	ds_read_b128 v[26:29], v63
	ds_read_b128 v[34:37], v63 offset:2048
	ds_read_b128 v[38:41], v64
	ds_read_b128 v[42:45], v64 offset:2048
	v_mfma_f32_16x16x32_f16 v[10:13], v[46:49], v[30:33], v[10:13]
	v_mfma_f32_16x16x32_f16 v[18:21], v[50:53], v[30:33], v[18:21]
	v_add_u32_e32 v30, s20, v54
	s_add_u32 s24, s0, 0x480
	v_readfirstlane_b32 s22, v30
	v_add_u32_e32 v31, 0x2000, v30
	s_waitcnt vmcnt(12) lgkmcnt(0)
	s_barrier
	s_addc_u32 s25, s1, 0
	s_mov_b32 m0, s22
	v_readfirstlane_b32 s20, v31
	v_add_u32_e32 v30, 0x4000, v30
	s_add_u32 s26, s4, 0x480
	global_load_lds_dwordx4 v3, s[24:25]
	s_mov_b32 m0, s20
	v_readfirstlane_b32 s21, v30
	s_addc_u32 s27, s5, 0
	global_load_lds_dwordx4 v4, s[24:25]
	s_mov_b32 m0, s21
	s_nop 0
	global_load_lds_dwordx4 v3, s[26:27]
	s_waitcnt lgkmcnt(0)
	v_mfma_f32_16x16x32_f16 v[22:25], v[38:41], v[26:29], v[22:25]
	v_mfma_f32_16x16x32_f16 v[14:17], v[42:45], v[26:29], v[14:17]
	v_add_u32_e32 v65, 0x18000, v5
	v_add_u32_e32 v67, 0x1c000, v8
	v_add_u32_e32 v66, 0x18800, v5
	ds_read_b128 v[26:29], v65
	ds_read_b128 v[30:33], v66
	v_add_u32_e32 v68, 0x1c800, v8
	ds_read_b128 v[46:49], v67
	ds_read_b128 v[50:53], v68
	v_mfma_f32_16x16x32_f16 v[10:13], v[38:41], v[34:37], v[10:13]
	v_mfma_f32_16x16x32_f16 v[18:21], v[42:45], v[34:37], v[18:21]
	s_waitcnt lgkmcnt(0)
	v_mfma_f32_16x16x32_f16 v[22:25], v[46:49], v[26:29], v[22:25]
	v_mfma_f32_16x16x32_f16 v[14:17], v[50:53], v[26:29], v[14:17]
	s_add_i32 s23, 0, 0x18000
	v_add_u32_e32 v38, s23, v57
	v_add_u32_e32 v69, v38, v55
	v_add_u32_e32 v70, v38, v56
	ds_read_b128 v[26:29], v69
	ds_read_b128 v[34:37], v69 offset:2048
	ds_read_b128 v[38:41], v70
	ds_read_b128 v[42:45], v70 offset:2048
	v_mfma_f32_16x16x32_f16 v[10:13], v[46:49], v[30:33], v[10:13]
	v_mfma_f32_16x16x32_f16 v[18:21], v[50:53], v[30:33], v[18:21]
	v_add_u32_e32 v30, s23, v54
	s_add_u32 s24, s0, 0x500
	v_readfirstlane_b32 s23, v30
	v_add_u32_e32 v31, 0x2000, v30
	s_waitcnt vmcnt(12) lgkmcnt(0)
	s_barrier
	s_addc_u32 s25, s1, 0
	s_mov_b32 m0, s23
	v_readfirstlane_b32 s23, v31
	v_add_u32_e32 v30, 0x4000, v30
	s_add_u32 s26, s4, 0x500
	global_load_lds_dwordx4 v3, s[24:25]
	s_mov_b32 m0, s23
	v_readfirstlane_b32 s23, v30
	s_addc_u32 s27, s5, 0
	global_load_lds_dwordx4 v4, s[24:25]
	s_mov_b32 m0, s23
	s_nop 0
	global_load_lds_dwordx4 v3, s[26:27]
	s_waitcnt lgkmcnt(0)
	v_mfma_f32_16x16x32_f16 v[22:25], v[38:41], v[26:29], v[22:25]
	v_mfma_f32_16x16x32_f16 v[14:17], v[42:45], v[26:29], v[14:17]
	v_add_u32_e32 v71, 0x1e000, v5
	v_add_u32_e32 v73, 0x22000, v8
	v_add_u32_e32 v72, 0x1e800, v5
	ds_read_b128 v[26:29], v71
	ds_read_b128 v[30:33], v72
	v_add_u32_e32 v74, 0x22800, v8
	ds_read_b128 v[46:49], v73
	ds_read_b128 v[50:53], v74
	v_mfma_f32_16x16x32_f16 v[10:13], v[38:41], v[34:37], v[10:13]
	v_mfma_f32_16x16x32_f16 v[18:21], v[42:45], v[34:37], v[18:21]
	s_waitcnt lgkmcnt(0)
	v_mfma_f32_16x16x32_f16 v[22:25], v[46:49], v[26:29], v[22:25]
	v_mfma_f32_16x16x32_f16 v[14:17], v[50:53], v[26:29], v[14:17]
	s_add_i32 s23, 0, 0x1e000
	v_add_u32_e32 v38, s23, v57
	v_add_u32_e32 v55, v38, v55
	v_add_u32_e32 v56, v38, v56
	ds_read_b128 v[26:29], v55
	ds_read_b128 v[34:37], v55 offset:2048
	ds_read_b128 v[38:41], v56
	ds_read_b128 v[42:45], v56 offset:2048
	v_mfma_f32_16x16x32_f16 v[10:13], v[46:49], v[30:33], v[10:13]
	v_mfma_f32_16x16x32_f16 v[18:21], v[50:53], v[30:33], v[18:21]
	v_add_u32_e32 v30, s23, v54
	s_add_u32 s24, s0, 0x580
	v_readfirstlane_b32 s23, v30
	v_add_u32_e32 v31, 0x2000, v30
	s_waitcnt vmcnt(12) lgkmcnt(0)
	s_barrier
	s_addc_u32 s25, s1, 0
	s_mov_b32 m0, s23
	v_readfirstlane_b32 s23, v31
	v_add_u32_e32 v30, 0x4000, v30
	s_add_u32 s26, s4, 0x580
	global_load_lds_dwordx4 v3, s[24:25]
	s_mov_b32 m0, s23
	v_readfirstlane_b32 s23, v30
	s_addc_u32 s27, s5, 0
	global_load_lds_dwordx4 v4, s[24:25]
	s_mov_b32 m0, s23
	s_nop 0
	global_load_lds_dwordx4 v3, s[26:27]
	s_waitcnt lgkmcnt(0)
	v_mfma_f32_16x16x32_f16 v[22:25], v[38:41], v[26:29], v[22:25]
	v_mfma_f32_16x16x32_f16 v[14:17], v[42:45], v[26:29], v[14:17]
	ds_read_b128 v[26:29], v5
	ds_read_b128 v[30:33], v5 offset:2048
	ds_read_b128 v[46:49], v8 offset:16384
	ds_read_b128 v[50:53], v8 offset:18432
	v_mfma_f32_16x16x32_f16 v[10:13], v[38:41], v[34:37], v[10:13]
	v_mfma_f32_16x16x32_f16 v[18:21], v[42:45], v[34:37], v[18:21]
	s_waitcnt lgkmcnt(0)
	v_mfma_f32_16x16x32_f16 v[22:25], v[46:49], v[26:29], v[22:25]
	v_mfma_f32_16x16x32_f16 v[14:17], v[50:53], v[26:29], v[14:17]
	ds_read_b128 v[26:29], v6
	ds_read_b128 v[34:37], v6 offset:2048
	ds_read_b128 v[38:41], v9 offset:16384
	ds_read_b128 v[42:45], v9 offset:18432
	v_mfma_f32_16x16x32_f16 v[10:13], v[46:49], v[30:33], v[10:13]
	v_mfma_f32_16x16x32_f16 v[18:21], v[50:53], v[30:33], v[18:21]
	s_add_u32 s24, s0, 0x600
	s_mov_b32 m0, s19
	s_waitcnt vmcnt(12) lgkmcnt(0)
	s_barrier
	s_addc_u32 s25, s1, 0
	s_add_u32 s26, s4, 0x600
	global_load_lds_dwordx4 v3, s[24:25]
	s_mov_b32 m0, s17
	s_addc_u32 s27, s5, 0
	global_load_lds_dwordx4 v4, s[24:25]
	s_mov_b32 m0, s18
	s_nop 0
	global_load_lds_dwordx4 v3, s[26:27]
	s_waitcnt lgkmcnt(0)
	v_mfma_f32_16x16x32_f16 v[22:25], v[38:41], v[26:29], v[22:25]
	v_mfma_f32_16x16x32_f16 v[14:17], v[42:45], v[26:29], v[14:17]
	ds_read_b128 v[26:29], v5 offset:24576
	ds_read_b128 v[30:33], v5 offset:26624
	ds_read_b128 v[46:49], v8 offset:40960
	ds_read_b128 v[50:53], v8 offset:43008
	v_mfma_f32_16x16x32_f16 v[10:13], v[38:41], v[34:37], v[10:13]
	v_mfma_f32_16x16x32_f16 v[18:21], v[42:45], v[34:37], v[18:21]
	s_waitcnt lgkmcnt(0)
	v_mfma_f32_16x16x32_f16 v[22:25], v[46:49], v[26:29], v[22:25]
	v_mfma_f32_16x16x32_f16 v[14:17], v[50:53], v[26:29], v[14:17]
	ds_read_b128 v[26:29], v6 offset:24576
	ds_read_b128 v[34:37], v6 offset:26624
	ds_read_b128 v[38:41], v9 offset:40960
	ds_read_b128 v[42:45], v9 offset:43008
	v_mfma_f32_16x16x32_f16 v[10:13], v[46:49], v[30:33], v[10:13]
	v_mfma_f32_16x16x32_f16 v[18:21], v[50:53], v[30:33], v[18:21]
	s_mov_b32 m0, s16
	s_add_u32 s16, s0, 0x680
	s_waitcnt vmcnt(12) lgkmcnt(0)
	s_barrier
	s_addc_u32 s17, s1, 0
	s_add_u32 s18, s4, 0x680
	global_load_lds_dwordx4 v3, s[16:17]
	s_mov_b32 m0, s14
	s_addc_u32 s19, s5, 0
	global_load_lds_dwordx4 v4, s[16:17]
	s_mov_b32 m0, s15
	s_nop 0
	global_load_lds_dwordx4 v3, s[18:19]
	s_waitcnt lgkmcnt(0)
	v_mfma_f32_16x16x32_f16 v[22:25], v[38:41], v[26:29], v[22:25]
	v_mfma_f32_16x16x32_f16 v[14:17], v[42:45], v[26:29], v[14:17]
	ds_read_b128 v[26:29], v5 offset:49152
	ds_read_b128 v[30:33], v5 offset:51200
	ds_read_b128 v[46:49], v7 offset:49152
	ds_read_b128 v[50:53], v7 offset:51200
	v_mfma_f32_16x16x32_f16 v[10:13], v[38:41], v[34:37], v[10:13]
	v_mfma_f32_16x16x32_f16 v[18:21], v[42:45], v[34:37], v[18:21]
	s_waitcnt lgkmcnt(0)
	v_mfma_f32_16x16x32_f16 v[22:25], v[46:49], v[26:29], v[22:25]
	v_mfma_f32_16x16x32_f16 v[14:17], v[50:53], v[26:29], v[14:17]
	ds_read_b128 v[26:29], v6 offset:49152
	ds_read_b128 v[34:37], v6 offset:51200
	ds_read_b128 v[38:41], v58
	ds_read_b128 v[42:45], v58 offset:2048
	v_mfma_f32_16x16x32_f16 v[10:13], v[46:49], v[30:33], v[10:13]
	v_mfma_f32_16x16x32_f16 v[18:21], v[50:53], v[30:33], v[18:21]
	s_add_u32 s14, s0, 0x700
	s_mov_b32 m0, s7
	s_waitcnt vmcnt(12) lgkmcnt(0)
	s_barrier
	s_addc_u32 s15, s1, 0
	s_add_u32 s16, s4, 0x700
	global_load_lds_dwordx4 v3, s[14:15]
	s_mov_b32 m0, s3
	s_addc_u32 s17, s5, 0
	global_load_lds_dwordx4 v4, s[14:15]
	s_mov_b32 m0, s6
	s_nop 0
	global_load_lds_dwordx4 v3, s[16:17]
	s_waitcnt lgkmcnt(0)
	v_mfma_f32_16x16x32_f16 v[22:25], v[38:41], v[26:29], v[22:25]
	v_mfma_f32_16x16x32_f16 v[14:17], v[42:45], v[26:29], v[14:17]
	ds_read_b128 v[26:29], v59
	ds_read_b128 v[30:33], v60
	ds_read_b128 v[46:49], v61
	ds_read_b128 v[50:53], v62
	v_mfma_f32_16x16x32_f16 v[10:13], v[38:41], v[34:37], v[10:13]
	v_mfma_f32_16x16x32_f16 v[18:21], v[42:45], v[34:37], v[18:21]
	s_waitcnt lgkmcnt(0)
	v_mfma_f32_16x16x32_f16 v[22:25], v[46:49], v[26:29], v[22:25]
	v_mfma_f32_16x16x32_f16 v[14:17], v[50:53], v[26:29], v[14:17]
	ds_read_b128 v[26:29], v63
	ds_read_b128 v[34:37], v63 offset:2048
	ds_read_b128 v[38:41], v64
	ds_read_b128 v[42:45], v64 offset:2048
	v_mfma_f32_16x16x32_f16 v[10:13], v[46:49], v[30:33], v[10:13]
	v_mfma_f32_16x16x32_f16 v[18:21], v[50:53], v[30:33], v[18:21]
	s_add_u32 s0, s0, 0x780
	s_mov_b32 m0, s22
	s_waitcnt vmcnt(12) lgkmcnt(0)
	s_barrier
	s_addc_u32 s1, s1, 0
	s_add_u32 s4, s4, 0x780
	global_load_lds_dwordx4 v3, s[0:1]
	s_mov_b32 m0, s20
	s_addc_u32 s5, s5, 0
	global_load_lds_dwordx4 v4, s[0:1]
	s_mov_b32 m0, s21
	s_nop 0
	global_load_lds_dwordx4 v3, s[4:5]
	s_waitcnt lgkmcnt(0)
	v_mfma_f32_16x16x32_f16 v[22:25], v[38:41], v[26:29], v[22:25]
	v_mfma_f32_16x16x32_f16 v[14:17], v[42:45], v[26:29], v[14:17]
	ds_read_b128 v[26:29], v65
	ds_read_b128 v[30:33], v66
	ds_read_b128 v[46:49], v67
	ds_read_b128 v[50:53], v68
	v_mfma_f32_16x16x32_f16 v[10:13], v[38:41], v[34:37], v[10:13]
	v_mfma_f32_16x16x32_f16 v[18:21], v[42:45], v[34:37], v[18:21]
	s_waitcnt lgkmcnt(0)
	v_mfma_f32_16x16x32_f16 v[22:25], v[46:49], v[26:29], v[22:25]
	v_mfma_f32_16x16x32_f16 v[14:17], v[50:53], v[26:29], v[14:17]
	ds_read_b128 v[26:29], v69
	ds_read_b128 v[34:37], v69 offset:2048
	ds_read_b128 v[38:41], v70
	ds_read_b128 v[42:45], v70 offset:2048
	v_mfma_f32_16x16x32_f16 v[10:13], v[46:49], v[30:33], v[10:13]
	v_mfma_f32_16x16x32_f16 v[18:21], v[50:53], v[30:33], v[18:21]
	s_waitcnt vmcnt(12) lgkmcnt(0)
	s_barrier
	s_waitcnt lgkmcnt(0)
	v_mfma_f32_16x16x32_f16 v[22:25], v[38:41], v[26:29], v[22:25]
	v_mfma_f32_16x16x32_f16 v[14:17], v[42:45], v[26:29], v[14:17]
	ds_read_b128 v[26:29], v71
	ds_read_b128 v[30:33], v72
	ds_read_b128 v[46:49], v73
	ds_read_b128 v[50:53], v74
	v_mfma_f32_16x16x32_f16 v[10:13], v[38:41], v[34:37], v[10:13]
	v_mfma_f32_16x16x32_f16 v[18:21], v[42:45], v[34:37], v[18:21]
	s_waitcnt lgkmcnt(0)
	v_mfma_f32_16x16x32_f16 v[22:25], v[46:49], v[26:29], v[22:25]
	v_mfma_f32_16x16x32_f16 v[14:17], v[50:53], v[26:29], v[14:17]
	ds_read_b128 v[26:29], v55
	ds_read_b128 v[34:37], v55 offset:2048
	ds_read_b128 v[38:41], v56
	ds_read_b128 v[42:45], v56 offset:2048
	v_mfma_f32_16x16x32_f16 v[10:13], v[46:49], v[30:33], v[10:13]
	v_mfma_f32_16x16x32_f16 v[18:21], v[50:53], v[30:33], v[18:21]
	s_waitcnt vmcnt(0) lgkmcnt(0)
	s_barrier
	s_waitcnt lgkmcnt(0)
	v_mfma_f32_16x16x32_f16 v[22:25], v[38:41], v[26:29], v[22:25]
	v_mfma_f32_16x16x32_f16 v[14:17], v[42:45], v[26:29], v[14:17]
	ds_read_b128 v[26:29], v5
	ds_read_b128 v[30:33], v5 offset:2048
	ds_read_b128 v[46:49], v8 offset:16384
	ds_read_b128 v[50:53], v8 offset:18432
	v_mfma_f32_16x16x32_f16 v[10:13], v[38:41], v[34:37], v[10:13]
	v_mfma_f32_16x16x32_f16 v[18:21], v[42:45], v[34:37], v[18:21]
	s_waitcnt lgkmcnt(0)
	v_mfma_f32_16x16x32_f16 v[22:25], v[46:49], v[26:29], v[22:25]
	v_mfma_f32_16x16x32_f16 v[14:17], v[50:53], v[26:29], v[14:17]
	ds_read_b128 v[26:29], v6
	ds_read_b128 v[34:37], v6 offset:2048
	ds_read_b128 v[38:41], v9 offset:16384
	ds_read_b128 v[42:45], v9 offset:18432
	v_mfma_f32_16x16x32_f16 v[10:13], v[46:49], v[30:33], v[10:13]
	v_mfma_f32_16x16x32_f16 v[18:21], v[50:53], v[30:33], v[18:21]
	s_waitcnt vmcnt(0) lgkmcnt(0)
	s_barrier
	s_waitcnt lgkmcnt(0)
	v_mfma_f32_16x16x32_f16 v[22:25], v[38:41], v[26:29], v[22:25]
	v_mfma_f32_16x16x32_f16 v[14:17], v[42:45], v[26:29], v[14:17]
	ds_read_b128 v[26:29], v5 offset:24576
	ds_read_b128 v[30:33], v5 offset:26624
	ds_read_b128 v[46:49], v8 offset:40960
	ds_read_b128 v[50:53], v8 offset:43008
	v_mfma_f32_16x16x32_f16 v[10:13], v[38:41], v[34:37], v[10:13]
	v_mfma_f32_16x16x32_f16 v[18:21], v[42:45], v[34:37], v[18:21]
	s_waitcnt lgkmcnt(0)
	v_mfma_f32_16x16x32_f16 v[22:25], v[46:49], v[26:29], v[22:25]
	v_mfma_f32_16x16x32_f16 v[14:17], v[50:53], v[26:29], v[14:17]
	ds_read_b128 v[26:29], v6 offset:24576
	ds_read_b128 v[34:37], v6 offset:26624
	ds_read_b128 v[38:41], v9 offset:40960
	ds_read_b128 v[42:45], v9 offset:43008
	v_mfma_f32_16x16x32_f16 v[8:11], v[46:49], v[30:33], v[10:13]
	v_mfma_f32_16x16x32_f16 v[18:21], v[50:53], v[30:33], v[18:21]
	s_waitcnt vmcnt(0) lgkmcnt(0)
	s_barrier
	s_waitcnt lgkmcnt(0)
	v_mfma_f32_16x16x32_f16 v[22:25], v[38:41], v[26:29], v[22:25]
	v_mfma_f32_16x16x32_f16 v[12:15], v[42:45], v[26:29], v[14:17]
	ds_read_b128 v[26:29], v5 offset:49152
	ds_read_b128 v[30:33], v5 offset:51200
	ds_read_b128 v[46:49], v7 offset:49152
	ds_read_b128 v[50:53], v7 offset:51200
	v_mfma_f32_16x16x32_f16 v[8:11], v[38:41], v[34:37], v[8:11]
	v_mfma_f32_16x16x32_f16 v[16:19], v[42:45], v[34:37], v[18:21]
	s_waitcnt lgkmcnt(0)
	v_mfma_f32_16x16x32_f16 v[20:23], v[46:49], v[26:29], v[22:25]
	v_mfma_f32_16x16x32_f16 v[12:15], v[50:53], v[26:29], v[12:15]
	s_nop 1
	ds_read_b128 v[24:27], v6 offset:49152
	ds_read_b128 v[4:7], v6 offset:51200
	ds_read_b128 v[34:37], v58
	ds_read_b128 v[38:41], v58 offset:2048
	v_mfma_f32_16x16x32_f16 v[8:11], v[46:49], v[30:33], v[8:11]
	v_mfma_f32_16x16x32_f16 v[16:19], v[50:53], v[30:33], v[16:19]
	s_waitcnt vmcnt(0) lgkmcnt(0)
	s_barrier
	s_waitcnt lgkmcnt(0)
	v_mfma_f32_16x16x32_f16 v[20:23], v[34:37], v[24:27], v[20:23]
	v_mfma_f32_16x16x32_f16 v[12:15], v[38:41], v[24:27], v[12:15]
	ds_read_b128 v[24:27], v59
	ds_read_b128 v[28:31], v60
	ds_read_b128 v[42:45], v61
	ds_read_b128 v[46:49], v62
	v_mfma_f32_16x16x32_f16 v[8:11], v[34:37], v[4:7], v[8:11]
	v_mfma_f32_16x16x32_f16 v[4:7], v[38:41], v[4:7], v[16:19]
	s_waitcnt lgkmcnt(0)
	v_mfma_f32_16x16x32_f16 v[16:19], v[42:45], v[24:27], v[20:23]
	v_mfma_f32_16x16x32_f16 v[12:15], v[46:49], v[24:27], v[12:15]
	s_nop 1
	ds_read_b128 v[20:23], v63
	ds_read_b128 v[24:27], v63 offset:2048
	ds_read_b128 v[32:35], v64
	ds_read_b128 v[36:39], v64 offset:2048
	v_mfma_f32_16x16x32_f16 v[8:11], v[42:45], v[28:31], v[8:11]
	v_mfma_f32_16x16x32_f16 v[4:7], v[46:49], v[28:31], v[4:7]
	s_waitcnt lgkmcnt(0)
	v_mfma_f32_16x16x32_f16 v[16:19], v[32:35], v[20:23], v[16:19]
	v_mfma_f32_16x16x32_f16 v[12:15], v[36:39], v[20:23], v[12:15]
	v_mfma_f32_16x16x32_f16 v[8:11], v[32:35], v[24:27], v[8:11]
	v_mfma_f32_16x16x32_f16 v[4:7], v[36:39], v[24:27], v[4:7]
	v_or_b32_e32 v38, s12, v1
	v_lshlrev_b32_e32 v0, 2, v0
	v_or3_b32 v0, v0, v2, s13
	v_mad_u64_u32 v[2:3], s[0:1], v38, s2, 0
	s_ashr_i32 s3, s2, 31
	v_mov_b32_e32 v20, v3
	v_mad_u64_u32 v[20:21], s[0:1], v38, s3, v[20:21]
	v_mov_b32_e32 v3, v20
	v_mov_b32_e32 v1, 0
	v_lshl_add_u64 v[2:3], v[2:3], 2, s[8:9]
	v_lshlrev_b64 v[32:33], 2, v[0:1]
	v_lshl_add_u64 v[34:35], v[2:3], 0, v[32:33]
	global_load_dwordx4 v[0:3], v[34:35], off
	global_load_dwordx4 v[20:23], v[34:35], off offset:64
	v_lshl_add_u64 v[36:37], s[10:11], 0, v[32:33]
	global_load_dwordx4 v[24:27], v[36:37], off
	global_load_dwordx4 v[28:31], v[36:37], off offset:64
	v_or_b32_e32 v39, 16, v38
	v_mad_u64_u32 v[36:37], s[0:1], v39, s2, 0
	v_mov_b32_e32 v38, v37
	v_mad_u64_u32 v[38:39], s[0:1], v39, s3, v[38:39]
	v_mov_b32_e32 v37, v38
	v_lshl_add_u64 v[36:37], v[36:37], 2, s[8:9]
	v_lshl_add_u64 v[32:33], v[36:37], 0, v[32:33]
	s_waitcnt vmcnt(0)
	v_pk_add_f32 v[2:3], v[18:19], v[2:3]
	v_pk_add_f32 v[0:1], v[16:17], v[0:1]
	v_pk_add_f32 v[14:15], v[14:15], v[22:23]
	v_pk_add_f32 v[12:13], v[12:13], v[20:21]
	v_pk_add_f32 v[2:3], v[26:27], v[2:3]
	v_pk_add_f32 v[0:1], v[24:25], v[0:1]
	v_pk_add_f32 v[14:15], v[30:31], v[14:15]
	v_pk_add_f32 v[12:13], v[28:29], v[12:13]
	global_store_dwordx4 v[34:35], v[0:3], off
	global_store_dwordx4 v[34:35], v[12:15], off offset:64
	global_load_dwordx4 v[0:3], v[32:33], off
	s_nop 0
	global_load_dwordx4 v[12:15], v[32:33], off offset:64
	s_waitcnt vmcnt(1)
	v_pk_add_f32 v[2:3], v[10:11], v[2:3]
	v_pk_add_f32 v[0:1], v[8:9], v[0:1]
	s_waitcnt vmcnt(0)
	v_pk_add_f32 v[6:7], v[6:7], v[14:15]
	v_pk_add_f32 v[4:5], v[4:5], v[12:13]
	v_pk_add_f32 v[2:3], v[26:27], v[2:3]
	v_pk_add_f32 v[0:1], v[24:25], v[0:1]
	v_pk_add_f32 v[6:7], v[30:31], v[6:7]
	v_pk_add_f32 v[4:5], v[28:29], v[4:5]
	global_store_dwordx4 v[32:33], v[0:3], off
	global_store_dwordx4 v[32:33], v[4:7], off offset:64
	s_endpgm
	s_endpgm
	s_endpgm
	s_endpgm
	s_endpgm
	s_endpgm
	s_endpgm
	s_endpgm
	s_endpgm
	s_endpgm
	s_endpgm
	s_endpgm
	s_endpgm
	s_endpgm
	s_endpgm
	s_endpgm
	s_endpgm
	s_endpgm
	s_endpgm
	s_endpgm
	s_endpgm

_Z5gemm8ILi128ELi2ELi4ELi4ELi2ELi32EEvPKDF16_S1_iiiPDF16_PfPKf:
	s_load_dwordx8 s[4:11], s[0:1], 0x0
	s_lshl_b32 s3, s2, 2
	s_waitcnt lgkmcnt(0)
	s_and_b32 s11, s2, 4
	s_lshr_b32 s12, s2, 6
	s_bfe_u32 s13, s2, 0x30003
	s_add_i32 s11, s11, s12
	s_and_b32 s12, s2, 1
	s_and_b32 s2, s3, 8
	s_or_b32 s2, s2, s13
	s_lshl_b32 s13, s2, 7
	s_lshr_b32 s2, s10, 31
	s_add_i32 s2, s10, s2
	s_ashr_i32 s14, s2, 1
	s_mul_hi_i32 s3, s10, s13
	s_mul_i32 s2, s10, s13
	s_lshl_b32 s11, s11, 7
	s_lshl_b64 s[2:3], s[2:3], 1
	v_lshrrev_b32_e32 v2, 4, v0
	s_add_u32 s15, s4, s2
	s_mul_i32 s2, s14, s12
	v_xor_b32_e32 v1, v2, v0
	v_or_b32_e32 v4, 0x200, v0
	s_addc_u32 s16, s5, s3
	s_ashr_i32 s3, s2, 31
	v_lshlrev_b32_e32 v1, 3, v1
	v_lshrrev_b32_e32 v3, 3, v0
	v_lshrrev_b32_e32 v4, 3, v4
	s_lshl_b64 s[4:5], s[2:3], 1
	v_and_b32_e32 v1, 56, v1
	v_mul_lo_u32 v3, v3, s10
	v_mul_lo_u32 v4, v4, s10
	s_add_u32 s2, s15, s4
	s_mul_hi_i32 s15, s10, s11
	s_mul_i32 s14, s10, s11
	v_lshlrev_b32_e32 v106, 4, v0
	v_add_lshl_u32 v3, v3, v1, 1
	v_add_lshl_u32 v4, v4, v1, 1
	s_addc_u32 s3, s16, s5
	s_lshl_b64 s[14:15], s[14:15], 1
	v_add_u32_e32 v1, 0, v106
	s_add_u32 s6, s6, s14
	v_readfirstlane_b32 s18, v1
	v_add_u32_e32 v5, 0x2000, v1
	s_addc_u32 s7, s7, s15
	s_mov_b32 m0, s18
	v_readfirstlane_b32 s15, v5
	v_add_u32_e32 v5, 0x4000, v1
	s_add_u32 s4, s6, s4
	global_load_lds_dwordx4 v3, s[2:3]
	s_mov_b32 m0, s15
	v_readfirstlane_b32 s16, v5
	v_add_u32_e32 v5, 0x6000, v1
	s_addc_u32 s5, s7, s5
	global_load_lds_dwordx4 v4, s[2:3]
	s_mov_b32 m0, s16
	v_readfirstlane_b32 s17, v5
	v_add_u32_e32 v5, 0x8000, v1
	global_load_lds_dwordx4 v3, s[4:5]
	s_mov_b32 m0, s17
	s_add_u32 s20, s2, 0x80
	v_readfirstlane_b32 s14, v5
	v_add_u32_e32 v5, 0xa000, v1
	global_load_lds_dwordx4 v4, s[4:5]
	s_addc_u32 s21, s3, 0
	s_mov_b32 m0, s14
	v_readfirstlane_b32 s6, v5
	v_add_u32_e32 v5, 0xc000, v1
	s_add_u32 s22, s4, 0x80
	global_load_lds_dwordx4 v3, s[20:21]
	s_mov_b32 m0, s6
	v_readfirstlane_b32 s7, v5
	v_add_u32_e32 v5, 0xe000, v1
	s_addc_u32 s23, s5, 0
	global_load_lds_dwordx4 v4, s[20:21]
	s_mov_b32 m0, s7
	v_readfirstlane_b32 s10, v5
	v_add_u32_e32 v5, 0x10000, v1
	global_load_lds_dwordx4 v3, s[22:23]
	s_mov_b32 m0, s10
	s_add_u32 s20, s2, 0x100
	v_readfirstlane_b32 s19, v5
	v_add_u32_e32 v5, 0x12000, v1
	global_load_lds_dwordx4 v4, s[22:23]
	s_addc_u32 s21, s3, 0
	s_mov_b32 m0, s19
	v_readfirstlane_b32 s19, v5
	v_add_u32_e32 v5, 0x14000, v1
	s_add_u32 s22, s4, 0x100
	global_load_lds_dwordx4 v3, s[20:21]
	s_mov_b32 m0, s19
	v_readfirstlane_b32 s19, v5
	v_add_u32_e32 v5, 0x16000, v1
	s_addc_u32 s23, s5, 0
	global_load_lds_dwordx4 v4, s[20:21]
	s_mov_b32 m0, s19
	v_readfirstlane_b32 s19, v5
	v_add_u32_e32 v5, 0x18000, v1
	global_load_lds_dwordx4 v3, s[22:23]
	s_mov_b32 m0, s19
	s_add_u32 s20, s2, 0x180
	v_readfirstlane_b32 s19, v5
	v_add_u32_e32 v5, 0x1a000, v1
	global_load_lds_dwordx4 v4, s[22:23]
	s_addc_u32 s21, s3, 0
	s_mov_b32 m0, s19
	v_readfirstlane_b32 s19, v5
	v_add_u32_e32 v5, 0x1c000, v1
	s_add_u32 s22, s4, 0x180
	global_load_lds_dwordx4 v3, s[20:21]
	s_mov_b32 m0, s19
	v_readfirstlane_b32 s19, v5
	v_add_u32_e32 v1, 0x1e000, v1
	s_addc_u32 s23, s5, 0
	global_load_lds_dwordx4 v4, s[20:21]
	s_mov_b32 m0, s19
	v_readfirstlane_b32 s19, v1
	global_load_lds_dwordx4 v3, s[22:23]
	s_mov_b32 m0, s19
	v_bfe_u32 v8, v0, 1, 3
	global_load_lds_dwordx4 v4, s[22:23]
	v_lshrrev_b32_e32 v6, 1, v0
	v_bitop3_b32 v2, v2, v8, 3 bitop3:0x6c
	v_and_b32_e32 v5, 15, v0
	v_lshrrev_b32_e32 v1, 2, v0
	v_lshlrev_b32_e32 v7, 4, v2
	v_and_b32_e32 v2, 0x60, v6
	v_and_or_b32 v1, v1, 64, v5
	v_or_b32_e32 v5, v2, v5
	v_lshlrev_b32_e32 v6, 7, v5
	v_lshlrev_b32_e32 v102, 7, v1
	v_add_u32_e32 v9, 0, v6
	v_add_u32_e32 v38, 0, v102
	s_waitcnt vmcnt(12)
	s_barrier
	v_add_u32_e32 v5, v9, v7
	v_add_u32_e32 v7, v38, v7
	ds_read_b128 v[10:13], v5 offset:18432
	ds_read_b128 v[14:17], v5 offset:16384
	ds_read_b128 v[18:21], v7
	ds_read_b128 v[22:25], v7 offset:2048
	ds_read_b128 v[30:33], v7 offset:4096
	ds_read_b128 v[34:37], v7 offset:6144
	s_load_dwordx2 s[0:1], s[0:1], 0x20
	v_bfe_u32 v0, v0, 4, 2
	v_bitop3_b32 v8, v0, v8, 4 bitop3:0x36
	v_or_b32_e32 v103, 0x4000, v6
	s_waitcnt lgkmcnt(0)
	v_mfma_f32_16x16x32_f16 v[26:29], v[14:17], v[18:21], 0
	v_lshlrev_b32_e32 v104, 4, v8
	v_mfma_f32_16x16x32_f16 v[18:21], v[10:13], v[18:21], 0
	v_add_u32_e32 v6, v38, v104
	ds_read_b128 v[38:41], v6
	ds_read_b128 v[42:45], v6 offset:2048
	ds_read_b128 v[46:49], v6 offset:4096
	ds_read_b128 v[50:53], v6 offset:6144
	v_add_u32_e32 v8, v9, v104
	ds_read_b128 v[54:57], v8 offset:16384
	ds_read_b128 v[58:61], v8 offset:18432
	v_mfma_f32_16x16x32_f16 v[62:65], v[14:17], v[22:25], 0
	v_mfma_f32_16x16x32_f16 v[22:25], v[10:13], v[22:25], 0
	v_mfma_f32_16x16x32_f16 v[66:69], v[14:17], v[30:33], 0
	v_mfma_f32_16x16x32_f16 v[30:33], v[10:13], v[30:33], 0
	v_mfma_f32_16x16x32_f16 v[14:17], v[14:17], v[34:37], 0
	v_mfma_f32_16x16x32_f16 v[10:13], v[10:13], v[34:37], 0
	s_add_u32 s20, s2, 0x200
	s_mov_b32 m0, s18
	s_waitcnt vmcnt(8) lgkmcnt(0)
	s_barrier
	s_addc_u32 s21, s3, 0
	s_add_u32 s22, s4, 0x200
	global_load_lds_dwordx4 v3, s[20:21]
	s_mov_b32 m0, s15
	s_addc_u32 s23, s5, 0
	global_load_lds_dwordx4 v4, s[20:21]
	s_mov_b32 m0, s16
	s_nop 0
	global_load_lds_dwordx4 v3, s[22:23]
	s_mov_b32 m0, s17
	s_nop 0
	global_load_lds_dwordx4 v4, s[22:23]
	s_waitcnt lgkmcnt(0)
	v_mfma_f32_16x16x32_f16 v[26:29], v[54:57], v[38:41], v[26:29]
	v_mfma_f32_16x16x32_f16 v[18:21], v[58:61], v[38:41], v[18:21]
	ds_read_b128 v[34:37], v7 offset:32768
	ds_read_b128 v[38:41], v7 offset:34816
	ds_read_b128 v[70:73], v7 offset:36864
	ds_read_b128 v[74:77], v7 offset:38912
	ds_read_b128 v[78:81], v5 offset:49152
	ds_read_b128 v[82:85], v5 offset:51200
	v_mfma_f32_16x16x32_f16 v[62:65], v[54:57], v[42:45], v[62:65]
	v_mfma_f32_16x16x32_f16 v[22:25], v[58:61], v[42:45], v[22:25]
	v_mfma_f32_16x16x32_f16 v[42:45], v[54:57], v[46:49], v[66:69]
	v_mfma_f32_16x16x32_f16 v[30:33], v[58:61], v[46:49], v[30:33]
	v_mfma_f32_16x16x32_f16 v[14:17], v[54:57], v[50:53], v[14:17]
	v_mfma_f32_16x16x32_f16 v[10:13], v[58:61], v[50:53], v[10:13]
	s_waitcnt lgkmcnt(0)
	v_mfma_f32_16x16x32_f16 v[26:29], v[78:81], v[34:37], v[26:29]
	v_mfma_f32_16x16x32_f16 v[18:21], v[82:85], v[34:37], v[18:21]
	ds_read_b128 v[34:37], v6 offset:32768
	ds_read_b128 v[46:49], v6 offset:34816
	ds_read_b128 v[50:53], v6 offset:36864
	ds_read_b128 v[54:57], v6 offset:38912
	ds_read_b128 v[58:61], v8 offset:49152
	ds_read_b128 v[66:69], v8 offset:51200
	v_mfma_f32_16x16x32_f16 v[62:65], v[78:81], v[38:41], v[62:65]
	v_mfma_f32_16x16x32_f16 v[22:25], v[82:85], v[38:41], v[22:25]
	v_mfma_f32_16x16x32_f16 v[38:41], v[78:81], v[70:73], v[42:45]
	v_mfma_f32_16x16x32_f16 v[30:33], v[82:85], v[70:73], v[30:33]
	v_mfma_f32_16x16x32_f16 v[42:45], v[78:81], v[74:77], v[14:17]
	v_mfma_f32_16x16x32_f16 v[70:73], v[82:85], v[74:77], v[10:13]
	s_add_u32 s20, s2, 0x280
	s_mov_b32 m0, s14
	s_waitcnt vmcnt(8) lgkmcnt(0)
	s_barrier
	s_addc_u32 s21, s3, 0
	s_add_u32 s22, s4, 0x280
	global_load_lds_dwordx4 v3, s[20:21]
	s_mov_b32 m0, s6
	s_addc_u32 s23, s5, 0
	global_load_lds_dwordx4 v4, s[20:21]
	s_mov_b32 m0, s7
	s_nop 0
	global_load_lds_dwordx4 v3, s[22:23]
	s_mov_b32 m0, s10
	s_nop 0
	global_load_lds_dwordx4 v4, s[22:23]
	s_waitcnt lgkmcnt(0)
	v_mfma_f32_16x16x32_f16 v[26:29], v[58:61], v[34:37], v[26:29]
	v_mfma_f32_16x16x32_f16 v[16:19], v[66:69], v[34:37], v[18:21]
	v_add_u32_e32 v9, 0x10000, v7
	v_add_u32_e32 v11, 0x11000, v7
	v_add_u32_e32 v13, 0x14000, v5
	v_add_u32_e32 v10, 0x10800, v7
	ds_read_b128 v[34:37], v9
	ds_read_b128 v[74:77], v10
	v_add_u32_e32 v12, 0x11800, v7
	ds_read_b128 v[78:81], v11
	ds_read_b128 v[82:85], v12
	v_add_u32_e32 v14, 0x14800, v5
	ds_read_b128 v[86:89], v13
	ds_read_b128 v[90:93], v14
	v_mfma_f32_16x16x32_f16 v[62:65], v[58:61], v[46:49], v[62:65]
	v_mfma_f32_16x16x32_f16 v[20:23], v[66:69], v[46:49], v[22:25]
	v_mfma_f32_16x16x32_f16 v[38:41], v[58:61], v[50:53], v[38:41]
	v_mfma_f32_16x16x32_f16 v[30:33], v[66:69], v[50:53], v[30:33]
	v_mfma_f32_16x16x32_f16 v[42:45], v[58:61], v[54:57], v[42:45]
	v_mfma_f32_16x16x32_f16 v[46:49], v[66:69], v[54:57], v[70:73]
	s_waitcnt lgkmcnt(0)
	v_mfma_f32_16x16x32_f16 v[24:27], v[86:89], v[34:37], v[26:29]
	v_mfma_f32_16x16x32_f16 v[34:37], v[90:93], v[34:37], v[16:19]
	s_add_i32 s19, 0, 0x10000
	s_nop 1
	v_add_u32_e32 v16, s19, v104
	v_add_u32_e32 v15, v16, v102
	ds_read_b128 v[50:53], v15
	ds_read_b128 v[54:57], v15 offset:2048
	ds_read_b128 v[58:61], v15 offset:4096
	ds_read_b128 v[66:69], v15 offset:6144
	v_add_u32_e32 v16, v16, v103
	ds_read_b128 v[70:73], v16
	ds_read_b128 v[94:97], v16 offset:2048
	v_mfma_f32_16x16x32_f16 v[62:65], v[86:89], v[74:77], v[62:65]
	v_mfma_f32_16x16x32_f16 v[74:77], v[90:93], v[74:77], v[20:23]
	v_mfma_f32_16x16x32_f16 v[38:41], v[86:89], v[78:81], v[38:41]
	v_mfma_f32_16x16x32_f16 v[28:31], v[90:93], v[78:81], v[30:33]
	v_mfma_f32_16x16x32_f16 v[42:45], v[86:89], v[82:85], v[42:45]
	v_mfma_f32_16x16x32_f16 v[46:49], v[90:93], v[82:85], v[46:49]
	v_add_u32_e32 v17, s19, v106
	s_add_u32 s20, s2, 0x300
	v_readfirstlane_b32 s22, v17
	v_add_u32_e32 v18, 0x2000, v17
	s_waitcnt vmcnt(8) lgkmcnt(0)
	s_barrier
	s_addc_u32 s21, s3, 0
	s_mov_b32 m0, s22
	v_readfirstlane_b32 s19, v18
	global_load_lds_dwordx4 v3, s[20:21]
	s_mov_b32 m0, s19
	v_add_u32_e32 v18, 0x4000, v17
	s_add_u32 s24, s4, 0x300
	global_load_lds_dwordx4 v4, s[20:21]
	v_readfirstlane_b32 s20, v18
	v_add_u32_e32 v17, 0x6000, v17
	s_addc_u32 s25, s5, 0
	s_mov_b32 m0, s20
	v_readfirstlane_b32 s21, v17
	global_load_lds_dwordx4 v3, s[24:25]
	s_mov_b32 m0, s21
	s_nop 0
	global_load_lds_dwordx4 v4, s[24:25]
	s_waitcnt lgkmcnt(0)
	v_mfma_f32_16x16x32_f16 v[24:27], v[70:73], v[50:53], v[24:27]
	v_mfma_f32_16x16x32_f16 v[32:35], v[94:97], v[50:53], v[34:37]
	v_add_u32_e32 v17, 0x18000, v7
	v_add_u32_e32 v19, 0x19000, v7
	v_add_u32_e32 v21, 0x1c000, v5
	v_add_u32_e32 v18, 0x18800, v7
	ds_read_b128 v[50:53], v17
	ds_read_b128 v[78:81], v18
	v_add_u32_e32 v20, 0x19800, v7
	ds_read_b128 v[82:85], v19
	ds_read_b128 v[86:89], v20
	v_add_u32_e32 v22, 0x1c800, v5
	ds_read_b128 v[90:93], v21
	ds_read_b128 v[98:101], v22
	v_mfma_f32_16x16x32_f16 v[62:65], v[70:73], v[54:57], v[62:65]
	v_mfma_f32_16x16x32_f16 v[54:57], v[94:97], v[54:57], v[74:77]
	v_mfma_f32_16x16x32_f16 v[36:39], v[70:73], v[58:61], v[38:41]
	v_mfma_f32_16x16x32_f16 v[28:31], v[94:97], v[58:61], v[28:31]
	v_mfma_f32_16x16x32_f16 v[40:43], v[70:73], v[66:69], v[42:45]
	v_mfma_f32_16x16x32_f16 v[44:47], v[94:97], v[66:69], v[46:49]
	s_waitcnt lgkmcnt(0)
	v_mfma_f32_16x16x32_f16 v[58:61], v[90:93], v[50:53], v[24:27]
	v_mfma_f32_16x16x32_f16 v[32:35], v[98:101], v[50:53], v[32:35]
	s_add_i32 s23, 0, 0x18000
	s_nop 0
	v_add_u32_e32 v24, s23, v104
	v_add_u32_e32 v23, v24, v102
	ds_read_b128 v[48:51], v23
	ds_read_b128 v[66:69], v23 offset:2048
	ds_read_b128 v[70:73], v23 offset:4096
	ds_read_b128 v[74:77], v23 offset:6144
	v_add_u32_e32 v24, v24, v103
	ds_read_b128 v[94:97], v24
	ds_read_b128 v[102:105], v24 offset:2048
	v_mfma_f32_16x16x32_f16 v[62:65], v[90:93], v[78:81], v[62:65]
	v_mfma_f32_16x16x32_f16 v[52:55], v[98:101], v[78:81], v[54:57]
	v_mfma_f32_16x16x32_f16 v[36:39], v[90:93], v[82:85], v[36:39]
	v_mfma_f32_16x16x32_f16 v[26:29], v[98:101], v[82:85], v[28:31]
	v_mfma_f32_16x16x32_f16 v[40:43], v[90:93], v[86:89], v[40:43]
	v_mfma_f32_16x16x32_f16 v[44:47], v[98:101], v[86:89], v[44:47]
	v_add_u32_e32 v25, s23, v106
	s_add_u32 s24, s2, 0x380
	v_readfirstlane_b32 s26, v25
	v_add_u32_e32 v30, 0x2000, v25
	s_waitcnt vmcnt(8) lgkmcnt(0)
	s_barrier
	s_addc_u32 s25, s3, 0
	s_mov_b32 m0, s26
	v_readfirstlane_b32 s23, v30
	global_load_lds_dwordx4 v3, s[24:25]
	s_mov_b32 m0, s23
	v_add_u32_e32 v30, 0x4000, v25
	s_add_u32 s28, s4, 0x380
	global_load_lds_dwordx4 v4, s[24:25]
	v_readfirstlane_b32 s24, v30
	v_add_u32_e32 v25, 0x6000, v25
	s_addc_u32 s29, s5, 0
	s_mov_b32 m0, s24
	v_readfirstlane_b32 s25, v25
	global_load_lds_dwordx4 v3, s[28:29]
	s_mov_b32 m0, s25
	s_nop 0
	global_load_lds_dwordx4 v4, s[28:29]
	s_waitcnt lgkmcnt(0)
	v_mfma_f32_16x16x32_f16 v[56:59], v[94:97], v[48:51], v[58:61]
	v_mfma_f32_16x16x32_f16 v[30:33], v[102:105], v[48:51], v[32:35]
	ds_read_b128 v[48:51], v7
	ds_read_b128 v[78:81], v7 offset:2048
	ds_read_b128 v[82:85], v7 offset:4096
	ds_read_b128 v[86:89], v7 offset:6144
	ds_read_b128 v[90:93], v5 offset:16384
	ds_read_b128 v[98:101], v5 offset:18432
	v_mfma_f32_16x16x32_f16 v[60:63], v[94:97], v[66:69], v[62:65]
	v_mfma_f32_16x16x32_f16 v[52:55], v[102:105], v[66:69], v[52:55]
	v_mfma_f32_16x16x32_f16 v[34:37], v[94:97], v[70:73], v[36:39]
	v_mfma_f32_16x16x32_f16 v[26:29], v[102:105], v[70:73], v[26:29]
	v_mfma_f32_16x16x32_f16 v[38:41], v[94:97], v[74:77], v[40:43]
	v_mfma_f32_16x16x32_f16 v[42:45], v[102:105], v[74:77], v[44:47]
	s_waitcnt lgkmcnt(0)
	v_mfma_f32_16x16x32_f16 v[56:59], v[90:93], v[48:51], v[56:59]
	v_mfma_f32_16x16x32_f16 v[30:33], v[98:101], v[48:51], v[30:33]
	ds_read_b128 v[46:49], v6
	ds_read_b128 v[64:67], v6 offset:2048
	ds_read_b128 v[68:71], v6 offset:4096
	ds_read_b128 v[72:75], v6 offset:6144
	ds_read_b128 v[94:97], v8 offset:16384
	ds_read_b128 v[102:105], v8 offset:18432
	v_mfma_f32_16x16x32_f16 v[60:63], v[90:93], v[78:81], v[60:63]
	v_mfma_f32_16x16x32_f16 v[50:53], v[98:101], v[78:81], v[52:55]
	v_mfma_f32_16x16x32_f16 v[34:37], v[90:93], v[82:85], v[34:37]
	v_mfma_f32_16x16x32_f16 v[26:29], v[98:101], v[82:85], v[26:29]
	v_mfma_f32_16x16x32_f16 v[38:41], v[90:93], v[86:89], v[38:41]
	v_mfma_f32_16x16x32_f16 v[42:45], v[98:101], v[86:89], v[42:45]
	s_add_u32 s28, s2, 0x400
	s_mov_b32 m0, s18
	s_waitcnt vmcnt(8) lgkmcnt(0)
	s_barrier
	s_addc_u32 s29, s3, 0
	s_add_u32 s30, s4, 0x400
	global_load_lds_dwordx4 v3, s[28:29]
	s_mov_b32 m0, s15
	s_addc_u32 s31, s5, 0
	global_load_lds_dwordx4 v4, s[28:29]
	s_mov_b32 m0, s16
	s_nop 0
	global_load_lds_dwordx4 v3, s[30:31]
	s_mov_b32 m0, s17
	s_nop 0
	global_load_lds_dwordx4 v4, s[30:31]
	s_waitcnt lgkmcnt(0)
	v_mfma_f32_16x16x32_f16 v[54:57], v[94:97], v[46:49], v[56:59]
	v_mfma_f32_16x16x32_f16 v[30:33], v[102:105], v[46:49], v[30:33]
	ds_read_b128 v[46:49], v7 offset:32768
	ds_read_b128 v[76:79], v7 offset:34816
	ds_read_b128 v[80:83], v7 offset:36864
	ds_read_b128 v[84:87], v7 offset:38912
	ds_read_b128 v[88:91], v5 offset:49152
	ds_read_b128 v[98:101], v5 offset:51200
	v_mfma_f32_16x16x32_f16 v[58:61], v[94:97], v[64:67], v[60:63]
	v_mfma_f32_16x16x32_f16 v[50:53], v[102:105], v[64:67], v[50:53]
	v_mfma_f32_16x16x32_f16 v[34:37], v[94:97], v[68:71], v[34:37]
	v_mfma_f32_16x16x32_f16 v[26:29], v[102:105], v[68:71], v[26:29]
	v_mfma_f32_16x16x32_f16 v[38:41], v[94:97], v[72:75], v[38:41]
	v_mfma_f32_16x16x32_f16 v[42:45], v[102:105], v[72:75], v[42:45]
	s_waitcnt lgkmcnt(0)
	v_mfma_f32_16x16x32_f16 v[54:57], v[88:91], v[46:49], v[54:57]
	v_mfma_f32_16x16x32_f16 v[30:33], v[98:101], v[46:49], v[30:33]
	ds_read_b128 v[46:49], v6 offset:32768
	ds_read_b128 v[62:65], v6 offset:34816
	ds_read_b128 v[66:69], v6 offset:36864
	ds_read_b128 v[70:73], v6 offset:38912
	ds_read_b128 v[92:95], v8 offset:49152
	ds_read_b128 v[102:105], v8 offset:51200
	v_mfma_f32_16x16x32_f16 v[58:61], v[88:91], v[76:79], v[58:61]
	v_mfma_f32_16x16x32_f16 v[50:53], v[98:101], v[76:79], v[50:53]
	v_mfma_f32_16x16x32_f16 v[34:37], v[88:91], v[80:83], v[34:37]
	v_mfma_f32_16x16x32_f16 v[26:29], v[98:101], v[80:83], v[26:29]
	v_mfma_f32_16x16x32_f16 v[38:41], v[88:91], v[84:87], v[38:41]
	v_mfma_f32_16x16x32_f16 v[42:45], v[98:101], v[84:87], v[42:45]
	s_add_u32 s28, s2, 0x480
	s_mov_b32 m0, s14
	s_waitcnt vmcnt(8) lgkmcnt(0)
	s_barrier
	s_addc_u32 s29, s3, 0
	s_add_u32 s30, s4, 0x480
	global_load_lds_dwordx4 v3, s[28:29]
	s_mov_b32 m0, s6
	s_addc_u32 s31, s5, 0
	global_load_lds_dwordx4 v4, s[28:29]
	s_mov_b32 m0, s7
	s_nop 0
	global_load_lds_dwordx4 v3, s[30:31]
	s_mov_b32 m0, s10
	s_nop 0
	global_load_lds_dwordx4 v4, s[30:31]
	s_waitcnt lgkmcnt(0)
	v_mfma_f32_16x16x32_f16 v[54:57], v[92:95], v[46:49], v[54:57]
	v_mfma_f32_16x16x32_f16 v[30:33], v[102:105], v[46:49], v[30:33]
	ds_read_b128 v[46:49], v9
	ds_read_b128 v[74:77], v10
	ds_read_b128 v[78:81], v11
	ds_read_b128 v[82:85], v12
	ds_read_b128 v[86:89], v13
	ds_read_b128 v[96:99], v14
	v_mfma_f32_16x16x32_f16 v[58:61], v[92:95], v[62:65], v[58:61]
	v_mfma_f32_16x16x32_f16 v[50:53], v[102:105], v[62:65], v[50:53]
	v_mfma_f32_16x16x32_f16 v[34:37], v[92:95], v[66:69], v[34:37]
	v_mfma_f32_16x16x32_f16 v[26:29], v[102:105], v[66:69], v[26:29]
	v_mfma_f32_16x16x32_f16 v[38:41], v[92:95], v[70:73], v[38:41]
	v_mfma_f32_16x16x32_f16 v[42:45], v[102:105], v[70:73], v[42:45]
	s_waitcnt lgkmcnt(0)
	v_mfma_f32_16x16x32_f16 v[54:57], v[86:89], v[46:49], v[54:57]
	v_mfma_f32_16x16x32_f16 v[30:33], v[96:99], v[46:49], v[30:33]
	ds_read_b128 v[46:49], v15
	ds_read_b128 v[62:65], v15 offset:2048
	ds_read_b128 v[66:69], v15 offset:4096
	ds_read_b128 v[70:73], v15 offset:6144
	ds_read_b128 v[90:93], v16
	ds_read_b128 v[100:103], v16 offset:2048
	v_mfma_f32_16x16x32_f16 v[58:61], v[86:89], v[74:77], v[58:61]
	v_mfma_f32_16x16x32_f16 v[50:53], v[96:99], v[74:77], v[50:53]
	v_mfma_f32_16x16x32_f16 v[34:37], v[86:89], v[78:81], v[34:37]
	v_mfma_f32_16x16x32_f16 v[26:29], v[96:99], v[78:81], v[26:29]
	v_mfma_f32_16x16x32_f16 v[38:41], v[86:89], v[82:85], v[38:41]
	v_mfma_f32_16x16x32_f16 v[42:45], v[96:99], v[82:85], v[42:45]
	s_add_u32 s28, s2, 0x500
	s_mov_b32 m0, s22
	s_waitcnt vmcnt(8) lgkmcnt(0)
	s_barrier
	s_addc_u32 s29, s3, 0
	s_add_u32 s30, s4, 0x500
	global_load_lds_dwordx4 v3, s[28:29]
	s_mov_b32 m0, s19
	s_addc_u32 s31, s5, 0
	global_load_lds_dwordx4 v4, s[28:29]
	s_mov_b32 m0, s20
	s_nop 0
	global_load_lds_dwordx4 v3, s[30:31]
	s_mov_b32 m0, s21
	s_nop 0
	global_load_lds_dwordx4 v4, s[30:31]
	s_waitcnt lgkmcnt(0)
	v_mfma_f32_16x16x32_f16 v[54:57], v[90:93], v[46:49], v[54:57]
	v_mfma_f32_16x16x32_f16 v[30:33], v[100:103], v[46:49], v[30:33]
	ds_read_b128 v[46:49], v17
	ds_read_b128 v[74:77], v18
	ds_read_b128 v[78:81], v19
	ds_read_b128 v[82:85], v20
	ds_read_b128 v[86:89], v21
	ds_read_b128 v[94:97], v22
	v_mfma_f32_16x16x32_f16 v[58:61], v[90:93], v[62:65], v[58:61]
	v_mfma_f32_16x16x32_f16 v[50:53], v[100:103], v[62:65], v[50:53]
	v_mfma_f32_16x16x32_f16 v[34:37], v[90:93], v[66:69], v[34:37]
	v_mfma_f32_16x16x32_f16 v[26:29], v[100:103], v[66:69], v[26:29]
	v_mfma_f32_16x16x32_f16 v[38:41], v[90:93], v[70:73], v[38:41]
	v_mfma_f32_16x16x32_f16 v[42:45], v[100:103], v[70:73], v[42:45]
	s_waitcnt lgkmcnt(0)
	v_mfma_f32_16x16x32_f16 v[54:57], v[86:89], v[46:49], v[54:57]
	v_mfma_f32_16x16x32_f16 v[30:33], v[94:97], v[46:49], v[30:33]
	ds_read_b128 v[46:49], v23
	ds_read_b128 v[62:65], v23 offset:2048
	ds_read_b128 v[66:69], v23 offset:4096
	ds_read_b128 v[70:73], v23 offset:6144
	ds_read_b128 v[90:93], v24
	ds_read_b128 v[98:101], v24 offset:2048
	v_mfma_f32_16x16x32_f16 v[58:61], v[86:89], v[74:77], v[58:61]
	v_mfma_f32_16x16x32_f16 v[50:53], v[94:97], v[74:77], v[50:53]
	v_mfma_f32_16x16x32_f16 v[34:37], v[86:89], v[78:81], v[34:37]
	v_mfma_f32_16x16x32_f16 v[26:29], v[94:97], v[78:81], v[26:29]
	v_mfma_f32_16x16x32_f16 v[38:41], v[86:89], v[82:85], v[38:41]
	v_mfma_f32_16x16x32_f16 v[42:45], v[94:97], v[82:85], v[42:45]
	s_add_u32 s28, s2, 0x580
	s_mov_b32 m0, s26
	s_waitcnt vmcnt(8) lgkmcnt(0)
	s_barrier
	s_addc_u32 s29, s3, 0
	s_add_u32 s30, s4, 0x580
	global_load_lds_dwordx4 v3, s[28:29]
	s_mov_b32 m0, s23
	s_addc_u32 s31, s5, 0
	global_load_lds_dwordx4 v4, s[28:29]
	s_mov_b32 m0, s24
	s_nop 0
	global_load_lds_dwordx4 v3, s[30:31]
	s_mov_b32 m0, s25
	s_nop 0
	global_load_lds_dwordx4 v4, s[30:31]
	s_waitcnt lgkmcnt(0)
	v_mfma_f32_16x16x32_f16 v[54:57], v[90:93], v[46:49], v[54:57]
	v_mfma_f32_16x16x32_f16 v[30:33], v[98:101], v[46:49], v[30:33]
	ds_read_b128 v[46:49], v7
	ds_read_b128 v[74:77], v7 offset:2048
	ds_read_b128 v[78:81], v7 offset:4096
	ds_read_b128 v[82:85], v7 offset:6144
	ds_read_b128 v[86:89], v5 offset:16384
	ds_read_b128 v[94:97], v5 offset:18432
	v_mfma_f32_16x16x32_f16 v[58:61], v[90:93], v[62:65], v[58:61]
	v_mfma_f32_16x16x32_f16 v[50:53], v[98:101], v[62:65], v[50:53]
	v_mfma_f32_16x16x32_f16 v[34:37], v[90:93], v[66:69], v[34:37]
	v_mfma_f32_16x16x32_f16 v[26:29], v[98:101], v[66:69], v[26:29]
	v_mfma_f32_16x16x32_f16 v[38:41], v[90:93], v[70:73], v[38:41]
	v_mfma_f32_16x16x32_f16 v[42:45], v[98:101], v[70:73], v[42:45]
	s_waitcnt lgkmcnt(0)
	v_mfma_f32_16x16x32_f16 v[54:57], v[86:89], v[46:49], v[54:57]
	v_mfma_f32_16x16x32_f16 v[30:33], v[94:97], v[46:49], v[30:33]
	ds_read_b128 v[46:49], v6
	ds_read_b128 v[62:65], v6 offset:2048
	ds_read_b128 v[66:69], v6 offset:4096
	ds_read_b128 v[70:73], v6 offset:6144
	ds_read_b128 v[90:93], v8 offset:16384
	ds_read_b128 v[98:101], v8 offset:18432
	v_mfma_f32_16x16x32_f16 v[58:61], v[86:89], v[74:77], v[58:61]
	v_mfma_f32_16x16x32_f16 v[50:53], v[94:97], v[74:77], v[50:53]
	v_mfma_f32_16x16x32_f16 v[34:37], v[86:89], v[78:81], v[34:37]
	v_mfma_f32_16x16x32_f16 v[26:29], v[94:97], v[78:81], v[26:29]
	v_mfma_f32_16x16x32_f16 v[38:41], v[86:89], v[82:85], v[38:41]
	v_mfma_f32_16x16x32_f16 v[42:45], v[94:97], v[82:85], v[42:45]
	s_add_u32 s28, s2, 0x600
	s_mov_b32 m0, s18
	s_waitcnt vmcnt(8) lgkmcnt(0)
	s_barrier
	s_addc_u32 s29, s3, 0
	s_add_u32 s30, s4, 0x600
	global_load_lds_dwordx4 v3, s[28:29]
	s_mov_b32 m0, s15
	s_addc_u32 s31, s5, 0
	global_load_lds_dwordx4 v4, s[28:29]
	s_mov_b32 m0, s16
	s_nop 0
	global_load_lds_dwordx4 v3, s[30:31]
	s_mov_b32 m0, s17
	s_nop 0
	global_load_lds_dwordx4 v4, s[30:31]
	s_waitcnt lgkmcnt(0)
	v_mfma_f32_16x16x32_f16 v[54:57], v[90:93], v[46:49], v[54:57]
	v_mfma_f32_16x16x32_f16 v[30:33], v[98:101], v[46:49], v[30:33]
	ds_read_b128 v[46:49], v7 offset:32768
	ds_read_b128 v[74:77], v7 offset:34816
	ds_read_b128 v[78:81], v7 offset:36864
	ds_read_b128 v[82:85], v7 offset:38912
	ds_read_b128 v[86:89], v5 offset:49152
	ds_read_b128 v[94:97], v5 offset:51200
	v_mfma_f32_16x16x32_f16 v[58:61], v[90:93], v[62:65], v[58:61]
	v_mfma_f32_16x16x32_f16 v[50:53], v[98:101], v[62:65], v[50:53]
	v_mfma_f32_16x16x32_f16 v[34:37], v[90:93], v[66:69], v[34:37]
	v_mfma_f32_16x16x32_f16 v[26:29], v[98:101], v[66:69], v[26:29]
	v_mfma_f32_16x16x32_f16 v[38:41], v[90:93], v[70:73], v[38:41]
	v_mfma_f32_16x16x32_f16 v[42:45], v[98:101], v[70:73], v[42:45]
	s_waitcnt lgkmcnt(0)
	v_mfma_f32_16x16x32_f16 v[54:57], v[86:89], v[46:49], v[54:57]
	v_mfma_f32_16x16x32_f16 v[30:33], v[94:97], v[46:49], v[30:33]
	ds_read_b128 v[46:49], v6 offset:32768
	ds_read_b128 v[62:65], v6 offset:34816
	ds_read_b128 v[66:69], v6 offset:36864
	ds_read_b128 v[70:73], v6 offset:38912
	ds_read_b128 v[90:93], v8 offset:49152
	ds_read_b128 v[98:101], v8 offset:51200
	v_mfma_f32_16x16x32_f16 v[58:61], v[86:89], v[74:77], v[58:61]
	v_mfma_f32_16x16x32_f16 v[50:53], v[94:97], v[74:77], v[50:53]
	v_mfma_f32_16x16x32_f16 v[34:37], v[86:89], v[78:81], v[34:37]
	v_mfma_f32_16x16x32_f16 v[26:29], v[94:97], v[78:81], v[26:29]
	v_mfma_f32_16x16x32_f16 v[38:41], v[86:89], v[82:85], v[38:41]
	v_mfma_f32_16x16x32_f16 v[42:45], v[94:97], v[82:85], v[42:45]
	s_add_u32 s28, s2, 0x680
	s_mov_b32 m0, s14
	s_waitcnt vmcnt(8) lgkmcnt(0)
	s_barrier
	s_addc_u32 s29, s3, 0
	s_add_u32 s30, s4, 0x680
	global_load_lds_dwordx4 v3, s[28:29]
	s_mov_b32 m0, s6
	s_addc_u32 s31, s5, 0
	global_load_lds_dwordx4 v4, s[28:29]
	s_mov_b32 m0, s7
	s_nop 0
	global_load_lds_dwordx4 v3, s[30:31]
	s_mov_b32 m0, s10
	s_nop 0
	global_load_lds_dwordx4 v4, s[30:31]
	s_waitcnt lgkmcnt(0)
	v_mfma_f32_16x16x32_f16 v[54:57], v[90:93], v[46:49], v[54:57]
	v_mfma_f32_16x16x32_f16 v[30:33], v[98:101], v[46:49], v[30:33]
	ds_read_b128 v[46:49], v9
	ds_read_b128 v[74:77], v10
	ds_read_b128 v[78:81], v11
	ds_read_b128 v[82:85], v12
	ds_read_b128 v[86:89], v13
	ds_read_b128 v[94:97], v14
	v_mfma_f32_16x16x32_f16 v[58:61], v[90:93], v[62:65], v[58:61]
	v_mfma_f32_16x16x32_f16 v[50:53], v[98:101], v[62:65], v[50:53]
	v_mfma_f32_16x16x32_f16 v[34:37], v[90:93], v[66:69], v[34:37]
	v_mfma_f32_16x16x32_f16 v[26:29], v[98:101], v[66:69], v[26:29]
	v_mfma_f32_16x16x32_f16 v[38:41], v[90:93], v[70:73], v[38:41]
	v_mfma_f32_16x16x32_f16 v[42:45], v[98:101], v[70:73], v[42:45]
	s_waitcnt lgkmcnt(0)
	v_mfma_f32_16x16x32_f16 v[54:57], v[86:89], v[46:49], v[54:57]
	v_mfma_f32_16x16x32_f16 v[30:33], v[94:97], v[46:49], v[30:33]
	ds_read_b128 v[46:49], v15
	ds_read_b128 v[62:65], v15 offset:2048
	ds_read_b128 v[66:69], v15 offset:4096
	ds_read_b128 v[70:73], v15 offset:6144
	ds_read_b128 v[90:93], v16
	ds_read_b128 v[98:101], v16 offset:2048
	v_mfma_f32_16x16x32_f16 v[58:61], v[86:89], v[74:77], v[58:61]
	v_mfma_f32_16x16x32_f16 v[50:53], v[94:97], v[74:77], v[50:53]
	v_mfma_f32_16x16x32_f16 v[34:37], v[86:89], v[78:81], v[34:37]
	v_mfma_f32_16x16x32_f16 v[26:29], v[94:97], v[78:81], v[26:29]
	v_mfma_f32_16x16x32_f16 v[38:41], v[86:89], v[82:85], v[38:41]
	v_mfma_f32_16x16x32_f16 v[42:45], v[94:97], v[82:85], v[42:45]
	s_add_u32 s28, s2, 0x700
	s_mov_b32 m0, s22
	s_waitcnt vmcnt(8) lgkmcnt(0)
	s_barrier
	s_addc_u32 s29, s3, 0
	s_add_u32 s30, s4, 0x700
	global_load_lds_dwordx4 v3, s[28:29]
	s_mov_b32 m0, s19
	s_addc_u32 s31, s5, 0
	global_load_lds_dwordx4 v4, s[28:29]
	s_mov_b32 m0, s20
	s_nop 0
	global_load_lds_dwordx4 v3, s[30:31]
	s_mov_b32 m0, s21
	s_nop 0
	global_load_lds_dwordx4 v4, s[30:31]
	s_waitcnt lgkmcnt(0)
	v_mfma_f32_16x16x32_f16 v[54:57], v[90:93], v[46:49], v[54:57]
	v_mfma_f32_16x16x32_f16 v[30:33], v[98:101], v[46:49], v[30:33]
	ds_read_b128 v[46:49], v17
	ds_read_b128 v[74:77], v18
	ds_read_b128 v[78:81], v19
	ds_read_b128 v[82:85], v20
	ds_read_b128 v[86:89], v21
	ds_read_b128 v[94:97], v22
	v_mfma_f32_16x16x32_f16 v[58:61], v[90:93], v[62:65], v[58:61]
	v_mfma_f32_16x16x32_f16 v[50:53], v[98:101], v[62:65], v[50:53]
	v_mfma_f32_16x16x32_f16 v[34:37], v[90:93], v[66:69], v[34:37]
	v_mfma_f32_16x16x32_f16 v[26:29], v[98:101], v[66:69], v[26:29]
	v_mfma_f32_16x16x32_f16 v[38:41], v[90:93], v[70:73], v[38:41]
	v_mfma_f32_16x16x32_f16 v[42:45], v[98:101], v[70:73], v[42:45]
	s_waitcnt lgkmcnt(0)
	v_mfma_f32_16x16x32_f16 v[54:57], v[86:89], v[46:49], v[54:57]
	v_mfma_f32_16x16x32_f16 v[30:33], v[94:97], v[46:49], v[30:33]
	ds_read_b128 v[46:49], v23
	ds_read_b128 v[62:65], v23 offset:2048
	ds_read_b128 v[66:69], v23 offset:4096
	ds_read_b128 v[70:73], v23 offset:6144
	ds_read_b128 v[90:93], v24
	ds_read_b128 v[98:101], v24 offset:2048
	v_mfma_f32_16x16x32_f16 v[58:61], v[86:89], v[74:77], v[58:61]
	v_mfma_f32_16x16x32_f16 v[50:53], v[94:97], v[74:77], v[50:53]
	v_mfma_f32_16x16x32_f16 v[34:37], v[86:89], v[78:81], v[34:37]
	v_mfma_f32_16x16x32_f16 v[26:29], v[94:97], v[78:81], v[26:29]
	v_mfma_f32_16x16x32_f16 v[38:41], v[86:89], v[82:85], v[38:41]
	v_mfma_f32_16x16x32_f16 v[42:45], v[94:97], v[82:85], v[42:45]
	s_add_u32 s28, s2, 0x780
	s_mov_b32 m0, s26
	s_waitcnt vmcnt(8) lgkmcnt(0)
	s_barrier
	s_addc_u32 s29, s3, 0
	s_add_u32 s30, s4, 0x780
	global_load_lds_dwordx4 v3, s[28:29]
	s_mov_b32 m0, s23
	s_addc_u32 s31, s5, 0
	global_load_lds_dwordx4 v4, s[28:29]
	s_mov_b32 m0, s24
	s_nop 0
	global_load_lds_dwordx4 v3, s[30:31]
	s_mov_b32 m0, s25
	s_nop 0
	global_load_lds_dwordx4 v4, s[30:31]
	s_waitcnt lgkmcnt(0)
	v_mfma_f32_16x16x32_f16 v[54:57], v[90:93], v[46:49], v[54:57]
	v_mfma_f32_16x16x32_f16 v[30:33], v[98:101], v[46:49], v[30:33]
	ds_read_b128 v[46:49], v7
	ds_read_b128 v[74:77], v7 offset:2048
	ds_read_b128 v[78:81], v7 offset:4096
	ds_read_b128 v[82:85], v7 offset:6144
	ds_read_b128 v[86:89], v5 offset:16384
	ds_read_b128 v[94:97], v5 offset:18432
	v_mfma_f32_16x16x32_f16 v[58:61], v[90:93], v[62:65], v[58:61]
	v_mfma_f32_16x16x32_f16 v[50:53], v[98:101], v[62:65], v[50:53]
	v_mfma_f32_16x16x32_f16 v[34:37], v[90:93], v[66:69], v[34:37]
	v_mfma_f32_16x16x32_f16 v[26:29], v[98:101], v[66:69], v[26:29]
	v_mfma_f32_16x16x32_f16 v[38:41], v[90:93], v[70:73], v[38:41]
	v_mfma_f32_16x16x32_f16 v[42:45], v[98:101], v[70:73], v[42:45]
	s_waitcnt lgkmcnt(0)
	v_mfma_f32_16x16x32_f16 v[54:57], v[86:89], v[46:49], v[54:57]
	v_mfma_f32_16x16x32_f16 v[30:33], v[94:97], v[46:49], v[30:33]
	ds_read_b128 v[46:49], v6
	ds_read_b128 v[62:65], v6 offset:2048
	ds_read_b128 v[66:69], v6 offset:4096
	ds_read_b128 v[70:73], v6 offset:6144
	ds_read_b128 v[90:93], v8 offset:16384
	ds_read_b128 v[98:101], v8 offset:18432
	v_mfma_f32_16x16x32_f16 v[58:61], v[86:89], v[74:77], v[58:61]
	v_mfma_f32_16x16x32_f16 v[50:53], v[94:97], v[74:77], v[50:53]
	v_mfma_f32_16x16x32_f16 v[34:37], v[86:89], v[78:81], v[34:37]
	v_mfma_f32_16x16x32_f16 v[26:29], v[94:97], v[78:81], v[26:29]
	v_mfma_f32_16x16x32_f16 v[38:41], v[86:89], v[82:85], v[38:41]
	v_mfma_f32_16x16x32_f16 v[42:45], v[94:97], v[82:85], v[42:45]
	s_add_u32 s28, s2, 0x800
	s_mov_b32 m0, s18
	s_waitcnt vmcnt(8) lgkmcnt(0)
	s_barrier
	s_addc_u32 s29, s3, 0
	s_add_u32 s30, s4, 0x800
	global_load_lds_dwordx4 v3, s[28:29]
	s_mov_b32 m0, s15
	s_addc_u32 s31, s5, 0
	global_load_lds_dwordx4 v4, s[28:29]
	s_mov_b32 m0, s16
	s_nop 0
	global_load_lds_dwordx4 v3, s[30:31]
	s_mov_b32 m0, s17
	s_nop 0
	global_load_lds_dwordx4 v4, s[30:31]
	s_waitcnt lgkmcnt(0)
	v_mfma_f32_16x16x32_f16 v[54:57], v[90:93], v[46:49], v[54:57]
	v_mfma_f32_16x16x32_f16 v[30:33], v[98:101], v[46:49], v[30:33]
	ds_read_b128 v[46:49], v7 offset:32768
	ds_read_b128 v[74:77], v7 offset:34816
	ds_read_b128 v[78:81], v7 offset:36864
	ds_read_b128 v[82:85], v7 offset:38912
	ds_read_b128 v[86:89], v5 offset:49152
	ds_read_b128 v[94:97], v5 offset:51200
	v_mfma_f32_16x16x32_f16 v[58:61], v[90:93], v[62:65], v[58:61]
	v_mfma_f32_16x16x32_f16 v[50:53], v[98:101], v[62:65], v[50:53]
	v_mfma_f32_16x16x32_f16 v[34:37], v[90:93], v[66:69], v[34:37]
	v_mfma_f32_16x16x32_f16 v[26:29], v[98:101], v[66:69], v[26:29]
	v_mfma_f32_16x16x32_f16 v[38:41], v[90:93], v[70:73], v[38:41]
	v_mfma_f32_16x16x32_f16 v[42:45], v[98:101], v[70:73], v[42:45]
	s_waitcnt lgkmcnt(0)
	v_mfma_f32_16x16x32_f16 v[54:57], v[86:89], v[46:49], v[54:57]
	v_mfma_f32_16x16x32_f16 v[30:33], v[94:97], v[46:49], v[30:33]
	ds_read_b128 v[46:49], v6 offset:32768
	ds_read_b128 v[62:65], v6 offset:34816
	ds_read_b128 v[66:69], v6 offset:36864
	ds_read_b128 v[70:73], v6 offset:38912
	ds_read_b128 v[90:93], v8 offset:49152
	ds_read_b128 v[98:101], v8 offset:51200
	v_mfma_f32_16x16x32_f16 v[58:61], v[86:89], v[74:77], v[58:61]
	v_mfma_f32_16x16x32_f16 v[50:53], v[94:97], v[74:77], v[50:53]
	v_mfma_f32_16x16x32_f16 v[34:37], v[86:89], v[78:81], v[34:37]
	v_mfma_f32_16x16x32_f16 v[26:29], v[94:97], v[78:81], v[26:29]
	v_mfma_f32_16x16x32_f16 v[38:41], v[86:89], v[82:85], v[38:41]
	v_mfma_f32_16x16x32_f16 v[42:45], v[94:97], v[82:85], v[42:45]
	s_add_u32 s28, s2, 0x880
	s_mov_b32 m0, s14
	s_waitcnt vmcnt(8) lgkmcnt(0)
	s_barrier
	s_addc_u32 s29, s3, 0
	s_add_u32 s30, s4, 0x880
	global_load_lds_dwordx4 v3, s[28:29]
	s_mov_b32 m0, s6
	s_addc_u32 s31, s5, 0
	global_load_lds_dwordx4 v4, s[28:29]
	s_mov_b32 m0, s7
	s_nop 0
	global_load_lds_dwordx4 v3, s[30:31]
	s_mov_b32 m0, s10
	s_nop 0
	global_load_lds_dwordx4 v4, s[30:31]
	s_waitcnt lgkmcnt(0)
	v_mfma_f32_16x16x32_f16 v[54:57], v[90:93], v[46:49], v[54:57]
	v_mfma_f32_16x16x32_f16 v[30:33], v[98:101], v[46:49], v[30:33]
	ds_read_b128 v[46:49], v9
	ds_read_b128 v[74:77], v10
	ds_read_b128 v[78:81], v11
	ds_read_b128 v[82:85], v12
	ds_read_b128 v[86:89], v13
	ds_read_b128 v[94:97], v14
	v_mfma_f32_16x16x32_f16 v[58:61], v[90:93], v[62:65], v[58:61]
	v_mfma_f32_16x16x32_f16 v[50:53], v[98:101], v[62:65], v[50:53]
	v_mfma_f32_16x16x32_f16 v[34:37], v[90:93], v[66:69], v[34:37]
	v_mfma_f32_16x16x32_f16 v[26:29], v[98:101], v[66:69], v[26:29]
	v_mfma_f32_16x16x32_f16 v[38:41], v[90:93], v[70:73], v[38:41]
	v_mfma_f32_16x16x32_f16 v[42:45], v[98:101], v[70:73], v[42:45]
	s_waitcnt lgkmcnt(0)
	v_mfma_f32_16x16x32_f16 v[54:57], v[86:89], v[46:49], v[54:57]
	v_mfma_f32_16x16x32_f16 v[30:33], v[94:97], v[46:49], v[30:33]
	ds_read_b128 v[46:49], v15
	ds_read_b128 v[62:65], v15 offset:2048
	ds_read_b128 v[66:69], v15 offset:4096
	ds_read_b128 v[70:73], v15 offset:6144
	ds_read_b128 v[90:93], v16
	ds_read_b128 v[98:101], v16 offset:2048
	v_mfma_f32_16x16x32_f16 v[58:61], v[86:89], v[74:77], v[58:61]
	v_mfma_f32_16x16x32_f16 v[50:53], v[94:97], v[74:77], v[50:53]
	v_mfma_f32_16x16x32_f16 v[34:37], v[86:89], v[78:81], v[34:37]
	v_mfma_f32_16x16x32_f16 v[26:29], v[94:97], v[78:81], v[26:29]
	v_mfma_f32_16x16x32_f16 v[38:41], v[86:89], v[82:85], v[38:41]
	v_mfma_f32_16x16x32_f16 v[42:45], v[94:97], v[82:85], v[42:45]
	s_add_u32 s28, s2, 0x900
	s_mov_b32 m0, s22
	s_waitcnt vmcnt(8) lgkmcnt(0)
	s_barrier
	s_addc_u32 s29, s3, 0
	s_add_u32 s30, s4, 0x900
	global_load_lds_dwordx4 v3, s[28:29]
	s_mov_b32 m0, s19
	s_addc_u32 s31, s5, 0
	global_load_lds_dwordx4 v4, s[28:29]
	s_mov_b32 m0, s20
	s_nop 0
	global_load_lds_dwordx4 v3, s[30:31]
	s_mov_b32 m0, s21
	s_nop 0
	global_load_lds_dwordx4 v4, s[30:31]
	s_waitcnt lgkmcnt(0)
	v_mfma_f32_16x16x32_f16 v[54:57], v[90:93], v[46:49], v[54:57]
	v_mfma_f32_16x16x32_f16 v[30:33], v[98:101], v[46:49], v[30:33]
	ds_read_b128 v[46:49], v17
	ds_read_b128 v[74:77], v18
	ds_read_b128 v[78:81], v19
	ds_read_b128 v[82:85], v20
	ds_read_b128 v[86:89], v21
	ds_read_b128 v[94:97], v22
	v_mfma_f32_16x16x32_f16 v[58:61], v[90:93], v[62:65], v[58:61]
	v_mfma_f32_16x16x32_f16 v[50:53], v[98:101], v[62:65], v[50:53]
	v_mfma_f32_16x16x32_f16 v[34:37], v[90:93], v[66:69], v[34:37]
	v_mfma_f32_16x16x32_f16 v[26:29], v[98:101], v[66:69], v[26:29]
	v_mfma_f32_16x16x32_f16 v[38:41], v[90:93], v[70:73], v[38:41]
	v_mfma_f32_16x16x32_f16 v[42:45], v[98:101], v[70:73], v[42:45]
	s_waitcnt lgkmcnt(0)
	v_mfma_f32_16x16x32_f16 v[54:57], v[86:89], v[46:49], v[54:57]
	v_mfma_f32_16x16x32_f16 v[30:33], v[94:97], v[46:49], v[30:33]
	ds_read_b128 v[46:49], v23
	ds_read_b128 v[62:65], v23 offset:2048
	ds_read_b128 v[66:69], v23 offset:4096
	ds_read_b128 v[70:73], v23 offset:6144
	ds_read_b128 v[90:93], v24
	ds_read_b128 v[98:101], v24 offset:2048
	v_mfma_f32_16x16x32_f16 v[58:61], v[86:89], v[74:77], v[58:61]
	v_mfma_f32_16x16x32_f16 v[50:53], v[94:97], v[74:77], v[50:53]
	v_mfma_f32_16x16x32_f16 v[34:37], v[86:89], v[78:81], v[34:37]
	v_mfma_f32_16x16x32_f16 v[26:29], v[94:97], v[78:81], v[26:29]
	v_mfma_f32_16x16x32_f16 v[38:41], v[86:89], v[82:85], v[38:41]
	v_mfma_f32_16x16x32_f16 v[42:45], v[94:97], v[82:85], v[42:45]
	s_add_u32 s28, s2, 0x980
	s_mov_b32 m0, s26
	s_waitcnt vmcnt(8) lgkmcnt(0)
	s_barrier
	s_addc_u32 s29, s3, 0
	s_add_u32 s30, s4, 0x980
	global_load_lds_dwordx4 v3, s[28:29]
	s_mov_b32 m0, s23
	s_addc_u32 s31, s5, 0
	global_load_lds_dwordx4 v4, s[28:29]
	s_mov_b32 m0, s24
	s_nop 0
	global_load_lds_dwordx4 v3, s[30:31]
	s_mov_b32 m0, s25
	s_nop 0
	global_load_lds_dwordx4 v4, s[30:31]
	s_waitcnt lgkmcnt(0)
	v_mfma_f32_16x16x32_f16 v[54:57], v[90:93], v[46:49], v[54:57]
	v_mfma_f32_16x16x32_f16 v[30:33], v[98:101], v[46:49], v[30:33]
	ds_read_b128 v[46:49], v7
	ds_read_b128 v[74:77], v7 offset:2048
	ds_read_b128 v[78:81], v7 offset:4096
	ds_read_b128 v[82:85], v7 offset:6144
	ds_read_b128 v[86:89], v5 offset:16384
	ds_read_b128 v[94:97], v5 offset:18432
	v_mfma_f32_16x16x32_f16 v[58:61], v[90:93], v[62:65], v[58:61]
	v_mfma_f32_16x16x32_f16 v[50:53], v[98:101], v[62:65], v[50:53]
	v_mfma_f32_16x16x32_f16 v[34:37], v[90:93], v[66:69], v[34:37]
	v_mfma_f32_16x16x32_f16 v[26:29], v[98:101], v[66:69], v[26:29]
	v_mfma_f32_16x16x32_f16 v[38:41], v[90:93], v[70:73], v[38:41]
	v_mfma_f32_16x16x32_f16 v[42:45], v[98:101], v[70:73], v[42:45]
	s_waitcnt lgkmcnt(0)
	v_mfma_f32_16x16x32_f16 v[54:57], v[86:89], v[46:49], v[54:57]
	v_mfma_f32_16x16x32_f16 v[30:33], v[94:97], v[46:49], v[30:33]
	ds_read_b128 v[46:49], v6
	ds_read_b128 v[62:65], v6 offset:2048
	ds_read_b128 v[66:69], v6 offset:4096
	ds_read_b128 v[70:73], v6 offset:6144
	ds_read_b128 v[90:93], v8 offset:16384
	ds_read_b128 v[98:101], v8 offset:18432
	v_mfma_f32_16x16x32_f16 v[58:61], v[86:89], v[74:77], v[58:61]
	v_mfma_f32_16x16x32_f16 v[50:53], v[94:97], v[74:77], v[50:53]
	v_mfma_f32_16x16x32_f16 v[34:37], v[86:89], v[78:81], v[34:37]
	v_mfma_f32_16x16x32_f16 v[26:29], v[94:97], v[78:81], v[26:29]
	v_mfma_f32_16x16x32_f16 v[38:41], v[86:89], v[82:85], v[38:41]
	v_mfma_f32_16x16x32_f16 v[42:45], v[94:97], v[82:85], v[42:45]
	s_add_u32 s28, s2, 0xa00
	s_mov_b32 m0, s18
	s_waitcnt vmcnt(8) lgkmcnt(0)
	s_barrier
	s_addc_u32 s29, s3, 0
	s_add_u32 s30, s4, 0xa00
	global_load_lds_dwordx4 v3, s[28:29]
	s_mov_b32 m0, s15
	s_addc_u32 s31, s5, 0
	global_load_lds_dwordx4 v4, s[28:29]
	s_mov_b32 m0, s16
	s_nop 0
	global_load_lds_dwordx4 v3, s[30:31]
	s_mov_b32 m0, s17
	s_nop 0
	global_load_lds_dwordx4 v4, s[30:31]
	s_waitcnt lgkmcnt(0)
	v_mfma_f32_16x16x32_f16 v[54:57], v[90:93], v[46:49], v[54:57]
	v_mfma_f32_16x16x32_f16 v[30:33], v[98:101], v[46:49], v[30:33]
	ds_read_b128 v[46:49], v7 offset:32768
	ds_read_b128 v[74:77], v7 offset:34816
	ds_read_b128 v[78:81], v7 offset:36864
	ds_read_b128 v[82:85], v7 offset:38912
	ds_read_b128 v[86:89], v5 offset:49152
	ds_read_b128 v[94:97], v5 offset:51200
	v_mfma_f32_16x16x32_f16 v[58:61], v[90:93], v[62:65], v[58:61]
	v_mfma_f32_16x16x32_f16 v[50:53], v[98:101], v[62:65], v[50:53]
	v_mfma_f32_16x16x32_f16 v[34:37], v[90:93], v[66:69], v[34:37]
	v_mfma_f32_16x16x32_f16 v[26:29], v[98:101], v[66:69], v[26:29]
	v_mfma_f32_16x16x32_f16 v[38:41], v[90:93], v[70:73], v[38:41]
	v_mfma_f32_16x16x32_f16 v[42:45], v[98:101], v[70:73], v[42:45]
	s_waitcnt lgkmcnt(0)
	v_mfma_f32_16x16x32_f16 v[54:57], v[86:89], v[46:49], v[54:57]
	v_mfma_f32_16x16x32_f16 v[30:33], v[94:97], v[46:49], v[30:33]
	ds_read_b128 v[46:49], v6 offset:32768
	ds_read_b128 v[62:65], v6 offset:34816
	ds_read_b128 v[66:69], v6 offset:36864
	ds_read_b128 v[70:73], v6 offset:38912
	ds_read_b128 v[90:93], v8 offset:49152
	ds_read_b128 v[98:101], v8 offset:51200
	v_mfma_f32_16x16x32_f16 v[58:61], v[86:89], v[74:77], v[58:61]
	v_mfma_f32_16x16x32_f16 v[50:53], v[94:97], v[74:77], v[50:53]
	v_mfma_f32_16x16x32_f16 v[34:37], v[86:89], v[78:81], v[34:37]
	v_mfma_f32_16x16x32_f16 v[26:29], v[94:97], v[78:81], v[26:29]
	v_mfma_f32_16x16x32_f16 v[38:41], v[86:89], v[82:85], v[38:41]
	v_mfma_f32_16x16x32_f16 v[42:45], v[94:97], v[82:85], v[42:45]
	s_add_u32 s28, s2, 0xa80
	s_mov_b32 m0, s14
	s_waitcnt vmcnt(8) lgkmcnt(0)
	s_barrier
	s_addc_u32 s29, s3, 0
	s_add_u32 s30, s4, 0xa80
	global_load_lds_dwordx4 v3, s[28:29]
	s_mov_b32 m0, s6
	s_addc_u32 s31, s5, 0
	global_load_lds_dwordx4 v4, s[28:29]
	s_mov_b32 m0, s7
	s_nop 0
	global_load_lds_dwordx4 v3, s[30:31]
	s_mov_b32 m0, s10
	s_nop 0
	global_load_lds_dwordx4 v4, s[30:31]
	s_waitcnt lgkmcnt(0)
	v_mfma_f32_16x16x32_f16 v[54:57], v[90:93], v[46:49], v[54:57]
	v_mfma_f32_16x16x32_f16 v[30:33], v[98:101], v[46:49], v[30:33]
	ds_read_b128 v[46:49], v9
	ds_read_b128 v[74:77], v10
	ds_read_b128 v[78:81], v11
	ds_read_b128 v[82:85], v12
	ds_read_b128 v[86:89], v13
	ds_read_b128 v[94:97], v14
	v_mfma_f32_16x16x32_f16 v[58:61], v[90:93], v[62:65], v[58:61]
	v_mfma_f32_16x16x32_f16 v[50:53], v[98:101], v[62:65], v[50:53]
	v_mfma_f32_16x16x32_f16 v[34:37], v[90:93], v[66:69], v[34:37]
	v_mfma_f32_16x16x32_f16 v[26:29], v[98:101], v[66:69], v[26:29]
	v_mfma_f32_16x16x32_f16 v[38:41], v[90:93], v[70:73], v[38:41]
	v_mfma_f32_16x16x32_f16 v[42:45], v[98:101], v[70:73], v[42:45]
	s_waitcnt lgkmcnt(0)
	v_mfma_f32_16x16x32_f16 v[54:57], v[86:89], v[46:49], v[54:57]
	v_mfma_f32_16x16x32_f16 v[30:33], v[94:97], v[46:49], v[30:33]
	ds_read_b128 v[46:49], v15
	ds_read_b128 v[62:65], v15 offset:2048
	ds_read_b128 v[66:69], v15 offset:4096
	ds_read_b128 v[70:73], v15 offset:6144
	ds_read_b128 v[90:93], v16
	ds_read_b128 v[98:101], v16 offset:2048
	v_mfma_f32_16x16x32_f16 v[58:61], v[86:89], v[74:77], v[58:61]
	v_mfma_f32_16x16x32_f16 v[50:53], v[94:97], v[74:77], v[50:53]
	v_mfma_f32_16x16x32_f16 v[34:37], v[86:89], v[78:81], v[34:37]
	v_mfma_f32_16x16x32_f16 v[26:29], v[94:97], v[78:81], v[26:29]
	v_mfma_f32_16x16x32_f16 v[38:41], v[86:89], v[82:85], v[38:41]
	v_mfma_f32_16x16x32_f16 v[42:45], v[94:97], v[82:85], v[42:45]
	s_add_u32 s28, s2, 0xb00
	s_mov_b32 m0, s22
	s_waitcnt vmcnt(8) lgkmcnt(0)
	s_barrier
	s_addc_u32 s29, s3, 0
	s_add_u32 s30, s4, 0xb00
	global_load_lds_dwordx4 v3, s[28:29]
	s_mov_b32 m0, s19
	s_addc_u32 s31, s5, 0
	global_load_lds_dwordx4 v4, s[28:29]
	s_mov_b32 m0, s20
	s_nop 0
	global_load_lds_dwordx4 v3, s[30:31]
	s_mov_b32 m0, s21
	s_nop 0
	global_load_lds_dwordx4 v4, s[30:31]
	s_waitcnt lgkmcnt(0)
	v_mfma_f32_16x16x32_f16 v[54:57], v[90:93], v[46:49], v[54:57]
	v_mfma_f32_16x16x32_f16 v[30:33], v[98:101], v[46:49], v[30:33]
	ds_read_b128 v[46:49], v17
	ds_read_b128 v[74:77], v18
	ds_read_b128 v[78:81], v19
	ds_read_b128 v[82:85], v20
	ds_read_b128 v[86:89], v21
	ds_read_b128 v[94:97], v22
	v_mfma_f32_16x16x32_f16 v[58:61], v[90:93], v[62:65], v[58:61]
	v_mfma_f32_16x16x32_f16 v[50:53], v[98:101], v[62:65], v[50:53]
	v_mfma_f32_16x16x32_f16 v[34:37], v[90:93], v[66:69], v[34:37]
	v_mfma_f32_16x16x32_f16 v[26:29], v[98:101], v[66:69], v[26:29]
	v_mfma_f32_16x16x32_f16 v[38:41], v[90:93], v[70:73], v[38:41]
	v_mfma_f32_16x16x32_f16 v[42:45], v[98:101], v[70:73], v[42:45]
	s_waitcnt lgkmcnt(0)
	v_mfma_f32_16x16x32_f16 v[54:57], v[86:89], v[46:49], v[54:57]
	v_mfma_f32_16x16x32_f16 v[30:33], v[94:97], v[46:49], v[30:33]
	ds_read_b128 v[46:49], v23
	ds_read_b128 v[62:65], v23 offset:2048
	ds_read_b128 v[66:69], v23 offset:4096
	ds_read_b128 v[70:73], v23 offset:6144
	ds_read_b128 v[90:93], v24
	ds_read_b128 v[98:101], v24 offset:2048
	v_mfma_f32_16x16x32_f16 v[58:61], v[86:89], v[74:77], v[58:61]
	v_mfma_f32_16x16x32_f16 v[50:53], v[94:97], v[74:77], v[50:53]
	v_mfma_f32_16x16x32_f16 v[34:37], v[86:89], v[78:81], v[34:37]
	v_mfma_f32_16x16x32_f16 v[26:29], v[94:97], v[78:81], v[26:29]
	v_mfma_f32_16x16x32_f16 v[38:41], v[86:89], v[82:85], v[38:41]
	v_mfma_f32_16x16x32_f16 v[42:45], v[94:97], v[82:85], v[42:45]
	s_add_u32 s28, s2, 0xb80
	s_mov_b32 m0, s26
	s_waitcnt vmcnt(8) lgkmcnt(0)
	s_barrier
	s_addc_u32 s29, s3, 0
	s_add_u32 s30, s4, 0xb80
	global_load_lds_dwordx4 v3, s[28:29]
	s_mov_b32 m0, s23
	s_addc_u32 s31, s5, 0
	global_load_lds_dwordx4 v4, s[28:29]
	s_mov_b32 m0, s24
	s_nop 0
	global_load_lds_dwordx4 v3, s[30:31]
	s_mov_b32 m0, s25
	s_nop 0
	global_load_lds_dwordx4 v4, s[30:31]
	s_waitcnt lgkmcnt(0)
	v_mfma_f32_16x16x32_f16 v[54:57], v[90:93], v[46:49], v[54:57]
	v_mfma_f32_16x16x32_f16 v[30:33], v[98:101], v[46:49], v[30:33]
	ds_read_b128 v[46:49], v7
	ds_read_b128 v[74:77], v7 offset:2048
	ds_read_b128 v[78:81], v7 offset:4096
	ds_read_b128 v[82:85], v7 offset:6144
	ds_read_b128 v[86:89], v5 offset:16384
	ds_read_b128 v[94:97], v5 offset:18432
	v_mfma_f32_16x16x32_f16 v[58:61], v[90:93], v[62:65], v[58:61]
	v_mfma_f32_16x16x32_f16 v[50:53], v[98:101], v[62:65], v[50:53]
	v_mfma_f32_16x16x32_f16 v[34:37], v[90:93], v[66:69], v[34:37]
	v_mfma_f32_16x16x32_f16 v[26:29], v[98:101], v[66:69], v[26:29]
	v_mfma_f32_16x16x32_f16 v[38:41], v[90:93], v[70:73], v[38:41]
	v_mfma_f32_16x16x32_f16 v[42:45], v[98:101], v[70:73], v[42:45]
	s_waitcnt lgkmcnt(0)
	v_mfma_f32_16x16x32_f16 v[54:57], v[86:89], v[46:49], v[54:57]
	v_mfma_f32_16x16x32_f16 v[30:33], v[94:97], v[46:49], v[30:33]
	ds_read_b128 v[46:49], v6
	ds_read_b128 v[62:65], v6 offset:2048
	ds_read_b128 v[66:69], v6 offset:4096
	ds_read_b128 v[70:73], v6 offset:6144
	ds_read_b128 v[90:93], v8 offset:16384
	ds_read_b128 v[98:101], v8 offset:18432
	v_mfma_f32_16x16x32_f16 v[58:61], v[86:89], v[74:77], v[58:61]
	v_mfma_f32_16x16x32_f16 v[50:53], v[94:97], v[74:77], v[50:53]
	v_mfma_f32_16x16x32_f16 v[34:37], v[86:89], v[78:81], v[34:37]
	v_mfma_f32_16x16x32_f16 v[26:29], v[94:97], v[78:81], v[26:29]
	v_mfma_f32_16x16x32_f16 v[38:41], v[86:89], v[82:85], v[38:41]
	v_mfma_f32_16x16x32_f16 v[42:45], v[94:97], v[82:85], v[42:45]
	s_add_u32 s28, s2, 0xc00
	s_mov_b32 m0, s18
	s_waitcnt vmcnt(8) lgkmcnt(0)
	s_barrier
	s_addc_u32 s29, s3, 0
	s_add_u32 s30, s4, 0xc00
	global_load_lds_dwordx4 v3, s[28:29]
	s_mov_b32 m0, s15
	s_addc_u32 s31, s5, 0
	global_load_lds_dwordx4 v4, s[28:29]
	s_mov_b32 m0, s16
	s_nop 0
	global_load_lds_dwordx4 v3, s[30:31]
	s_mov_b32 m0, s17
	s_nop 0
	global_load_lds_dwordx4 v4, s[30:31]
	s_waitcnt lgkmcnt(0)
	v_mfma_f32_16x16x32_f16 v[54:57], v[90:93], v[46:49], v[54:57]
	v_mfma_f32_16x16x32_f16 v[30:33], v[98:101], v[46:49], v[30:33]
	ds_read_b128 v[46:49], v7 offset:32768
	ds_read_b128 v[74:77], v7 offset:34816
	ds_read_b128 v[78:81], v7 offset:36864
	ds_read_b128 v[82:85], v7 offset:38912
	ds_read_b128 v[86:89], v5 offset:49152
	ds_read_b128 v[94:97], v5 offset:51200
	v_mfma_f32_16x16x32_f16 v[58:61], v[90:93], v[62:65], v[58:61]
	v_mfma_f32_16x16x32_f16 v[50:53], v[98:101], v[62:65], v[50:53]
	v_mfma_f32_16x16x32_f16 v[34:37], v[90:93], v[66:69], v[34:37]
	v_mfma_f32_16x16x32_f16 v[26:29], v[98:101], v[66:69], v[26:29]
	v_mfma_f32_16x16x32_f16 v[38:41], v[90:93], v[70:73], v[38:41]
	v_mfma_f32_16x16x32_f16 v[42:45], v[98:101], v[70:73], v[42:45]
	s_waitcnt lgkmcnt(0)
	v_mfma_f32_16x16x32_f16 v[54:57], v[86:89], v[46:49], v[54:57]
	v_mfma_f32_16x16x32_f16 v[30:33], v[94:97], v[46:49], v[30:33]
	ds_read_b128 v[46:49], v6 offset:32768
	ds_read_b128 v[62:65], v6 offset:34816
	ds_read_b128 v[66:69], v6 offset:36864
	ds_read_b128 v[70:73], v6 offset:38912
	ds_read_b128 v[90:93], v8 offset:49152
	ds_read_b128 v[98:101], v8 offset:51200
	v_mfma_f32_16x16x32_f16 v[58:61], v[86:89], v[74:77], v[58:61]
	v_mfma_f32_16x16x32_f16 v[50:53], v[94:97], v[74:77], v[50:53]
	v_mfma_f32_16x16x32_f16 v[34:37], v[86:89], v[78:81], v[34:37]
	v_mfma_f32_16x16x32_f16 v[26:29], v[94:97], v[78:81], v[26:29]
	v_mfma_f32_16x16x32_f16 v[38:41], v[86:89], v[82:85], v[38:41]
	v_mfma_f32_16x16x32_f16 v[42:45], v[94:97], v[82:85], v[42:45]
	s_add_u32 s28, s2, 0xc80
	s_mov_b32 m0, s14
	s_waitcnt vmcnt(8) lgkmcnt(0)
	s_barrier
	s_addc_u32 s29, s3, 0
	s_add_u32 s30, s4, 0xc80
	global_load_lds_dwordx4 v3, s[28:29]
	s_mov_b32 m0, s6
	s_addc_u32 s31, s5, 0
	global_load_lds_dwordx4 v4, s[28:29]
	s_mov_b32 m0, s7
	s_nop 0
	global_load_lds_dwordx4 v3, s[30:31]
	s_mov_b32 m0, s10
	s_nop 0
	global_load_lds_dwordx4 v4, s[30:31]
	s_waitcnt lgkmcnt(0)
	v_mfma_f32_16x16x32_f16 v[54:57], v[90:93], v[46:49], v[54:57]
	v_mfma_f32_16x16x32_f16 v[30:33], v[98:101], v[46:49], v[30:33]
	ds_read_b128 v[46:49], v9
	ds_read_b128 v[74:77], v10
	ds_read_b128 v[78:81], v11
	ds_read_b128 v[82:85], v12
	ds_read_b128 v[86:89], v13
	ds_read_b128 v[94:97], v14
	v_mfma_f32_16x16x32_f16 v[58:61], v[90:93], v[62:65], v[58:61]
	v_mfma_f32_16x16x32_f16 v[50:53], v[98:101], v[62:65], v[50:53]
	v_mfma_f32_16x16x32_f16 v[34:37], v[90:93], v[66:69], v[34:37]
	v_mfma_f32_16x16x32_f16 v[26:29], v[98:101], v[66:69], v[26:29]
	v_mfma_f32_16x16x32_f16 v[38:41], v[90:93], v[70:73], v[38:41]
	v_mfma_f32_16x16x32_f16 v[42:45], v[98:101], v[70:73], v[42:45]
	s_waitcnt lgkmcnt(0)
	v_mfma_f32_16x16x32_f16 v[54:57], v[86:89], v[46:49], v[54:57]
	v_mfma_f32_16x16x32_f16 v[30:33], v[94:97], v[46:49], v[30:33]
	ds_read_b128 v[46:49], v15
	ds_read_b128 v[62:65], v15 offset:2048
	ds_read_b128 v[66:69], v15 offset:4096
	ds_read_b128 v[70:73], v15 offset:6144
	ds_read_b128 v[90:93], v16
	ds_read_b128 v[98:101], v16 offset:2048
	v_mfma_f32_16x16x32_f16 v[58:61], v[86:89], v[74:77], v[58:61]
	v_mfma_f32_16x16x32_f16 v[50:53], v[94:97], v[74:77], v[50:53]
	v_mfma_f32_16x16x32_f16 v[34:37], v[86:89], v[78:81], v[34:37]
	v_mfma_f32_16x16x32_f16 v[26:29], v[94:97], v[78:81], v[26:29]
	v_mfma_f32_16x16x32_f16 v[38:41], v[86:89], v[82:85], v[38:41]
	v_mfma_f32_16x16x32_f16 v[42:45], v[94:97], v[82:85], v[42:45]
	s_add_u32 s28, s2, 0xd00
	s_mov_b32 m0, s22
	s_waitcnt vmcnt(8) lgkmcnt(0)
	s_barrier
	s_addc_u32 s29, s3, 0
	s_add_u32 s30, s4, 0xd00
	global_load_lds_dwordx4 v3, s[28:29]
	s_mov_b32 m0, s19
	s_addc_u32 s31, s5, 0
	global_load_lds_dwordx4 v4, s[28:29]
	s_mov_b32 m0, s20
	s_nop 0
	global_load_lds_dwordx4 v3, s[30:31]
	s_mov_b32 m0, s21
	s_nop 0
	global_load_lds_dwordx4 v4, s[30:31]
	s_waitcnt lgkmcnt(0)
	v_mfma_f32_16x16x32_f16 v[54:57], v[90:93], v[46:49], v[54:57]
	v_mfma_f32_16x16x32_f16 v[30:33], v[98:101], v[46:49], v[30:33]
	ds_read_b128 v[46:49], v17
	ds_read_b128 v[74:77], v18
	ds_read_b128 v[78:81], v19
	ds_read_b128 v[82:85], v20
	ds_read_b128 v[86:89], v21
	ds_read_b128 v[94:97], v22
	v_mfma_f32_16x16x32_f16 v[58:61], v[90:93], v[62:65], v[58:61]
	v_mfma_f32_16x16x32_f16 v[50:53], v[98:101], v[62:65], v[50:53]
	v_mfma_f32_16x16x32_f16 v[34:37], v[90:93], v[66:69], v[34:37]
	v_mfma_f32_16x16x32_f16 v[26:29], v[98:101], v[66:69], v[26:29]
	v_mfma_f32_16x16x32_f16 v[38:41], v[90:93], v[70:73], v[38:41]
	v_mfma_f32_16x16x32_f16 v[42:45], v[98:101], v[70:73], v[42:45]
	s_waitcnt lgkmcnt(0)
	v_mfma_f32_16x16x32_f16 v[54:57], v[86:89], v[46:49], v[54:57]
	v_mfma_f32_16x16x32_f16 v[30:33], v[94:97], v[46:49], v[30:33]
	ds_read_b128 v[46:49], v23
	ds_read_b128 v[62:65], v23 offset:2048
	ds_read_b128 v[66:69], v23 offset:4096
	ds_read_b128 v[70:73], v23 offset:6144
	ds_read_b128 v[90:93], v24
	ds_read_b128 v[98:101], v24 offset:2048
	v_mfma_f32_16x16x32_f16 v[58:61], v[86:89], v[74:77], v[58:61]
	v_mfma_f32_16x16x32_f16 v[50:53], v[94:97], v[74:77], v[50:53]
	v_mfma_f32_16x16x32_f16 v[34:37], v[86:89], v[78:81], v[34:37]
	v_mfma_f32_16x16x32_f16 v[26:29], v[94:97], v[78:81], v[26:29]
	v_mfma_f32_16x16x32_f16 v[38:41], v[86:89], v[82:85], v[38:41]
	v_mfma_f32_16x16x32_f16 v[42:45], v[94:97], v[82:85], v[42:45]
	s_add_u32 s28, s2, 0xd80
	s_mov_b32 m0, s26
	s_waitcnt vmcnt(8) lgkmcnt(0)
	s_barrier
	s_addc_u32 s29, s3, 0
	s_add_u32 s30, s4, 0xd80
	global_load_lds_dwordx4 v3, s[28:29]
	s_mov_b32 m0, s23
	s_addc_u32 s31, s5, 0
	global_load_lds_dwordx4 v4, s[28:29]
	s_mov_b32 m0, s24
	s_nop 0
	global_load_lds_dwordx4 v3, s[30:31]
	s_mov_b32 m0, s25
	s_nop 0
	global_load_lds_dwordx4 v4, s[30:31]
	s_waitcnt lgkmcnt(0)
	v_mfma_f32_16x16x32_f16 v[54:57], v[90:93], v[46:49], v[54:57]
	v_mfma_f32_16x16x32_f16 v[30:33], v[98:101], v[46:49], v[30:33]
	ds_read_b128 v[46:49], v7
	ds_read_b128 v[74:77], v7 offset:2048
	ds_read_b128 v[78:81], v7 offset:4096
	ds_read_b128 v[82:85], v7 offset:6144
	ds_read_b128 v[86:89], v5 offset:16384
	ds_read_b128 v[94:97], v5 offset:18432
	v_mfma_f32_16x16x32_f16 v[58:61], v[90:93], v[62:65], v[58:61]
	v_mfma_f32_16x16x32_f16 v[50:53], v[98:101], v[62:65], v[50:53]
	v_mfma_f32_16x16x32_f16 v[34:37], v[90:93], v[66:69], v[34:37]
	v_mfma_f32_16x16x32_f16 v[26:29], v[98:101], v[66:69], v[26:29]
	v_mfma_f32_16x16x32_f16 v[38:41], v[90:93], v[70:73], v[38:41]
	v_mfma_f32_16x16x32_f16 v[42:45], v[98:101], v[70:73], v[42:45]
	s_waitcnt lgkmcnt(0)
	v_mfma_f32_16x16x32_f16 v[54:57], v[86:89], v[46:49], v[54:57]
	v_mfma_f32_16x16x32_f16 v[30:33], v[94:97], v[46:49], v[30:33]
	ds_read_b128 v[46:49], v6
	ds_read_b128 v[62:65], v6 offset:2048
	ds_read_b128 v[66:69], v6 offset:4096
	ds_read_b128 v[70:73], v6 offset:6144
	ds_read_b128 v[90:93], v8 offset:16384
	ds_read_b128 v[98:101], v8 offset:18432
	v_mfma_f32_16x16x32_f16 v[58:61], v[86:89], v[74:77], v[58:61]
	v_mfma_f32_16x16x32_f16 v[50:53], v[94:97], v[74:77], v[50:53]
	v_mfma_f32_16x16x32_f16 v[34:37], v[86:89], v[78:81], v[34:37]
	v_mfma_f32_16x16x32_f16 v[26:29], v[94:97], v[78:81], v[26:29]
	v_mfma_f32_16x16x32_f16 v[38:41], v[86:89], v[82:85], v[38:41]
	v_mfma_f32_16x16x32_f16 v[42:45], v[94:97], v[82:85], v[42:45]
	s_add_u32 s28, s2, 0xe00
	s_mov_b32 m0, s18
	s_waitcnt vmcnt(8) lgkmcnt(0)
	s_barrier
	s_addc_u32 s29, s3, 0
	s_add_u32 s30, s4, 0xe00
	global_load_lds_dwordx4 v3, s[28:29]
	s_mov_b32 m0, s15
	s_addc_u32 s31, s5, 0
	global_load_lds_dwordx4 v4, s[28:29]
	s_mov_b32 m0, s16
	s_nop 0
	global_load_lds_dwordx4 v3, s[30:31]
	s_mov_b32 m0, s17
	s_nop 0
	global_load_lds_dwordx4 v4, s[30:31]
	s_waitcnt lgkmcnt(0)
	v_mfma_f32_16x16x32_f16 v[54:57], v[90:93], v[46:49], v[54:57]
	v_mfma_f32_16x16x32_f16 v[30:33], v[98:101], v[46:49], v[30:33]
	ds_read_b128 v[46:49], v7 offset:32768
	ds_read_b128 v[74:77], v7 offset:34816
	ds_read_b128 v[78:81], v7 offset:36864
	ds_read_b128 v[82:85], v7 offset:38912
	ds_read_b128 v[86:89], v5 offset:49152
	ds_read_b128 v[94:97], v5 offset:51200
	v_mfma_f32_16x16x32_f16 v[58:61], v[90:93], v[62:65], v[58:61]
	v_mfma_f32_16x16x32_f16 v[50:53], v[98:101], v[62:65], v[50:53]
	v_mfma_f32_16x16x32_f16 v[34:37], v[90:93], v[66:69], v[34:37]
	v_mfma_f32_16x16x32_f16 v[26:29], v[98:101], v[66:69], v[26:29]
	v_mfma_f32_16x16x32_f16 v[38:41], v[90:93], v[70:73], v[38:41]
	v_mfma_f32_16x16x32_f16 v[42:45], v[98:101], v[70:73], v[42:45]
	s_waitcnt lgkmcnt(0)
	v_mfma_f32_16x16x32_f16 v[54:57], v[86:89], v[46:49], v[54:57]
	v_mfma_f32_16x16x32_f16 v[30:33], v[94:97], v[46:49], v[30:33]
	ds_read_b128 v[46:49], v6 offset:32768
	ds_read_b128 v[62:65], v6 offset:34816
	ds_read_b128 v[66:69], v6 offset:36864
	ds_read_b128 v[70:73], v6 offset:38912
	ds_read_b128 v[90:93], v8 offset:49152
	ds_read_b128 v[98:101], v8 offset:51200
	v_mfma_f32_16x16x32_f16 v[58:61], v[86:89], v[74:77], v[58:61]
	v_mfma_f32_16x16x32_f16 v[50:53], v[94:97], v[74:77], v[50:53]
	v_mfma_f32_16x16x32_f16 v[34:37], v[86:89], v[78:81], v[34:37]
	v_mfma_f32_16x16x32_f16 v[26:29], v[94:97], v[78:81], v[26:29]
	v_mfma_f32_16x16x32_f16 v[38:41], v[86:89], v[82:85], v[38:41]
	v_mfma_f32_16x16x32_f16 v[42:45], v[94:97], v[82:85], v[42:45]
	s_mov_b32 m0, s14
	s_add_u32 s14, s2, 0xe80
	s_waitcnt vmcnt(8) lgkmcnt(0)
	s_barrier
	s_addc_u32 s15, s3, 0
	s_add_u32 s16, s4, 0xe80
	global_load_lds_dwordx4 v3, s[14:15]
	s_mov_b32 m0, s6
	s_addc_u32 s17, s5, 0
	global_load_lds_dwordx4 v4, s[14:15]
	s_mov_b32 m0, s7
	s_nop 0
	global_load_lds_dwordx4 v3, s[16:17]
	s_mov_b32 m0, s10
	s_nop 0
	global_load_lds_dwordx4 v4, s[16:17]
	s_waitcnt lgkmcnt(0)
	v_mfma_f32_16x16x32_f16 v[54:57], v[90:93], v[46:49], v[54:57]
	v_mfma_f32_16x16x32_f16 v[30:33], v[98:101], v[46:49], v[30:33]
	ds_read_b128 v[46:49], v9
	ds_read_b128 v[74:77], v10
	ds_read_b128 v[78:81], v11
	ds_read_b128 v[82:85], v12
	ds_read_b128 v[86:89], v13
	ds_read_b128 v[94:97], v14
	v_mfma_f32_16x16x32_f16 v[58:61], v[90:93], v[62:65], v[58:61]
	v_mfma_f32_16x16x32_f16 v[50:53], v[98:101], v[62:65], v[50:53]
	v_mfma_f32_16x16x32_f16 v[34:37], v[90:93], v[66:69], v[34:37]
	v_mfma_f32_16x16x32_f16 v[26:29], v[98:101], v[66:69], v[26:29]
	v_mfma_f32_16x16x32_f16 v[38:41], v[90:93], v[70:73], v[38:41]
	v_mfma_f32_16x16x32_f16 v[42:45], v[98:101], v[70:73], v[42:45]
	s_waitcnt lgkmcnt(0)
	v_mfma_f32_16x16x32_f16 v[54:57], v[86:89], v[46:49], v[54:57]
	v_mfma_f32_16x16x32_f16 v[30:33], v[94:97], v[46:49], v[30:33]
	ds_read_b128 v[46:49], v15
	ds_read_b128 v[62:65], v15 offset:2048
	ds_read_b128 v[66:69], v15 offset:4096
	ds_read_b128 v[70:73], v15 offset:6144
	ds_read_b128 v[90:93], v16
	ds_read_b128 v[98:101], v16 offset:2048
	v_mfma_f32_16x16x32_f16 v[58:61], v[86:89], v[74:77], v[58:61]
	v_mfma_f32_16x16x32_f16 v[50:53], v[94:97], v[74:77], v[50:53]
	v_mfma_f32_16x16x32_f16 v[34:37], v[86:89], v[78:81], v[34:37]
	v_mfma_f32_16x16x32_f16 v[26:29], v[94:97], v[78:81], v[26:29]
	v_mfma_f32_16x16x32_f16 v[38:41], v[86:89], v[82:85], v[38:41]
	v_mfma_f32_16x16x32_f16 v[42:45], v[94:97], v[82:85], v[42:45]
	s_add_u32 s6, s2, 0xf00
	s_mov_b32 m0, s22
	s_waitcnt vmcnt(8) lgkmcnt(0)
	s_barrier
	s_addc_u32 s7, s3, 0
	s_add_u32 s14, s4, 0xf00
	global_load_lds_dwordx4 v3, s[6:7]
	s_mov_b32 m0, s19
	s_addc_u32 s15, s5, 0
	global_load_lds_dwordx4 v4, s[6:7]
	s_mov_b32 m0, s20
	s_nop 0
	global_load_lds_dwordx4 v3, s[14:15]
	s_mov_b32 m0, s21
	s_nop 0
	global_load_lds_dwordx4 v4, s[14:15]
	s_waitcnt lgkmcnt(0)
	v_mfma_f32_16x16x32_f16 v[54:57], v[90:93], v[46:49], v[54:57]
	v_mfma_f32_16x16x32_f16 v[30:33], v[98:101], v[46:49], v[30:33]
	ds_read_b128 v[46:49], v17
	ds_read_b128 v[74:77], v18
	ds_read_b128 v[78:81], v19
	ds_read_b128 v[82:85], v20
	ds_read_b128 v[86:89], v21
	ds_read_b128 v[94:97], v22
	v_mfma_f32_16x16x32_f16 v[58:61], v[90:93], v[62:65], v[58:61]
	v_mfma_f32_16x16x32_f16 v[50:53], v[98:101], v[62:65], v[50:53]
	v_mfma_f32_16x16x32_f16 v[34:37], v[90:93], v[66:69], v[34:37]
	v_mfma_f32_16x16x32_f16 v[26:29], v[98:101], v[66:69], v[26:29]
	v_mfma_f32_16x16x32_f16 v[38:41], v[90:93], v[70:73], v[38:41]
	v_mfma_f32_16x16x32_f16 v[42:45], v[98:101], v[70:73], v[42:45]
	s_waitcnt lgkmcnt(0)
	v_mfma_f32_16x16x32_f16 v[54:57], v[86:89], v[46:49], v[54:57]
	v_mfma_f32_16x16x32_f16 v[30:33], v[94:97], v[46:49], v[30:33]
	ds_read_b128 v[46:49], v23
	ds_read_b128 v[62:65], v23 offset:2048
	ds_read_b128 v[66:69], v23 offset:4096
	ds_read_b128 v[70:73], v23 offset:6144
	ds_read_b128 v[90:93], v24
	ds_read_b128 v[98:101], v24 offset:2048
	v_mfma_f32_16x16x32_f16 v[58:61], v[86:89], v[74:77], v[58:61]
	v_mfma_f32_16x16x32_f16 v[50:53], v[94:97], v[74:77], v[50:53]
	v_mfma_f32_16x16x32_f16 v[34:37], v[86:89], v[78:81], v[34:37]
	v_mfma_f32_16x16x32_f16 v[26:29], v[94:97], v[78:81], v[26:29]
	v_mfma_f32_16x16x32_f16 v[38:41], v[86:89], v[82:85], v[38:41]
	v_mfma_f32_16x16x32_f16 v[42:45], v[94:97], v[82:85], v[42:45]
	s_add_u32 s2, s2, 0xf80
	s_mov_b32 m0, s26
	s_waitcnt vmcnt(8) lgkmcnt(0)
	s_barrier
	s_addc_u32 s3, s3, 0
	s_add_u32 s4, s4, 0xf80
	global_load_lds_dwordx4 v3, s[2:3]
	s_mov_b32 m0, s23
	s_addc_u32 s5, s5, 0
	global_load_lds_dwordx4 v4, s[2:3]
	s_mov_b32 m0, s24
	s_nop 0
	global_load_lds_dwordx4 v3, s[4:5]
	s_mov_b32 m0, s25
	s_nop 0
	global_load_lds_dwordx4 v4, s[4:5]
	s_waitcnt lgkmcnt(0)
	v_mfma_f32_16x16x32_f16 v[54:57], v[90:93], v[46:49], v[54:57]
	v_mfma_f32_16x16x32_f16 v[30:33], v[98:101], v[46:49], v[30:33]
	ds_read_b128 v[46:49], v7
	ds_read_b128 v[74:77], v7 offset:2048
	ds_read_b128 v[78:81], v7 offset:4096
	ds_read_b128 v[82:85], v7 offset:6144
	ds_read_b128 v[86:89], v5 offset:16384
	ds_read_b128 v[94:97], v5 offset:18432
	v_mfma_f32_16x16x32_f16 v[58:61], v[90:93], v[62:65], v[58:61]
	v_mfma_f32_16x16x32_f16 v[50:53], v[98:101], v[62:65], v[50:53]
	v_mfma_f32_16x16x32_f16 v[34:37], v[90:93], v[66:69], v[34:37]
	v_mfma_f32_16x16x32_f16 v[26:29], v[98:101], v[66:69], v[26:29]
	v_mfma_f32_16x16x32_f16 v[38:41], v[90:93], v[70:73], v[38:41]
	v_mfma_f32_16x16x32_f16 v[42:45], v[98:101], v[70:73], v[42:45]
	s_waitcnt lgkmcnt(0)
	v_mfma_f32_16x16x32_f16 v[54:57], v[86:89], v[46:49], v[54:57]
	v_mfma_f32_16x16x32_f16 v[30:33], v[94:97], v[46:49], v[30:33]
	ds_read_b128 v[46:49], v6
	ds_read_b128 v[62:65], v6 offset:2048
	ds_read_b128 v[66:69], v6 offset:4096
	ds_read_b128 v[70:73], v6 offset:6144
	ds_read_b128 v[90:93], v8 offset:16384
	ds_read_b128 v[98:101], v8 offset:18432
	v_mfma_f32_16x16x32_f16 v[58:61], v[86:89], v[74:77], v[58:61]
	v_mfma_f32_16x16x32_f16 v[50:53], v[94:97], v[74:77], v[50:53]
	v_mfma_f32_16x16x32_f16 v[34:37], v[86:89], v[78:81], v[34:37]
	v_mfma_f32_16x16x32_f16 v[26:29], v[94:97], v[78:81], v[26:29]
	v_mfma_f32_16x16x32_f16 v[38:41], v[86:89], v[82:85], v[38:41]
	v_mfma_f32_16x16x32_f16 v[42:45], v[94:97], v[82:85], v[42:45]
	s_waitcnt vmcnt(8) lgkmcnt(0)
	s_barrier
	s_waitcnt lgkmcnt(0)
	v_mfma_f32_16x16x32_f16 v[54:57], v[90:93], v[46:49], v[54:57]
	v_mfma_f32_16x16x32_f16 v[30:33], v[98:101], v[46:49], v[30:33]
	ds_read_b128 v[46:49], v7 offset:32768
	ds_read_b128 v[74:77], v7 offset:34816
	ds_read_b128 v[78:81], v7 offset:36864
	ds_read_b128 v[82:85], v7 offset:38912
	ds_read_b128 v[86:89], v5 offset:49152
	ds_read_b128 v[94:97], v5 offset:51200
	v_mfma_f32_16x16x32_f16 v[58:61], v[90:93], v[62:65], v[58:61]
	v_mfma_f32_16x16x32_f16 v[50:53], v[98:101], v[62:65], v[50:53]
	v_mfma_f32_16x16x32_f16 v[34:37], v[90:93], v[66:69], v[34:37]
	v_mfma_f32_16x16x32_f16 v[26:29], v[98:101], v[66:69], v[26:29]
	v_mfma_f32_16x16x32_f16 v[38:41], v[90:93], v[70:73], v[38:41]
	v_mfma_f32_16x16x32_f16 v[42:45], v[98:101], v[70:73], v[42:45]
	s_waitcnt lgkmcnt(0)
	v_mfma_f32_16x16x32_f16 v[54:57], v[86:89], v[46:49], v[54:57]
	v_mfma_f32_16x16x32_f16 v[30:33], v[94:97], v[46:49], v[30:33]
	ds_read_b128 v[46:49], v6 offset:32768
	ds_read_b128 v[62:65], v6 offset:34816
	ds_read_b128 v[66:69], v6 offset:36864
	ds_read_b128 v[4:7], v6 offset:38912
	ds_read_b128 v[70:73], v8 offset:49152
	ds_read_b128 v[90:93], v8 offset:51200
	v_mfma_f32_16x16x32_f16 v[58:61], v[86:89], v[74:77], v[58:61]
	v_mfma_f32_16x16x32_f16 v[50:53], v[94:97], v[74:77], v[50:53]
	v_mfma_f32_16x16x32_f16 v[34:37], v[86:89], v[78:81], v[34:37]
	v_mfma_f32_16x16x32_f16 v[26:29], v[94:97], v[78:81], v[26:29]
	v_mfma_f32_16x16x32_f16 v[38:41], v[86:89], v[82:85], v[38:41]
	v_mfma_f32_16x16x32_f16 v[42:45], v[94:97], v[82:85], v[42:45]
	s_waitcnt vmcnt(0) lgkmcnt(0)
	s_barrier
	s_waitcnt lgkmcnt(0)
	v_mfma_f32_16x16x32_f16 v[54:57], v[70:73], v[46:49], v[54:57]
	v_mfma_f32_16x16x32_f16 v[30:33], v[90:93], v[46:49], v[30:33]
	ds_read_b128 v[46:49], v9
	ds_read_b128 v[74:77], v10
	ds_read_b128 v[8:11], v11
	ds_read_b128 v[78:81], v12
	ds_read_b128 v[82:85], v13
	ds_read_b128 v[86:89], v14
	v_mfma_f32_16x16x32_f16 v[58:61], v[70:73], v[62:65], v[58:61]
	v_mfma_f32_16x16x32_f16 v[50:53], v[90:93], v[62:65], v[50:53]
	v_mfma_f32_16x16x32_f16 v[34:37], v[70:73], v[66:69], v[34:37]
	v_mfma_f32_16x16x32_f16 v[26:29], v[90:93], v[66:69], v[26:29]
	v_mfma_f32_16x16x32_f16 v[38:41], v[70:73], v[4:7], v[38:41]
	v_mfma_f32_16x16x32_f16 v[4:7], v[90:93], v[4:7], v[42:45]
	s_waitcnt lgkmcnt(0)
	v_mfma_f32_16x16x32_f16 v[42:45], v[82:85], v[46:49], v[54:57]
	v_mfma_f32_16x16x32_f16 v[30:33], v[86:89], v[46:49], v[30:33]
	ds_read_b128 v[46:49], v15
	s_nop 0
	ds_read_b128 v[54:57], v15 offset:2048
	ds_read_b128 v[62:65], v15 offset:4096
	ds_read_b128 v[12:15], v15 offset:6144
	ds_read_b128 v[66:69], v16
	ds_read_b128 v[70:73], v16 offset:2048
	v_mfma_f32_16x16x32_f16 v[58:61], v[82:85], v[74:77], v[58:61]
	v_mfma_f32_16x16x32_f16 v[50:53], v[86:89], v[74:77], v[50:53]
	v_mfma_f32_16x16x32_f16 v[34:37], v[82:85], v[8:11], v[34:37]
	v_mfma_f32_16x16x32_f16 v[8:11], v[86:89], v[8:11], v[26:29]
	v_mfma_f32_16x16x32_f16 v[26:29], v[82:85], v[78:81], v[38:41]
	v_mfma_f32_16x16x32_f16 v[4:7], v[86:89], v[78:81], v[4:7]
	s_waitcnt vmcnt(0) lgkmcnt(0)
	s_barrier
	s_waitcnt lgkmcnt(0)
	v_mfma_f32_16x16x32_f16 v[38:41], v[66:69], v[46:49], v[42:45]
	v_mfma_f32_16x16x32_f16 v[30:33], v[70:73], v[46:49], v[30:33]
	s_nop 1
	ds_read_b128 v[42:45], v17
	ds_read_b128 v[46:49], v18
	ds_read_b128 v[16:19], v19
	ds_read_b128 v[74:77], v20
	ds_read_b128 v[78:81], v21
	ds_read_b128 v[82:85], v22
	v_mfma_f32_16x16x32_f16 v[58:61], v[66:69], v[54:57], v[58:61]
	v_mfma_f32_16x16x32_f16 v[50:53], v[70:73], v[54:57], v[50:53]
	v_mfma_f32_16x16x32_f16 v[34:37], v[66:69], v[62:65], v[34:37]
	v_mfma_f32_16x16x32_f16 v[8:11], v[70:73], v[62:65], v[8:11]
	v_mfma_f32_16x16x32_f16 v[26:29], v[66:69], v[12:15], v[26:29]
	v_mfma_f32_16x16x32_f16 v[4:7], v[70:73], v[12:15], v[4:7]
	s_waitcnt lgkmcnt(0)
	v_mfma_f32_16x16x32_f16 v[12:15], v[78:81], v[42:45], v[38:41]
	v_mfma_f32_16x16x32_f16 v[30:33], v[82:85], v[42:45], v[30:33]
	s_nop 1
	ds_read_b128 v[38:41], v23
	ds_read_b128 v[42:45], v23 offset:2048
	ds_read_b128 v[54:57], v23 offset:4096
	ds_read_b128 v[20:23], v23 offset:6144
	ds_read_b128 v[62:65], v24
	ds_read_b128 v[66:69], v24 offset:2048
	v_mfma_f32_16x16x32_f16 v[58:61], v[78:81], v[46:49], v[58:61]
	v_mfma_f32_16x16x32_f16 v[46:49], v[82:85], v[46:49], v[50:53]
	v_mfma_f32_16x16x32_f16 v[34:37], v[78:81], v[16:19], v[34:37]
	v_mfma_f32_16x16x32_f16 v[8:11], v[82:85], v[16:19], v[8:11]
	v_mfma_f32_16x16x32_f16 v[16:19], v[78:81], v[74:77], v[26:29]
	v_mfma_f32_16x16x32_f16 v[4:7], v[82:85], v[74:77], v[4:7]
	s_waitcnt lgkmcnt(0)
	v_mfma_f32_16x16x32_f16 v[12:15], v[62:65], v[38:41], v[12:15]
	v_mfma_f32_16x16x32_f16 v[24:27], v[66:69], v[38:41], v[30:33]
	v_mfma_f32_16x16x32_f16 v[28:31], v[62:65], v[42:45], v[58:61]
	v_mfma_f32_16x16x32_f16 v[38:41], v[66:69], v[42:45], v[46:49]
	v_mfma_f32_16x16x32_f16 v[32:35], v[62:65], v[54:57], v[34:37]
	v_mfma_f32_16x16x32_f16 v[8:11], v[66:69], v[54:57], v[8:11]
	v_mfma_f32_16x16x32_f16 v[16:19], v[62:65], v[20:23], v[16:19]
	v_mfma_f32_16x16x32_f16 v[4:7], v[66:69], v[20:23], v[4:7]
	s_mul_i32 s4, s8, s12
	s_ashr_i32 s3, s9, 31
	s_mul_hi_i32 s2, s8, s12
	s_mul_i32 s3, s4, s3
	s_mul_hi_u32 s5, s4, s9
	s_add_i32 s3, s5, s3
	s_mul_i32 s2, s2, s9
	s_add_i32 s3, s3, s2
	s_mul_i32 s2, s4, s9
	s_lshl_b64 s[2:3], s[2:3], 1
	v_or_b32_e32 v20, s13, v1
	v_lshlrev_b32_e32 v0, 2, v0
	s_add_u32 s0, s0, s2
	v_or3_b32 v21, v0, v2, s11
	s_addc_u32 s1, s1, s3
	v_mad_i64_i32 v[0:1], s[2:3], v20, s9, 0
	v_lshl_add_u64 v[0:1], v[0:1], 1, s[0:1]
	v_cvt_pk_f16_f32 v2, v12, v13
	v_lshlrev_b32_e32 v12, 1, v21
	v_mov_b32_e32 v13, 0
	v_cvt_pk_f16_f32 v3, v14, v15
	v_lshl_add_u64 v[0:1], v[0:1], 0, v[12:13]
	global_store_dwordx2 v[0:1], v[2:3], off
	v_cvt_pk_f16_f32 v3, v26, v27
	v_cvt_pk_f16_f32 v2, v24, v25
	global_store_dwordx2 v[0:1], v[2:3], off offset:32
	v_or_b32_e32 v0, 16, v20
	v_mad_i64_i32 v[0:1], s[2:3], v0, s9, 0
	v_lshl_add_u64 v[0:1], v[0:1], 1, s[0:1]
	v_cvt_pk_f16_f32 v3, v30, v31
	v_cvt_pk_f16_f32 v2, v28, v29
	v_lshl_add_u64 v[0:1], v[0:1], 0, v[12:13]
	global_store_dwordx2 v[0:1], v[2:3], off
	v_cvt_pk_f16_f32 v3, v40, v41
	v_cvt_pk_f16_f32 v2, v38, v39
	global_store_dwordx2 v[0:1], v[2:3], off offset:32
	v_or_b32_e32 v0, 32, v20
	v_mad_i64_i32 v[0:1], s[2:3], v0, s9, 0
	v_lshl_add_u64 v[0:1], v[0:1], 1, s[0:1]
	v_cvt_pk_f16_f32 v3, v34, v35
	v_cvt_pk_f16_f32 v2, v32, v33
	v_lshl_add_u64 v[0:1], v[0:1], 0, v[12:13]
	global_store_dwordx2 v[0:1], v[2:3], off
	v_cvt_pk_f16_f32 v3, v10, v11
	v_cvt_pk_f16_f32 v2, v8, v9
	global_store_dwordx2 v[0:1], v[2:3], off offset:32
	v_or_b32_e32 v0, 48, v20
	v_mad_i64_i32 v[0:1], s[2:3], v0, s9, 0
	v_lshl_add_u64 v[0:1], v[0:1], 1, s[0:1]
	v_cvt_pk_f16_f32 v3, v18, v19
	v_cvt_pk_f16_f32 v2, v16, v17
	v_lshl_add_u64 v[0:1], v[0:1], 0, v[12:13]
	global_store_dwordx2 v[0:1], v[2:3], off
	v_cvt_pk_f16_f32 v3, v6, v7
	v_cvt_pk_f16_f32 v2, v4, v5
	global_store_dwordx2 v[0:1], v[2:3], off offset:32
	s_endpgm
	s_endpgm
	s_endpgm
	s_endpgm
	s_endpgm
	s_endpgm
	s_endpgm
	s_endpgm
	s_endpgm
	s_endpgm
	s_endpgm
	s_endpgm
	s_endpgm
	s_endpgm
	s_endpgm
	s_endpgm
	s_endpgm
	s_endpgm
	s_endpgm
	s_endpgm
	s_endpgm
	s_endpgm
	s_endpgm
	s_endpgm
	s_endpgm
	s_endpgm
	s_endpgm
	s_endpgm
	s_endpgm
	s_endpgm
	s_endpgm
	s_endpgm
	s_endpgm
	s_endpgm
	s_endpgm
	s_endpgm
	s_endpgm
	s_endpgm
	s_endpgm
	s_endpgm
	s_endpgm
	s_endpgm
	s_endpgm
	s_endpgm
	s_endpgm
	s_endpgm
	s_endpgm
	s_endpgm
	s_endpgm
	s_endpgm
	s_endpgm
	s_endpgm
	s_endpgm
	s_endpgm

_Z9ln_kernelILi2EEvPKiPKfS3_PfS3_S3_PDF16_:
	s_load_dwordx8 s[4:11], s[0:1], 0x8
	v_and_b32_e32 v12, 63, v0
	v_lshrrev_b32_e32 v0, 6, v0
	v_lshl_or_b32 v6, s2, 2, v0
	v_ashrrev_i32_e32 v7, 31, v6
	v_lshlrev_b64 v[2:3], 11, v[6:7]
	v_mov_b32_e32 v1, 0
	s_waitcnt lgkmcnt(0)
	v_lshl_add_u64 v[8:9], s[4:5], 0, v[2:3]
	v_lshlrev_b32_e32 v4, 3, v12
	v_mov_b32_e32 v5, v1
	v_lshl_add_u64 v[8:9], v[8:9], 0, v[4:5]
	s_mov_b64 s[2:3], 0x400000
	v_lshl_add_u64 v[10:11], v[8:9], 0, s[2:3]
	s_mov_b32 s2, 0x400000
	global_load_dwordx2 v[16:17], v[8:9], off
	global_load_dwordx2 v[18:19], v[8:9], off offset:512
	global_load_dwordx2 v[20:21], v[8:9], off offset:1024
	global_load_dwordx2 v[22:23], v[8:9], off offset:1536
	v_add_co_u32_e32 v8, vcc, s2, v8
	global_load_dwordx2 v[24:25], v[10:11], off offset:512
	global_load_dwordx2 v[26:27], v[10:11], off offset:1024
	global_load_dwordx2 v[28:29], v[10:11], off offset:1536
	v_addc_co_u32_e32 v9, vcc, 0, v9, vcc
	global_load_dwordx2 v[30:31], v[8:9], off
	v_lshlrev_b64 v[6:7], 12, v[6:7]
	v_lshlrev_b32_e32 v0, 4, v12
	v_lshl_add_u64 v[6:7], s[8:9], 0, v[6:7]
	v_lshl_add_u64 v[6:7], v[6:7], 0, v[0:1]
	global_load_dwordx4 v[8:11], v[6:7], off offset:1024
	global_load_dwordx4 v[12:15], v0, s[6:7] offset:1024
	s_waitcnt vmcnt(9)
	v_cvt_f32_f16_e32 v32, v16
	s_waitcnt vmcnt(8)
	v_cvt_f32_f16_e32 v36, v18
	v_cvt_f32_f16_sdwa v37, v18 dst_sel:DWORD dst_unused:UNUSED_PAD src0_sel:WORD_1
	v_cvt_f32_f16_e32 v38, v19
	v_cvt_f32_f16_sdwa v39, v19 dst_sel:DWORD dst_unused:UNUSED_PAD src0_sel:WORD_1
	s_waitcnt vmcnt(7)
	v_cvt_f32_f16_e32 v40, v20
	v_cvt_f32_f16_sdwa v41, v20 dst_sel:DWORD dst_unused:UNUSED_PAD src0_sel:WORD_1
	v_cvt_f32_f16_e32 v42, v21
	v_cvt_f32_f16_sdwa v43, v21 dst_sel:DWORD dst_unused:UNUSED_PAD src0_sel:WORD_1
	s_waitcnt vmcnt(6)
	v_cvt_f32_f16_e32 v44, v22
	v_cvt_f32_f16_sdwa v45, v22 dst_sel:DWORD dst_unused:UNUSED_PAD src0_sel:WORD_1
	v_cvt_f32_f16_e32 v46, v23
	v_cvt_f32_f16_sdwa v47, v23 dst_sel:DWORD dst_unused:UNUSED_PAD src0_sel:WORD_1
	s_waitcnt vmcnt(5)
	v_cvt_f32_f16_e32 v20, v24
	v_cvt_f32_f16_sdwa v21, v24 dst_sel:DWORD dst_unused:UNUSED_PAD src0_sel:WORD_1
	v_cvt_f32_f16_e32 v22, v25
	v_cvt_f32_f16_sdwa v23, v25 dst_sel:DWORD dst_unused:UNUSED_PAD src0_sel:WORD_1
	s_waitcnt vmcnt(4)
	v_cvt_f32_f16_e32 v24, v26
	v_cvt_f32_f16_sdwa v25, v26 dst_sel:DWORD dst_unused:UNUSED_PAD src0_sel:WORD_1
	v_cvt_f32_f16_e32 v26, v27
	v_cvt_f32_f16_sdwa v27, v27 dst_sel:DWORD dst_unused:UNUSED_PAD src0_sel:WORD_1
	s_waitcnt vmcnt(3)
	v_cvt_f32_f16_e32 v48, v28
	v_cvt_f32_f16_sdwa v49, v28 dst_sel:DWORD dst_unused:UNUSED_PAD src0_sel:WORD_1
	v_cvt_f32_f16_e32 v28, v29
	v_cvt_f32_f16_sdwa v29, v29 dst_sel:DWORD dst_unused:UNUSED_PAD src0_sel:WORD_1
	v_cvt_f32_f16_sdwa v33, v16 dst_sel:DWORD dst_unused:UNUSED_PAD src0_sel:WORD_1
	v_cvt_f32_f16_e32 v34, v17
	v_cvt_f32_f16_sdwa v35, v17 dst_sel:DWORD dst_unused:UNUSED_PAD src0_sel:WORD_1
	s_waitcnt vmcnt(2)
	v_cvt_f32_f16_e32 v50, v30
	v_cvt_f32_f16_sdwa v51, v30 dst_sel:DWORD dst_unused:UNUSED_PAD src0_sel:WORD_1
	v_cvt_f32_f16_e32 v52, v31
	v_cvt_f32_f16_sdwa v53, v31 dst_sel:DWORD dst_unused:UNUSED_PAD src0_sel:WORD_1
	global_load_dwordx4 v[16:19], v[6:7], off
	v_pk_add_f32 v[36:37], v[36:37], v[20:21]
	v_pk_add_f32 v[38:39], v[38:39], v[22:23]
	global_load_dwordx4 v[20:23], v[6:7], off offset:2048
	v_pk_add_f32 v[40:41], v[40:41], v[24:25]
	v_pk_add_f32 v[42:43], v[42:43], v[26:27]
	global_load_dwordx4 v[24:27], v[6:7], off offset:3072
	v_pk_add_f32 v[46:47], v[46:47], v[28:29]
	global_load_dwordx4 v[28:31], v0, s[6:7] offset:2048
	s_waitcnt vmcnt(5)
	v_pk_add_f32 v[36:37], v[8:9], v[36:37]
	v_pk_add_f32 v[38:39], v[10:11], v[38:39]
	global_load_dwordx4 v[8:11], v0, s[6:7]
	v_pk_add_f32 v[44:45], v[44:45], v[48:49]
	v_pk_add_f32 v[48:49], v[32:33], v[50:51]
	v_pk_add_f32 v[50:51], v[34:35], v[52:53]
	global_load_dwordx4 v[32:35], v0, s[6:7] offset:3072
	s_waitcnt vmcnt(6)
	v_pk_add_f32 v[12:13], v[12:13], v[36:37]
	v_pk_add_f32 v[14:15], v[14:15], v[38:39]
	s_load_dwordx4 s[4:7], s[0:1], 0x28
	s_mov_b32 s0, 0xf800000
	s_waitcnt lgkmcnt(0)
	v_lshl_add_u64 v[2:3], s[6:7], 0, v[2:3]
	s_waitcnt vmcnt(4)
	v_pk_add_f32 v[20:21], v[20:21], v[40:41]
	v_pk_add_f32 v[22:23], v[22:23], v[42:43]
	v_pk_add_f32 v[40:41], v[16:17], v[48:49]
	v_pk_add_f32 v[42:43], v[18:19], v[50:51]
	s_waitcnt vmcnt(3)
	v_pk_add_f32 v[24:25], v[24:25], v[44:45]
	v_pk_add_f32 v[26:27], v[26:27], v[46:47]
	s_waitcnt vmcnt(2)
	v_pk_add_f32 v[16:17], v[28:29], v[20:21]
	v_pk_add_f32 v[18:19], v[30:31], v[22:23]
	s_waitcnt vmcnt(1)
	v_pk_add_f32 v[8:9], v[8:9], v[40:41]
	v_pk_add_f32 v[10:11], v[10:11], v[42:43]
	v_mov_b32_e32 v28, v13
	v_mov_b32_e32 v29, v15
	s_waitcnt vmcnt(0)
	v_pk_add_f32 v[20:21], v[32:33], v[24:25]
	v_pk_add_f32 v[22:23], v[34:35], v[26:27]
	v_mov_b32_e32 v24, v8
	v_mov_b32_e32 v25, v10
	v_mov_b32_e32 v26, v9
	v_mov_b32_e32 v27, v11
	v_pk_add_f32 v[24:25], v[24:25], v[26:27]
	v_mov_b32_e32 v26, v12
	v_mov_b32_e32 v27, v14
	v_pk_add_f32 v[26:27], v[26:27], v[28:29]
	v_add_f32_e32 v1, v24, v25
	v_pk_add_f32 v[26:27], v[26:27], v[26:27] op_sel:[0,1] op_sel_hi:[1,0]
	v_pk_add_f32 v[28:29], v[16:17], v[16:17] op_sel:[0,1] op_sel_hi:[1,0]
	v_pk_add_f32 v[30:31], v[18:19], v[18:19] op_sel:[0,1] op_sel_hi:[1,0]
	v_add_f32_e32 v24, 0, v1
	v_mov_b32_e32 v25, v20
	v_mov_b32_e32 v27, v21
	v_mov_b32_e32 v29, v22
	v_mov_b32_e32 v31, v23
	v_pk_add_f32 v[24:25], v[24:25], v[26:27]
	v_pk_add_f32 v[26:27], v[28:29], v[30:31]
	s_nop 0
	v_pk_add_f32 v[24:25], v[24:25], v[26:27]
	s_nop 0
	v_add_f32_e32 v1, v24, v25
	v_mbcnt_lo_u32_b32 v24, -1, 0
	v_mbcnt_hi_u32_b32 v24, -1, v24
	v_and_b32_e32 v25, 64, v24
	v_add_u32_e32 v25, 64, v25
	v_xor_b32_e32 v26, 32, v24
	v_cmp_lt_i32_e32 vcc, v26, v25
	s_nop 1
	v_cndmask_b32_e32 v26, v24, v26, vcc
	v_lshlrev_b32_e32 v52, 2, v26
	ds_bpermute_b32 v26, v52, v1
	s_waitcnt lgkmcnt(0)
	v_add_f32_e32 v1, v1, v26
	v_xor_b32_e32 v26, 16, v24
	v_cmp_lt_i32_e32 vcc, v26, v25
	s_nop 1
	v_cndmask_b32_e32 v26, v24, v26, vcc
	v_lshlrev_b32_e32 v53, 2, v26
	ds_bpermute_b32 v26, v53, v1
	s_waitcnt lgkmcnt(0)
	v_add_f32_e32 v1, v1, v26
	v_xor_b32_e32 v26, 8, v24
	v_cmp_lt_i32_e32 vcc, v26, v25
	s_nop 1
	v_cndmask_b32_e32 v26, v24, v26, vcc
	v_lshlrev_b32_e32 v54, 2, v26
	ds_bpermute_b32 v26, v54, v1
	s_waitcnt lgkmcnt(0)
	v_add_f32_e32 v1, v1, v26
	v_xor_b32_e32 v26, 4, v24
	v_cmp_lt_i32_e32 vcc, v26, v25
	s_nop 1
	v_cndmask_b32_e32 v26, v24, v26, vcc
	v_lshlrev_b32_e32 v55, 2, v26
	ds_bpermute_b32 v26, v55, v1
	s_waitcnt lgkmcnt(0)
	v_add_f32_e32 v1, v1, v26
	v_xor_b32_e32 v26, 2, v24
	v_cmp_lt_i32_e32 vcc, v26, v25
	s_nop 1
	v_cndmask_b32_e32 v26, v24, v26, vcc
	v_lshlrev_b32_e32 v56, 2, v26
	ds_bpermute_b32 v26, v56, v1
	s_waitcnt lgkmcnt(0)
	v_add_f32_e32 v1, v1, v26
	v_xor_b32_e32 v26, 1, v24
	v_cmp_lt_i32_e32 vcc, v26, v25
	s_nop 1
	v_cndmask_b32_e32 v24, v24, v26, vcc
	v_lshlrev_b32_e32 v57, 2, v24
	ds_bpermute_b32 v24, v57, v1
	s_waitcnt lgkmcnt(0)
	v_add_f32_e32 v1, v1, v24
	v_mul_f32_e32 v24, 0x3a800000, v1
	v_pk_add_f32 v[36:37], v[8:9], v[24:25] op_sel_hi:[1,0] neg_lo:[0,1] neg_hi:[0,1]
	v_pk_add_f32 v[38:39], v[10:11], v[24:25] op_sel_hi:[1,0] neg_lo:[0,1] neg_hi:[0,1]
	v_mov_b32_e32 v28, v37
	v_mov_b32_e32 v29, v39
	v_pk_add_f32 v[40:41], v[12:13], v[24:25] op_sel_hi:[1,0] neg_lo:[0,1] neg_hi:[0,1]
	v_pk_add_f32 v[42:43], v[14:15], v[24:25] op_sel_hi:[1,0] neg_lo:[0,1] neg_hi:[0,1]
	v_mov_b32_e32 v26, v36
	v_mov_b32_e32 v27, v38
	v_pk_mul_f32 v[28:29], v[28:29], v[28:29]
	v_mov_b32_e32 v30, v41
	v_mov_b32_e32 v31, v43
	v_pk_fma_f32 v[26:27], v[26:27], v[26:27], v[28:29]
	v_mov_b32_e32 v28, v40
	v_mov_b32_e32 v29, v42
	v_pk_mul_f32 v[30:31], v[30:31], v[30:31]
	v_pk_add_f32 v[44:45], v[16:17], v[24:25] op_sel_hi:[1,0] neg_lo:[0,1] neg_hi:[0,1]
	v_pk_fma_f32 v[28:29], v[28:29], v[28:29], v[30:31]
	v_mul_f32_e32 v30, v44, v44
	v_pk_fma_f32 v[30:31], v[44:45], v[44:45], v[30:31] op_sel_hi:[1,1,0]
	v_pk_add_f32 v[46:47], v[18:19], v[24:25] op_sel_hi:[1,0] neg_lo:[0,1] neg_hi:[0,1]
	v_pk_add_f32 v[48:49], v[20:21], v[24:25] op_sel_hi:[1,0] neg_lo:[0,1] neg_hi:[0,1]
	v_mul_f32_e32 v30, v46, v46
	v_pk_add_f32 v[50:51], v[22:23], v[24:25] op_sel_hi:[1,0] neg_lo:[0,1] neg_hi:[0,1]
	v_pk_fma_f32 v[32:33], v[46:47], v[46:47], v[30:31] op_sel_hi:[1,1,0]
	v_pk_mul_f32 v[34:35], v[48:49], v[48:49]
	v_pk_add_f32 v[26:27], v[26:27], v[26:27] op_sel_hi:[0,1]
	v_pk_add_f32 v[28:29], v[28:29], v[28:29] op_sel_hi:[0,1]
	v_pk_mul_f32 v[24:25], v[50:51], v[50:51]
	v_mov_b32_e32 v30, v34
	v_mov_b32_e32 v32, v35
	v_mov_b32_e32 v26, v24
	v_mov_b32_e32 v28, v25
	v_pk_add_f32 v[30:31], v[30:31], v[32:33]
	v_pk_add_f32 v[24:25], v[26:27], v[28:29]
	s_nop 0
	v_pk_add_f32 v[24:25], v[30:31], v[24:25]
	s_nop 0
	v_add_f32_e32 v1, v24, v25
	ds_bpermute_b32 v24, v52, v1
	s_waitcnt lgkmcnt(0)
	v_add_f32_e32 v1, v1, v24
	ds_bpermute_b32 v24, v53, v1
	s_waitcnt lgkmcnt(0)
	v_add_f32_e32 v1, v1, v24
	ds_bpermute_b32 v24, v54, v1
	s_waitcnt lgkmcnt(0)
	v_add_f32_e32 v1, v1, v24
	ds_bpermute_b32 v24, v55, v1
	s_waitcnt lgkmcnt(0)
	v_add_f32_e32 v1, v1, v24
	ds_bpermute_b32 v32, v56, v1
	global_load_dwordx4 v[24:27], v0, s[10:11]
	global_load_dwordx4 v[28:31], v0, s[10:11] offset:1024
	s_waitcnt lgkmcnt(0)
	v_add_f32_e32 v1, v1, v32
	ds_bpermute_b32 v32, v57, v1
	global_store_dwordx4 v[6:7], v[8:11], off
	global_store_dwordx4 v[6:7], v[12:15], off offset:1024
	global_store_dwordx4 v[6:7], v[16:19], off offset:2048
	global_store_dwordx4 v[6:7], v[20:23], off offset:3072
	s_waitcnt lgkmcnt(0)
	v_add_f32_e32 v1, v1, v32
	v_mov_b32_e32 v32, 0x3727c5ac
	v_fmac_f32_e32 v32, 0x3a800000, v1
	v_mul_f32_e32 v1, 0x4f800000, v32
	v_cmp_gt_f32_e32 vcc, s0, v32
	global_load_dwordx4 v[12:15], v0, s[4:5]
	global_load_dwordx4 v[16:19], v0, s[4:5] offset:1024
	v_cndmask_b32_e32 v1, v32, v1, vcc
	v_sqrt_f32_e32 v32, v1
	global_load_dwordx4 v[8:11], v0, s[10:11] offset:2048
	v_add_u32_e32 v6, -1, v32
	v_fma_f32 v7, -v6, v32, v1
	v_cmp_ge_f32_e64 s[0:1], 0, v7
	v_add_u32_e32 v7, 1, v32
	v_fma_f32 v20, -v7, v32, v1
	v_cndmask_b32_e64 v6, v32, v6, s[0:1]
	v_cmp_lt_f32_e64 s[0:1], 0, v20
	global_load_dwordx4 v[20:23], v0, s[4:5] offset:2048
	s_nop 0
	v_cndmask_b32_e64 v6, v6, v7, s[0:1]
	v_mul_f32_e32 v7, 0x37800000, v6
	v_cndmask_b32_e32 v6, v6, v7, vcc
	v_mov_b32_e32 v7, 0x260
	v_cmp_class_f32_e32 vcc, v1, v7
	s_nop 1
	v_cndmask_b32_e32 v1, v6, v1, vcc
	v_div_scale_f32 v32, s[0:1], v1, v1, 1.0
	v_rcp_f32_e32 v33, v32
	v_lshl_add_u64 v[6:7], v[2:3], 0, v[4:5]
	v_div_scale_f32 v34, vcc, 1.0, v1, 1.0
	v_fma_f32 v2, -v32, v33, 1.0
	v_fmac_f32_e32 v33, v2, v33
	v_mul_f32_e32 v35, v34, v33
	v_fma_f32 v2, -v32, v35, v34
	v_fmac_f32_e32 v35, v2, v33
	v_fma_f32 v32, -v32, v35, v34
	global_load_dwordx4 v[2:5], v0, s[10:11] offset:3072
	v_div_fmas_f32 v52, v32, v33, v35
	global_load_dwordx4 v[32:35], v0, s[4:5] offset:3072
	v_div_fixup_f32 v0, v52, v1, 1.0
	v_pk_mul_f32 v[36:37], v[36:37], v[0:1] op_sel_hi:[1,0]
	s_waitcnt vmcnt(5)
	v_pk_fma_f32 v[12:13], v[24:25], v[36:37], v[12:13]
	v_pk_mul_f32 v[24:25], v[38:39], v[0:1] op_sel_hi:[1,0]
	v_cvt_pk_f16_f32 v12, v12, v13
	v_pk_fma_f32 v[14:15], v[26:27], v[24:25], v[14:15]
	s_nop 0
	v_cvt_pk_f16_f32 v13, v14, v15
	global_store_dwordx2 v[6:7], v[12:13], off
	v_pk_mul_f32 v[12:13], v[40:41], v[0:1] op_sel_hi:[1,0]
	v_pk_mul_f32 v[14:15], v[42:43], v[0:1] op_sel_hi:[1,0]
	s_waitcnt vmcnt(5)
	v_pk_fma_f32 v[12:13], v[28:29], v[12:13], v[16:17]
	v_pk_fma_f32 v[14:15], v[30:31], v[14:15], v[18:19]
	v_cvt_pk_f16_f32 v12, v12, v13
	v_cvt_pk_f16_f32 v13, v14, v15
	global_store_dwordx2 v[6:7], v[12:13], off offset:512
	v_pk_mul_f32 v[12:13], v[44:45], v[0:1] op_sel_hi:[1,0]
	s_waitcnt vmcnt(4)
	v_pk_fma_f32 v[8:9], v[12:13], v[8:9], v[20:21]
	v_pk_mul_f32 v[12:13], v[46:47], v[0:1] op_sel_hi:[1,0]
	v_cvt_pk_f16_f32 v8, v8, v9
	v_pk_fma_f32 v[10:11], v[12:13], v[10:11], v[22:23]
	s_nop 0
	v_cvt_pk_f16_f32 v9, v10, v11
	global_store_dwordx2 v[6:7], v[8:9], off offset:1024
	v_pk_mul_f32 v[8:9], v[48:49], v[0:1] op_sel_hi:[1,0]
	v_pk_mul_f32 v[0:1], v[50:51], v[0:1] op_sel_hi:[1,0]
	s_waitcnt vmcnt(3)
	v_pk_fma_f32 v[2:3], v[8:9], v[2:3], v[32:33]
	v_pk_fma_f32 v[0:1], v[0:1], v[4:5], v[34:35]
	v_cvt_pk_f16_f32 v2, v2, v3
	v_cvt_pk_f16_f32 v3, v0, v1
	global_store_dwordx2 v[6:7], v[2:3], off offset:1536
	s_endpgm
	s_endpgm
	s_endpgm
	s_endpgm
	s_endpgm
	s_endpgm
	s_endpgm
	s_endpgm
	s_endpgm
	s_endpgm
	s_endpgm
	s_endpgm
	s_endpgm
	s_endpgm

_Z9ln_kernelILi0EEvPKiPKfS3_PfS3_S3_PDF16_:
	s_load_dwordx8 s[4:11], s[0:1], 0x18
	v_and_b32_e32 v52, 63, v0
	v_lshrrev_b32_e32 v0, 6, v0
	v_lshl_or_b32 v0, s2, 2, v0
	v_ashrrev_i32_e32 v1, 31, v0
	v_lshlrev_b64 v[2:3], 12, v[0:1]
	s_waitcnt lgkmcnt(0)
	v_lshl_add_u64 v[4:5], s[4:5], 0, v[2:3]
	v_lshlrev_b32_e32 v2, 4, v52
	v_mov_b32_e32 v3, 0
	v_lshl_add_u64 v[20:21], v[4:5], 0, v[2:3]
	global_load_dwordx4 v[4:7], v[20:21], off offset:1024
	global_load_dwordx4 v[8:11], v[20:21], off offset:2048
	global_load_dwordx4 v[12:15], v[20:21], off
	global_load_dwordx4 v[16:19], v[20:21], off offset:3072
	v_mbcnt_lo_u32_b32 v20, -1, 0
	v_mbcnt_hi_u32_b32 v32, -1, v20
	v_and_b32_e32 v20, 64, v32
	v_xor_b32_e32 v21, 32, v32
	v_add_u32_e32 v34, 64, v20
	v_cmp_lt_i32_e32 vcc, v21, v34
	v_xor_b32_e32 v33, 16, v32
	s_mov_b32 s0, 0xf800000
	v_cndmask_b32_e32 v20, v32, v21, vcc
	v_lshlrev_b32_e32 v53, 2, v20
	v_cmp_lt_i32_e32 vcc, v33, v34
	v_lshlrev_b64 v[0:1], 11, v[0:1]
	v_lshl_add_u64 v[0:1], s[10:11], 0, v[0:1]
	s_waitcnt vmcnt(3)
	v_mov_b32_e32 v36, v5
	v_mov_b32_e32 v37, v6
	v_mov_b32_e32 v5, v7
	s_waitcnt vmcnt(1)
	v_mov_b32_e32 v22, v12
	v_mov_b32_e32 v23, v14
	v_mov_b32_e32 v24, v13
	v_mov_b32_e32 v25, v15
	v_mov_b32_e32 v6, v9
	v_mov_b32_e32 v20, v11
	s_waitcnt vmcnt(0)
	v_mov_b32_e32 v21, v16
	v_pk_add_f32 v[26:27], v[36:37], v[4:5]
	v_pk_add_f32 v[22:23], v[22:23], v[24:25]
	v_pk_add_f32 v[28:29], v[8:9], v[6:7]
	v_pk_add_f32 v[30:31], v[10:11], v[20:21]
	v_pk_add_f32 v[24:25], v[26:27], v[26:27] op_sel:[0,1] op_sel_hi:[1,0]
	v_add_f32_e32 v5, v22, v23
	v_mov_b32_e32 v29, v18
	v_mov_b32_e32 v31, v19
	v_add_f32_e32 v20, 0, v5
	v_mov_b32_e32 v25, v17
	v_pk_add_f32 v[22:23], v[28:29], v[30:31]
	v_pk_add_f32 v[20:21], v[20:21], v[24:25]
	v_pk_mov_b32 v[36:37], v[36:37], v[36:37] op_sel:[1,0]
	v_pk_add_f32 v[20:21], v[20:21], v[22:23]
	s_nop 0
	v_add_f32_e32 v5, v20, v21
	ds_bpermute_b32 v6, v53, v5
	v_cndmask_b32_e32 v21, v32, v33, vcc
	v_lshlrev_b32_e32 v54, 2, v21
	v_xor_b32_e32 v20, 8, v32
	v_cmp_lt_i32_e32 vcc, v20, v34
	s_waitcnt lgkmcnt(0)
	v_add_f32_e32 v5, v5, v6
	ds_bpermute_b32 v6, v54, v5
	v_cndmask_b32_e32 v20, v32, v20, vcc
	v_lshlrev_b32_e32 v55, 2, v20
	v_xor_b32_e32 v21, 4, v32
	v_cmp_lt_i32_e32 vcc, v21, v34
	s_waitcnt lgkmcnt(0)
	v_add_f32_e32 v5, v5, v6
	ds_bpermute_b32 v6, v55, v5
	v_cndmask_b32_e32 v21, v32, v21, vcc
	v_lshlrev_b32_e32 v56, 2, v21
	v_xor_b32_e32 v20, 2, v32
	v_cmp_lt_i32_e32 vcc, v20, v34
	s_waitcnt lgkmcnt(0)
	v_add_f32_e32 v5, v5, v6
	ds_bpermute_b32 v6, v56, v5
	v_cndmask_b32_e32 v20, v32, v20, vcc
	v_lshlrev_b32_e32 v57, 2, v20
	v_xor_b32_e32 v21, 1, v32
	v_cmp_lt_i32_e32 vcc, v21, v34
	s_waitcnt lgkmcnt(0)
	v_add_f32_e32 v5, v5, v6
	ds_bpermute_b32 v6, v57, v5
	v_cndmask_b32_e32 v20, v32, v21, vcc
	v_lshlrev_b32_e32 v58, 2, v20
	global_load_dwordx4 v[20:23], v2, s[6:7]
	global_load_dwordx4 v[24:27], v2, s[8:9]
	global_load_dwordx4 v[28:31], v2, s[6:7] offset:1024
	global_load_dwordx4 v[32:35], v2, s[8:9] offset:1024
	s_waitcnt lgkmcnt(0)
	v_add_f32_e32 v6, v5, v6
	ds_bpermute_b32 v38, v58, v6
	v_mov_b32_e32 v5, v37
	v_mov_b32_e32 v37, v7
	s_waitcnt lgkmcnt(0)
	v_add_f32_e32 v6, v6, v38
	v_mul_f32_e32 v6, 0x3a800000, v6
	v_pk_add_f32 v[38:39], v[12:13], v[6:7] op_sel_hi:[1,0] neg_lo:[0,1] neg_hi:[0,1]
	v_pk_add_f32 v[40:41], v[14:15], v[6:7] op_sel_hi:[1,0] neg_lo:[0,1] neg_hi:[0,1]
	v_pk_add_f32 v[46:47], v[4:5], v[6:7] op_sel_hi:[1,0] neg_lo:[0,1] neg_hi:[0,1]
	v_pk_add_f32 v[36:37], v[36:37], v[6:7] op_sel_hi:[1,0] neg_lo:[0,1] neg_hi:[0,1]
	v_pk_add_f32 v[42:43], v[16:17], v[6:7] op_sel_hi:[1,0] neg_lo:[0,1] neg_hi:[0,1]
	v_pk_add_f32 v[44:45], v[18:19], v[6:7] op_sel_hi:[1,0] neg_lo:[0,1] neg_hi:[0,1]
	v_pk_add_f32 v[48:49], v[8:9], v[6:7] op_sel_hi:[1,0] neg_lo:[0,1] neg_hi:[0,1]
	v_pk_add_f32 v[50:51], v[10:11], v[6:7] op_sel_hi:[1,0] neg_lo:[0,1] neg_hi:[0,1]
	v_mov_b32_e32 v6, v39
	v_mov_b32_e32 v7, v41
	v_mov_b32_e32 v14, v47
	v_mov_b32_e32 v15, v37
	v_mov_b32_e32 v4, v38
	v_mov_b32_e32 v5, v40
	v_mov_b32_e32 v12, v46
	v_mov_b32_e32 v13, v36
	v_pk_mul_f32 v[6:7], v[6:7], v[6:7]
	v_pk_mul_f32 v[14:15], v[14:15], v[14:15]
	v_mul_f32_e32 v16, v48, v48
	v_mul_f32_e32 v18, v50, v50
	v_pk_fma_f32 v[4:5], v[4:5], v[4:5], v[6:7]
	v_pk_fma_f32 v[6:7], v[12:13], v[12:13], v[14:15]
	v_pk_mul_f32 v[8:9], v[42:43], v[42:43]
	v_pk_mul_f32 v[10:11], v[44:45], v[44:45]
	v_pk_fma_f32 v[16:17], v[48:49], v[48:49], v[16:17] op_sel_hi:[1,1,0]
	v_pk_fma_f32 v[18:19], v[50:51], v[50:51], v[18:19] op_sel_hi:[1,1,0]
	v_pk_add_f32 v[4:5], v[4:5], v[4:5] op_sel_hi:[0,1]
	v_pk_add_f32 v[6:7], v[6:7], v[6:7] op_sel_hi:[0,1]
	v_mov_b32_e32 v16, v8
	v_mov_b32_e32 v18, v9
	v_mov_b32_e32 v4, v10
	v_mov_b32_e32 v6, v11
	v_pk_add_f32 v[8:9], v[16:17], v[18:19]
	v_pk_add_f32 v[4:5], v[4:5], v[6:7]
	s_nop 0
	v_pk_add_f32 v[4:5], v[8:9], v[4:5]
	s_nop 0
	v_add_f32_e32 v59, v4, v5
	global_load_dwordx4 v[4:7], v2, s[6:7] offset:2048
	global_load_dwordx4 v[8:11], v2, s[8:9] offset:2048
	global_load_dwordx4 v[12:15], v2, s[6:7] offset:3072
	global_load_dwordx4 v[16:19], v2, s[8:9] offset:3072
	ds_bpermute_b32 v53, v53, v59
	s_waitcnt lgkmcnt(0)
	v_add_f32_e32 v2, v59, v53
	ds_bpermute_b32 v53, v54, v2
	v_mov_b32_e32 v54, 0x3727c5ac
	s_waitcnt lgkmcnt(0)
	v_add_f32_e32 v2, v2, v53
	ds_bpermute_b32 v53, v55, v2
	v_mov_b32_e32 v55, 0x260
	s_waitcnt lgkmcnt(0)
	v_add_f32_e32 v2, v2, v53
	ds_bpermute_b32 v53, v56, v2
	s_waitcnt lgkmcnt(0)
	v_add_f32_e32 v2, v2, v53
	ds_bpermute_b32 v53, v57, v2
	s_waitcnt lgkmcnt(0)
	v_add_f32_e32 v2, v2, v53
	ds_bpermute_b32 v53, v58, v2
	s_waitcnt lgkmcnt(0)
	v_add_f32_e32 v2, v2, v53
	v_fmac_f32_e32 v54, 0x3a800000, v2
	v_mul_f32_e32 v2, 0x4f800000, v54
	v_cmp_gt_f32_e32 vcc, s0, v54
	s_nop 1
	v_cndmask_b32_e32 v53, v54, v2, vcc
	v_sqrt_f32_e32 v54, v53
	v_lshlrev_b32_e32 v2, 3, v52
	v_lshl_add_u64 v[0:1], v[0:1], 0, v[2:3]
	v_add_u32_e32 v52, -1, v54
	v_add_u32_e32 v56, 1, v54
	v_fma_f32 v57, -v52, v54, v53
	v_fma_f32 v58, -v56, v54, v53
	v_cmp_ge_f32_e64 s[0:1], 0, v57
	s_nop 1
	v_cndmask_b32_e64 v52, v54, v52, s[0:1]
	v_cmp_lt_f32_e64 s[0:1], 0, v58
	s_nop 1
	v_cndmask_b32_e64 v52, v52, v56, s[0:1]
	v_mul_f32_e32 v54, 0x37800000, v52
	v_cndmask_b32_e32 v52, v52, v54, vcc
	v_cmp_class_f32_e32 vcc, v53, v55
	s_nop 1
	v_cndmask_b32_e32 v52, v52, v53, vcc
	v_div_scale_f32 v53, s[0:1], v52, v52, 1.0
	v_rcp_f32_e32 v54, v53
	v_div_scale_f32 v2, vcc, 1.0, v52, 1.0
	v_fma_f32 v3, -v53, v54, 1.0
	v_fmac_f32_e32 v54, v3, v54
	v_mul_f32_e32 v3, v2, v54
	v_fma_f32 v55, -v53, v3, v2
	v_fmac_f32_e32 v3, v55, v54
	v_fma_f32 v2, -v53, v3, v2
	v_div_fmas_f32 v2, v2, v54, v3
	v_div_fixup_f32 v2, v2, v52, 1.0
	v_pk_mul_f32 v[38:39], v[38:39], v[2:3] op_sel_hi:[1,0]
	v_pk_mul_f32 v[40:41], v[40:41], v[2:3] op_sel_hi:[1,0]
	v_pk_mul_f32 v[46:47], v[46:47], v[2:3] op_sel_hi:[1,0]
	v_pk_mul_f32 v[36:37], v[36:37], v[2:3] op_sel_hi:[1,0]
	v_pk_mul_f32 v[48:49], v[48:49], v[2:3] op_sel_hi:[1,0]
	v_pk_mul_f32 v[50:51], v[50:51], v[2:3] op_sel_hi:[1,0]
	v_pk_mul_f32 v[42:43], v[42:43], v[2:3] op_sel_hi:[1,0]
	v_pk_mul_f32 v[2:3], v[44:45], v[2:3] op_sel_hi:[1,0]
	s_waitcnt vmcnt(6)
	v_pk_fma_f32 v[20:21], v[20:21], v[38:39], v[24:25]
	v_pk_fma_f32 v[22:23], v[22:23], v[40:41], v[26:27]
	s_waitcnt vmcnt(4)
	v_pk_fma_f32 v[24:25], v[28:29], v[46:47], v[32:33]
	v_pk_fma_f32 v[26:27], v[30:31], v[36:37], v[34:35]
	s_waitcnt vmcnt(2)
	v_pk_fma_f32 v[4:5], v[48:49], v[4:5], v[8:9]
	v_pk_fma_f32 v[6:7], v[50:51], v[6:7], v[10:11]
	s_waitcnt vmcnt(0)
	v_pk_fma_f32 v[8:9], v[42:43], v[12:13], v[16:17]
	v_pk_fma_f32 v[2:3], v[2:3], v[14:15], v[18:19]
	v_cvt_pk_f16_f32 v10, v20, v21
	v_cvt_pk_f16_f32 v11, v22, v23
	v_cvt_pk_f16_f32 v12, v24, v25
	v_cvt_pk_f16_f32 v13, v26, v27
	v_cvt_pk_f16_f32 v4, v4, v5
	v_cvt_pk_f16_f32 v5, v6, v7
	v_cvt_pk_f16_f32 v6, v8, v9
	v_cvt_pk_f16_f32 v7, v2, v3
	global_store_dwordx2 v[0:1], v[10:11], off
	global_store_dwordx2 v[0:1], v[12:13], off offset:512
	global_store_dwordx2 v[0:1], v[4:5], off offset:1024
	global_store_dwordx2 v[0:1], v[6:7], off offset:1536
	s_endpgm
	s_endpgm
	s_endpgm
	s_endpgm
	s_endpgm
	s_endpgm
	s_endpgm
	s_endpgm
	s_endpgm
	s_endpgm
	s_endpgm
	s_endpgm
	s_endpgm
	s_endpgm
	s_endpgm
	s_endpgm
	s_endpgm
	s_endpgm
	s_endpgm
	s_endpgm
	s_endpgm
	s_endpgm
	s_endpgm
	s_endpgm
	s_endpgm
	s_endpgm
	s_endpgm
	s_endpgm
	s_endpgm
	s_endpgm
	s_endpgm
	s_endpgm
	s_endpgm
	s_endpgm
	s_endpgm
	s_endpgm
	s_endpgm
	s_endpgm
	s_endpgm
	s_endpgm
	s_endpgm
	s_endpgm
	s_endpgm
	s_endpgm

_Z9ln_kernelILi4EEvPKiPKfS3_PfS3_S3_PDF16_:
	s_load_dwordx8 s[4:11], s[0:1], 0x8
	v_and_b32_e32 v12, 63, v0
	v_lshrrev_b32_e32 v0, 6, v0
	v_lshl_or_b32 v0, s2, 2, v0
	v_ashrrev_i32_e32 v1, 31, v0
	v_lshlrev_b64 v[24:25], 11, v[0:1]
	v_mov_b32_e32 v29, 0
	s_waitcnt lgkmcnt(0)
	v_lshl_add_u64 v[2:3], s[4:5], 0, v[24:25]
	v_lshlrev_b32_e32 v26, 3, v12
	v_mov_b32_e32 v27, v29
	v_lshl_add_u64 v[4:5], v[2:3], 0, v[26:27]
	s_mov_b64 s[2:3], 0x400000
	v_lshl_add_u64 v[10:11], v[4:5], 0, s[2:3]
	global_load_dwordx2 v[6:7], v[4:5], off offset:512
	global_load_dwordx2 v[8:9], v[4:5], off
	global_load_dwordx2 v[46:47], v[10:11], off offset:512
	s_mov_b32 s2, 0x400000
	v_add_co_u32_e32 v2, vcc, s2, v4
	v_lshlrev_b64 v[0:1], 12, v[0:1]
	s_nop 0
	v_addc_co_u32_e32 v3, vcc, 0, v5, vcc
	global_load_dwordx2 v[48:49], v[2:3], off
	v_lshl_add_u64 v[0:1], s[8:9], 0, v[0:1]
	v_lshlrev_b32_e32 v28, 4, v12
	v_lshl_add_u64 v[50:51], v[0:1], 0, v[28:29]
	global_load_dwordx4 v[0:3], v[50:51], off
	global_load_dwordx4 v[34:37], v28, s[6:7] offset:1024
	global_load_dwordx4 v[38:41], v[50:51], off offset:1024
	global_load_dwordx2 v[52:53], v[4:5], off offset:1024
	global_load_dwordx2 v[54:55], v[10:11], off offset:1024
	global_load_dwordx2 v[32:33], v[4:5], off offset:1536
	global_load_dwordx2 v[30:31], v[10:11], off offset:1536
	global_load_dwordx4 v[16:19], v[50:51], off offset:2048
	global_load_dwordx4 v[42:45], v28, s[6:7]
	global_load_dwordx4 v[20:23], v28, s[6:7] offset:2048
	global_load_dwordx4 v[12:15], v[50:51], off offset:3072
	global_load_dwordx4 v[60:63], v28, s[6:7] offset:3072
	s_load_dwordx4 s[4:7], s[0:1], 0x28
	s_mov_b32 s0, 0xf800000
	s_waitcnt lgkmcnt(0)
	v_lshl_add_u64 v[24:25], s[6:7], 0, v[24:25]
	v_lshl_add_u64 v[24:25], v[24:25], 0, v[26:27]
	s_waitcnt vmcnt(15)
	v_cvt_f32_f16_e32 v4, v6
	v_cvt_f32_f16_sdwa v5, v6 dst_sel:DWORD dst_unused:UNUSED_PAD src0_sel:WORD_1
	v_cvt_f32_f16_e32 v56, v7
	v_cvt_f32_f16_sdwa v57, v7 dst_sel:DWORD dst_unused:UNUSED_PAD src0_sel:WORD_1
	s_waitcnt vmcnt(13)
	v_cvt_f32_f16_e32 v6, v46
	v_cvt_f32_f16_sdwa v7, v46 dst_sel:DWORD dst_unused:UNUSED_PAD src0_sel:WORD_1
	v_cvt_f32_f16_e32 v58, v47
	v_cvt_f32_f16_sdwa v59, v47 dst_sel:DWORD dst_unused:UNUSED_PAD src0_sel:WORD_1
	v_cvt_f32_f16_e32 v10, v8
	v_pk_add_f32 v[50:51], v[4:5], v[6:7]
	v_add_f32_e32 v58, v56, v58
	v_add_f32_e32 v57, v57, v59
	s_waitcnt vmcnt(10)
	v_mov_b32_e32 v56, v37
	s_waitcnt vmcnt(9)
	v_pk_add_f32 v[38:39], v[38:39], v[50:51]
	v_add_f32_e32 v37, v40, v58
	v_add_f32_e32 v40, v41, v57
	s_waitcnt vmcnt(8)
	v_cvt_f32_f16_e32 v41, v52
	v_cvt_f32_f16_sdwa v50, v52 dst_sel:DWORD dst_unused:UNUSED_PAD src0_sel:WORD_1
	s_waitcnt vmcnt(7)
	v_cvt_f32_f16_e32 v52, v54
	v_cvt_f32_f16_sdwa v11, v8 dst_sel:DWORD dst_unused:UNUSED_PAD src0_sel:WORD_1
	v_cvt_f32_f16_e32 v46, v48
	v_cvt_f32_f16_sdwa v47, v48 dst_sel:DWORD dst_unused:UNUSED_PAD src0_sel:WORD_1
	v_cvt_f32_f16_e32 v8, v9
	v_cvt_f32_f16_sdwa v9, v9 dst_sel:DWORD dst_unused:UNUSED_PAD src0_sel:WORD_1
	v_cvt_f32_f16_e32 v48, v49
	v_cvt_f32_f16_sdwa v49, v49 dst_sel:DWORD dst_unused:UNUSED_PAD src0_sel:WORD_1
	v_cvt_f32_f16_e32 v51, v53
	v_cvt_f32_f16_sdwa v53, v53 dst_sel:DWORD dst_unused:UNUSED_PAD src0_sel:WORD_1
	v_pk_add_f32 v[34:35], v[34:35], v[38:39]
	v_add_f32_e32 v36, v36, v37
	v_cvt_f32_f16_sdwa v37, v54 dst_sel:DWORD dst_unused:UNUSED_PAD src0_sel:WORD_1
	v_cvt_f32_f16_e32 v38, v55
	v_cvt_f32_f16_sdwa v54, v55 dst_sel:DWORD dst_unused:UNUSED_PAD src0_sel:WORD_1
	s_waitcnt vmcnt(6)
	v_cvt_f32_f16_e32 v39, v32
	v_cvt_f32_f16_sdwa v57, v32 dst_sel:DWORD dst_unused:UNUSED_PAD src0_sel:WORD_1
	v_add_f32_e32 v32, v41, v52
	s_waitcnt vmcnt(4)
	v_add_f32_e32 v16, v16, v32
	v_pk_add_f32 v[46:47], v[10:11], v[46:47]
	s_waitcnt vmcnt(2)
	v_add_f32_e32 v32, v20, v16
	v_mbcnt_lo_u32_b32 v16, -1, 0
	v_pk_add_f32 v[48:49], v[8:9], v[48:49]
	v_pk_add_f32 v[46:47], v[0:1], v[46:47]
	v_add_f32_e32 v38, v51, v38
	v_cvt_f32_f16_e32 v51, v30
	v_cvt_f32_f16_sdwa v41, v30 dst_sel:DWORD dst_unused:UNUSED_PAD src0_sel:WORD_1
	v_add_f32_e32 v30, v53, v54
	v_mbcnt_hi_u32_b32 v54, -1, v16
	v_pk_add_f32 v[48:49], v[2:3], v[48:49]
	v_pk_add_f32 v[42:43], v[42:43], v[46:47]
	v_cvt_f32_f16_e32 v47, v33
	v_cvt_f32_f16_e32 v53, v31
	v_and_b32_e32 v16, 64, v54
	v_pk_add_f32 v[44:45], v[44:45], v[48:49]
	v_cvt_f32_f16_sdwa v49, v33 dst_sel:DWORD dst_unused:UNUSED_PAD src0_sel:WORD_1
	v_cvt_f32_f16_sdwa v31, v31 dst_sel:DWORD dst_unused:UNUSED_PAD src0_sel:WORD_1
	v_add_u32_e32 v55, 64, v16
	v_xor_b32_e32 v16, 32, v54
	v_cmp_lt_i32_e32 vcc, v16, v55
	v_add_f32_e32 v52, v50, v37
	v_add_f32_e32 v18, v18, v38
	v_cndmask_b32_e32 v16, v54, v16, vcc
	v_mov_b32_e32 v46, v17
	v_mov_b32_e32 v38, v44
	v_mov_b32_e32 v50, v45
	v_lshlrev_b32_e32 v58, 2, v16
	v_pk_add_f32 v[16:17], v[46:47], v[52:53]
	v_mov_b32_e32 v20, v21
	s_waitcnt vmcnt(1)
	v_mov_b32_e32 v21, v14
	v_mov_b32_e32 v48, v19
	v_pk_add_f32 v[38:39], v[38:39], v[50:51]
	v_pk_add_f32 v[50:51], v[42:43], v[42:43] op_sel:[0,1] op_sel_hi:[1,0]
	v_pk_add_f32 v[40:41], v[56:57], v[40:41]
	v_pk_add_f32 v[20:21], v[20:21], v[16:17]
	v_pk_add_f32 v[16:17], v[48:49], v[30:31]
	v_mov_b32_e32 v14, v23
	v_mov_b32_e32 v37, v13
	v_pk_add_f32 v[46:47], v[34:35], v[34:35] op_sel:[0,1] op_sel_hi:[1,0]
	v_mov_b32_e32 v51, v12
	v_add_f32_e32 v22, v22, v18
	v_pk_add_f32 v[30:31], v[14:15], v[16:17]
	v_pk_add_f32 v[18:19], v[36:37], v[40:41]
	s_waitcnt vmcnt(0)
	v_mov_b32_e32 v47, v61
	v_mov_b32_e32 v33, v62
	v_mov_b32_e32 v23, v63
	v_pk_add_f32 v[12:13], v[50:51], v[38:39]
	v_mov_b32_e32 v38, v29
	v_mov_b32_e32 v39, v60
	v_pk_add_f32 v[46:47], v[46:47], v[18:19]
	v_pk_add_f32 v[48:49], v[32:33], v[20:21]
	v_pk_add_f32 v[52:53], v[22:23], v[30:31]
	v_pk_add_f32 v[12:13], v[38:39], v[12:13]
	v_pk_add_f32 v[18:19], v[48:49], v[52:53]
	v_pk_add_f32 v[38:39], v[12:13], v[46:47]
	v_mov_b32_e32 v37, v40
	v_pk_add_f32 v[18:19], v[38:39], v[18:19]
	v_mov_b32_e32 v33, v20
	v_add_f32_e32 v12, v18, v19
	ds_bpermute_b32 v18, v58, v12
	v_xor_b32_e32 v19, 16, v54
	v_cmp_lt_i32_e32 vcc, v19, v55
	v_mov_b32_e32 v23, v30
	v_mov_b32_e32 v46, v13
	v_cndmask_b32_e32 v19, v54, v19, vcc
	v_lshlrev_b32_e32 v29, 2, v19
	s_waitcnt lgkmcnt(0)
	v_add_f32_e32 v12, v12, v18
	ds_bpermute_b32 v18, v29, v12
	v_xor_b32_e32 v19, 8, v54
	v_cmp_lt_i32_e32 vcc, v19, v55
	v_mov_b32_e32 v52, v49
	global_load_dwordx4 v[4:7], v28, s[10:11]
	global_load_dwordx4 v[8:11], v28, s[10:11] offset:1024
	v_cndmask_b32_e32 v19, v54, v19, vcc
	v_lshlrev_b32_e32 v48, 2, v19
	s_waitcnt lgkmcnt(0)
	v_add_f32_e32 v12, v12, v18
	ds_bpermute_b32 v18, v48, v12
	v_xor_b32_e32 v19, 4, v54
	v_cmp_lt_i32_e32 vcc, v19, v55
	global_load_dwordx4 v[0:3], v28, s[10:11] offset:2048
	global_load_dwordx4 v[14:17], v28, s[10:11] offset:3072
	v_cndmask_b32_e32 v19, v54, v19, vcc
	v_lshlrev_b32_e32 v59, 2, v19
	s_waitcnt lgkmcnt(0)
	v_add_f32_e32 v12, v12, v18
	ds_bpermute_b32 v18, v59, v12
	v_xor_b32_e32 v19, 2, v54
	v_cmp_lt_i32_e32 vcc, v19, v55
	s_waitcnt lgkmcnt(0)
	v_add_f32_e32 v12, v12, v18
	v_cndmask_b32_e32 v19, v54, v19, vcc
	v_lshlrev_b32_e32 v60, 2, v19
	ds_bpermute_b32 v18, v60, v12
	v_xor_b32_e32 v19, 1, v54
	v_cmp_lt_i32_e32 vcc, v19, v55
	s_waitcnt lgkmcnt(0)
	v_add_f32_e32 v12, v12, v18
	v_cndmask_b32_e32 v19, v54, v19, vcc
	v_lshlrev_b32_e32 v61, 2, v19
	ds_bpermute_b32 v18, v61, v12
	s_waitcnt lgkmcnt(0)
	v_add_f32_e32 v12, v12, v18
	v_mul_f32_e32 v12, 0x3a800000, v12
	v_pk_add_f32 v[42:43], v[42:43], v[12:13] op_sel_hi:[1,0] neg_lo:[0,1] neg_hi:[0,1]
	v_pk_add_f32 v[44:45], v[44:45], v[12:13] op_sel_hi:[1,0] neg_lo:[0,1] neg_hi:[0,1]
	v_mov_b32_e32 v38, v43
	v_mov_b32_e32 v39, v45
	v_pk_add_f32 v[50:51], v[34:35], v[12:13] op_sel_hi:[1,0] neg_lo:[0,1] neg_hi:[0,1]
	v_pk_add_f32 v[54:55], v[36:37], v[12:13] op_sel_hi:[1,0] neg_lo:[0,1] neg_hi:[0,1]
	v_pk_add_f32 v[56:57], v[32:33], v[12:13] op_sel_hi:[1,0] neg_lo:[0,1] neg_hi:[0,1]
	v_mov_b32_e32 v18, v42
	v_mov_b32_e32 v19, v44
	v_pk_mul_f32 v[38:39], v[38:39], v[38:39]
	v_mov_b32_e32 v34, v51
	v_mov_b32_e32 v35, v55
	v_mul_f32_e32 v30, v56, v56
	v_pk_fma_f32 v[38:39], v[18:19], v[18:19], v[38:39]
	v_mov_b32_e32 v18, v50
	v_mov_b32_e32 v19, v54
	v_pk_mul_f32 v[34:35], v[34:35], v[34:35]
	v_pk_fma_f32 v[30:31], v[56:57], v[56:57], v[30:31] op_sel_hi:[1,1,0]
	v_pk_add_f32 v[22:23], v[22:23], v[12:13] op_sel_hi:[1,0] neg_lo:[0,1] neg_hi:[0,1]
	v_pk_fma_f32 v[34:35], v[18:19], v[18:19], v[34:35]
	v_mul_f32_e32 v30, v22, v22
	v_pk_add_f32 v[46:47], v[46:47], v[12:13] op_sel_hi:[1,0] neg_lo:[0,1] neg_hi:[0,1]
	v_pk_add_f32 v[12:13], v[52:53], v[12:13] op_sel_hi:[1,0] neg_lo:[0,1] neg_hi:[0,1]
	v_pk_add_f32 v[36:37], v[38:39], v[38:39] op_sel_hi:[0,1]
	v_pk_add_f32 v[34:35], v[34:35], v[34:35] op_sel_hi:[0,1]
	v_pk_fma_f32 v[32:33], v[22:23], v[22:23], v[30:31] op_sel_hi:[1,1,0]
	v_pk_mul_f32 v[38:39], v[46:47], v[46:47]
	v_pk_mul_f32 v[40:41], v[12:13], v[12:13]
	v_mov_b32_e32 v30, v38
	v_mov_b32_e32 v32, v39
	v_mov_b32_e32 v36, v40
	v_mov_b32_e32 v34, v41
	v_pk_add_f32 v[30:31], v[30:31], v[32:33]
	v_pk_add_f32 v[32:33], v[36:37], v[34:35]
	global_load_dwordx4 v[18:21], v28, s[4:5]
	v_pk_add_f32 v[30:31], v[30:31], v[32:33]
	s_nop 0
	v_add_f32_e32 v34, v30, v31
	ds_bpermute_b32 v35, v58, v34
	global_load_dwordx4 v[30:33], v28, s[4:5] offset:1024
	s_waitcnt lgkmcnt(0)
	v_add_f32_e32 v38, v34, v35
	ds_bpermute_b32 v29, v29, v38
	global_load_dwordx4 v[34:37], v28, s[4:5] offset:2048
	s_waitcnt lgkmcnt(0)
	v_add_f32_e32 v29, v38, v29
	global_load_dwordx4 v[38:41], v28, s[4:5] offset:3072
	ds_bpermute_b32 v48, v48, v29
	s_waitcnt lgkmcnt(0)
	v_add_f32_e32 v28, v29, v48
	ds_bpermute_b32 v29, v59, v28
	s_waitcnt lgkmcnt(0)
	v_add_f32_e32 v28, v28, v29
	ds_bpermute_b32 v29, v60, v28
	s_waitcnt lgkmcnt(0)
	v_add_f32_e32 v28, v28, v29
	ds_bpermute_b32 v29, v61, v28
	s_waitcnt lgkmcnt(0)
	v_add_f32_e32 v28, v28, v29
	v_mov_b32_e32 v29, 0x3727c5ac
	v_fmac_f32_e32 v29, 0x3a800000, v28
	v_mul_f32_e32 v28, 0x4f800000, v29
	v_cmp_gt_f32_e32 vcc, s0, v29
	s_nop 1
	v_cndmask_b32_e32 v28, v29, v28, vcc
	v_sqrt_f32_e32 v29, v28
	s_nop 0
	v_add_u32_e32 v48, -1, v29
	v_fma_f32 v49, -v48, v29, v28
	v_cmp_ge_f32_e64 s[0:1], 0, v49
	v_add_u32_e32 v49, 1, v29
	s_nop 0
	v_cndmask_b32_e64 v48, v29, v48, s[0:1]
	v_fma_f32 v29, -v49, v29, v28
	v_cmp_lt_f32_e64 s[0:1], 0, v29
	s_nop 1
	v_cndmask_b32_e64 v29, v48, v49, s[0:1]
	v_mul_f32_e32 v48, 0x37800000, v29
	v_cndmask_b32_e32 v29, v29, v48, vcc
	v_mov_b32_e32 v48, 0x260
	v_cmp_class_f32_e32 vcc, v28, v48
	s_nop 1
	v_cndmask_b32_e32 v28, v29, v28, vcc
	v_div_scale_f32 v29, s[0:1], v28, v28, 1.0
	v_rcp_f32_e32 v48, v29
	s_nop 0
	v_fma_f32 v26, -v29, v48, 1.0
	v_fmac_f32_e32 v48, v26, v48
	v_div_scale_f32 v26, vcc, 1.0, v28, 1.0
	v_mul_f32_e32 v27, v26, v48
	v_fma_f32 v49, -v29, v27, v26
	v_fmac_f32_e32 v27, v49, v48
	v_fma_f32 v26, -v29, v27, v26
	v_div_fmas_f32 v26, v26, v48, v27
	v_div_fixup_f32 v26, v26, v28, 1.0
	v_pk_mul_f32 v[28:29], v[42:43], v[26:27] op_sel_hi:[1,0]
	s_waitcnt vmcnt(3)
	v_pk_fma_f32 v[4:5], v[4:5], v[28:29], v[18:19]
	v_pk_mul_f32 v[18:19], v[44:45], v[26:27] op_sel_hi:[1,0]
	v_cvt_pk_f16_f32 v4, v4, v5
	v_pk_fma_f32 v[6:7], v[6:7], v[18:19], v[20:21]
	s_nop 0
	v_cvt_pk_f16_f32 v5, v6, v7
	global_store_dwordx2 v[24:25], v[4:5], off
	v_pk_mul_f32 v[4:5], v[50:51], v[26:27] op_sel_hi:[1,0]
	v_pk_mul_f32 v[6:7], v[54:55], v[26:27] op_sel_hi:[1,0]
	s_waitcnt vmcnt(3)
	v_pk_fma_f32 v[4:5], v[8:9], v[4:5], v[30:31]
	v_pk_fma_f32 v[6:7], v[10:11], v[6:7], v[32:33]
	v_cvt_pk_f16_f32 v4, v4, v5
	v_cvt_pk_f16_f32 v5, v6, v7
	global_store_dwordx2 v[24:25], v[4:5], off offset:512
	v_pk_mul_f32 v[4:5], v[56:57], v[26:27] op_sel_hi:[1,0]
	s_waitcnt vmcnt(3)
	v_pk_fma_f32 v[0:1], v[0:1], v[4:5], v[34:35]
	v_pk_mul_f32 v[4:5], v[22:23], v[26:27] op_sel_hi:[1,0]
	v_cvt_pk_f16_f32 v0, v0, v1
	v_pk_fma_f32 v[2:3], v[4:5], v[2:3], v[36:37]
	s_nop 0
	v_cvt_pk_f16_f32 v1, v2, v3
	global_store_dwordx2 v[24:25], v[0:1], off offset:1024
	v_pk_mul_f32 v[0:1], v[46:47], v[26:27] op_sel_hi:[1,0]
	v_pk_mul_f32 v[2:3], v[12:13], v[26:27] op_sel_hi:[1,0]
	s_waitcnt vmcnt(3)
	v_pk_fma_f32 v[0:1], v[0:1], v[14:15], v[38:39]
	v_pk_fma_f32 v[2:3], v[2:3], v[16:17], v[40:41]
	v_cvt_pk_f16_f32 v0, v0, v1
	v_cvt_pk_f16_f32 v1, v2, v3
	global_store_dwordx2 v[24:25], v[0:1], off offset:1536
	s_endpgm
	s_endpgm
	s_endpgm
	s_endpgm
	s_endpgm
	s_endpgm
	s_endpgm
	s_endpgm
	s_endpgm
	s_endpgm
	s_endpgm
	s_endpgm
	s_endpgm
	s_endpgm
	s_endpgm
	s_endpgm
	s_endpgm
	s_endpgm
	s_endpgm
	s_endpgm
	s_endpgm
	s_endpgm
	s_endpgm

amdhsa.kernels:
  - .agpr_count:     0
    .args:
      - .offset:         0
        .size:           400
        .value_kind:     by_value
    .group_segment_fixed_size: 33280
    .kernarg_segment_align: 8
    .kernarg_segment_size: 400
    .language:       OpenCL C
    .language_version:
      - 2
      - 0
    .max_flat_workgroup_size: 256
    .name:           _Z10wt_convert7CvtJobs
    .private_segment_fixed_size: 0
    .sgpr_count:     54
    .sgpr_spill_count: 0
    .symbol:         _Z10wt_convert7CvtJobs.kd
    .uniform_work_group_size: 1
    .uses_dynamic_stack: false
    .vgpr_count:     45
    .vgpr_spill_count: 0
    .wavefront_size: 64
  - .agpr_count:     0
    .args:
      - .actual_access:  read_only
        .address_space:  global
        .offset:         0
        .size:           8
        .value_kind:     global_buffer
      - .actual_access:  read_only
        .address_space:  global
        .offset:         8
        .size:           8
        .value_kind:     global_buffer
      - .actual_access:  read_only
        .address_space:  global
        .offset:         16
        .size:           8
        .value_kind:     global_buffer
      - .actual_access:  write_only
        .address_space:  global
        .offset:         24
        .size:           8
        .value_kind:     global_buffer
      - .actual_access:  read_only
        .address_space:  global
        .offset:         32
        .size:           8
        .value_kind:     global_buffer
      - .actual_access:  read_only
        .address_space:  global
        .offset:         40
        .size:           8
        .value_kind:     global_buffer
      - .actual_access:  write_only
        .address_space:  global
        .offset:         48
        .size:           8
        .value_kind:     global_buffer
      - .offset:         56
        .size:           400
        .value_kind:     by_value
    .group_segment_fixed_size: 33280
    .kernarg_segment_align: 8
    .kernarg_segment_size: 456
    .language:       OpenCL C
    .language_version:
      - 2
      - 0
    .max_flat_workgroup_size: 256
    .name:           _Z13embed_ln_convPKiPKfS2_PfS2_S2_PDF16_7CvtJobs
    .private_segment_fixed_size: 0
    .sgpr_count:     36
    .sgpr_spill_count: 0
    .symbol:         _Z13embed_ln_convPKiPKfS2_PfS2_S2_PDF16_7CvtJobs.kd
    .uniform_work_group_size: 1
    .uses_dynamic_stack: false
    .vgpr_count:     79
    .vgpr_spill_count: 0
    .wavefront_size: 64
  - .agpr_count:     0
    .args:
      - .address_space:  global
        .offset:         0
        .size:           8
        .value_kind:     global_buffer
      - .address_space:  global
        .offset:         8
        .size:           8
        .value_kind:     global_buffer
      - .actual_access:  write_only
        .address_space:  global
        .offset:         16
        .size:           8
        .value_kind:     global_buffer
      - .actual_access:  read_only
        .address_space:  global
        .offset:         24
        .size:           8
        .value_kind:     global_buffer
      - .offset:         32
        .size:           4
        .value_kind:     by_value
      - .offset:         36
        .size:           4
        .value_kind:     by_value
      - .offset:         40
        .size:           4
        .value_kind:     by_value
    .group_segment_fixed_size: 0
    .kernarg_segment_align: 8
    .kernarg_segment_size: 44
    .language:       OpenCL C
    .language_version:
      - 2
      - 0
    .max_flat_workgroup_size: 512
    .name:           _Z17gemm_256sq_8phasePKDF16_S0_PfPKfiii
    .private_segment_fixed_size: 0
    .sgpr_count:     47
    .sgpr_spill_count: 0
    .symbol:         _Z17gemm_256sq_8phasePKDF16_S0_PfPKfiii.kd
    .uniform_work_group_size: 1
    .uses_dynamic_stack: false
    .vgpr_count:     244
    .vgpr_spill_count: 0
    .wavefront_size: 64
  - .agpr_count:     0
    .args:
      - .actual_access:  read_only
        .address_space:  global
        .offset:         0
        .size:           8
        .value_kind:     global_buffer
      - .actual_access:  read_only
        .address_space:  global
        .offset:         8
        .size:           8
        .value_kind:     global_buffer
      - .actual_access:  read_only
        .address_space:  global
        .offset:         16
        .size:           8
        .value_kind:     global_buffer
      - .actual_access:  write_only
        .address_space:  global
        .offset:         24
        .size:           8
        .value_kind:     global_buffer
      - .offset:         32
        .size:           400
        .value_kind:     by_value
    .group_segment_fixed_size: 33280
    .kernarg_segment_align: 8
    .kernarg_segment_size: 432
    .language:       OpenCL C
    .language_version:
      - 2
      - 0
    .max_flat_workgroup_size: 256
    .name:           _Z11attn_kernelPKDF16_S0_S0_PDF16_7CvtJobs
    .private_segment_fixed_size: 0
    .sgpr_count:     36
    .sgpr_spill_count: 0
    .symbol:         _Z11attn_kernelPKDF16_S0_S0_PDF16_7CvtJobs.kd
    .uniform_work_group_size: 1
    .uses_dynamic_stack: false
    .vgpr_count:     116
    .vgpr_spill_count: 0
    .wavefront_size: 64
  - .agpr_count:     0
    .args:
      - .address_space:  global
        .offset:         0
        .size:           8
        .value_kind:     global_buffer
      - .address_space:  global
        .offset:         8
        .size:           8
        .value_kind:     global_buffer
      - .offset:         16
        .size:           4
        .value_kind:     by_value
      - .offset:         20
        .size:           4
        .value_kind:     by_value
      - .offset:         24
        .size:           4
        .value_kind:     by_value
      - .actual_access:  write_only
        .address_space:  global
        .offset:         32
        .size:           8
        .value_kind:     global_buffer
      - .actual_access:  read_only
        .address_space:  global
        .offset:         40
        .size:           8
        .value_kind:     global_buffer
      - .actual_access:  read_only
        .address_space:  global
        .offset:         48
        .size:           8
        .value_kind:     global_buffer
      - .offset:         56
        .size:           4
        .value_kind:     hidden_block_count_x
      - .offset:         60
        .size:           4
        .value_kind:     hidden_block_count_y
      - .offset:         64
        .size:           4
        .value_kind:     hidden_block_count_z
      - .offset:         68
        .size:           2
        .value_kind:     hidden_group_size_x
      - .offset:         70
        .size:           2
        .value_kind:     hidden_group_size_y
      - .offset:         72
        .size:           2
        .value_kind:     hidden_group_size_z
      - .offset:         74
        .size:           2
        .value_kind:     hidden_remainder_x
      - .offset:         76
        .size:           2
        .value_kind:     hidden_remainder_y
      - .offset:         78
        .size:           2
        .value_kind:     hidden_remainder_z
      - .offset:         96
        .size:           8
        .value_kind:     hidden_global_offset_x
      - .offset:         104
        .size:           8
        .value_kind:     hidden_global_offset_y
      - .offset:         112
        .size:           8
        .value_kind:     hidden_global_offset_z
      - .offset:         120
        .size:           2
        .value_kind:     hidden_grid_dims
      - .offset:         176
        .size:           4
        .value_kind:     hidden_dynamic_lds_size
    .group_segment_fixed_size: 0
    .kernarg_segment_align: 8
    .kernarg_segment_size: 312
    .language:       OpenCL C
    .language_version:
      - 2
      - 0
    .max_flat_workgroup_size: 512
    .name:           _Z5gemm8ILi192ELi2ELi3ELi0ELi1ELi16EEvPKDF16_S1_iiiPDF16_PfPKf
    .private_segment_fixed_size: 0
    .sgpr_count:     34
    .sgpr_spill_count: 0
    .symbol:         _Z5gemm8ILi192ELi2ELi3ELi0ELi1ELi16EEvPKDF16_S1_iiiPDF16_PfPKf.kd
    .uniform_work_group_size: 1
    .uses_dynamic_stack: false
    .vgpr_count:     125
    .vgpr_spill_count: 0
    .wavefront_size: 64
  - .agpr_count:     0
    .args:
      - .address_space:  global
        .offset:         0
        .size:           8
        .value_kind:     global_buffer
      - .address_space:  global
        .offset:         8
        .size:           8
        .value_kind:     global_buffer
      - .offset:         16
        .size:           4
        .value_kind:     by_value
      - .offset:         20
        .size:           4
        .value_kind:     by_value
      - .offset:         24
        .size:           4
        .value_kind:     by_value
      - .actual_access:  write_only
        .address_space:  global
        .offset:         32
        .size:           8
        .value_kind:     global_buffer
      - .actual_access:  read_only
        .address_space:  global
        .offset:         40
        .size:           8
        .value_kind:     global_buffer
      - .actual_access:  read_only
        .address_space:  global
        .offset:         48
        .size:           8
        .value_kind:     global_buffer
      - .offset:         56
        .size:           4
        .value_kind:     hidden_block_count_x
      - .offset:         60
        .size:           4
        .value_kind:     hidden_block_count_y
      - .offset:         64
        .size:           4
        .value_kind:     hidden_block_count_z
      - .offset:         68
        .size:           2
        .value_kind:     hidden_group_size_x
      - .offset:         70
        .size:           2
        .value_kind:     hidden_group_size_y
      - .offset:         72
        .size:           2
        .value_kind:     hidden_group_size_z
      - .offset:         74
        .size:           2
        .value_kind:     hidden_remainder_x
      - .offset:         76
        .size:           2
        .value_kind:     hidden_remainder_y
      - .offset:         78
        .size:           2
        .value_kind:     hidden_remainder_z
      - .offset:         96
        .size:           8
        .value_kind:     hidden_global_offset_x
      - .offset:         104
        .size:           8
        .value_kind:     hidden_global_offset_y
      - .offset:         112
        .size:           8
        .value_kind:     hidden_global_offset_z
      - .offset:         120
        .size:           2
        .value_kind:     hidden_grid_dims
      - .offset:         176
        .size:           4
        .value_kind:     hidden_dynamic_lds_size
    .group_segment_fixed_size: 0
    .kernarg_segment_align: 8
    .kernarg_segment_size: 312
    .language:       OpenCL C
    .language_version:
      - 2
      - 0
    .max_flat_workgroup_size: 512
    .name:           _Z5gemm8ILi128ELi2ELi2ELi2ELi1ELi16EEvPKDF16_S1_iiiPDF16_PfPKf
    .private_segment_fixed_size: 0
    .sgpr_count:     30
    .sgpr_spill_count: 0
    .symbol:         _Z5gemm8ILi128ELi2ELi2ELi2ELi1ELi16EEvPKDF16_S1_iiiPDF16_PfPKf.kd
    .uniform_work_group_size: 1
    .uses_dynamic_stack: false
    .vgpr_count:     90
    .vgpr_spill_count: 0
    .wavefront_size: 64
  - .agpr_count:     0
    .args:
      - .address_space:  global
        .offset:         0
        .size:           8
        .value_kind:     global_buffer
      - .address_space:  global
        .offset:         8
        .size:           8
        .value_kind:     global_buffer
      - .offset:         16
        .size:           4
        .value_kind:     by_value
      - .offset:         20
        .size:           4
        .value_kind:     by_value
      - .offset:         24
        .size:           4
        .value_kind:     by_value
      - .actual_access:  read_only
        .address_space:  global
        .offset:         32
        .size:           8
        .value_kind:     global_buffer
      - .address_space:  global
        .offset:         40
        .size:           8
        .value_kind:     global_buffer
      - .actual_access:  read_only
        .address_space:  global
        .offset:         48
        .size:           8
        .value_kind:     global_buffer
      - .offset:         56
        .size:           4
        .value_kind:     hidden_block_count_x
      - .offset:         60
        .size:           4
        .value_kind:     hidden_block_count_y
      - .offset:         64
        .size:           4
        .value_kind:     hidden_block_count_z
      - .offset:         68
        .size:           2
        .value_kind:     hidden_group_size_x
      - .offset:         70
        .size:           2
        .value_kind:     hidden_group_size_y
      - .offset:         72
        .size:           2
        .value_kind:     hidden_group_size_z
      - .offset:         74
        .size:           2
        .value_kind:     hidden_remainder_x
      - .offset:         76
        .size:           2
        .value_kind:     hidden_remainder_y
      - .offset:         78
        .size:           2
        .value_kind:     hidden_remainder_z
      - .offset:         96
        .size:           8
        .value_kind:     hidden_global_offset_x
      - .offset:         104
        .size:           8
        .value_kind:     hidden_global_offset_y
      - .offset:         112
        .size:           8
        .value_kind:     hidden_global_offset_z
      - .offset:         120
        .size:           2
        .value_kind:     hidden_grid_dims
      - .offset:         176
        .size:           4
        .value_kind:     hidden_dynamic_lds_size
    .group_segment_fixed_size: 0
    .kernarg_segment_align: 8
    .kernarg_segment_size: 312
    .language:       OpenCL C
    .language_version:
      - 2
      - 0
    .max_flat_workgroup_size: 512
    .name:           _Z5gemm8ILi64ELi4ELi6ELi1ELi1ELi16EEvPKDF16_S1_iiiPDF16_PfPKf
    .private_segment_fixed_size: 0
    .sgpr_count:     34
    .sgpr_spill_count: 0
    .symbol:         _Z5gemm8ILi64ELi4ELi6ELi1ELi1ELi16EEvPKDF16_S1_iiiPDF16_PfPKf.kd
    .uniform_work_group_size: 1
    .uses_dynamic_stack: false
    .vgpr_count:     75
    .vgpr_spill_count: 0
    .wavefront_size: 64
  - .agpr_count:     0
    .args:
      - .address_space:  global
        .offset:         0
        .size:           8
        .value_kind:     global_buffer
      - .address_space:  global
        .offset:         8
        .size:           8
        .value_kind:     global_buffer
      - .offset:         16
        .size:           4
        .value_kind:     by_value
      - .offset:         20
        .size:           4
        .value_kind:     by_value
      - .offset:         24
        .size:           4
        .value_kind:     by_value
      - .actual_access:  write_only
        .address_space:  global
        .offset:         32
        .size:           8
        .value_kind:     global_buffer
      - .actual_access:  read_only
        .address_space:  global
        .offset:         40
        .size:           8
        .value_kind:     global_buffer
      - .actual_access:  read_only
        .address_space:  global
        .offset:         48
        .size:           8
        .value_kind:     global_buffer
    .group_segment_fixed_size: 0
    .kernarg_segment_align: 8
    .kernarg_segment_size: 56
    .language:       OpenCL C
    .language_version:
      - 2
      - 0
    .max_flat_workgroup_size: 512
    .name:           _Z5gemm8ILi128ELi2ELi4ELi4ELi2ELi32EEvPKDF16_S1_iiiPDF16_PfPKf
    .private_segment_fixed_size: 0
    .sgpr_count:     38
    .sgpr_spill_count: 0
    .symbol:         _Z5gemm8ILi128ELi2ELi4ELi4ELi2ELi32EEvPKDF16_S1_iiiPDF16_PfPKf.kd
    .uniform_work_group_size: 1
    .uses_dynamic_stack: false
    .vgpr_count:     107
    .vgpr_spill_count: 0
    .wavefront_size: 64
  - .agpr_count:     0
    .args:
      - .actual_access:  read_only
        .address_space:  global
        .offset:         0
        .size:           8
        .value_kind:     global_buffer
      - .actual_access:  read_only
        .address_space:  global
        .offset:         8
        .size:           8
        .value_kind:     global_buffer
      - .actual_access:  read_only
        .address_space:  global
        .offset:         16
        .size:           8
        .value_kind:     global_buffer
      - .address_space:  global
        .offset:         24
        .size:           8
        .value_kind:     global_buffer
      - .actual_access:  read_only
        .address_space:  global
        .offset:         32
        .size:           8
        .value_kind:     global_buffer
      - .actual_access:  read_only
        .address_space:  global
        .offset:         40
        .size:           8
        .value_kind:     global_buffer
      - .actual_access:  write_only
        .address_space:  global
        .offset:         48
        .size:           8
        .value_kind:     global_buffer
    .group_segment_fixed_size: 0
    .kernarg_segment_align: 8
    .kernarg_segment_size: 56
    .language:       OpenCL C
    .language_version:
      - 2
      - 0
    .max_flat_workgroup_size: 256
    .name:           _Z9ln_kernelILi2EEvPKiPKfS3_PfS3_S3_PDF16_
    .private_segment_fixed_size: 0
    .sgpr_count:     18
    .sgpr_spill_count: 0
    .symbol:         _Z9ln_kernelILi2EEvPKiPKfS3_PfS3_S3_PDF16_.kd
    .uniform_work_group_size: 1
    .uses_dynamic_stack: false
    .vgpr_count:     58
    .vgpr_spill_count: 0
    .wavefront_size: 64
  - .agpr_count:     0
    .args:
      - .actual_access:  read_only
        .address_space:  global
        .offset:         0
        .size:           8
        .value_kind:     global_buffer
      - .actual_access:  read_only
        .address_space:  global
        .offset:         8
        .size:           8
        .value_kind:     global_buffer
      - .actual_access:  read_only
        .address_space:  global
        .offset:         16
        .size:           8
        .value_kind:     global_buffer
      - .actual_access:  read_only
        .address_space:  global
        .offset:         24
        .size:           8
        .value_kind:     global_buffer
      - .actual_access:  read_only
        .address_space:  global
        .offset:         32
        .size:           8
        .value_kind:     global_buffer
      - .actual_access:  read_only
        .address_space:  global
        .offset:         40
        .size:           8
        .value_kind:     global_buffer
      - .actual_access:  write_only
        .address_space:  global
        .offset:         48
        .size:           8
        .value_kind:     global_buffer
    .group_segment_fixed_size: 0
    .kernarg_segment_align: 8
    .kernarg_segment_size: 56
    .language:       OpenCL C
    .language_version:
      - 2
      - 0
    .max_flat_workgroup_size: 256
    .name:           _Z9ln_kernelILi0EEvPKiPKfS3_PfS3_S3_PDF16_
    .private_segment_fixed_size: 0
    .sgpr_count:     18
    .sgpr_spill_count: 0
    .symbol:         _Z9ln_kernelILi0EEvPKiPKfS3_PfS3_S3_PDF16_.kd
    .uniform_work_group_size: 1
    .uses_dynamic_stack: false
    .vgpr_count:     60
    .vgpr_spill_count: 0
    .wavefront_size: 64
  - .agpr_count:     0
    .args:
      - .actual_access:  read_only
        .address_space:  global
        .offset:         0
        .size:           8
        .value_kind:     global_buffer
      - .actual_access:  read_only
        .address_space:  global
        .offset:         8
        .size:           8
        .value_kind:     global_buffer
      - .actual_access:  read_only
        .address_space:  global
        .offset:         16
        .size:           8
        .value_kind:     global_buffer
      - .actual_access:  read_only
        .address_space:  global
        .offset:         24
        .size:           8
        .value_kind:     global_buffer
      - .actual_access:  read_only
        .address_space:  global
        .offset:         32
        .size:           8
        .value_kind:     global_buffer
      - .actual_access:  read_only
        .address_space:  global
        .offset:         40
        .size:           8
        .value_kind:     global_buffer
      - .actual_access:  write_only
        .address_space:  global
        .offset:         48
        .size:           8
        .value_kind:     global_buffer
    .group_segment_fixed_size: 0
    .kernarg_segment_align: 8
    .kernarg_segment_size: 56
    .language:       OpenCL C
    .language_version:
      - 2
      - 0
    .max_flat_workgroup_size: 256
    .name:           _Z9ln_kernelILi4EEvPKiPKfS3_PfS3_S3_PDF16_
    .private_segment_fixed_size: 0
    .sgpr_count:     18
    .sgpr_spill_count: 0
    .symbol:         _Z9ln_kernelILi4EEvPKiPKfS3_PfS3_S3_PDF16_.kd
    .uniform_work_group_size: 1
    .uses_dynamic_stack: false
    .vgpr_count:     64
    .vgpr_spill_count: 0
    .wavefront_size: 64
